# speedup vs baseline: 1.0072x; 1.0043x over previous
.Lpf_vQ:
	s_lshl_b32 s25, s25, 6
	s_add_u32 s29, s10, s25
	s_lshr_b32 s29, s29, 4
	v_add_u32_e32 v5, s25, v3
	v_lshlrev_b32_e32 v5, 7, v5
	v_add_u32_e32 v15, v5, v6
	v_add_u32_e32 v16, v5, v7
	v_add_u32_e32 v5, 0x8000, v9
	v_add_u32_e32 v17, v5, v6
	v_add_u32_e32 v18, v5, v7
	v_add_u32_e32 v19, 0x18000, v15
	v_add_u32_e32 v20, 0x18000, v16
	v_add_u32_e32 v21, 0x18000, v17
	v_add_u32_e32 v22, 0x18000, v18
	v_lshlrev_b32_e32 v5, 4, v4
	global_load_dwordx4 v[24:27], v5, s[14:15] offset:0
	global_load_dwordx4 v[28:31], v5, s[14:15] offset:64
	global_load_dwordx4 v[32:35], v5, s[14:15] offset:128
	global_load_dwordx4 v[36:39], v5, s[14:15] offset:192
	global_load_dwordx4 v[40:43], v5, s[16:17] offset:0
	global_load_dwordx4 v[44:47], v5, s[16:17] offset:64
	global_load_dwordx4 v[48:51], v5, s[16:17] offset:128
	global_load_dwordx4 v[52:55], v5, s[16:17] offset:192
	s_add_u32 m0, s28, 0x0
	s_nop 0
	global_load_lds_dwordx4 v10, s[4:5]
	s_add_u32 m0, s28, 0x2000
	s_nop 0
	global_load_lds_dwordx4 v11, s[4:5]
	s_add_u32 m0, s28, 0x4000
	s_nop 0
	global_load_lds_dwordx4 v12, s[4:5]
	s_add_u32 m0, s28, 0x6000
	s_nop 0
	global_load_lds_dwordx4 v13, s[4:5]
	s_add_u32 s4, s4, s20
	s_addc_u32 s5, s5, 0
	s_add_u32 m0, s28, 0x8000
	s_nop 0
	global_load_lds_dwordx4 v10, s[6:7]
	s_add_u32 m0, s28, 0xa000
	s_nop 0
	global_load_lds_dwordx4 v11, s[6:7]
	s_add_u32 s6, s6, s20
	s_addc_u32 s7, s7, 0
	s_add_u32 m0, s28, 0xc000
	s_nop 0
	global_load_lds_dwordx4 v10, s[4:5]
	s_add_u32 m0, s28, 0xe000
	s_nop 0
	global_load_lds_dwordx4 v11, s[4:5]
	s_add_u32 m0, s28, 0x10000
	s_nop 0
	global_load_lds_dwordx4 v12, s[4:5]
	s_add_u32 m0, s28, 0x12000
	s_nop 0
	global_load_lds_dwordx4 v13, s[4:5]
	s_add_u32 s4, s4, s20
	s_addc_u32 s5, s5, 0
	s_add_u32 m0, s28, 0x14000
	s_nop 0
	global_load_lds_dwordx4 v10, s[6:7]
	s_add_u32 m0, s28, 0x16000
	s_nop 0
	global_load_lds_dwordx4 v11, s[6:7]
	s_add_u32 s6, s6, s20
	s_addc_u32 s7, s7, 0
	s_waitcnt vmcnt(6) lgkmcnt(0)
	s_barrier
	s_waitcnt lgkmcnt(7)
	ds_read_b128 v[136:139], v15
	ds_read_b128 v[156:159], v17
	ds_read_b128 v[160:163], v17 offset:2048
	ds_read_b128 v[164:167], v17 offset:4096
	ds_read_b128 v[168:171], v17 offset:6144
	ds_read_b128 v[140:143], v15 offset:2048
	ds_read_b128 v[144:147], v15 offset:4096
	ds_read_b128 v[148:151], v15 offset:6144
	s_waitcnt lgkmcnt(7)
	ds_read_b128 v[172:175], v16
	ds_read_b128 v[192:195], v18
	ds_read_b128 v[196:199], v18 offset:2048
	ds_read_b128 v[200:203], v18 offset:4096
	ds_read_b128 v[204:207], v18 offset:6144
	ds_read_b128 v[176:179], v16 offset:2048
	ds_read_b128 v[180:183], v16 offset:4096
	ds_read_b128 v[184:187], v16 offset:6144
	s_waitcnt lgkmcnt(14)
	v_mfma_f32_16x16x32_f16 v[56:59], v[156:159], v[136:139], 0
	s_add_u32 m0, s28, 0x18000
	s_nop 0
	global_load_lds_dwordx4 v10, s[4:5]
	s_waitcnt lgkmcnt(13)
	v_mfma_f32_16x16x32_f16 v[60:63], v[160:163], v[136:139], 0
	s_waitcnt lgkmcnt(12)
	v_mfma_f32_16x16x32_f16 v[64:67], v[164:167], v[136:139], 0
	s_add_u32 m0, s28, 0x1a000
	s_nop 0
	global_load_lds_dwordx4 v11, s[4:5]
	s_waitcnt lgkmcnt(11)
	v_mfma_f32_16x16x32_f16 v[68:71], v[168:171], v[136:139], 0
	s_waitcnt lgkmcnt(10)
	v_mfma_f32_16x16x32_f16 v[72:75], v[156:159], v[140:143], 0
	v_mfma_f32_16x16x32_f16 v[76:79], v[160:163], v[140:143], 0
	s_add_u32 m0, s28, 0x1c000
	s_nop 0
	global_load_lds_dwordx4 v12, s[4:5]
	v_mfma_f32_16x16x32_f16 v[80:83], v[164:167], v[140:143], 0
	v_mfma_f32_16x16x32_f16 v[84:87], v[168:171], v[140:143], 0
	s_waitcnt lgkmcnt(9)
	v_mfma_f32_16x16x32_f16 v[88:91], v[156:159], v[144:147], 0
	s_add_u32 m0, s28, 0x1e000
	s_nop 0
	global_load_lds_dwordx4 v13, s[4:5]
	s_add_u32 s4, s4, s20
	s_addc_u32 s5, s5, 0
	v_mfma_f32_16x16x32_f16 v[92:95], v[160:163], v[144:147], 0
	v_mfma_f32_16x16x32_f16 v[96:99], v[164:167], v[144:147], 0
	s_add_u32 m0, s28, 0x20000
	s_nop 0
	global_load_lds_dwordx4 v10, s[6:7]
	v_mfma_f32_16x16x32_f16 v[100:103], v[168:171], v[144:147], 0
	s_waitcnt lgkmcnt(8)
	v_mfma_f32_16x16x32_f16 v[104:107], v[156:159], v[148:151], 0
	v_mfma_f32_16x16x32_f16 v[108:111], v[160:163], v[148:151], 0
	s_add_u32 m0, s28, 0x22000
	s_nop 0
	global_load_lds_dwordx4 v11, s[6:7]
	s_add_u32 s6, s6, s20
	s_addc_u32 s7, s7, 0
	v_mfma_f32_16x16x32_f16 v[112:115], v[164:167], v[148:151], 0
	v_mfma_f32_16x16x32_f16 v[116:119], v[168:171], v[148:151], 0
	s_waitcnt vmcnt(6) lgkmcnt(0)
	s_barrier
	s_waitcnt lgkmcnt(7)
	ds_read_b128 v[136:139], v15 offset:49152
	ds_read_b128 v[156:159], v17 offset:49152
	ds_read_b128 v[160:163], v17 offset:51200
	ds_read_b128 v[164:167], v17 offset:53248
	ds_read_b128 v[168:171], v17 offset:55296
	ds_read_b128 v[140:143], v15 offset:51200
	ds_read_b128 v[144:147], v15 offset:53248
	ds_read_b128 v[148:151], v15 offset:55296
	s_waitcnt lgkmcnt(14)
	v_mfma_f32_16x16x32_f16 v[56:59], v[192:195], v[172:175], v[56:59]
	s_add_u32 m0, s28, 0x0
	s_nop 0
	global_load_lds_dwordx4 v10, s[4:5]
	s_waitcnt lgkmcnt(13)
	v_mfma_f32_16x16x32_f16 v[60:63], v[196:199], v[172:175], v[60:63]
	s_waitcnt lgkmcnt(12)
	v_mfma_f32_16x16x32_f16 v[64:67], v[200:203], v[172:175], v[64:67]
	s_waitcnt lgkmcnt(11)
	v_mfma_f32_16x16x32_f16 v[68:71], v[204:207], v[172:175], v[68:71]
	s_waitcnt lgkmcnt(10)
	v_mfma_f32_16x16x32_f16 v[72:75], v[192:195], v[176:179], v[72:75]
	v_mfma_f32_16x16x32_f16 v[76:79], v[196:199], v[176:179], v[76:79]
	s_add_u32 m0, s28, 0x2000
	s_nop 0
	global_load_lds_dwordx4 v11, s[4:5]
	v_mfma_f32_16x16x32_f16 v[80:83], v[200:203], v[176:179], v[80:83]
	v_mfma_f32_16x16x32_f16 v[84:87], v[204:207], v[176:179], v[84:87]
	s_waitcnt lgkmcnt(9)
	v_mfma_f32_16x16x32_f16 v[88:91], v[192:195], v[180:183], v[88:91]
	v_mfma_f32_16x16x32_f16 v[92:95], v[196:199], v[180:183], v[92:95]
	v_mfma_f32_16x16x32_f16 v[96:99], v[200:203], v[180:183], v[96:99]
	s_add_u32 m0, s28, 0x4000
	s_nop 0
	global_load_lds_dwordx4 v12, s[4:5]
	v_mfma_f32_16x16x32_f16 v[100:103], v[204:207], v[180:183], v[100:103]
	s_waitcnt lgkmcnt(8)
	v_mfma_f32_16x16x32_f16 v[104:107], v[192:195], v[184:187], v[104:107]
	v_mfma_f32_16x16x32_f16 v[108:111], v[196:199], v[184:187], v[108:111]
	v_mfma_f32_16x16x32_f16 v[112:115], v[200:203], v[184:187], v[112:115]
	v_mfma_f32_16x16x32_f16 v[116:119], v[204:207], v[184:187], v[116:119]
	s_waitcnt lgkmcnt(7)
	ds_read_b128 v[172:175], v16 offset:49152
	ds_read_b128 v[192:195], v18 offset:49152
	ds_read_b128 v[196:199], v18 offset:51200
	ds_read_b128 v[200:203], v18 offset:53248
	ds_read_b128 v[204:207], v18 offset:55296
	ds_read_b128 v[176:179], v16 offset:51200
	ds_read_b128 v[180:183], v16 offset:53248
	ds_read_b128 v[184:187], v16 offset:55296
	s_waitcnt lgkmcnt(14)
	v_mfma_f32_16x16x32_f16 v[56:59], v[156:159], v[136:139], v[56:59]
	s_add_u32 m0, s28, 0x6000
	s_nop 0
	global_load_lds_dwordx4 v13, s[4:5]
	s_add_u32 s4, s4, s20
	s_addc_u32 s5, s5, 0
	s_waitcnt lgkmcnt(13)
	v_mfma_f32_16x16x32_f16 v[60:63], v[160:163], v[136:139], v[60:63]
	s_waitcnt lgkmcnt(12)
	v_mfma_f32_16x16x32_f16 v[64:67], v[164:167], v[136:139], v[64:67]
	s_waitcnt lgkmcnt(11)
	v_mfma_f32_16x16x32_f16 v[68:71], v[168:171], v[136:139], v[68:71]
	s_waitcnt lgkmcnt(10)
	v_mfma_f32_16x16x32_f16 v[72:75], v[156:159], v[140:143], v[72:75]
	v_mfma_f32_16x16x32_f16 v[76:79], v[160:163], v[140:143], v[76:79]
	s_add_u32 m0, s28, 0x8000
	s_nop 0
	global_load_lds_dwordx4 v10, s[6:7]
	v_mfma_f32_16x16x32_f16 v[80:83], v[164:167], v[140:143], v[80:83]
	v_mfma_f32_16x16x32_f16 v[84:87], v[168:171], v[140:143], v[84:87]
	s_waitcnt lgkmcnt(9)
	v_mfma_f32_16x16x32_f16 v[88:91], v[156:159], v[144:147], v[88:91]
	v_mfma_f32_16x16x32_f16 v[92:95], v[160:163], v[144:147], v[92:95]
	v_mfma_f32_16x16x32_f16 v[96:99], v[164:167], v[144:147], v[96:99]
	s_add_u32 m0, s28, 0xa000
	s_nop 0
	global_load_lds_dwordx4 v11, s[6:7]
	s_add_u32 s6, s6, s20
	s_addc_u32 s7, s7, 0
	v_mfma_f32_16x16x32_f16 v[100:103], v[168:171], v[144:147], v[100:103]
	s_waitcnt lgkmcnt(8)
	v_mfma_f32_16x16x32_f16 v[104:107], v[156:159], v[148:151], v[104:107]
	v_mfma_f32_16x16x32_f16 v[108:111], v[160:163], v[148:151], v[108:111]
	v_mfma_f32_16x16x32_f16 v[112:115], v[164:167], v[148:151], v[112:115]
	v_mfma_f32_16x16x32_f16 v[116:119], v[168:171], v[148:151], v[116:119]
	s_waitcnt vmcnt(6) lgkmcnt(0)
	s_barrier
	s_waitcnt lgkmcnt(7)
	ds_read_b128 v[136:139], v19
	ds_read_b128 v[156:159], v21
	ds_read_b128 v[160:163], v21 offset:2048
	ds_read_b128 v[164:167], v21 offset:4096
	ds_read_b128 v[168:171], v21 offset:6144
	ds_read_b128 v[140:143], v19 offset:2048
	ds_read_b128 v[144:147], v19 offset:4096
	ds_read_b128 v[148:151], v19 offset:6144
	s_waitcnt lgkmcnt(14)
	v_mfma_f32_16x16x32_f16 v[56:59], v[192:195], v[172:175], v[56:59]
	s_add_u32 m0, s28, 0xc000
	s_nop 0
	global_load_lds_dwordx4 v10, s[4:5]
	s_waitcnt lgkmcnt(13)
	v_mfma_f32_16x16x32_f16 v[60:63], v[196:199], v[172:175], v[60:63]
	s_waitcnt lgkmcnt(12)
	v_mfma_f32_16x16x32_f16 v[64:67], v[200:203], v[172:175], v[64:67]
	s_waitcnt lgkmcnt(11)
	v_mfma_f32_16x16x32_f16 v[68:71], v[204:207], v[172:175], v[68:71]
	s_waitcnt lgkmcnt(10)
	v_mfma_f32_16x16x32_f16 v[72:75], v[192:195], v[176:179], v[72:75]
	v_mfma_f32_16x16x32_f16 v[76:79], v[196:199], v[176:179], v[76:79]
	s_add_u32 m0, s28, 0xe000
	s_nop 0
	global_load_lds_dwordx4 v11, s[4:5]
	v_mfma_f32_16x16x32_f16 v[80:83], v[200:203], v[176:179], v[80:83]
	v_mfma_f32_16x16x32_f16 v[84:87], v[204:207], v[176:179], v[84:87]
	s_waitcnt lgkmcnt(9)
	v_mfma_f32_16x16x32_f16 v[88:91], v[192:195], v[180:183], v[88:91]
	v_mfma_f32_16x16x32_f16 v[92:95], v[196:199], v[180:183], v[92:95]
	v_mfma_f32_16x16x32_f16 v[96:99], v[200:203], v[180:183], v[96:99]
	s_add_u32 m0, s28, 0x10000
	s_nop 0
	global_load_lds_dwordx4 v12, s[4:5]
	v_mfma_f32_16x16x32_f16 v[100:103], v[204:207], v[180:183], v[100:103]
	s_waitcnt lgkmcnt(8)
	v_mfma_f32_16x16x32_f16 v[104:107], v[192:195], v[184:187], v[104:107]
	v_mfma_f32_16x16x32_f16 v[108:111], v[196:199], v[184:187], v[108:111]
	v_mfma_f32_16x16x32_f16 v[112:115], v[200:203], v[184:187], v[112:115]
	v_mfma_f32_16x16x32_f16 v[116:119], v[204:207], v[184:187], v[116:119]
	s_waitcnt lgkmcnt(7)
	ds_read_b128 v[172:175], v20
	ds_read_b128 v[192:195], v22
	ds_read_b128 v[196:199], v22 offset:2048
	ds_read_b128 v[200:203], v22 offset:4096
	ds_read_b128 v[204:207], v22 offset:6144
	ds_read_b128 v[176:179], v20 offset:2048
	ds_read_b128 v[180:183], v20 offset:4096
	ds_read_b128 v[184:187], v20 offset:6144
	s_waitcnt lgkmcnt(14)
	v_mfma_f32_16x16x32_f16 v[56:59], v[156:159], v[136:139], v[56:59]
	s_add_u32 m0, s28, 0x12000
	s_nop 0
	global_load_lds_dwordx4 v13, s[4:5]
	s_add_u32 s4, s4, s20
	s_addc_u32 s5, s5, 0
	s_waitcnt lgkmcnt(13)
	v_mfma_f32_16x16x32_f16 v[60:63], v[160:163], v[136:139], v[60:63]
	s_waitcnt lgkmcnt(12)
	v_mfma_f32_16x16x32_f16 v[64:67], v[164:167], v[136:139], v[64:67]
	s_waitcnt lgkmcnt(11)
	v_mfma_f32_16x16x32_f16 v[68:71], v[168:171], v[136:139], v[68:71]
	s_waitcnt lgkmcnt(10)
	v_mfma_f32_16x16x32_f16 v[72:75], v[156:159], v[140:143], v[72:75]
	v_mfma_f32_16x16x32_f16 v[76:79], v[160:163], v[140:143], v[76:79]
	s_add_u32 m0, s28, 0x14000
	s_nop 0
	global_load_lds_dwordx4 v10, s[6:7]
	v_mfma_f32_16x16x32_f16 v[80:83], v[164:167], v[140:143], v[80:83]
	v_mfma_f32_16x16x32_f16 v[84:87], v[168:171], v[140:143], v[84:87]
	s_waitcnt lgkmcnt(9)
	v_mfma_f32_16x16x32_f16 v[88:91], v[156:159], v[144:147], v[88:91]
	v_mfma_f32_16x16x32_f16 v[92:95], v[160:163], v[144:147], v[92:95]
	v_mfma_f32_16x16x32_f16 v[96:99], v[164:167], v[144:147], v[96:99]
	s_add_u32 m0, s28, 0x16000
	s_nop 0
	global_load_lds_dwordx4 v11, s[6:7]
	s_add_u32 s6, s6, s20
	s_addc_u32 s7, s7, 0
	v_mfma_f32_16x16x32_f16 v[100:103], v[168:171], v[144:147], v[100:103]
	s_waitcnt lgkmcnt(8)
	v_mfma_f32_16x16x32_f16 v[104:107], v[156:159], v[148:151], v[104:107]
	v_mfma_f32_16x16x32_f16 v[108:111], v[160:163], v[148:151], v[108:111]
	v_mfma_f32_16x16x32_f16 v[112:115], v[164:167], v[148:151], v[112:115]
	v_mfma_f32_16x16x32_f16 v[116:119], v[168:171], v[148:151], v[116:119]
	s_waitcnt vmcnt(6) lgkmcnt(0)
	s_barrier
	s_waitcnt lgkmcnt(7)
	ds_read_b128 v[136:139], v15
	ds_read_b128 v[156:159], v17
	ds_read_b128 v[160:163], v17 offset:2048
	ds_read_b128 v[164:167], v17 offset:4096
	ds_read_b128 v[168:171], v17 offset:6144
	ds_read_b128 v[140:143], v15 offset:2048
	ds_read_b128 v[144:147], v15 offset:4096
	ds_read_b128 v[148:151], v15 offset:6144
	s_waitcnt lgkmcnt(14)
	v_mfma_f32_16x16x32_f16 v[56:59], v[192:195], v[172:175], v[56:59]
	s_add_u32 m0, s28, 0x18000
	s_nop 0
	global_load_lds_dwordx4 v10, s[4:5]
	s_waitcnt lgkmcnt(13)
	v_mfma_f32_16x16x32_f16 v[60:63], v[196:199], v[172:175], v[60:63]
	s_waitcnt lgkmcnt(12)
	v_mfma_f32_16x16x32_f16 v[64:67], v[200:203], v[172:175], v[64:67]
	s_waitcnt lgkmcnt(11)
	v_mfma_f32_16x16x32_f16 v[68:71], v[204:207], v[172:175], v[68:71]
	s_waitcnt lgkmcnt(10)
	v_mfma_f32_16x16x32_f16 v[72:75], v[192:195], v[176:179], v[72:75]
	v_mfma_f32_16x16x32_f16 v[76:79], v[196:199], v[176:179], v[76:79]
	s_add_u32 m0, s28, 0x1a000
	s_nop 0
	global_load_lds_dwordx4 v11, s[4:5]
	v_mfma_f32_16x16x32_f16 v[80:83], v[200:203], v[176:179], v[80:83]
	v_mfma_f32_16x16x32_f16 v[84:87], v[204:207], v[176:179], v[84:87]
	s_waitcnt lgkmcnt(9)
	v_mfma_f32_16x16x32_f16 v[88:91], v[192:195], v[180:183], v[88:91]
	v_mfma_f32_16x16x32_f16 v[92:95], v[196:199], v[180:183], v[92:95]
	v_mfma_f32_16x16x32_f16 v[96:99], v[200:203], v[180:183], v[96:99]
	s_add_u32 m0, s28, 0x1c000
	s_nop 0
	global_load_lds_dwordx4 v12, s[4:5]
	v_mfma_f32_16x16x32_f16 v[100:103], v[204:207], v[180:183], v[100:103]
	s_waitcnt lgkmcnt(8)
	v_mfma_f32_16x16x32_f16 v[104:107], v[192:195], v[184:187], v[104:107]
	v_mfma_f32_16x16x32_f16 v[108:111], v[196:199], v[184:187], v[108:111]
	v_mfma_f32_16x16x32_f16 v[112:115], v[200:203], v[184:187], v[112:115]
	v_mfma_f32_16x16x32_f16 v[116:119], v[204:207], v[184:187], v[116:119]
	s_waitcnt lgkmcnt(7)
	ds_read_b128 v[172:175], v16
	ds_read_b128 v[192:195], v18
	ds_read_b128 v[196:199], v18 offset:2048
	ds_read_b128 v[200:203], v18 offset:4096
	ds_read_b128 v[204:207], v18 offset:6144
	ds_read_b128 v[176:179], v16 offset:2048
	ds_read_b128 v[180:183], v16 offset:4096
	ds_read_b128 v[184:187], v16 offset:6144
	s_waitcnt lgkmcnt(14)
	v_mfma_f32_16x16x32_f16 v[56:59], v[156:159], v[136:139], v[56:59]
	s_add_u32 m0, s28, 0x1e000
	s_nop 0
	global_load_lds_dwordx4 v13, s[4:5]
	s_add_u32 s4, s4, s20
	s_addc_u32 s5, s5, 0
	s_waitcnt lgkmcnt(13)
	v_mfma_f32_16x16x32_f16 v[60:63], v[160:163], v[136:139], v[60:63]
	s_waitcnt lgkmcnt(12)
	v_mfma_f32_16x16x32_f16 v[64:67], v[164:167], v[136:139], v[64:67]
	s_waitcnt lgkmcnt(11)
	v_mfma_f32_16x16x32_f16 v[68:71], v[168:171], v[136:139], v[68:71]
	s_waitcnt lgkmcnt(10)
	v_mfma_f32_16x16x32_f16 v[72:75], v[156:159], v[140:143], v[72:75]
	v_mfma_f32_16x16x32_f16 v[76:79], v[160:163], v[140:143], v[76:79]
	s_add_u32 m0, s28, 0x20000
	s_nop 0
	global_load_lds_dwordx4 v10, s[6:7]
	v_mfma_f32_16x16x32_f16 v[80:83], v[164:167], v[140:143], v[80:83]
	v_mfma_f32_16x16x32_f16 v[84:87], v[168:171], v[140:143], v[84:87]
	s_waitcnt lgkmcnt(9)
	v_mfma_f32_16x16x32_f16 v[88:91], v[156:159], v[144:147], v[88:91]
	v_mfma_f32_16x16x32_f16 v[92:95], v[160:163], v[144:147], v[92:95]
	v_mfma_f32_16x16x32_f16 v[96:99], v[164:167], v[144:147], v[96:99]
	s_add_u32 m0, s28, 0x22000
	s_nop 0
	global_load_lds_dwordx4 v11, s[6:7]
	s_add_u32 s6, s6, s20
	s_addc_u32 s7, s7, 0
	v_mfma_f32_16x16x32_f16 v[100:103], v[168:171], v[144:147], v[100:103]
	s_waitcnt lgkmcnt(8)
	v_mfma_f32_16x16x32_f16 v[104:107], v[156:159], v[148:151], v[104:107]
	v_mfma_f32_16x16x32_f16 v[108:111], v[160:163], v[148:151], v[108:111]
	v_mfma_f32_16x16x32_f16 v[112:115], v[164:167], v[148:151], v[112:115]
	v_mfma_f32_16x16x32_f16 v[116:119], v[168:171], v[148:151], v[116:119]
	s_waitcnt vmcnt(6) lgkmcnt(0)
	s_barrier
	s_waitcnt lgkmcnt(7)
	ds_read_b128 v[136:139], v15 offset:49152
	ds_read_b128 v[156:159], v17 offset:49152
	ds_read_b128 v[160:163], v17 offset:51200
	ds_read_b128 v[164:167], v17 offset:53248
	ds_read_b128 v[168:171], v17 offset:55296
	ds_read_b128 v[140:143], v15 offset:51200
	ds_read_b128 v[144:147], v15 offset:53248
	ds_read_b128 v[148:151], v15 offset:55296
	s_waitcnt lgkmcnt(14)
	v_mfma_f32_16x16x32_f16 v[56:59], v[192:195], v[172:175], v[56:59]
	s_add_u32 m0, s28, 0x0
	s_nop 0
	global_load_lds_dwordx4 v10, s[4:5]
	s_waitcnt lgkmcnt(13)
	v_mfma_f32_16x16x32_f16 v[60:63], v[196:199], v[172:175], v[60:63]
	s_waitcnt lgkmcnt(12)
	v_mfma_f32_16x16x32_f16 v[64:67], v[200:203], v[172:175], v[64:67]
	s_waitcnt lgkmcnt(11)
	v_mfma_f32_16x16x32_f16 v[68:71], v[204:207], v[172:175], v[68:71]
	s_waitcnt lgkmcnt(10)
	v_mfma_f32_16x16x32_f16 v[72:75], v[192:195], v[176:179], v[72:75]
	v_mfma_f32_16x16x32_f16 v[76:79], v[196:199], v[176:179], v[76:79]
	s_add_u32 m0, s28, 0x2000
	s_nop 0
	global_load_lds_dwordx4 v11, s[4:5]
	v_mfma_f32_16x16x32_f16 v[80:83], v[200:203], v[176:179], v[80:83]
	v_mfma_f32_16x16x32_f16 v[84:87], v[204:207], v[176:179], v[84:87]
	s_waitcnt lgkmcnt(9)
	v_mfma_f32_16x16x32_f16 v[88:91], v[192:195], v[180:183], v[88:91]
	v_mfma_f32_16x16x32_f16 v[92:95], v[196:199], v[180:183], v[92:95]
	v_mfma_f32_16x16x32_f16 v[96:99], v[200:203], v[180:183], v[96:99]
	s_add_u32 m0, s28, 0x4000
	s_nop 0
	global_load_lds_dwordx4 v12, s[4:5]
	v_mfma_f32_16x16x32_f16 v[100:103], v[204:207], v[180:183], v[100:103]
	s_waitcnt lgkmcnt(8)
	v_mfma_f32_16x16x32_f16 v[104:107], v[192:195], v[184:187], v[104:107]
	v_mfma_f32_16x16x32_f16 v[108:111], v[196:199], v[184:187], v[108:111]
	v_mfma_f32_16x16x32_f16 v[112:115], v[200:203], v[184:187], v[112:115]
	v_mfma_f32_16x16x32_f16 v[116:119], v[204:207], v[184:187], v[116:119]
	s_waitcnt lgkmcnt(7)
	ds_read_b128 v[172:175], v16 offset:49152
	ds_read_b128 v[192:195], v18 offset:49152
	ds_read_b128 v[196:199], v18 offset:51200
	ds_read_b128 v[200:203], v18 offset:53248
	ds_read_b128 v[204:207], v18 offset:55296
	ds_read_b128 v[176:179], v16 offset:51200
	ds_read_b128 v[180:183], v16 offset:53248
	ds_read_b128 v[184:187], v16 offset:55296
	s_waitcnt lgkmcnt(14)
	v_mfma_f32_16x16x32_f16 v[56:59], v[156:159], v[136:139], v[56:59]
	s_add_u32 m0, s28, 0x6000
	s_nop 0
	global_load_lds_dwordx4 v13, s[4:5]
	s_add_u32 s4, s4, s20
	s_addc_u32 s5, s5, 0
	s_waitcnt lgkmcnt(13)
	v_mfma_f32_16x16x32_f16 v[60:63], v[160:163], v[136:139], v[60:63]
	s_waitcnt lgkmcnt(12)
	v_mfma_f32_16x16x32_f16 v[64:67], v[164:167], v[136:139], v[64:67]
	s_waitcnt lgkmcnt(11)
	v_mfma_f32_16x16x32_f16 v[68:71], v[168:171], v[136:139], v[68:71]
	s_waitcnt lgkmcnt(10)
	v_mfma_f32_16x16x32_f16 v[72:75], v[156:159], v[140:143], v[72:75]
	v_mfma_f32_16x16x32_f16 v[76:79], v[160:163], v[140:143], v[76:79]
	s_add_u32 m0, s28, 0x8000
	s_nop 0
	global_load_lds_dwordx4 v10, s[6:7]
	v_mfma_f32_16x16x32_f16 v[80:83], v[164:167], v[140:143], v[80:83]
	v_mfma_f32_16x16x32_f16 v[84:87], v[168:171], v[140:143], v[84:87]
	s_waitcnt lgkmcnt(9)
	v_mfma_f32_16x16x32_f16 v[88:91], v[156:159], v[144:147], v[88:91]
	v_mfma_f32_16x16x32_f16 v[92:95], v[160:163], v[144:147], v[92:95]
	v_mfma_f32_16x16x32_f16 v[96:99], v[164:167], v[144:147], v[96:99]
	s_add_u32 m0, s28, 0xa000
	s_nop 0
	global_load_lds_dwordx4 v11, s[6:7]
	s_add_u32 s6, s6, s20
	s_addc_u32 s7, s7, 0
	v_mfma_f32_16x16x32_f16 v[100:103], v[168:171], v[144:147], v[100:103]
	s_waitcnt lgkmcnt(8)
	v_mfma_f32_16x16x32_f16 v[104:107], v[156:159], v[148:151], v[104:107]
	v_mfma_f32_16x16x32_f16 v[108:111], v[160:163], v[148:151], v[108:111]
	v_mfma_f32_16x16x32_f16 v[112:115], v[164:167], v[148:151], v[112:115]
	v_mfma_f32_16x16x32_f16 v[116:119], v[168:171], v[148:151], v[116:119]
	s_waitcnt vmcnt(6) lgkmcnt(0)
	s_barrier
	s_waitcnt lgkmcnt(7)
	ds_read_b128 v[136:139], v19
	ds_read_b128 v[156:159], v21
	ds_read_b128 v[160:163], v21 offset:2048
	ds_read_b128 v[164:167], v21 offset:4096
	ds_read_b128 v[168:171], v21 offset:6144
	ds_read_b128 v[140:143], v19 offset:2048
	ds_read_b128 v[144:147], v19 offset:4096
	ds_read_b128 v[148:151], v19 offset:6144
	s_waitcnt lgkmcnt(14)
	v_mfma_f32_16x16x32_f16 v[56:59], v[192:195], v[172:175], v[56:59]
	s_add_u32 m0, s28, 0xc000
	s_nop 0
	global_load_lds_dwordx4 v10, s[4:5]
	s_waitcnt lgkmcnt(13)
	v_mfma_f32_16x16x32_f16 v[60:63], v[196:199], v[172:175], v[60:63]
	s_waitcnt lgkmcnt(12)
	v_mfma_f32_16x16x32_f16 v[64:67], v[200:203], v[172:175], v[64:67]
	s_waitcnt lgkmcnt(11)
	v_mfma_f32_16x16x32_f16 v[68:71], v[204:207], v[172:175], v[68:71]
	s_waitcnt lgkmcnt(10)
	v_mfma_f32_16x16x32_f16 v[72:75], v[192:195], v[176:179], v[72:75]
	v_mfma_f32_16x16x32_f16 v[76:79], v[196:199], v[176:179], v[76:79]
	s_add_u32 m0, s28, 0xe000
	s_nop 0
	global_load_lds_dwordx4 v11, s[4:5]
	v_mfma_f32_16x16x32_f16 v[80:83], v[200:203], v[176:179], v[80:83]
	v_mfma_f32_16x16x32_f16 v[84:87], v[204:207], v[176:179], v[84:87]
	s_waitcnt lgkmcnt(9)
	v_mfma_f32_16x16x32_f16 v[88:91], v[192:195], v[180:183], v[88:91]
	v_mfma_f32_16x16x32_f16 v[92:95], v[196:199], v[180:183], v[92:95]
	v_mfma_f32_16x16x32_f16 v[96:99], v[200:203], v[180:183], v[96:99]
	s_add_u32 m0, s28, 0x10000
	s_nop 0
	global_load_lds_dwordx4 v12, s[4:5]
	v_mfma_f32_16x16x32_f16 v[100:103], v[204:207], v[180:183], v[100:103]
	s_waitcnt lgkmcnt(8)
	v_mfma_f32_16x16x32_f16 v[104:107], v[192:195], v[184:187], v[104:107]
	v_mfma_f32_16x16x32_f16 v[108:111], v[196:199], v[184:187], v[108:111]
	v_mfma_f32_16x16x32_f16 v[112:115], v[200:203], v[184:187], v[112:115]
	v_mfma_f32_16x16x32_f16 v[116:119], v[204:207], v[184:187], v[116:119]
	s_waitcnt lgkmcnt(7)
	ds_read_b128 v[172:175], v20
	ds_read_b128 v[192:195], v22
	ds_read_b128 v[196:199], v22 offset:2048
	ds_read_b128 v[200:203], v22 offset:4096
	ds_read_b128 v[204:207], v22 offset:6144
	ds_read_b128 v[176:179], v20 offset:2048
	ds_read_b128 v[180:183], v20 offset:4096
	ds_read_b128 v[184:187], v20 offset:6144
	s_waitcnt lgkmcnt(14)
	v_mfma_f32_16x16x32_f16 v[56:59], v[156:159], v[136:139], v[56:59]
	s_add_u32 m0, s28, 0x12000
	s_nop 0
	global_load_lds_dwordx4 v13, s[4:5]
	s_add_u32 s4, s4, s20
	s_addc_u32 s5, s5, 0
	s_waitcnt lgkmcnt(13)
	v_mfma_f32_16x16x32_f16 v[60:63], v[160:163], v[136:139], v[60:63]
	s_waitcnt lgkmcnt(12)
	v_mfma_f32_16x16x32_f16 v[64:67], v[164:167], v[136:139], v[64:67]
	s_waitcnt lgkmcnt(11)
	v_mfma_f32_16x16x32_f16 v[68:71], v[168:171], v[136:139], v[68:71]
	s_waitcnt lgkmcnt(10)
	v_mfma_f32_16x16x32_f16 v[72:75], v[156:159], v[140:143], v[72:75]
	v_mfma_f32_16x16x32_f16 v[76:79], v[160:163], v[140:143], v[76:79]
	s_add_u32 m0, s28, 0x14000
	s_nop 0
	global_load_lds_dwordx4 v10, s[6:7]
	v_mfma_f32_16x16x32_f16 v[80:83], v[164:167], v[140:143], v[80:83]
	v_mfma_f32_16x16x32_f16 v[84:87], v[168:171], v[140:143], v[84:87]
	s_waitcnt lgkmcnt(9)
	v_mfma_f32_16x16x32_f16 v[88:91], v[156:159], v[144:147], v[88:91]
	v_mfma_f32_16x16x32_f16 v[92:95], v[160:163], v[144:147], v[92:95]
	v_mfma_f32_16x16x32_f16 v[96:99], v[164:167], v[144:147], v[96:99]
	s_add_u32 m0, s28, 0x16000
	s_nop 0
	global_load_lds_dwordx4 v11, s[6:7]
	s_add_u32 s6, s6, s20
	s_addc_u32 s7, s7, 0
	v_mfma_f32_16x16x32_f16 v[100:103], v[168:171], v[144:147], v[100:103]
	s_waitcnt lgkmcnt(8)
	v_mfma_f32_16x16x32_f16 v[104:107], v[156:159], v[148:151], v[104:107]
	v_mfma_f32_16x16x32_f16 v[108:111], v[160:163], v[148:151], v[108:111]
	v_mfma_f32_16x16x32_f16 v[112:115], v[164:167], v[148:151], v[112:115]
	v_mfma_f32_16x16x32_f16 v[116:119], v[168:171], v[148:151], v[116:119]
	s_waitcnt vmcnt(6) lgkmcnt(0)
	s_barrier
	s_waitcnt lgkmcnt(7)
	ds_read_b128 v[136:139], v15
	ds_read_b128 v[156:159], v17
	ds_read_b128 v[160:163], v17 offset:2048
	ds_read_b128 v[164:167], v17 offset:4096
	ds_read_b128 v[168:171], v17 offset:6144
	ds_read_b128 v[140:143], v15 offset:2048
	ds_read_b128 v[144:147], v15 offset:4096
	ds_read_b128 v[148:151], v15 offset:6144
	s_waitcnt lgkmcnt(14)
	v_mfma_f32_16x16x32_f16 v[56:59], v[192:195], v[172:175], v[56:59]
	s_add_u32 m0, s28, 0x18000
	s_nop 0
	global_load_lds_dwordx4 v10, s[4:5]
	s_waitcnt lgkmcnt(13)
	v_mfma_f32_16x16x32_f16 v[60:63], v[196:199], v[172:175], v[60:63]
	s_waitcnt lgkmcnt(12)
	v_mfma_f32_16x16x32_f16 v[64:67], v[200:203], v[172:175], v[64:67]
	s_waitcnt lgkmcnt(11)
	v_mfma_f32_16x16x32_f16 v[68:71], v[204:207], v[172:175], v[68:71]
	s_waitcnt lgkmcnt(10)
	v_mfma_f32_16x16x32_f16 v[72:75], v[192:195], v[176:179], v[72:75]
	v_mfma_f32_16x16x32_f16 v[76:79], v[196:199], v[176:179], v[76:79]
	s_add_u32 m0, s28, 0x1a000
	s_nop 0
	global_load_lds_dwordx4 v11, s[4:5]
	v_mfma_f32_16x16x32_f16 v[80:83], v[200:203], v[176:179], v[80:83]
	v_mfma_f32_16x16x32_f16 v[84:87], v[204:207], v[176:179], v[84:87]
	s_waitcnt lgkmcnt(9)
	v_mfma_f32_16x16x32_f16 v[88:91], v[192:195], v[180:183], v[88:91]
	v_mfma_f32_16x16x32_f16 v[92:95], v[196:199], v[180:183], v[92:95]
	v_mfma_f32_16x16x32_f16 v[96:99], v[200:203], v[180:183], v[96:99]
	s_add_u32 m0, s28, 0x1c000
	s_nop 0
	global_load_lds_dwordx4 v12, s[4:5]
	v_mfma_f32_16x16x32_f16 v[100:103], v[204:207], v[180:183], v[100:103]
	s_waitcnt lgkmcnt(8)
	v_mfma_f32_16x16x32_f16 v[104:107], v[192:195], v[184:187], v[104:107]
	v_mfma_f32_16x16x32_f16 v[108:111], v[196:199], v[184:187], v[108:111]
	v_mfma_f32_16x16x32_f16 v[112:115], v[200:203], v[184:187], v[112:115]
	v_mfma_f32_16x16x32_f16 v[116:119], v[204:207], v[184:187], v[116:119]
	s_waitcnt lgkmcnt(7)
	ds_read_b128 v[172:175], v16
	ds_read_b128 v[192:195], v18
	ds_read_b128 v[196:199], v18 offset:2048
	ds_read_b128 v[200:203], v18 offset:4096
	ds_read_b128 v[204:207], v18 offset:6144
	ds_read_b128 v[176:179], v16 offset:2048
	ds_read_b128 v[180:183], v16 offset:4096
	ds_read_b128 v[184:187], v16 offset:6144
	s_waitcnt lgkmcnt(14)
	v_mfma_f32_16x16x32_f16 v[56:59], v[156:159], v[136:139], v[56:59]
	s_add_u32 m0, s28, 0x1e000
	s_nop 0
	global_load_lds_dwordx4 v13, s[4:5]
	s_add_u32 s4, s4, s20
	s_addc_u32 s5, s5, 0
	s_waitcnt lgkmcnt(13)
	v_mfma_f32_16x16x32_f16 v[60:63], v[160:163], v[136:139], v[60:63]
	s_waitcnt lgkmcnt(12)
	v_mfma_f32_16x16x32_f16 v[64:67], v[164:167], v[136:139], v[64:67]
	s_waitcnt lgkmcnt(11)
	v_mfma_f32_16x16x32_f16 v[68:71], v[168:171], v[136:139], v[68:71]
	s_waitcnt lgkmcnt(10)
	v_mfma_f32_16x16x32_f16 v[72:75], v[156:159], v[140:143], v[72:75]
	v_mfma_f32_16x16x32_f16 v[76:79], v[160:163], v[140:143], v[76:79]
	s_add_u32 m0, s28, 0x20000
	s_nop 0
	global_load_lds_dwordx4 v10, s[6:7]
	v_mfma_f32_16x16x32_f16 v[80:83], v[164:167], v[140:143], v[80:83]
	v_mfma_f32_16x16x32_f16 v[84:87], v[168:171], v[140:143], v[84:87]
	s_waitcnt lgkmcnt(9)
	v_mfma_f32_16x16x32_f16 v[88:91], v[156:159], v[144:147], v[88:91]
	v_mfma_f32_16x16x32_f16 v[92:95], v[160:163], v[144:147], v[92:95]
	v_mfma_f32_16x16x32_f16 v[96:99], v[164:167], v[144:147], v[96:99]
	s_add_u32 m0, s28, 0x22000
	s_nop 0
	global_load_lds_dwordx4 v11, s[6:7]
	s_add_u32 s6, s6, s20
	s_addc_u32 s7, s7, 0
	v_mfma_f32_16x16x32_f16 v[100:103], v[168:171], v[144:147], v[100:103]
	s_waitcnt lgkmcnt(8)
	v_mfma_f32_16x16x32_f16 v[104:107], v[156:159], v[148:151], v[104:107]
	v_mfma_f32_16x16x32_f16 v[108:111], v[160:163], v[148:151], v[108:111]
	v_mfma_f32_16x16x32_f16 v[112:115], v[164:167], v[148:151], v[112:115]
	v_mfma_f32_16x16x32_f16 v[116:119], v[168:171], v[148:151], v[116:119]
	s_waitcnt vmcnt(6) lgkmcnt(0)
	s_barrier
	s_waitcnt lgkmcnt(7)
	ds_read_b128 v[136:139], v15 offset:49152
	ds_read_b128 v[156:159], v17 offset:49152
	ds_read_b128 v[160:163], v17 offset:51200
	ds_read_b128 v[164:167], v17 offset:53248
	ds_read_b128 v[168:171], v17 offset:55296
	ds_read_b128 v[140:143], v15 offset:51200
	ds_read_b128 v[144:147], v15 offset:53248
	ds_read_b128 v[148:151], v15 offset:55296
	s_waitcnt lgkmcnt(14)
	v_mfma_f32_16x16x32_f16 v[56:59], v[192:195], v[172:175], v[56:59]
	s_add_u32 m0, s28, 0x0
	s_nop 0
	global_load_lds_dwordx4 v10, s[4:5]
	s_waitcnt lgkmcnt(13)
	v_mfma_f32_16x16x32_f16 v[60:63], v[196:199], v[172:175], v[60:63]
	s_waitcnt lgkmcnt(12)
	v_mfma_f32_16x16x32_f16 v[64:67], v[200:203], v[172:175], v[64:67]
	s_waitcnt lgkmcnt(11)
	v_mfma_f32_16x16x32_f16 v[68:71], v[204:207], v[172:175], v[68:71]
	s_waitcnt lgkmcnt(10)
	v_mfma_f32_16x16x32_f16 v[72:75], v[192:195], v[176:179], v[72:75]
	v_mfma_f32_16x16x32_f16 v[76:79], v[196:199], v[176:179], v[76:79]
	s_add_u32 m0, s28, 0x2000
	s_nop 0
	global_load_lds_dwordx4 v11, s[4:5]
	v_mfma_f32_16x16x32_f16 v[80:83], v[200:203], v[176:179], v[80:83]
	v_mfma_f32_16x16x32_f16 v[84:87], v[204:207], v[176:179], v[84:87]
	s_waitcnt lgkmcnt(9)
	v_mfma_f32_16x16x32_f16 v[88:91], v[192:195], v[180:183], v[88:91]
	v_mfma_f32_16x16x32_f16 v[92:95], v[196:199], v[180:183], v[92:95]
	v_mfma_f32_16x16x32_f16 v[96:99], v[200:203], v[180:183], v[96:99]
	s_add_u32 m0, s28, 0x4000
	s_nop 0
	global_load_lds_dwordx4 v12, s[4:5]
	v_mfma_f32_16x16x32_f16 v[100:103], v[204:207], v[180:183], v[100:103]
	s_waitcnt lgkmcnt(8)
	v_mfma_f32_16x16x32_f16 v[104:107], v[192:195], v[184:187], v[104:107]
	v_mfma_f32_16x16x32_f16 v[108:111], v[196:199], v[184:187], v[108:111]
	v_mfma_f32_16x16x32_f16 v[112:115], v[200:203], v[184:187], v[112:115]
	v_mfma_f32_16x16x32_f16 v[116:119], v[204:207], v[184:187], v[116:119]
	s_waitcnt lgkmcnt(7)
	ds_read_b128 v[172:175], v16 offset:49152
	ds_read_b128 v[192:195], v18 offset:49152
	ds_read_b128 v[196:199], v18 offset:51200
	ds_read_b128 v[200:203], v18 offset:53248
	ds_read_b128 v[204:207], v18 offset:55296
	ds_read_b128 v[176:179], v16 offset:51200
	ds_read_b128 v[180:183], v16 offset:53248
	ds_read_b128 v[184:187], v16 offset:55296
	s_waitcnt lgkmcnt(14)
	v_mfma_f32_16x16x32_f16 v[56:59], v[156:159], v[136:139], v[56:59]
	s_add_u32 m0, s28, 0x6000
	s_nop 0
	global_load_lds_dwordx4 v13, s[4:5]
	s_add_u32 s4, s4, s20
	s_addc_u32 s5, s5, 0
	s_waitcnt lgkmcnt(13)
	v_mfma_f32_16x16x32_f16 v[60:63], v[160:163], v[136:139], v[60:63]
	s_waitcnt lgkmcnt(12)
	v_mfma_f32_16x16x32_f16 v[64:67], v[164:167], v[136:139], v[64:67]
	s_waitcnt lgkmcnt(11)
	v_mfma_f32_16x16x32_f16 v[68:71], v[168:171], v[136:139], v[68:71]
	s_waitcnt lgkmcnt(10)
	v_mfma_f32_16x16x32_f16 v[72:75], v[156:159], v[140:143], v[72:75]
	v_mfma_f32_16x16x32_f16 v[76:79], v[160:163], v[140:143], v[76:79]
	s_add_u32 m0, s28, 0x8000
	s_nop 0
	global_load_lds_dwordx4 v10, s[6:7]
	v_mfma_f32_16x16x32_f16 v[80:83], v[164:167], v[140:143], v[80:83]
	v_mfma_f32_16x16x32_f16 v[84:87], v[168:171], v[140:143], v[84:87]
	s_waitcnt lgkmcnt(9)
	v_mfma_f32_16x16x32_f16 v[88:91], v[156:159], v[144:147], v[88:91]
	v_mfma_f32_16x16x32_f16 v[92:95], v[160:163], v[144:147], v[92:95]
	v_mfma_f32_16x16x32_f16 v[96:99], v[164:167], v[144:147], v[96:99]
	s_add_u32 m0, s28, 0xa000
	s_nop 0
	global_load_lds_dwordx4 v11, s[6:7]
	s_add_u32 s6, s6, s20
	s_addc_u32 s7, s7, 0
	v_mfma_f32_16x16x32_f16 v[100:103], v[168:171], v[144:147], v[100:103]
	s_waitcnt lgkmcnt(8)
	v_mfma_f32_16x16x32_f16 v[104:107], v[156:159], v[148:151], v[104:107]
	v_mfma_f32_16x16x32_f16 v[108:111], v[160:163], v[148:151], v[108:111]
	v_mfma_f32_16x16x32_f16 v[112:115], v[164:167], v[148:151], v[112:115]
	v_mfma_f32_16x16x32_f16 v[116:119], v[168:171], v[148:151], v[116:119]
	s_waitcnt vmcnt(6) lgkmcnt(0)
	s_barrier
	s_waitcnt lgkmcnt(7)
	ds_read_b128 v[136:139], v19
	ds_read_b128 v[156:159], v21
	ds_read_b128 v[160:163], v21 offset:2048
	ds_read_b128 v[164:167], v21 offset:4096
	ds_read_b128 v[168:171], v21 offset:6144
	ds_read_b128 v[140:143], v19 offset:2048
	ds_read_b128 v[144:147], v19 offset:4096
	ds_read_b128 v[148:151], v19 offset:6144
	s_waitcnt lgkmcnt(14)
	v_mfma_f32_16x16x32_f16 v[56:59], v[192:195], v[172:175], v[56:59]
	s_add_u32 m0, s28, 0xc000
	s_nop 0
	global_load_lds_dwordx4 v10, s[4:5]
	s_waitcnt lgkmcnt(13)
	v_mfma_f32_16x16x32_f16 v[60:63], v[196:199], v[172:175], v[60:63]
	s_waitcnt lgkmcnt(12)
	v_mfma_f32_16x16x32_f16 v[64:67], v[200:203], v[172:175], v[64:67]
	s_waitcnt lgkmcnt(11)
	v_mfma_f32_16x16x32_f16 v[68:71], v[204:207], v[172:175], v[68:71]
	s_waitcnt lgkmcnt(10)
	v_mfma_f32_16x16x32_f16 v[72:75], v[192:195], v[176:179], v[72:75]
	v_mfma_f32_16x16x32_f16 v[76:79], v[196:199], v[176:179], v[76:79]
	s_add_u32 m0, s28, 0xe000
	s_nop 0
	global_load_lds_dwordx4 v11, s[4:5]
	v_mfma_f32_16x16x32_f16 v[80:83], v[200:203], v[176:179], v[80:83]
	v_mfma_f32_16x16x32_f16 v[84:87], v[204:207], v[176:179], v[84:87]
	s_waitcnt lgkmcnt(9)
	v_mfma_f32_16x16x32_f16 v[88:91], v[192:195], v[180:183], v[88:91]
	v_mfma_f32_16x16x32_f16 v[92:95], v[196:199], v[180:183], v[92:95]
	v_mfma_f32_16x16x32_f16 v[96:99], v[200:203], v[180:183], v[96:99]
	s_add_u32 m0, s28, 0x10000
	s_nop 0
	global_load_lds_dwordx4 v12, s[4:5]
	v_mfma_f32_16x16x32_f16 v[100:103], v[204:207], v[180:183], v[100:103]
	s_waitcnt lgkmcnt(8)
	v_mfma_f32_16x16x32_f16 v[104:107], v[192:195], v[184:187], v[104:107]
	v_mfma_f32_16x16x32_f16 v[108:111], v[196:199], v[184:187], v[108:111]
	v_mfma_f32_16x16x32_f16 v[112:115], v[200:203], v[184:187], v[112:115]
	v_mfma_f32_16x16x32_f16 v[116:119], v[204:207], v[184:187], v[116:119]
	s_waitcnt lgkmcnt(7)
	ds_read_b128 v[172:175], v20
	ds_read_b128 v[192:195], v22
	ds_read_b128 v[196:199], v22 offset:2048
	ds_read_b128 v[200:203], v22 offset:4096
	ds_read_b128 v[204:207], v22 offset:6144
	ds_read_b128 v[176:179], v20 offset:2048
	ds_read_b128 v[180:183], v20 offset:4096
	ds_read_b128 v[184:187], v20 offset:6144
	s_waitcnt lgkmcnt(14)
	v_mfma_f32_16x16x32_f16 v[56:59], v[156:159], v[136:139], v[56:59]
	s_add_u32 m0, s28, 0x12000
	s_nop 0
	global_load_lds_dwordx4 v13, s[4:5]
	s_add_u32 s4, s4, s20
	s_addc_u32 s5, s5, 0
	s_waitcnt lgkmcnt(13)
	v_mfma_f32_16x16x32_f16 v[60:63], v[160:163], v[136:139], v[60:63]
	s_waitcnt lgkmcnt(12)
	v_mfma_f32_16x16x32_f16 v[64:67], v[164:167], v[136:139], v[64:67]
	s_waitcnt lgkmcnt(11)
	v_mfma_f32_16x16x32_f16 v[68:71], v[168:171], v[136:139], v[68:71]
	s_waitcnt lgkmcnt(10)
	v_mfma_f32_16x16x32_f16 v[72:75], v[156:159], v[140:143], v[72:75]
	v_mfma_f32_16x16x32_f16 v[76:79], v[160:163], v[140:143], v[76:79]
	s_add_u32 m0, s28, 0x14000
	s_nop 0
	global_load_lds_dwordx4 v10, s[6:7]
	v_mfma_f32_16x16x32_f16 v[80:83], v[164:167], v[140:143], v[80:83]
	v_mfma_f32_16x16x32_f16 v[84:87], v[168:171], v[140:143], v[84:87]
	s_waitcnt lgkmcnt(9)
	v_mfma_f32_16x16x32_f16 v[88:91], v[156:159], v[144:147], v[88:91]
	v_mfma_f32_16x16x32_f16 v[92:95], v[160:163], v[144:147], v[92:95]
	v_mfma_f32_16x16x32_f16 v[96:99], v[164:167], v[144:147], v[96:99]
	s_add_u32 m0, s28, 0x16000
	s_nop 0
	global_load_lds_dwordx4 v11, s[6:7]
	s_add_u32 s6, s6, s20
	s_addc_u32 s7, s7, 0
	v_mfma_f32_16x16x32_f16 v[100:103], v[168:171], v[144:147], v[100:103]
	s_waitcnt lgkmcnt(8)
	v_mfma_f32_16x16x32_f16 v[104:107], v[156:159], v[148:151], v[104:107]
	v_mfma_f32_16x16x32_f16 v[108:111], v[160:163], v[148:151], v[108:111]
	v_mfma_f32_16x16x32_f16 v[112:115], v[164:167], v[148:151], v[112:115]
	v_mfma_f32_16x16x32_f16 v[116:119], v[168:171], v[148:151], v[116:119]
	s_waitcnt vmcnt(6) lgkmcnt(0)
	s_barrier
	s_waitcnt lgkmcnt(7)
	ds_read_b128 v[136:139], v15
	ds_read_b128 v[156:159], v17
	ds_read_b128 v[160:163], v17 offset:2048
	ds_read_b128 v[164:167], v17 offset:4096
	ds_read_b128 v[168:171], v17 offset:6144
	ds_read_b128 v[140:143], v15 offset:2048
	ds_read_b128 v[144:147], v15 offset:4096
	ds_read_b128 v[148:151], v15 offset:6144
	s_waitcnt lgkmcnt(14)
	v_mfma_f32_16x16x32_f16 v[56:59], v[192:195], v[172:175], v[56:59]
	s_add_u32 m0, s28, 0x18000
	s_nop 0
	global_load_lds_dwordx4 v10, s[4:5]
	s_waitcnt lgkmcnt(13)
	v_mfma_f32_16x16x32_f16 v[60:63], v[196:199], v[172:175], v[60:63]
	s_waitcnt lgkmcnt(12)
	v_mfma_f32_16x16x32_f16 v[64:67], v[200:203], v[172:175], v[64:67]
	s_waitcnt lgkmcnt(11)
	v_mfma_f32_16x16x32_f16 v[68:71], v[204:207], v[172:175], v[68:71]
	s_waitcnt lgkmcnt(10)
	v_mfma_f32_16x16x32_f16 v[72:75], v[192:195], v[176:179], v[72:75]
	v_mfma_f32_16x16x32_f16 v[76:79], v[196:199], v[176:179], v[76:79]
	s_add_u32 m0, s28, 0x1a000
	s_nop 0
	global_load_lds_dwordx4 v11, s[4:5]
	v_mfma_f32_16x16x32_f16 v[80:83], v[200:203], v[176:179], v[80:83]
	v_mfma_f32_16x16x32_f16 v[84:87], v[204:207], v[176:179], v[84:87]
	s_waitcnt lgkmcnt(9)
	v_mfma_f32_16x16x32_f16 v[88:91], v[192:195], v[180:183], v[88:91]
	v_mfma_f32_16x16x32_f16 v[92:95], v[196:199], v[180:183], v[92:95]
	v_mfma_f32_16x16x32_f16 v[96:99], v[200:203], v[180:183], v[96:99]
	s_add_u32 m0, s28, 0x1c000
	s_nop 0
	global_load_lds_dwordx4 v12, s[4:5]
	v_mfma_f32_16x16x32_f16 v[100:103], v[204:207], v[180:183], v[100:103]
	s_waitcnt lgkmcnt(8)
	v_mfma_f32_16x16x32_f16 v[104:107], v[192:195], v[184:187], v[104:107]
	v_mfma_f32_16x16x32_f16 v[108:111], v[196:199], v[184:187], v[108:111]
	v_mfma_f32_16x16x32_f16 v[112:115], v[200:203], v[184:187], v[112:115]
	v_mfma_f32_16x16x32_f16 v[116:119], v[204:207], v[184:187], v[116:119]
	s_waitcnt lgkmcnt(7)
	ds_read_b128 v[172:175], v16
	ds_read_b128 v[192:195], v18
	ds_read_b128 v[196:199], v18 offset:2048
	ds_read_b128 v[200:203], v18 offset:4096
	ds_read_b128 v[204:207], v18 offset:6144
	ds_read_b128 v[176:179], v16 offset:2048
	ds_read_b128 v[180:183], v16 offset:4096
	ds_read_b128 v[184:187], v16 offset:6144
	s_waitcnt lgkmcnt(14)
	v_mfma_f32_16x16x32_f16 v[56:59], v[156:159], v[136:139], v[56:59]
	s_add_u32 m0, s28, 0x1e000
	s_nop 0
	global_load_lds_dwordx4 v13, s[4:5]
	s_add_u32 s4, s4, s20
	s_addc_u32 s5, s5, 0
	s_waitcnt lgkmcnt(13)
	v_mfma_f32_16x16x32_f16 v[60:63], v[160:163], v[136:139], v[60:63]
	s_waitcnt lgkmcnt(12)
	v_mfma_f32_16x16x32_f16 v[64:67], v[164:167], v[136:139], v[64:67]
	s_waitcnt lgkmcnt(11)
	v_mfma_f32_16x16x32_f16 v[68:71], v[168:171], v[136:139], v[68:71]
	s_waitcnt lgkmcnt(10)
	v_mfma_f32_16x16x32_f16 v[72:75], v[156:159], v[140:143], v[72:75]
	v_mfma_f32_16x16x32_f16 v[76:79], v[160:163], v[140:143], v[76:79]
	s_add_u32 m0, s28, 0x20000
	s_nop 0
	global_load_lds_dwordx4 v10, s[6:7]
	v_mfma_f32_16x16x32_f16 v[80:83], v[164:167], v[140:143], v[80:83]
	v_mfma_f32_16x16x32_f16 v[84:87], v[168:171], v[140:143], v[84:87]
	s_waitcnt lgkmcnt(9)
	v_mfma_f32_16x16x32_f16 v[88:91], v[156:159], v[144:147], v[88:91]
	v_mfma_f32_16x16x32_f16 v[92:95], v[160:163], v[144:147], v[92:95]
	v_mfma_f32_16x16x32_f16 v[96:99], v[164:167], v[144:147], v[96:99]
	s_add_u32 m0, s28, 0x22000
	s_nop 0
	global_load_lds_dwordx4 v11, s[6:7]
	s_add_u32 s6, s6, s20
	s_addc_u32 s7, s7, 0
	v_mfma_f32_16x16x32_f16 v[100:103], v[168:171], v[144:147], v[100:103]
	s_waitcnt lgkmcnt(8)
	v_mfma_f32_16x16x32_f16 v[104:107], v[156:159], v[148:151], v[104:107]
	v_mfma_f32_16x16x32_f16 v[108:111], v[160:163], v[148:151], v[108:111]
	v_mfma_f32_16x16x32_f16 v[112:115], v[164:167], v[148:151], v[112:115]
	v_mfma_f32_16x16x32_f16 v[116:119], v[168:171], v[148:151], v[116:119]
	s_waitcnt vmcnt(6) lgkmcnt(0)
	s_barrier
	s_waitcnt lgkmcnt(7)
	ds_read_b128 v[136:139], v15 offset:49152
	ds_read_b128 v[156:159], v17 offset:49152
	ds_read_b128 v[160:163], v17 offset:51200
	ds_read_b128 v[164:167], v17 offset:53248
	ds_read_b128 v[168:171], v17 offset:55296
	ds_read_b128 v[140:143], v15 offset:51200
	ds_read_b128 v[144:147], v15 offset:53248
	ds_read_b128 v[148:151], v15 offset:55296
	s_waitcnt lgkmcnt(14)
	v_mfma_f32_16x16x32_f16 v[56:59], v[192:195], v[172:175], v[56:59]
	s_add_u32 m0, s28, 0x0
	s_nop 0
	global_load_lds_dwordx4 v10, s[4:5]
	s_waitcnt lgkmcnt(13)
	v_mfma_f32_16x16x32_f16 v[60:63], v[196:199], v[172:175], v[60:63]
	s_waitcnt lgkmcnt(12)
	v_mfma_f32_16x16x32_f16 v[64:67], v[200:203], v[172:175], v[64:67]
	s_waitcnt lgkmcnt(11)
	v_mfma_f32_16x16x32_f16 v[68:71], v[204:207], v[172:175], v[68:71]
	s_waitcnt lgkmcnt(10)
	v_mfma_f32_16x16x32_f16 v[72:75], v[192:195], v[176:179], v[72:75]
	v_mfma_f32_16x16x32_f16 v[76:79], v[196:199], v[176:179], v[76:79]
	s_add_u32 m0, s28, 0x2000
	s_nop 0
	global_load_lds_dwordx4 v11, s[4:5]
	v_mfma_f32_16x16x32_f16 v[80:83], v[200:203], v[176:179], v[80:83]
	v_mfma_f32_16x16x32_f16 v[84:87], v[204:207], v[176:179], v[84:87]
	s_waitcnt lgkmcnt(9)
	v_mfma_f32_16x16x32_f16 v[88:91], v[192:195], v[180:183], v[88:91]
	v_mfma_f32_16x16x32_f16 v[92:95], v[196:199], v[180:183], v[92:95]
	v_mfma_f32_16x16x32_f16 v[96:99], v[200:203], v[180:183], v[96:99]
	s_add_u32 m0, s28, 0x4000
	s_nop 0
	global_load_lds_dwordx4 v12, s[4:5]
	v_mfma_f32_16x16x32_f16 v[100:103], v[204:207], v[180:183], v[100:103]
	s_waitcnt lgkmcnt(8)
	v_mfma_f32_16x16x32_f16 v[104:107], v[192:195], v[184:187], v[104:107]
	v_mfma_f32_16x16x32_f16 v[108:111], v[196:199], v[184:187], v[108:111]
	v_mfma_f32_16x16x32_f16 v[112:115], v[200:203], v[184:187], v[112:115]
	v_mfma_f32_16x16x32_f16 v[116:119], v[204:207], v[184:187], v[116:119]
	s_waitcnt lgkmcnt(7)
	ds_read_b128 v[172:175], v16 offset:49152
	ds_read_b128 v[192:195], v18 offset:49152
	ds_read_b128 v[196:199], v18 offset:51200
	ds_read_b128 v[200:203], v18 offset:53248
	ds_read_b128 v[204:207], v18 offset:55296
	ds_read_b128 v[176:179], v16 offset:51200
	ds_read_b128 v[180:183], v16 offset:53248
	ds_read_b128 v[184:187], v16 offset:55296
	s_waitcnt lgkmcnt(14)
	v_mfma_f32_16x16x32_f16 v[56:59], v[156:159], v[136:139], v[56:59]
	s_add_u32 m0, s28, 0x6000
	s_nop 0
	global_load_lds_dwordx4 v13, s[4:5]
	s_add_u32 s4, s4, s20
	s_addc_u32 s5, s5, 0
	s_waitcnt lgkmcnt(13)
	v_mfma_f32_16x16x32_f16 v[60:63], v[160:163], v[136:139], v[60:63]
	s_waitcnt lgkmcnt(12)
	v_mfma_f32_16x16x32_f16 v[64:67], v[164:167], v[136:139], v[64:67]
	s_waitcnt lgkmcnt(11)
	v_mfma_f32_16x16x32_f16 v[68:71], v[168:171], v[136:139], v[68:71]
	s_waitcnt lgkmcnt(10)
	v_mfma_f32_16x16x32_f16 v[72:75], v[156:159], v[140:143], v[72:75]
	v_mfma_f32_16x16x32_f16 v[76:79], v[160:163], v[140:143], v[76:79]
	s_add_u32 m0, s28, 0x8000
	s_nop 0
	global_load_lds_dwordx4 v10, s[6:7]
	v_mfma_f32_16x16x32_f16 v[80:83], v[164:167], v[140:143], v[80:83]
	v_mfma_f32_16x16x32_f16 v[84:87], v[168:171], v[140:143], v[84:87]
	s_waitcnt lgkmcnt(9)
	v_mfma_f32_16x16x32_f16 v[88:91], v[156:159], v[144:147], v[88:91]
	v_mfma_f32_16x16x32_f16 v[92:95], v[160:163], v[144:147], v[92:95]
	v_mfma_f32_16x16x32_f16 v[96:99], v[164:167], v[144:147], v[96:99]
	s_add_u32 m0, s28, 0xa000
	s_nop 0
	global_load_lds_dwordx4 v11, s[6:7]
	s_add_u32 s6, s6, s20
	s_addc_u32 s7, s7, 0
	v_mfma_f32_16x16x32_f16 v[100:103], v[168:171], v[144:147], v[100:103]
	s_waitcnt lgkmcnt(8)
	v_mfma_f32_16x16x32_f16 v[104:107], v[156:159], v[148:151], v[104:107]
	v_mfma_f32_16x16x32_f16 v[108:111], v[160:163], v[148:151], v[108:111]
	v_mfma_f32_16x16x32_f16 v[112:115], v[164:167], v[148:151], v[112:115]
	v_mfma_f32_16x16x32_f16 v[116:119], v[168:171], v[148:151], v[116:119]
	s_waitcnt vmcnt(6) lgkmcnt(0)
	s_barrier
	s_waitcnt lgkmcnt(7)
	ds_read_b128 v[136:139], v19
	ds_read_b128 v[156:159], v21
	ds_read_b128 v[160:163], v21 offset:2048
	ds_read_b128 v[164:167], v21 offset:4096
	ds_read_b128 v[168:171], v21 offset:6144
	ds_read_b128 v[140:143], v19 offset:2048
	ds_read_b128 v[144:147], v19 offset:4096
	ds_read_b128 v[148:151], v19 offset:6144
	s_waitcnt lgkmcnt(14)
	v_mfma_f32_16x16x32_f16 v[56:59], v[192:195], v[172:175], v[56:59]
	s_add_u32 m0, s28, 0xc000
	s_nop 0
	global_load_lds_dwordx4 v10, s[4:5]
	s_waitcnt lgkmcnt(13)
	v_mfma_f32_16x16x32_f16 v[60:63], v[196:199], v[172:175], v[60:63]
	s_waitcnt lgkmcnt(12)
	v_mfma_f32_16x16x32_f16 v[64:67], v[200:203], v[172:175], v[64:67]
	s_waitcnt lgkmcnt(11)
	v_mfma_f32_16x16x32_f16 v[68:71], v[204:207], v[172:175], v[68:71]
	s_waitcnt lgkmcnt(10)
	v_mfma_f32_16x16x32_f16 v[72:75], v[192:195], v[176:179], v[72:75]
	v_mfma_f32_16x16x32_f16 v[76:79], v[196:199], v[176:179], v[76:79]
	s_add_u32 m0, s28, 0xe000
	s_nop 0
	global_load_lds_dwordx4 v11, s[4:5]
	v_mfma_f32_16x16x32_f16 v[80:83], v[200:203], v[176:179], v[80:83]
	v_mfma_f32_16x16x32_f16 v[84:87], v[204:207], v[176:179], v[84:87]
	s_waitcnt lgkmcnt(9)
	v_mfma_f32_16x16x32_f16 v[88:91], v[192:195], v[180:183], v[88:91]
	v_mfma_f32_16x16x32_f16 v[92:95], v[196:199], v[180:183], v[92:95]
	v_mfma_f32_16x16x32_f16 v[96:99], v[200:203], v[180:183], v[96:99]
	s_add_u32 m0, s28, 0x10000
	s_nop 0
	global_load_lds_dwordx4 v12, s[4:5]
	v_mfma_f32_16x16x32_f16 v[100:103], v[204:207], v[180:183], v[100:103]
	s_waitcnt lgkmcnt(8)
	v_mfma_f32_16x16x32_f16 v[104:107], v[192:195], v[184:187], v[104:107]
	v_mfma_f32_16x16x32_f16 v[108:111], v[196:199], v[184:187], v[108:111]
	v_mfma_f32_16x16x32_f16 v[112:115], v[200:203], v[184:187], v[112:115]
	v_mfma_f32_16x16x32_f16 v[116:119], v[204:207], v[184:187], v[116:119]
	s_waitcnt lgkmcnt(7)
	ds_read_b128 v[172:175], v20
	ds_read_b128 v[192:195], v22
	ds_read_b128 v[196:199], v22 offset:2048
	ds_read_b128 v[200:203], v22 offset:4096
	ds_read_b128 v[204:207], v22 offset:6144
	ds_read_b128 v[176:179], v20 offset:2048
	ds_read_b128 v[180:183], v20 offset:4096
	ds_read_b128 v[184:187], v20 offset:6144
	s_waitcnt lgkmcnt(14)
	v_mfma_f32_16x16x32_f16 v[56:59], v[156:159], v[136:139], v[56:59]
	s_add_u32 m0, s28, 0x12000
	s_nop 0
	global_load_lds_dwordx4 v13, s[4:5]
	s_add_u32 s4, s4, s20
	s_addc_u32 s5, s5, 0
	s_waitcnt lgkmcnt(13)
	v_mfma_f32_16x16x32_f16 v[60:63], v[160:163], v[136:139], v[60:63]
	s_waitcnt lgkmcnt(12)
	v_mfma_f32_16x16x32_f16 v[64:67], v[164:167], v[136:139], v[64:67]
	s_waitcnt lgkmcnt(11)
	v_mfma_f32_16x16x32_f16 v[68:71], v[168:171], v[136:139], v[68:71]
	s_waitcnt lgkmcnt(10)
	v_mfma_f32_16x16x32_f16 v[72:75], v[156:159], v[140:143], v[72:75]
	v_mfma_f32_16x16x32_f16 v[76:79], v[160:163], v[140:143], v[76:79]
	s_add_u32 m0, s28, 0x14000
	s_nop 0
	global_load_lds_dwordx4 v10, s[6:7]
	v_mfma_f32_16x16x32_f16 v[80:83], v[164:167], v[140:143], v[80:83]
	v_mfma_f32_16x16x32_f16 v[84:87], v[168:171], v[140:143], v[84:87]
	s_waitcnt lgkmcnt(9)
	v_mfma_f32_16x16x32_f16 v[88:91], v[156:159], v[144:147], v[88:91]
	v_mfma_f32_16x16x32_f16 v[92:95], v[160:163], v[144:147], v[92:95]
	v_mfma_f32_16x16x32_f16 v[96:99], v[164:167], v[144:147], v[96:99]
	s_add_u32 m0, s28, 0x16000
	s_nop 0
	global_load_lds_dwordx4 v11, s[6:7]
	s_add_u32 s6, s6, s20
	s_addc_u32 s7, s7, 0
	v_mfma_f32_16x16x32_f16 v[100:103], v[168:171], v[144:147], v[100:103]
	s_waitcnt lgkmcnt(8)
	v_mfma_f32_16x16x32_f16 v[104:107], v[156:159], v[148:151], v[104:107]
	v_mfma_f32_16x16x32_f16 v[108:111], v[160:163], v[148:151], v[108:111]
	v_mfma_f32_16x16x32_f16 v[112:115], v[164:167], v[148:151], v[112:115]
	v_mfma_f32_16x16x32_f16 v[116:119], v[168:171], v[148:151], v[116:119]
	s_waitcnt vmcnt(6) lgkmcnt(0)
	s_barrier
	s_waitcnt lgkmcnt(7)
	ds_read_b128 v[136:139], v15
	ds_read_b128 v[156:159], v17
	ds_read_b128 v[160:163], v17 offset:2048
	ds_read_b128 v[164:167], v17 offset:4096
	ds_read_b128 v[168:171], v17 offset:6144
	ds_read_b128 v[140:143], v15 offset:2048
	ds_read_b128 v[144:147], v15 offset:4096
	ds_read_b128 v[148:151], v15 offset:6144
	s_waitcnt lgkmcnt(14)
	v_mfma_f32_16x16x32_f16 v[56:59], v[192:195], v[172:175], v[56:59]
	s_add_u32 m0, s28, 0x18000
	s_nop 0
	global_load_lds_dwordx4 v10, s[4:5]
	s_waitcnt lgkmcnt(13)
	v_mfma_f32_16x16x32_f16 v[60:63], v[196:199], v[172:175], v[60:63]
	s_waitcnt lgkmcnt(12)
	v_mfma_f32_16x16x32_f16 v[64:67], v[200:203], v[172:175], v[64:67]
	s_waitcnt lgkmcnt(11)
	v_mfma_f32_16x16x32_f16 v[68:71], v[204:207], v[172:175], v[68:71]
	s_waitcnt lgkmcnt(10)
	v_mfma_f32_16x16x32_f16 v[72:75], v[192:195], v[176:179], v[72:75]
	v_mfma_f32_16x16x32_f16 v[76:79], v[196:199], v[176:179], v[76:79]
	s_add_u32 m0, s28, 0x1a000
	s_nop 0
	global_load_lds_dwordx4 v11, s[4:5]
	v_mfma_f32_16x16x32_f16 v[80:83], v[200:203], v[176:179], v[80:83]
	v_mfma_f32_16x16x32_f16 v[84:87], v[204:207], v[176:179], v[84:87]
	s_waitcnt lgkmcnt(9)
	v_mfma_f32_16x16x32_f16 v[88:91], v[192:195], v[180:183], v[88:91]
	v_mfma_f32_16x16x32_f16 v[92:95], v[196:199], v[180:183], v[92:95]
	v_mfma_f32_16x16x32_f16 v[96:99], v[200:203], v[180:183], v[96:99]
	s_add_u32 m0, s28, 0x1c000
	s_nop 0
	global_load_lds_dwordx4 v12, s[4:5]
	v_mfma_f32_16x16x32_f16 v[100:103], v[204:207], v[180:183], v[100:103]
	s_waitcnt lgkmcnt(8)
	v_mfma_f32_16x16x32_f16 v[104:107], v[192:195], v[184:187], v[104:107]
	v_mfma_f32_16x16x32_f16 v[108:111], v[196:199], v[184:187], v[108:111]
	v_mfma_f32_16x16x32_f16 v[112:115], v[200:203], v[184:187], v[112:115]
	v_mfma_f32_16x16x32_f16 v[116:119], v[204:207], v[184:187], v[116:119]
	s_waitcnt lgkmcnt(7)
	ds_read_b128 v[172:175], v16
	ds_read_b128 v[192:195], v18
	ds_read_b128 v[196:199], v18 offset:2048
	ds_read_b128 v[200:203], v18 offset:4096
	ds_read_b128 v[204:207], v18 offset:6144
	ds_read_b128 v[176:179], v16 offset:2048
	ds_read_b128 v[180:183], v16 offset:4096
	ds_read_b128 v[184:187], v16 offset:6144
	s_waitcnt lgkmcnt(14)
	v_mfma_f32_16x16x32_f16 v[56:59], v[156:159], v[136:139], v[56:59]
	s_add_u32 m0, s28, 0x1e000
	s_nop 0
	global_load_lds_dwordx4 v13, s[4:5]
	s_add_u32 s4, s4, s20
	s_addc_u32 s5, s5, 0
	s_waitcnt lgkmcnt(13)
	v_mfma_f32_16x16x32_f16 v[60:63], v[160:163], v[136:139], v[60:63]
	s_waitcnt lgkmcnt(12)
	v_mfma_f32_16x16x32_f16 v[64:67], v[164:167], v[136:139], v[64:67]
	s_waitcnt lgkmcnt(11)
	v_mfma_f32_16x16x32_f16 v[68:71], v[168:171], v[136:139], v[68:71]
	s_waitcnt lgkmcnt(10)
	v_mfma_f32_16x16x32_f16 v[72:75], v[156:159], v[140:143], v[72:75]
	v_mfma_f32_16x16x32_f16 v[76:79], v[160:163], v[140:143], v[76:79]
	s_add_u32 m0, s28, 0x20000
	s_nop 0
	global_load_lds_dwordx4 v10, s[6:7]
	v_mfma_f32_16x16x32_f16 v[80:83], v[164:167], v[140:143], v[80:83]
	v_mfma_f32_16x16x32_f16 v[84:87], v[168:171], v[140:143], v[84:87]
	s_waitcnt lgkmcnt(9)
	v_mfma_f32_16x16x32_f16 v[88:91], v[156:159], v[144:147], v[88:91]
	v_mfma_f32_16x16x32_f16 v[92:95], v[160:163], v[144:147], v[92:95]
	v_mfma_f32_16x16x32_f16 v[96:99], v[164:167], v[144:147], v[96:99]
	s_add_u32 m0, s28, 0x22000
	s_nop 0
	global_load_lds_dwordx4 v11, s[6:7]
	s_add_u32 s6, s6, s20
	s_addc_u32 s7, s7, 0
	v_mfma_f32_16x16x32_f16 v[100:103], v[168:171], v[144:147], v[100:103]
	s_waitcnt lgkmcnt(8)
	v_mfma_f32_16x16x32_f16 v[104:107], v[156:159], v[148:151], v[104:107]
	v_mfma_f32_16x16x32_f16 v[108:111], v[160:163], v[148:151], v[108:111]
	v_mfma_f32_16x16x32_f16 v[112:115], v[164:167], v[148:151], v[112:115]
	v_mfma_f32_16x16x32_f16 v[116:119], v[168:171], v[148:151], v[116:119]
	s_waitcnt vmcnt(6) lgkmcnt(0)
	s_barrier
	s_waitcnt lgkmcnt(7)
	ds_read_b128 v[136:139], v15 offset:49152
	ds_read_b128 v[156:159], v17 offset:49152
	ds_read_b128 v[160:163], v17 offset:51200
	ds_read_b128 v[164:167], v17 offset:53248
	ds_read_b128 v[168:171], v17 offset:55296
	ds_read_b128 v[140:143], v15 offset:51200
	ds_read_b128 v[144:147], v15 offset:53248
	ds_read_b128 v[148:151], v15 offset:55296
	s_waitcnt lgkmcnt(14)
	v_mfma_f32_16x16x32_f16 v[56:59], v[192:195], v[172:175], v[56:59]
	s_add_u32 m0, s28, 0x0
	s_nop 0
	global_load_lds_dwordx4 v10, s[4:5]
	s_waitcnt lgkmcnt(13)
	v_mfma_f32_16x16x32_f16 v[60:63], v[196:199], v[172:175], v[60:63]
	s_waitcnt lgkmcnt(12)
	v_mfma_f32_16x16x32_f16 v[64:67], v[200:203], v[172:175], v[64:67]
	s_waitcnt lgkmcnt(11)
	v_mfma_f32_16x16x32_f16 v[68:71], v[204:207], v[172:175], v[68:71]
	s_waitcnt lgkmcnt(10)
	v_mfma_f32_16x16x32_f16 v[72:75], v[192:195], v[176:179], v[72:75]
	v_mfma_f32_16x16x32_f16 v[76:79], v[196:199], v[176:179], v[76:79]
	s_add_u32 m0, s28, 0x2000
	s_nop 0
	global_load_lds_dwordx4 v11, s[4:5]
	v_mfma_f32_16x16x32_f16 v[80:83], v[200:203], v[176:179], v[80:83]
	v_mfma_f32_16x16x32_f16 v[84:87], v[204:207], v[176:179], v[84:87]
	s_waitcnt lgkmcnt(9)
	v_mfma_f32_16x16x32_f16 v[88:91], v[192:195], v[180:183], v[88:91]
	v_mfma_f32_16x16x32_f16 v[92:95], v[196:199], v[180:183], v[92:95]
	v_mfma_f32_16x16x32_f16 v[96:99], v[200:203], v[180:183], v[96:99]
	s_add_u32 m0, s28, 0x4000
	s_nop 0
	global_load_lds_dwordx4 v12, s[4:5]
	v_mfma_f32_16x16x32_f16 v[100:103], v[204:207], v[180:183], v[100:103]
	s_waitcnt lgkmcnt(8)
	v_mfma_f32_16x16x32_f16 v[104:107], v[192:195], v[184:187], v[104:107]
	v_mfma_f32_16x16x32_f16 v[108:111], v[196:199], v[184:187], v[108:111]
	v_mfma_f32_16x16x32_f16 v[112:115], v[200:203], v[184:187], v[112:115]
	v_mfma_f32_16x16x32_f16 v[116:119], v[204:207], v[184:187], v[116:119]
	s_waitcnt lgkmcnt(7)
	ds_read_b128 v[172:175], v16 offset:49152
	ds_read_b128 v[192:195], v18 offset:49152
	ds_read_b128 v[196:199], v18 offset:51200
	ds_read_b128 v[200:203], v18 offset:53248
	ds_read_b128 v[204:207], v18 offset:55296
	ds_read_b128 v[176:179], v16 offset:51200
	ds_read_b128 v[180:183], v16 offset:53248
	ds_read_b128 v[184:187], v16 offset:55296
	s_waitcnt lgkmcnt(14)
	v_mfma_f32_16x16x32_f16 v[56:59], v[156:159], v[136:139], v[56:59]
	s_add_u32 m0, s28, 0x6000
	s_nop 0
	global_load_lds_dwordx4 v13, s[4:5]
	s_add_u32 s4, s4, s20
	s_addc_u32 s5, s5, 0
	s_waitcnt lgkmcnt(13)
	v_mfma_f32_16x16x32_f16 v[60:63], v[160:163], v[136:139], v[60:63]
	s_waitcnt lgkmcnt(12)
	v_mfma_f32_16x16x32_f16 v[64:67], v[164:167], v[136:139], v[64:67]
	s_waitcnt lgkmcnt(11)
	v_mfma_f32_16x16x32_f16 v[68:71], v[168:171], v[136:139], v[68:71]
	s_waitcnt lgkmcnt(10)
	v_mfma_f32_16x16x32_f16 v[72:75], v[156:159], v[140:143], v[72:75]
	v_mfma_f32_16x16x32_f16 v[76:79], v[160:163], v[140:143], v[76:79]
	s_add_u32 m0, s28, 0x8000
	s_nop 0
	global_load_lds_dwordx4 v10, s[6:7]
	v_mfma_f32_16x16x32_f16 v[80:83], v[164:167], v[140:143], v[80:83]
	v_mfma_f32_16x16x32_f16 v[84:87], v[168:171], v[140:143], v[84:87]
	s_waitcnt lgkmcnt(9)
	v_mfma_f32_16x16x32_f16 v[88:91], v[156:159], v[144:147], v[88:91]
	v_mfma_f32_16x16x32_f16 v[92:95], v[160:163], v[144:147], v[92:95]
	v_mfma_f32_16x16x32_f16 v[96:99], v[164:167], v[144:147], v[96:99]
	s_add_u32 m0, s28, 0xa000
	s_nop 0
	global_load_lds_dwordx4 v11, s[6:7]
	s_add_u32 s6, s6, s20
	s_addc_u32 s7, s7, 0
	v_mfma_f32_16x16x32_f16 v[100:103], v[168:171], v[144:147], v[100:103]
	s_waitcnt lgkmcnt(8)
	v_mfma_f32_16x16x32_f16 v[104:107], v[156:159], v[148:151], v[104:107]
	v_mfma_f32_16x16x32_f16 v[108:111], v[160:163], v[148:151], v[108:111]
	v_mfma_f32_16x16x32_f16 v[112:115], v[164:167], v[148:151], v[112:115]
	v_mfma_f32_16x16x32_f16 v[116:119], v[168:171], v[148:151], v[116:119]
	s_waitcnt vmcnt(6) lgkmcnt(0)
	s_barrier
	s_waitcnt lgkmcnt(7)
	ds_read_b128 v[136:139], v19
	ds_read_b128 v[156:159], v21
	ds_read_b128 v[160:163], v21 offset:2048
	ds_read_b128 v[164:167], v21 offset:4096
	ds_read_b128 v[168:171], v21 offset:6144
	ds_read_b128 v[140:143], v19 offset:2048
	ds_read_b128 v[144:147], v19 offset:4096
	ds_read_b128 v[148:151], v19 offset:6144
	s_waitcnt lgkmcnt(14)
	v_mfma_f32_16x16x32_f16 v[56:59], v[192:195], v[172:175], v[56:59]
	s_waitcnt lgkmcnt(13)
	v_mfma_f32_16x16x32_f16 v[60:63], v[196:199], v[172:175], v[60:63]
	s_waitcnt lgkmcnt(12)
	v_mfma_f32_16x16x32_f16 v[64:67], v[200:203], v[172:175], v[64:67]
	s_waitcnt lgkmcnt(11)
	v_mfma_f32_16x16x32_f16 v[68:71], v[204:207], v[172:175], v[68:71]
	s_waitcnt lgkmcnt(10)
	v_mfma_f32_16x16x32_f16 v[72:75], v[192:195], v[176:179], v[72:75]
	v_mfma_f32_16x16x32_f16 v[76:79], v[196:199], v[176:179], v[76:79]
	v_mfma_f32_16x16x32_f16 v[80:83], v[200:203], v[176:179], v[80:83]
	v_mfma_f32_16x16x32_f16 v[84:87], v[204:207], v[176:179], v[84:87]
	s_waitcnt lgkmcnt(9)
	v_mfma_f32_16x16x32_f16 v[88:91], v[192:195], v[180:183], v[88:91]
	v_mfma_f32_16x16x32_f16 v[92:95], v[196:199], v[180:183], v[92:95]
	v_mfma_f32_16x16x32_f16 v[96:99], v[200:203], v[180:183], v[96:99]
	v_mfma_f32_16x16x32_f16 v[100:103], v[204:207], v[180:183], v[100:103]
	s_waitcnt lgkmcnt(8)
	v_mfma_f32_16x16x32_f16 v[104:107], v[192:195], v[184:187], v[104:107]
	v_mfma_f32_16x16x32_f16 v[108:111], v[196:199], v[184:187], v[108:111]
	v_mfma_f32_16x16x32_f16 v[112:115], v[200:203], v[184:187], v[112:115]
	v_mfma_f32_16x16x32_f16 v[116:119], v[204:207], v[184:187], v[116:119]
	s_waitcnt lgkmcnt(7)
	ds_read_b128 v[172:175], v20
	ds_read_b128 v[192:195], v22
	ds_read_b128 v[196:199], v22 offset:2048
	ds_read_b128 v[200:203], v22 offset:4096
	ds_read_b128 v[204:207], v22 offset:6144
	ds_read_b128 v[176:179], v20 offset:2048
	ds_read_b128 v[180:183], v20 offset:4096
	ds_read_b128 v[184:187], v20 offset:6144
	s_waitcnt lgkmcnt(14)
	v_mfma_f32_16x16x32_f16 v[56:59], v[156:159], v[136:139], v[56:59]
	s_waitcnt lgkmcnt(13)
	v_mfma_f32_16x16x32_f16 v[60:63], v[160:163], v[136:139], v[60:63]
	s_waitcnt lgkmcnt(12)
	v_mfma_f32_16x16x32_f16 v[64:67], v[164:167], v[136:139], v[64:67]
	s_waitcnt lgkmcnt(11)
	v_mfma_f32_16x16x32_f16 v[68:71], v[168:171], v[136:139], v[68:71]
	s_waitcnt lgkmcnt(10)
	v_mfma_f32_16x16x32_f16 v[72:75], v[156:159], v[140:143], v[72:75]
	v_mfma_f32_16x16x32_f16 v[76:79], v[160:163], v[140:143], v[76:79]
	v_mfma_f32_16x16x32_f16 v[80:83], v[164:167], v[140:143], v[80:83]
	v_mfma_f32_16x16x32_f16 v[84:87], v[168:171], v[140:143], v[84:87]
	s_waitcnt lgkmcnt(9)
	v_mfma_f32_16x16x32_f16 v[88:91], v[156:159], v[144:147], v[88:91]
	v_mfma_f32_16x16x32_f16 v[92:95], v[160:163], v[144:147], v[92:95]
	v_mfma_f32_16x16x32_f16 v[96:99], v[164:167], v[144:147], v[96:99]
	v_mfma_f32_16x16x32_f16 v[100:103], v[168:171], v[144:147], v[100:103]
	s_waitcnt lgkmcnt(8)
	v_mfma_f32_16x16x32_f16 v[104:107], v[156:159], v[148:151], v[104:107]
	v_mfma_f32_16x16x32_f16 v[108:111], v[160:163], v[148:151], v[108:111]
	v_mfma_f32_16x16x32_f16 v[112:115], v[164:167], v[148:151], v[112:115]
	v_mfma_f32_16x16x32_f16 v[116:119], v[168:171], v[148:151], v[116:119]
	s_waitcnt vmcnt(0) lgkmcnt(0)
	s_barrier
	s_waitcnt lgkmcnt(7)
	ds_read_b128 v[136:139], v15
	ds_read_b128 v[156:159], v17
	ds_read_b128 v[160:163], v17 offset:2048
	ds_read_b128 v[164:167], v17 offset:4096
	ds_read_b128 v[168:171], v17 offset:6144
	ds_read_b128 v[140:143], v15 offset:2048
	ds_read_b128 v[144:147], v15 offset:4096
	ds_read_b128 v[148:151], v15 offset:6144
	s_waitcnt lgkmcnt(14)
	v_mfma_f32_16x16x32_f16 v[56:59], v[192:195], v[172:175], v[56:59]
	s_waitcnt lgkmcnt(13)
	v_mfma_f32_16x16x32_f16 v[60:63], v[196:199], v[172:175], v[60:63]
	s_waitcnt lgkmcnt(12)
	v_mfma_f32_16x16x32_f16 v[64:67], v[200:203], v[172:175], v[64:67]
	s_waitcnt lgkmcnt(11)
	v_mfma_f32_16x16x32_f16 v[68:71], v[204:207], v[172:175], v[68:71]
	s_waitcnt lgkmcnt(10)
	v_mfma_f32_16x16x32_f16 v[72:75], v[192:195], v[176:179], v[72:75]
	v_mfma_f32_16x16x32_f16 v[76:79], v[196:199], v[176:179], v[76:79]
	v_mfma_f32_16x16x32_f16 v[80:83], v[200:203], v[176:179], v[80:83]
	v_mfma_f32_16x16x32_f16 v[84:87], v[204:207], v[176:179], v[84:87]
	s_waitcnt lgkmcnt(9)
	v_mfma_f32_16x16x32_f16 v[88:91], v[192:195], v[180:183], v[88:91]
	v_mfma_f32_16x16x32_f16 v[92:95], v[196:199], v[180:183], v[92:95]
	v_mfma_f32_16x16x32_f16 v[96:99], v[200:203], v[180:183], v[96:99]
	v_mfma_f32_16x16x32_f16 v[100:103], v[204:207], v[180:183], v[100:103]
	s_waitcnt lgkmcnt(8)
	v_mfma_f32_16x16x32_f16 v[104:107], v[192:195], v[184:187], v[104:107]
	v_mfma_f32_16x16x32_f16 v[108:111], v[196:199], v[184:187], v[108:111]
	v_mfma_f32_16x16x32_f16 v[112:115], v[200:203], v[184:187], v[112:115]
	v_mfma_f32_16x16x32_f16 v[116:119], v[204:207], v[184:187], v[116:119]
	s_waitcnt lgkmcnt(7)
	ds_read_b128 v[172:175], v16
	ds_read_b128 v[192:195], v18
	ds_read_b128 v[196:199], v18 offset:2048
	ds_read_b128 v[200:203], v18 offset:4096
	ds_read_b128 v[204:207], v18 offset:6144
	ds_read_b128 v[176:179], v16 offset:2048
	ds_read_b128 v[180:183], v16 offset:4096
	ds_read_b128 v[184:187], v16 offset:6144
	s_waitcnt lgkmcnt(14)
	v_mfma_f32_16x16x32_f16 v[56:59], v[156:159], v[136:139], v[56:59]
	s_waitcnt lgkmcnt(13)
	v_mfma_f32_16x16x32_f16 v[60:63], v[160:163], v[136:139], v[60:63]
	s_waitcnt lgkmcnt(12)
	v_mfma_f32_16x16x32_f16 v[64:67], v[164:167], v[136:139], v[64:67]
	s_waitcnt lgkmcnt(11)
	v_mfma_f32_16x16x32_f16 v[68:71], v[168:171], v[136:139], v[68:71]
	s_waitcnt lgkmcnt(10)
	v_mfma_f32_16x16x32_f16 v[72:75], v[156:159], v[140:143], v[72:75]
	v_mfma_f32_16x16x32_f16 v[76:79], v[160:163], v[140:143], v[76:79]
	v_mfma_f32_16x16x32_f16 v[80:83], v[164:167], v[140:143], v[80:83]
	v_mfma_f32_16x16x32_f16 v[84:87], v[168:171], v[140:143], v[84:87]
	s_waitcnt lgkmcnt(9)
	v_mfma_f32_16x16x32_f16 v[88:91], v[156:159], v[144:147], v[88:91]
	v_mfma_f32_16x16x32_f16 v[92:95], v[160:163], v[144:147], v[92:95]
	v_mfma_f32_16x16x32_f16 v[96:99], v[164:167], v[144:147], v[96:99]
	v_mfma_f32_16x16x32_f16 v[100:103], v[168:171], v[144:147], v[100:103]
	s_waitcnt lgkmcnt(8)
	v_mfma_f32_16x16x32_f16 v[104:107], v[156:159], v[148:151], v[104:107]
	v_mfma_f32_16x16x32_f16 v[108:111], v[160:163], v[148:151], v[108:111]
	v_mfma_f32_16x16x32_f16 v[112:115], v[164:167], v[148:151], v[112:115]
	v_mfma_f32_16x16x32_f16 v[116:119], v[168:171], v[148:151], v[116:119]
	s_waitcnt lgkmcnt(6)
	v_mfma_f32_16x16x32_f16 v[56:59], v[192:195], v[172:175], v[56:59]
	s_waitcnt lgkmcnt(5)
	v_mfma_f32_16x16x32_f16 v[60:63], v[196:199], v[172:175], v[60:63]
	s_waitcnt lgkmcnt(4)
	v_mfma_f32_16x16x32_f16 v[64:67], v[200:203], v[172:175], v[64:67]
	s_waitcnt lgkmcnt(3)
	v_mfma_f32_16x16x32_f16 v[68:71], v[204:207], v[172:175], v[68:71]
	s_waitcnt lgkmcnt(2)
	v_mfma_f32_16x16x32_f16 v[72:75], v[192:195], v[176:179], v[72:75]
	v_mfma_f32_16x16x32_f16 v[76:79], v[196:199], v[176:179], v[76:79]
	v_mfma_f32_16x16x32_f16 v[80:83], v[200:203], v[176:179], v[80:83]
	v_mfma_f32_16x16x32_f16 v[84:87], v[204:207], v[176:179], v[84:87]
	s_waitcnt lgkmcnt(1)
	v_mfma_f32_16x16x32_f16 v[88:91], v[192:195], v[180:183], v[88:91]
	v_mfma_f32_16x16x32_f16 v[92:95], v[196:199], v[180:183], v[92:95]
	v_mfma_f32_16x16x32_f16 v[96:99], v[200:203], v[180:183], v[96:99]
	v_mfma_f32_16x16x32_f16 v[100:103], v[204:207], v[180:183], v[100:103]
	s_waitcnt lgkmcnt(0)
	v_mfma_f32_16x16x32_f16 v[104:107], v[192:195], v[184:187], v[104:107]
	v_mfma_f32_16x16x32_f16 v[108:111], v[196:199], v[184:187], v[108:111]
	v_mfma_f32_16x16x32_f16 v[112:115], v[200:203], v[184:187], v[112:115]
	v_mfma_f32_16x16x32_f16 v[116:119], v[204:207], v[184:187], v[116:119]
	s_nop 7
	s_nop 1
	v_mov_b32_e32 v213, s19
	v_pk_add_f32 v[56:57], v[56:57], v[24:25]
	v_pk_add_f32 v[58:59], v[58:59], v[26:27]
	v_pk_add_f32 v[60:61], v[60:61], v[28:29]
	v_pk_add_f32 v[62:63], v[62:63], v[30:31]
	v_pk_add_f32 v[64:65], v[64:65], v[32:33]
	v_pk_add_f32 v[66:67], v[66:67], v[34:35]
	v_pk_add_f32 v[68:69], v[68:69], v[36:37]
	v_pk_add_f32 v[70:71], v[70:71], v[38:39]
	v_pk_mul_f32 v[208:209], v[56:57], v[56:57]
	v_pk_fma_f32 v[208:209], v[58:59], v[58:59], v[208:209]
	v_pk_fma_f32 v[208:209], v[60:61], v[60:61], v[208:209]
	v_pk_fma_f32 v[208:209], v[62:63], v[62:63], v[208:209]
	v_pk_fma_f32 v[208:209], v[64:65], v[64:65], v[208:209]
	v_pk_fma_f32 v[208:209], v[66:67], v[66:67], v[208:209]
	v_pk_fma_f32 v[208:209], v[68:69], v[68:69], v[208:209]
	v_pk_fma_f32 v[208:209], v[70:71], v[70:71], v[208:209]
	v_add_f32_e32 v208, v208, v209
	v_mov_b32_e32 v209, v208
	s_nop 1
	v_permlane16_swap_b32_e32 v208, v209
	v_add_f32_e32 v208, v208, v209
	v_mov_b32_e32 v209, v208
	s_nop 1
	v_permlane32_swap_b32_e32 v208, v209
	v_add_f32_e32 v208, v208, v209
	v_mov_b32_e32 v210, 0x358637bd
	v_fmac_f32_e32 v210, 0x3c800000, v208
	v_rsq_f32_e32 v210, v210
	s_add_u32 s24, s29, 0
	s_lshr_b32 s8, s24, 1
	s_lshl_b32 s8, s8, 12
	s_and_b32 s24, s24, 1
	s_lshl_b32 s24, s24, 8
	s_add_u32 s8, s8, s24
	v_mul_f32_e32 v210, v213, v210
	v_add_u32_e32 v212, s8, v23
	v_pk_mul_f32 v[56:57], v[56:57], v[210:211] op_sel_hi:[1,0]
	v_pk_mul_f32 v[58:59], v[58:59], v[210:211] op_sel_hi:[1,0]
	v_pk_mul_f32 v[56:57], v[56:57], v[40:41]
	v_pk_mul_f32 v[58:59], v[58:59], v[42:43]
	v_cvt_pk_f16_f32 v56, v56, v57
	v_cvt_pk_f16_f32 v57, v58, v59
	global_store_dwordx2 v212, v[56:57], s[22:23] offset:0
	v_pk_mul_f32 v[60:61], v[60:61], v[210:211] op_sel_hi:[1,0]
	v_pk_mul_f32 v[62:63], v[62:63], v[210:211] op_sel_hi:[1,0]
	v_pk_mul_f32 v[60:61], v[60:61], v[44:45]
	v_pk_mul_f32 v[62:63], v[62:63], v[46:47]
	v_cvt_pk_f16_f32 v60, v60, v61
	v_cvt_pk_f16_f32 v61, v62, v63
	global_store_dwordx2 v212, v[60:61], s[22:23] offset:1024
	v_pk_mul_f32 v[64:65], v[64:65], v[210:211] op_sel_hi:[1,0]
	v_pk_mul_f32 v[66:67], v[66:67], v[210:211] op_sel_hi:[1,0]
	v_pk_mul_f32 v[64:65], v[64:65], v[48:49]
	v_pk_mul_f32 v[66:67], v[66:67], v[50:51]
	v_cvt_pk_f16_f32 v64, v64, v65
	v_cvt_pk_f16_f32 v65, v66, v67
	global_store_dwordx2 v212, v[64:65], s[22:23] offset:2048
	v_pk_mul_f32 v[68:69], v[68:69], v[210:211] op_sel_hi:[1,0]
	v_pk_mul_f32 v[70:71], v[70:71], v[210:211] op_sel_hi:[1,0]
	v_pk_mul_f32 v[68:69], v[68:69], v[52:53]
	v_pk_mul_f32 v[70:71], v[70:71], v[54:55]
	v_cvt_pk_f16_f32 v68, v68, v69
	v_cvt_pk_f16_f32 v69, v70, v71
	global_store_dwordx2 v212, v[68:69], s[22:23] offset:3072
	v_pk_add_f32 v[72:73], v[72:73], v[24:25]
	v_pk_add_f32 v[74:75], v[74:75], v[26:27]
	v_pk_add_f32 v[76:77], v[76:77], v[28:29]
	v_pk_add_f32 v[78:79], v[78:79], v[30:31]
	v_pk_add_f32 v[80:81], v[80:81], v[32:33]
	v_pk_add_f32 v[82:83], v[82:83], v[34:35]
	v_pk_add_f32 v[84:85], v[84:85], v[36:37]
	v_pk_add_f32 v[86:87], v[86:87], v[38:39]
	v_pk_mul_f32 v[208:209], v[72:73], v[72:73]
	v_pk_fma_f32 v[208:209], v[74:75], v[74:75], v[208:209]
	v_pk_fma_f32 v[208:209], v[76:77], v[76:77], v[208:209]
	v_pk_fma_f32 v[208:209], v[78:79], v[78:79], v[208:209]
	v_pk_fma_f32 v[208:209], v[80:81], v[80:81], v[208:209]
	v_pk_fma_f32 v[208:209], v[82:83], v[82:83], v[208:209]
	v_pk_fma_f32 v[208:209], v[84:85], v[84:85], v[208:209]
	v_pk_fma_f32 v[208:209], v[86:87], v[86:87], v[208:209]
	v_add_f32_e32 v208, v208, v209
	v_mov_b32_e32 v209, v208
	s_nop 1
	v_permlane16_swap_b32_e32 v208, v209
	v_add_f32_e32 v208, v208, v209
	v_mov_b32_e32 v209, v208
	s_nop 1
	v_permlane32_swap_b32_e32 v208, v209
	v_add_f32_e32 v208, v208, v209
	v_mov_b32_e32 v210, 0x358637bd
	v_fmac_f32_e32 v210, 0x3c800000, v208
	v_rsq_f32_e32 v210, v210
	s_add_u32 s24, s29, 1
	s_lshr_b32 s8, s24, 1
	s_lshl_b32 s8, s8, 12
	s_and_b32 s24, s24, 1
	s_lshl_b32 s24, s24, 8
	s_add_u32 s8, s8, s24
	v_mul_f32_e32 v210, v213, v210
	v_add_u32_e32 v212, s8, v23
	v_pk_mul_f32 v[72:73], v[72:73], v[210:211] op_sel_hi:[1,0]
	v_pk_mul_f32 v[74:75], v[74:75], v[210:211] op_sel_hi:[1,0]
	v_pk_mul_f32 v[72:73], v[72:73], v[40:41]
	v_pk_mul_f32 v[74:75], v[74:75], v[42:43]
	v_cvt_pk_f16_f32 v72, v72, v73
	v_cvt_pk_f16_f32 v73, v74, v75
	global_store_dwordx2 v212, v[72:73], s[22:23] offset:0
	v_pk_mul_f32 v[76:77], v[76:77], v[210:211] op_sel_hi:[1,0]
	v_pk_mul_f32 v[78:79], v[78:79], v[210:211] op_sel_hi:[1,0]
	v_pk_mul_f32 v[76:77], v[76:77], v[44:45]
	v_pk_mul_f32 v[78:79], v[78:79], v[46:47]
	v_cvt_pk_f16_f32 v76, v76, v77
	v_cvt_pk_f16_f32 v77, v78, v79
	global_store_dwordx2 v212, v[76:77], s[22:23] offset:1024
	v_pk_mul_f32 v[80:81], v[80:81], v[210:211] op_sel_hi:[1,0]
	v_pk_mul_f32 v[82:83], v[82:83], v[210:211] op_sel_hi:[1,0]
	v_pk_mul_f32 v[80:81], v[80:81], v[48:49]
	v_pk_mul_f32 v[82:83], v[82:83], v[50:51]
	v_cvt_pk_f16_f32 v80, v80, v81
	v_cvt_pk_f16_f32 v81, v82, v83
	global_store_dwordx2 v212, v[80:81], s[22:23] offset:2048
	v_pk_mul_f32 v[84:85], v[84:85], v[210:211] op_sel_hi:[1,0]
	v_pk_mul_f32 v[86:87], v[86:87], v[210:211] op_sel_hi:[1,0]
	v_pk_mul_f32 v[84:85], v[84:85], v[52:53]
	v_pk_mul_f32 v[86:87], v[86:87], v[54:55]
	v_cvt_pk_f16_f32 v84, v84, v85
	v_cvt_pk_f16_f32 v85, v86, v87
	global_store_dwordx2 v212, v[84:85], s[22:23] offset:3072
	v_pk_add_f32 v[88:89], v[88:89], v[24:25]
	v_pk_add_f32 v[90:91], v[90:91], v[26:27]
	v_pk_add_f32 v[92:93], v[92:93], v[28:29]
	v_pk_add_f32 v[94:95], v[94:95], v[30:31]
	v_pk_add_f32 v[96:97], v[96:97], v[32:33]
	v_pk_add_f32 v[98:99], v[98:99], v[34:35]
	v_pk_add_f32 v[100:101], v[100:101], v[36:37]
	v_pk_add_f32 v[102:103], v[102:103], v[38:39]
	v_pk_mul_f32 v[208:209], v[88:89], v[88:89]
	v_pk_fma_f32 v[208:209], v[90:91], v[90:91], v[208:209]
	v_pk_fma_f32 v[208:209], v[92:93], v[92:93], v[208:209]
	v_pk_fma_f32 v[208:209], v[94:95], v[94:95], v[208:209]
	v_pk_fma_f32 v[208:209], v[96:97], v[96:97], v[208:209]
	v_pk_fma_f32 v[208:209], v[98:99], v[98:99], v[208:209]
	v_pk_fma_f32 v[208:209], v[100:101], v[100:101], v[208:209]
	v_pk_fma_f32 v[208:209], v[102:103], v[102:103], v[208:209]
	v_add_f32_e32 v208, v208, v209
	v_mov_b32_e32 v209, v208
	s_nop 1
	v_permlane16_swap_b32_e32 v208, v209
	v_add_f32_e32 v208, v208, v209
	v_mov_b32_e32 v209, v208
	s_nop 1
	v_permlane32_swap_b32_e32 v208, v209
	v_add_f32_e32 v208, v208, v209
	v_mov_b32_e32 v210, 0x358637bd
	v_fmac_f32_e32 v210, 0x3c800000, v208
	v_rsq_f32_e32 v210, v210
	s_add_u32 s24, s29, 2
	s_lshr_b32 s8, s24, 1
	s_lshl_b32 s8, s8, 12
	s_and_b32 s24, s24, 1
	s_lshl_b32 s24, s24, 8
	s_add_u32 s8, s8, s24
	v_mul_f32_e32 v210, v213, v210
	v_add_u32_e32 v212, s8, v23
	v_pk_mul_f32 v[88:89], v[88:89], v[210:211] op_sel_hi:[1,0]
	v_pk_mul_f32 v[90:91], v[90:91], v[210:211] op_sel_hi:[1,0]
	v_pk_mul_f32 v[88:89], v[88:89], v[40:41]
	v_pk_mul_f32 v[90:91], v[90:91], v[42:43]
	v_cvt_pk_f16_f32 v88, v88, v89
	v_cvt_pk_f16_f32 v89, v90, v91
	global_store_dwordx2 v212, v[88:89], s[22:23] offset:0
	v_pk_mul_f32 v[92:93], v[92:93], v[210:211] op_sel_hi:[1,0]
	v_pk_mul_f32 v[94:95], v[94:95], v[210:211] op_sel_hi:[1,0]
	v_pk_mul_f32 v[92:93], v[92:93], v[44:45]
	v_pk_mul_f32 v[94:95], v[94:95], v[46:47]
	v_cvt_pk_f16_f32 v92, v92, v93
	v_cvt_pk_f16_f32 v93, v94, v95
	global_store_dwordx2 v212, v[92:93], s[22:23] offset:1024
	v_pk_mul_f32 v[96:97], v[96:97], v[210:211] op_sel_hi:[1,0]
	v_pk_mul_f32 v[98:99], v[98:99], v[210:211] op_sel_hi:[1,0]
	v_pk_mul_f32 v[96:97], v[96:97], v[48:49]
	v_pk_mul_f32 v[98:99], v[98:99], v[50:51]
	v_cvt_pk_f16_f32 v96, v96, v97
	v_cvt_pk_f16_f32 v97, v98, v99
	global_store_dwordx2 v212, v[96:97], s[22:23] offset:2048
	v_pk_mul_f32 v[100:101], v[100:101], v[210:211] op_sel_hi:[1,0]
	v_pk_mul_f32 v[102:103], v[102:103], v[210:211] op_sel_hi:[1,0]
	v_pk_mul_f32 v[100:101], v[100:101], v[52:53]
	v_pk_mul_f32 v[102:103], v[102:103], v[54:55]
	v_cvt_pk_f16_f32 v100, v100, v101
	v_cvt_pk_f16_f32 v101, v102, v103
	global_store_dwordx2 v212, v[100:101], s[22:23] offset:3072
	v_pk_add_f32 v[104:105], v[104:105], v[24:25]
	v_pk_add_f32 v[106:107], v[106:107], v[26:27]
	v_pk_add_f32 v[108:109], v[108:109], v[28:29]
	v_pk_add_f32 v[110:111], v[110:111], v[30:31]
	v_pk_add_f32 v[112:113], v[112:113], v[32:33]
	v_pk_add_f32 v[114:115], v[114:115], v[34:35]
	v_pk_add_f32 v[116:117], v[116:117], v[36:37]
	v_pk_add_f32 v[118:119], v[118:119], v[38:39]
	v_pk_mul_f32 v[208:209], v[104:105], v[104:105]
	v_pk_fma_f32 v[208:209], v[106:107], v[106:107], v[208:209]
	v_pk_fma_f32 v[208:209], v[108:109], v[108:109], v[208:209]
	v_pk_fma_f32 v[208:209], v[110:111], v[110:111], v[208:209]
	v_pk_fma_f32 v[208:209], v[112:113], v[112:113], v[208:209]
	v_pk_fma_f32 v[208:209], v[114:115], v[114:115], v[208:209]
	v_pk_fma_f32 v[208:209], v[116:117], v[116:117], v[208:209]
	v_pk_fma_f32 v[208:209], v[118:119], v[118:119], v[208:209]
	v_add_f32_e32 v208, v208, v209
	v_mov_b32_e32 v209, v208
	s_nop 1
	v_permlane16_swap_b32_e32 v208, v209
	v_add_f32_e32 v208, v208, v209
	v_mov_b32_e32 v209, v208
	s_nop 1
	v_permlane32_swap_b32_e32 v208, v209
	v_add_f32_e32 v208, v208, v209
	v_mov_b32_e32 v210, 0x358637bd
	v_fmac_f32_e32 v210, 0x3c800000, v208
	v_rsq_f32_e32 v210, v210
	s_add_u32 s24, s29, 3
	s_lshr_b32 s8, s24, 1
	s_lshl_b32 s8, s8, 12
	s_and_b32 s24, s24, 1
	s_lshl_b32 s24, s24, 8
	s_add_u32 s8, s8, s24
	v_mul_f32_e32 v210, v213, v210
	v_add_u32_e32 v212, s8, v23
	v_pk_mul_f32 v[104:105], v[104:105], v[210:211] op_sel_hi:[1,0]
	v_pk_mul_f32 v[106:107], v[106:107], v[210:211] op_sel_hi:[1,0]
	v_pk_mul_f32 v[104:105], v[104:105], v[40:41]
	v_pk_mul_f32 v[106:107], v[106:107], v[42:43]
	v_cvt_pk_f16_f32 v104, v104, v105
	v_cvt_pk_f16_f32 v105, v106, v107
	global_store_dwordx2 v212, v[104:105], s[22:23] offset:0
	v_pk_mul_f32 v[108:109], v[108:109], v[210:211] op_sel_hi:[1,0]
	v_pk_mul_f32 v[110:111], v[110:111], v[210:211] op_sel_hi:[1,0]
	v_pk_mul_f32 v[108:109], v[108:109], v[44:45]
	v_pk_mul_f32 v[110:111], v[110:111], v[46:47]
	v_cvt_pk_f16_f32 v108, v108, v109
	v_cvt_pk_f16_f32 v109, v110, v111
	global_store_dwordx2 v212, v[108:109], s[22:23] offset:1024
	v_pk_mul_f32 v[112:113], v[112:113], v[210:211] op_sel_hi:[1,0]
	v_pk_mul_f32 v[114:115], v[114:115], v[210:211] op_sel_hi:[1,0]
	v_pk_mul_f32 v[112:113], v[112:113], v[48:49]
	v_pk_mul_f32 v[114:115], v[114:115], v[50:51]
	v_cvt_pk_f16_f32 v112, v112, v113
	v_cvt_pk_f16_f32 v113, v114, v115
	global_store_dwordx2 v212, v[112:113], s[22:23] offset:2048
	v_pk_mul_f32 v[116:117], v[116:117], v[210:211] op_sel_hi:[1,0]
	v_pk_mul_f32 v[118:119], v[118:119], v[210:211] op_sel_hi:[1,0]
	v_pk_mul_f32 v[116:117], v[116:117], v[52:53]
	v_pk_mul_f32 v[118:119], v[118:119], v[54:55]
	v_cvt_pk_f16_f32 v116, v116, v117
	v_cvt_pk_f16_f32 v117, v118, v119
	global_store_dwordx2 v212, v[116:117], s[22:23] offset:3072
	s_branch .Lpf_done
.Lpf_vKA:
	s_mul_i32 s25, s25, 0x50
	s_add_u32 s29, s10, s25
	s_lshr_b32 s29, s29, 4
	v_add_u32_e32 v5, s25, v3
	v_lshlrev_b32_e32 v5, 7, v5
	v_add_u32_e32 v15, v5, v6
	v_add_u32_e32 v16, v5, v7
	v_add_u32_e32 v5, 0x9000, v9
	v_add_u32_e32 v17, v5, v6
	v_add_u32_e32 v18, v5, v7
	v_add_u32_e32 v19, 0x1a000, v15
	v_add_u32_e32 v20, 0x1a000, v16
	v_add_u32_e32 v21, 0x1a000, v17
	v_add_u32_e32 v22, 0x1a000, v18
	v_lshlrev_b32_e32 v5, 4, v4
	global_load_dwordx4 v[24:27], v5, s[14:15] offset:0
	global_load_dwordx4 v[28:31], v5, s[14:15] offset:64
	global_load_dwordx4 v[32:35], v5, s[14:15] offset:128
	global_load_dwordx4 v[36:39], v5, s[14:15] offset:192
	global_load_dwordx4 v[40:43], v5, s[16:17] offset:0
	global_load_dwordx4 v[44:47], v5, s[16:17] offset:64
	global_load_dwordx4 v[48:51], v5, s[16:17] offset:128
	global_load_dwordx4 v[52:55], v5, s[16:17] offset:192
	s_add_u32 m0, s28, 0x0
	s_nop 0
	global_load_lds_dwordx4 v10, s[4:5]
	s_add_u32 m0, s28, 0x2000
	s_nop 0
	global_load_lds_dwordx4 v11, s[4:5]
	s_add_u32 m0, s28, 0x4000
	s_nop 0
	global_load_lds_dwordx4 v12, s[4:5]
	s_add_u32 m0, s28, 0x6000
	s_nop 0
	global_load_lds_dwordx4 v13, s[4:5]
	s_add_u32 m0, s28, 0x8000
	s_nop 0
	global_load_lds_dwordx4 v14, s[4:5]
	s_add_u32 s4, s4, s20
	s_addc_u32 s5, s5, 0
	s_add_u32 m0, s28, 0x9000
	s_nop 0
	global_load_lds_dwordx4 v10, s[6:7]
	s_add_u32 m0, s28, 0xb000
	s_nop 0
	global_load_lds_dwordx4 v11, s[6:7]
	s_add_u32 s6, s6, s20
	s_addc_u32 s7, s7, 0
	s_add_u32 m0, s28, 0xd000
	s_nop 0
	global_load_lds_dwordx4 v10, s[4:5]
	s_add_u32 m0, s28, 0xf000
	s_nop 0
	global_load_lds_dwordx4 v11, s[4:5]
	s_add_u32 m0, s28, 0x11000
	s_nop 0
	global_load_lds_dwordx4 v12, s[4:5]
	s_add_u32 m0, s28, 0x13000
	s_nop 0
	global_load_lds_dwordx4 v13, s[4:5]
	s_add_u32 m0, s28, 0x15000
	s_nop 0
	global_load_lds_dwordx4 v14, s[4:5]
	s_add_u32 s4, s4, s20
	s_addc_u32 s5, s5, 0
	s_add_u32 m0, s28, 0x16000
	s_nop 0
	global_load_lds_dwordx4 v10, s[6:7]
	s_add_u32 m0, s28, 0x18000
	s_nop 0
	global_load_lds_dwordx4 v11, s[6:7]
	s_add_u32 s6, s6, s20
	s_addc_u32 s7, s7, 0
	s_waitcnt vmcnt(7) lgkmcnt(0)
	s_barrier
	s_waitcnt lgkmcnt(6)
	ds_read_b128 v[136:139], v15
	ds_read_b128 v[156:159], v17
	ds_read_b128 v[160:163], v17 offset:2048
	ds_read_b128 v[164:167], v17 offset:4096
	ds_read_b128 v[168:171], v17 offset:6144
	ds_read_b128 v[140:143], v15 offset:2048
	ds_read_b128 v[144:147], v15 offset:4096
	ds_read_b128 v[148:151], v15 offset:6144
	ds_read_b128 v[152:155], v15 offset:8192
	s_waitcnt lgkmcnt(6)
	ds_read_b128 v[172:175], v16
	ds_read_b128 v[192:195], v18
	ds_read_b128 v[196:199], v18 offset:2048
	ds_read_b128 v[200:203], v18 offset:4096
	ds_read_b128 v[204:207], v18 offset:6144
	ds_read_b128 v[176:179], v16 offset:2048
	ds_read_b128 v[180:183], v16 offset:4096
	ds_read_b128 v[184:187], v16 offset:6144
	ds_read_b128 v[188:191], v16 offset:8192
	v_mfma_f32_16x16x32_f16 v[56:59], v[156:159], v[136:139], 0
	s_add_u32 m0, s28, 0x1a000
	s_nop 0
	global_load_lds_dwordx4 v10, s[4:5]
	s_waitcnt lgkmcnt(15)
	v_mfma_f32_16x16x32_f16 v[60:63], v[160:163], v[136:139], 0
	s_waitcnt lgkmcnt(14)
	v_mfma_f32_16x16x32_f16 v[64:67], v[164:167], v[136:139], 0
	s_add_u32 m0, s28, 0x1c000
	s_nop 0
	global_load_lds_dwordx4 v11, s[4:5]
	s_waitcnt lgkmcnt(13)
	v_mfma_f32_16x16x32_f16 v[68:71], v[168:171], v[136:139], 0
	s_waitcnt lgkmcnt(12)
	v_mfma_f32_16x16x32_f16 v[72:75], v[156:159], v[140:143], 0
	v_mfma_f32_16x16x32_f16 v[76:79], v[160:163], v[140:143], 0
	s_add_u32 m0, s28, 0x1e000
	s_nop 0
	global_load_lds_dwordx4 v12, s[4:5]
	v_mfma_f32_16x16x32_f16 v[80:83], v[164:167], v[140:143], 0
	v_mfma_f32_16x16x32_f16 v[84:87], v[168:171], v[140:143], 0
	s_waitcnt lgkmcnt(11)
	v_mfma_f32_16x16x32_f16 v[88:91], v[156:159], v[144:147], 0
	s_add_u32 m0, s28, 0x20000
	s_nop 0
	global_load_lds_dwordx4 v13, s[4:5]
	v_mfma_f32_16x16x32_f16 v[92:95], v[160:163], v[144:147], 0
	v_mfma_f32_16x16x32_f16 v[96:99], v[164:167], v[144:147], 0
	v_mfma_f32_16x16x32_f16 v[100:103], v[168:171], v[144:147], 0
	s_add_u32 m0, s28, 0x22000
	s_nop 0
	global_load_lds_dwordx4 v14, s[4:5]
	s_add_u32 s4, s4, s20
	s_addc_u32 s5, s5, 0
	s_waitcnt lgkmcnt(10)
	v_mfma_f32_16x16x32_f16 v[104:107], v[156:159], v[148:151], 0
	v_mfma_f32_16x16x32_f16 v[108:111], v[160:163], v[148:151], 0
	v_mfma_f32_16x16x32_f16 v[112:115], v[164:167], v[148:151], 0
	s_add_u32 m0, s28, 0x23000
	s_nop 0
	global_load_lds_dwordx4 v10, s[6:7]
	v_mfma_f32_16x16x32_f16 v[116:119], v[168:171], v[148:151], 0
	s_waitcnt lgkmcnt(9)
	v_mfma_f32_16x16x32_f16 v[120:123], v[156:159], v[152:155], 0
	v_mfma_f32_16x16x32_f16 v[124:127], v[160:163], v[152:155], 0
	s_add_u32 m0, s28, 0x25000
	s_nop 0
	global_load_lds_dwordx4 v11, s[6:7]
	s_add_u32 s6, s6, s20
	s_addc_u32 s7, s7, 0
	v_mfma_f32_16x16x32_f16 v[128:131], v[164:167], v[152:155], 0
	v_mfma_f32_16x16x32_f16 v[132:135], v[168:171], v[152:155], 0
	s_waitcnt vmcnt(7) lgkmcnt(0)
	s_barrier
	s_waitcnt lgkmcnt(6)
	ds_read_b128 v[136:139], v15 offset:53248
	ds_read_b128 v[156:159], v17 offset:53248
	ds_read_b128 v[160:163], v17 offset:55296
	ds_read_b128 v[164:167], v17 offset:57344
	ds_read_b128 v[168:171], v17 offset:59392
	ds_read_b128 v[140:143], v15 offset:55296
	ds_read_b128 v[144:147], v15 offset:57344
	ds_read_b128 v[148:151], v15 offset:59392
	ds_read_b128 v[152:155], v15 offset:61440
	v_mfma_f32_16x16x32_f16 v[56:59], v[192:195], v[172:175], v[56:59]
	s_add_u32 m0, s28, 0x0
	s_nop 0
	global_load_lds_dwordx4 v10, s[4:5]
	s_waitcnt lgkmcnt(15)
	v_mfma_f32_16x16x32_f16 v[60:63], v[196:199], v[172:175], v[60:63]
	s_waitcnt lgkmcnt(14)
	v_mfma_f32_16x16x32_f16 v[64:67], v[200:203], v[172:175], v[64:67]
	s_waitcnt lgkmcnt(13)
	v_mfma_f32_16x16x32_f16 v[68:71], v[204:207], v[172:175], v[68:71]
	s_waitcnt lgkmcnt(12)
	v_mfma_f32_16x16x32_f16 v[72:75], v[192:195], v[176:179], v[72:75]
	v_mfma_f32_16x16x32_f16 v[76:79], v[196:199], v[176:179], v[76:79]
	s_add_u32 m0, s28, 0x2000
	s_nop 0
	global_load_lds_dwordx4 v11, s[4:5]
	v_mfma_f32_16x16x32_f16 v[80:83], v[200:203], v[176:179], v[80:83]
	v_mfma_f32_16x16x32_f16 v[84:87], v[204:207], v[176:179], v[84:87]
	s_waitcnt lgkmcnt(11)
	v_mfma_f32_16x16x32_f16 v[88:91], v[192:195], v[180:183], v[88:91]
	v_mfma_f32_16x16x32_f16 v[92:95], v[196:199], v[180:183], v[92:95]
	v_mfma_f32_16x16x32_f16 v[96:99], v[200:203], v[180:183], v[96:99]
	s_add_u32 m0, s28, 0x4000
	s_nop 0
	global_load_lds_dwordx4 v12, s[4:5]
	v_mfma_f32_16x16x32_f16 v[100:103], v[204:207], v[180:183], v[100:103]
	s_waitcnt lgkmcnt(10)
	v_mfma_f32_16x16x32_f16 v[104:107], v[192:195], v[184:187], v[104:107]
	v_mfma_f32_16x16x32_f16 v[108:111], v[196:199], v[184:187], v[108:111]
	v_mfma_f32_16x16x32_f16 v[112:115], v[200:203], v[184:187], v[112:115]
	v_mfma_f32_16x16x32_f16 v[116:119], v[204:207], v[184:187], v[116:119]
	s_add_u32 m0, s28, 0x6000
	s_nop 0
	global_load_lds_dwordx4 v13, s[4:5]
	s_waitcnt lgkmcnt(9)
	v_mfma_f32_16x16x32_f16 v[120:123], v[192:195], v[188:191], v[120:123]
	v_mfma_f32_16x16x32_f16 v[124:127], v[196:199], v[188:191], v[124:127]
	v_mfma_f32_16x16x32_f16 v[128:131], v[200:203], v[188:191], v[128:131]
	v_mfma_f32_16x16x32_f16 v[132:135], v[204:207], v[188:191], v[132:135]
	s_waitcnt lgkmcnt(6)
	ds_read_b128 v[172:175], v16 offset:53248
	ds_read_b128 v[192:195], v18 offset:53248
	ds_read_b128 v[196:199], v18 offset:55296
	ds_read_b128 v[200:203], v18 offset:57344
	ds_read_b128 v[204:207], v18 offset:59392
	ds_read_b128 v[176:179], v16 offset:55296
	ds_read_b128 v[180:183], v16 offset:57344
	ds_read_b128 v[184:187], v16 offset:59392
	ds_read_b128 v[188:191], v16 offset:61440
	v_mfma_f32_16x16x32_f16 v[56:59], v[156:159], v[136:139], v[56:59]
	s_add_u32 m0, s28, 0x8000
	s_nop 0
	global_load_lds_dwordx4 v14, s[4:5]
	s_add_u32 s4, s4, s20
	s_addc_u32 s5, s5, 0
	s_waitcnt lgkmcnt(15)
	v_mfma_f32_16x16x32_f16 v[60:63], v[160:163], v[136:139], v[60:63]
	s_waitcnt lgkmcnt(14)
	v_mfma_f32_16x16x32_f16 v[64:67], v[164:167], v[136:139], v[64:67]
	s_waitcnt lgkmcnt(13)
	v_mfma_f32_16x16x32_f16 v[68:71], v[168:171], v[136:139], v[68:71]
	s_waitcnt lgkmcnt(12)
	v_mfma_f32_16x16x32_f16 v[72:75], v[156:159], v[140:143], v[72:75]
	v_mfma_f32_16x16x32_f16 v[76:79], v[160:163], v[140:143], v[76:79]
	v_mfma_f32_16x16x32_f16 v[80:83], v[164:167], v[140:143], v[80:83]
	s_add_u32 m0, s28, 0x9000
	s_nop 0
	global_load_lds_dwordx4 v10, s[6:7]
	v_mfma_f32_16x16x32_f16 v[84:87], v[168:171], v[140:143], v[84:87]
	s_waitcnt lgkmcnt(11)
	v_mfma_f32_16x16x32_f16 v[88:91], v[156:159], v[144:147], v[88:91]
	v_mfma_f32_16x16x32_f16 v[92:95], v[160:163], v[144:147], v[92:95]
	v_mfma_f32_16x16x32_f16 v[96:99], v[164:167], v[144:147], v[96:99]
	v_mfma_f32_16x16x32_f16 v[100:103], v[168:171], v[144:147], v[100:103]
	s_waitcnt lgkmcnt(10)
	v_mfma_f32_16x16x32_f16 v[104:107], v[156:159], v[148:151], v[104:107]
	v_mfma_f32_16x16x32_f16 v[108:111], v[160:163], v[148:151], v[108:111]
	s_add_u32 m0, s28, 0xb000
	s_nop 0
	global_load_lds_dwordx4 v11, s[6:7]
	s_add_u32 s6, s6, s20
	s_addc_u32 s7, s7, 0
	v_mfma_f32_16x16x32_f16 v[112:115], v[164:167], v[148:151], v[112:115]
	v_mfma_f32_16x16x32_f16 v[116:119], v[168:171], v[148:151], v[116:119]
	s_waitcnt lgkmcnt(9)
	v_mfma_f32_16x16x32_f16 v[120:123], v[156:159], v[152:155], v[120:123]
	v_mfma_f32_16x16x32_f16 v[124:127], v[160:163], v[152:155], v[124:127]
	v_mfma_f32_16x16x32_f16 v[128:131], v[164:167], v[152:155], v[128:131]
	v_mfma_f32_16x16x32_f16 v[132:135], v[168:171], v[152:155], v[132:135]
	s_waitcnt vmcnt(7) lgkmcnt(0)
	s_barrier
	s_waitcnt lgkmcnt(6)
	ds_read_b128 v[136:139], v19
	ds_read_b128 v[156:159], v21
	ds_read_b128 v[160:163], v21 offset:2048
	ds_read_b128 v[164:167], v21 offset:4096
	ds_read_b128 v[168:171], v21 offset:6144
	ds_read_b128 v[140:143], v19 offset:2048
	ds_read_b128 v[144:147], v19 offset:4096
	ds_read_b128 v[148:151], v19 offset:6144
	ds_read_b128 v[152:155], v19 offset:8192
	v_mfma_f32_16x16x32_f16 v[56:59], v[192:195], v[172:175], v[56:59]
	s_add_u32 m0, s28, 0xd000
	s_nop 0
	global_load_lds_dwordx4 v10, s[4:5]
	s_waitcnt lgkmcnt(15)
	v_mfma_f32_16x16x32_f16 v[60:63], v[196:199], v[172:175], v[60:63]
	s_waitcnt lgkmcnt(14)
	v_mfma_f32_16x16x32_f16 v[64:67], v[200:203], v[172:175], v[64:67]
	s_waitcnt lgkmcnt(13)
	v_mfma_f32_16x16x32_f16 v[68:71], v[204:207], v[172:175], v[68:71]
	s_waitcnt lgkmcnt(12)
	v_mfma_f32_16x16x32_f16 v[72:75], v[192:195], v[176:179], v[72:75]
	v_mfma_f32_16x16x32_f16 v[76:79], v[196:199], v[176:179], v[76:79]
	s_add_u32 m0, s28, 0xf000
	s_nop 0
	global_load_lds_dwordx4 v11, s[4:5]
	v_mfma_f32_16x16x32_f16 v[80:83], v[200:203], v[176:179], v[80:83]
	v_mfma_f32_16x16x32_f16 v[84:87], v[204:207], v[176:179], v[84:87]
	s_waitcnt lgkmcnt(11)
	v_mfma_f32_16x16x32_f16 v[88:91], v[192:195], v[180:183], v[88:91]
	v_mfma_f32_16x16x32_f16 v[92:95], v[196:199], v[180:183], v[92:95]
	v_mfma_f32_16x16x32_f16 v[96:99], v[200:203], v[180:183], v[96:99]
	s_add_u32 m0, s28, 0x11000
	s_nop 0
	global_load_lds_dwordx4 v12, s[4:5]
	v_mfma_f32_16x16x32_f16 v[100:103], v[204:207], v[180:183], v[100:103]
	s_waitcnt lgkmcnt(10)
	v_mfma_f32_16x16x32_f16 v[104:107], v[192:195], v[184:187], v[104:107]
	v_mfma_f32_16x16x32_f16 v[108:111], v[196:199], v[184:187], v[108:111]
	v_mfma_f32_16x16x32_f16 v[112:115], v[200:203], v[184:187], v[112:115]
	v_mfma_f32_16x16x32_f16 v[116:119], v[204:207], v[184:187], v[116:119]
	s_add_u32 m0, s28, 0x13000
	s_nop 0
	global_load_lds_dwordx4 v13, s[4:5]
	s_waitcnt lgkmcnt(9)
	v_mfma_f32_16x16x32_f16 v[120:123], v[192:195], v[188:191], v[120:123]
	v_mfma_f32_16x16x32_f16 v[124:127], v[196:199], v[188:191], v[124:127]
	v_mfma_f32_16x16x32_f16 v[128:131], v[200:203], v[188:191], v[128:131]
	v_mfma_f32_16x16x32_f16 v[132:135], v[204:207], v[188:191], v[132:135]
	s_waitcnt lgkmcnt(6)
	ds_read_b128 v[172:175], v20
	ds_read_b128 v[192:195], v22
	ds_read_b128 v[196:199], v22 offset:2048
	ds_read_b128 v[200:203], v22 offset:4096
	ds_read_b128 v[204:207], v22 offset:6144
	ds_read_b128 v[176:179], v20 offset:2048
	ds_read_b128 v[180:183], v20 offset:4096
	ds_read_b128 v[184:187], v20 offset:6144
	ds_read_b128 v[188:191], v20 offset:8192
	v_mfma_f32_16x16x32_f16 v[56:59], v[156:159], v[136:139], v[56:59]
	s_add_u32 m0, s28, 0x15000
	s_nop 0
	global_load_lds_dwordx4 v14, s[4:5]
	s_add_u32 s4, s4, s20
	s_addc_u32 s5, s5, 0
	s_waitcnt lgkmcnt(15)
	v_mfma_f32_16x16x32_f16 v[60:63], v[160:163], v[136:139], v[60:63]
	s_waitcnt lgkmcnt(14)
	v_mfma_f32_16x16x32_f16 v[64:67], v[164:167], v[136:139], v[64:67]
	s_waitcnt lgkmcnt(13)
	v_mfma_f32_16x16x32_f16 v[68:71], v[168:171], v[136:139], v[68:71]
	s_waitcnt lgkmcnt(12)
	v_mfma_f32_16x16x32_f16 v[72:75], v[156:159], v[140:143], v[72:75]
	v_mfma_f32_16x16x32_f16 v[76:79], v[160:163], v[140:143], v[76:79]
	v_mfma_f32_16x16x32_f16 v[80:83], v[164:167], v[140:143], v[80:83]
	s_add_u32 m0, s28, 0x16000
	s_nop 0
	global_load_lds_dwordx4 v10, s[6:7]
	v_mfma_f32_16x16x32_f16 v[84:87], v[168:171], v[140:143], v[84:87]
	s_waitcnt lgkmcnt(11)
	v_mfma_f32_16x16x32_f16 v[88:91], v[156:159], v[144:147], v[88:91]
	v_mfma_f32_16x16x32_f16 v[92:95], v[160:163], v[144:147], v[92:95]
	v_mfma_f32_16x16x32_f16 v[96:99], v[164:167], v[144:147], v[96:99]
	v_mfma_f32_16x16x32_f16 v[100:103], v[168:171], v[144:147], v[100:103]
	s_waitcnt lgkmcnt(10)
	v_mfma_f32_16x16x32_f16 v[104:107], v[156:159], v[148:151], v[104:107]
	v_mfma_f32_16x16x32_f16 v[108:111], v[160:163], v[148:151], v[108:111]
	s_add_u32 m0, s28, 0x18000
	s_nop 0
	global_load_lds_dwordx4 v11, s[6:7]
	s_add_u32 s6, s6, s20
	s_addc_u32 s7, s7, 0
	v_mfma_f32_16x16x32_f16 v[112:115], v[164:167], v[148:151], v[112:115]
	v_mfma_f32_16x16x32_f16 v[116:119], v[168:171], v[148:151], v[116:119]
	s_waitcnt lgkmcnt(9)
	v_mfma_f32_16x16x32_f16 v[120:123], v[156:159], v[152:155], v[120:123]
	v_mfma_f32_16x16x32_f16 v[124:127], v[160:163], v[152:155], v[124:127]
	v_mfma_f32_16x16x32_f16 v[128:131], v[164:167], v[152:155], v[128:131]
	v_mfma_f32_16x16x32_f16 v[132:135], v[168:171], v[152:155], v[132:135]
	s_waitcnt vmcnt(7) lgkmcnt(0)
	s_barrier
	s_waitcnt lgkmcnt(6)
	ds_read_b128 v[136:139], v15
	ds_read_b128 v[156:159], v17
	ds_read_b128 v[160:163], v17 offset:2048
	ds_read_b128 v[164:167], v17 offset:4096
	ds_read_b128 v[168:171], v17 offset:6144
	ds_read_b128 v[140:143], v15 offset:2048
	ds_read_b128 v[144:147], v15 offset:4096
	ds_read_b128 v[148:151], v15 offset:6144
	ds_read_b128 v[152:155], v15 offset:8192
	v_mfma_f32_16x16x32_f16 v[56:59], v[192:195], v[172:175], v[56:59]
	s_add_u32 m0, s28, 0x1a000
	s_nop 0
	global_load_lds_dwordx4 v10, s[4:5]
	s_waitcnt lgkmcnt(15)
	v_mfma_f32_16x16x32_f16 v[60:63], v[196:199], v[172:175], v[60:63]
	s_waitcnt lgkmcnt(14)
	v_mfma_f32_16x16x32_f16 v[64:67], v[200:203], v[172:175], v[64:67]
	s_waitcnt lgkmcnt(13)
	v_mfma_f32_16x16x32_f16 v[68:71], v[204:207], v[172:175], v[68:71]
	s_waitcnt lgkmcnt(12)
	v_mfma_f32_16x16x32_f16 v[72:75], v[192:195], v[176:179], v[72:75]
	v_mfma_f32_16x16x32_f16 v[76:79], v[196:199], v[176:179], v[76:79]
	s_add_u32 m0, s28, 0x1c000
	s_nop 0
	global_load_lds_dwordx4 v11, s[4:5]
	v_mfma_f32_16x16x32_f16 v[80:83], v[200:203], v[176:179], v[80:83]
	v_mfma_f32_16x16x32_f16 v[84:87], v[204:207], v[176:179], v[84:87]
	s_waitcnt lgkmcnt(11)
	v_mfma_f32_16x16x32_f16 v[88:91], v[192:195], v[180:183], v[88:91]
	v_mfma_f32_16x16x32_f16 v[92:95], v[196:199], v[180:183], v[92:95]
	v_mfma_f32_16x16x32_f16 v[96:99], v[200:203], v[180:183], v[96:99]
	s_add_u32 m0, s28, 0x1e000
	s_nop 0
	global_load_lds_dwordx4 v12, s[4:5]
	v_mfma_f32_16x16x32_f16 v[100:103], v[204:207], v[180:183], v[100:103]
	s_waitcnt lgkmcnt(10)
	v_mfma_f32_16x16x32_f16 v[104:107], v[192:195], v[184:187], v[104:107]
	v_mfma_f32_16x16x32_f16 v[108:111], v[196:199], v[184:187], v[108:111]
	v_mfma_f32_16x16x32_f16 v[112:115], v[200:203], v[184:187], v[112:115]
	v_mfma_f32_16x16x32_f16 v[116:119], v[204:207], v[184:187], v[116:119]
	s_add_u32 m0, s28, 0x20000
	s_nop 0
	global_load_lds_dwordx4 v13, s[4:5]
	s_waitcnt lgkmcnt(9)
	v_mfma_f32_16x16x32_f16 v[120:123], v[192:195], v[188:191], v[120:123]
	v_mfma_f32_16x16x32_f16 v[124:127], v[196:199], v[188:191], v[124:127]
	v_mfma_f32_16x16x32_f16 v[128:131], v[200:203], v[188:191], v[128:131]
	v_mfma_f32_16x16x32_f16 v[132:135], v[204:207], v[188:191], v[132:135]
	s_waitcnt lgkmcnt(6)
	ds_read_b128 v[172:175], v16
	ds_read_b128 v[192:195], v18
	ds_read_b128 v[196:199], v18 offset:2048
	ds_read_b128 v[200:203], v18 offset:4096
	ds_read_b128 v[204:207], v18 offset:6144
	ds_read_b128 v[176:179], v16 offset:2048
	ds_read_b128 v[180:183], v16 offset:4096
	ds_read_b128 v[184:187], v16 offset:6144
	ds_read_b128 v[188:191], v16 offset:8192
	v_mfma_f32_16x16x32_f16 v[56:59], v[156:159], v[136:139], v[56:59]
	s_add_u32 m0, s28, 0x22000
	s_nop 0
	global_load_lds_dwordx4 v14, s[4:5]
	s_add_u32 s4, s4, s20
	s_addc_u32 s5, s5, 0
	s_waitcnt lgkmcnt(15)
	v_mfma_f32_16x16x32_f16 v[60:63], v[160:163], v[136:139], v[60:63]
	s_waitcnt lgkmcnt(14)
	v_mfma_f32_16x16x32_f16 v[64:67], v[164:167], v[136:139], v[64:67]
	s_waitcnt lgkmcnt(13)
	v_mfma_f32_16x16x32_f16 v[68:71], v[168:171], v[136:139], v[68:71]
	s_waitcnt lgkmcnt(12)
	v_mfma_f32_16x16x32_f16 v[72:75], v[156:159], v[140:143], v[72:75]
	v_mfma_f32_16x16x32_f16 v[76:79], v[160:163], v[140:143], v[76:79]
	v_mfma_f32_16x16x32_f16 v[80:83], v[164:167], v[140:143], v[80:83]
	s_add_u32 m0, s28, 0x23000
	s_nop 0
	global_load_lds_dwordx4 v10, s[6:7]
	v_mfma_f32_16x16x32_f16 v[84:87], v[168:171], v[140:143], v[84:87]
	s_waitcnt lgkmcnt(11)
	v_mfma_f32_16x16x32_f16 v[88:91], v[156:159], v[144:147], v[88:91]
	v_mfma_f32_16x16x32_f16 v[92:95], v[160:163], v[144:147], v[92:95]
	v_mfma_f32_16x16x32_f16 v[96:99], v[164:167], v[144:147], v[96:99]
	v_mfma_f32_16x16x32_f16 v[100:103], v[168:171], v[144:147], v[100:103]
	s_waitcnt lgkmcnt(10)
	v_mfma_f32_16x16x32_f16 v[104:107], v[156:159], v[148:151], v[104:107]
	v_mfma_f32_16x16x32_f16 v[108:111], v[160:163], v[148:151], v[108:111]
	s_add_u32 m0, s28, 0x25000
	s_nop 0
	global_load_lds_dwordx4 v11, s[6:7]
	s_add_u32 s6, s6, s20
	s_addc_u32 s7, s7, 0
	v_mfma_f32_16x16x32_f16 v[112:115], v[164:167], v[148:151], v[112:115]
	v_mfma_f32_16x16x32_f16 v[116:119], v[168:171], v[148:151], v[116:119]
	s_waitcnt lgkmcnt(9)
	v_mfma_f32_16x16x32_f16 v[120:123], v[156:159], v[152:155], v[120:123]
	v_mfma_f32_16x16x32_f16 v[124:127], v[160:163], v[152:155], v[124:127]
	v_mfma_f32_16x16x32_f16 v[128:131], v[164:167], v[152:155], v[128:131]
	v_mfma_f32_16x16x32_f16 v[132:135], v[168:171], v[152:155], v[132:135]
	s_waitcnt vmcnt(7) lgkmcnt(0)
	s_barrier
	s_waitcnt lgkmcnt(6)
	ds_read_b128 v[136:139], v15 offset:53248
	ds_read_b128 v[156:159], v17 offset:53248
	ds_read_b128 v[160:163], v17 offset:55296
	ds_read_b128 v[164:167], v17 offset:57344
	ds_read_b128 v[168:171], v17 offset:59392
	ds_read_b128 v[140:143], v15 offset:55296
	ds_read_b128 v[144:147], v15 offset:57344
	ds_read_b128 v[148:151], v15 offset:59392
	ds_read_b128 v[152:155], v15 offset:61440
	v_mfma_f32_16x16x32_f16 v[56:59], v[192:195], v[172:175], v[56:59]
	s_add_u32 m0, s28, 0x0
	s_nop 0
	global_load_lds_dwordx4 v10, s[4:5]
	s_waitcnt lgkmcnt(15)
	v_mfma_f32_16x16x32_f16 v[60:63], v[196:199], v[172:175], v[60:63]
	s_waitcnt lgkmcnt(14)
	v_mfma_f32_16x16x32_f16 v[64:67], v[200:203], v[172:175], v[64:67]
	s_waitcnt lgkmcnt(13)
	v_mfma_f32_16x16x32_f16 v[68:71], v[204:207], v[172:175], v[68:71]
	s_waitcnt lgkmcnt(12)
	v_mfma_f32_16x16x32_f16 v[72:75], v[192:195], v[176:179], v[72:75]
	v_mfma_f32_16x16x32_f16 v[76:79], v[196:199], v[176:179], v[76:79]
	s_add_u32 m0, s28, 0x2000
	s_nop 0
	global_load_lds_dwordx4 v11, s[4:5]
	v_mfma_f32_16x16x32_f16 v[80:83], v[200:203], v[176:179], v[80:83]
	v_mfma_f32_16x16x32_f16 v[84:87], v[204:207], v[176:179], v[84:87]
	s_waitcnt lgkmcnt(11)
	v_mfma_f32_16x16x32_f16 v[88:91], v[192:195], v[180:183], v[88:91]
	v_mfma_f32_16x16x32_f16 v[92:95], v[196:199], v[180:183], v[92:95]
	v_mfma_f32_16x16x32_f16 v[96:99], v[200:203], v[180:183], v[96:99]
	s_add_u32 m0, s28, 0x4000
	s_nop 0
	global_load_lds_dwordx4 v12, s[4:5]
	v_mfma_f32_16x16x32_f16 v[100:103], v[204:207], v[180:183], v[100:103]
	s_waitcnt lgkmcnt(10)
	v_mfma_f32_16x16x32_f16 v[104:107], v[192:195], v[184:187], v[104:107]
	v_mfma_f32_16x16x32_f16 v[108:111], v[196:199], v[184:187], v[108:111]
	v_mfma_f32_16x16x32_f16 v[112:115], v[200:203], v[184:187], v[112:115]
	v_mfma_f32_16x16x32_f16 v[116:119], v[204:207], v[184:187], v[116:119]
	s_add_u32 m0, s28, 0x6000
	s_nop 0
	global_load_lds_dwordx4 v13, s[4:5]
	s_waitcnt lgkmcnt(9)
	v_mfma_f32_16x16x32_f16 v[120:123], v[192:195], v[188:191], v[120:123]
	v_mfma_f32_16x16x32_f16 v[124:127], v[196:199], v[188:191], v[124:127]
	v_mfma_f32_16x16x32_f16 v[128:131], v[200:203], v[188:191], v[128:131]
	v_mfma_f32_16x16x32_f16 v[132:135], v[204:207], v[188:191], v[132:135]
	s_waitcnt lgkmcnt(6)
	ds_read_b128 v[172:175], v16 offset:53248
	ds_read_b128 v[192:195], v18 offset:53248
	ds_read_b128 v[196:199], v18 offset:55296
	ds_read_b128 v[200:203], v18 offset:57344
	ds_read_b128 v[204:207], v18 offset:59392
	ds_read_b128 v[176:179], v16 offset:55296
	ds_read_b128 v[180:183], v16 offset:57344
	ds_read_b128 v[184:187], v16 offset:59392
	ds_read_b128 v[188:191], v16 offset:61440
	v_mfma_f32_16x16x32_f16 v[56:59], v[156:159], v[136:139], v[56:59]
	s_add_u32 m0, s28, 0x8000
	s_nop 0
	global_load_lds_dwordx4 v14, s[4:5]
	s_add_u32 s4, s4, s20
	s_addc_u32 s5, s5, 0
	s_waitcnt lgkmcnt(15)
	v_mfma_f32_16x16x32_f16 v[60:63], v[160:163], v[136:139], v[60:63]
	s_waitcnt lgkmcnt(14)
	v_mfma_f32_16x16x32_f16 v[64:67], v[164:167], v[136:139], v[64:67]
	s_waitcnt lgkmcnt(13)
	v_mfma_f32_16x16x32_f16 v[68:71], v[168:171], v[136:139], v[68:71]
	s_waitcnt lgkmcnt(12)
	v_mfma_f32_16x16x32_f16 v[72:75], v[156:159], v[140:143], v[72:75]
	v_mfma_f32_16x16x32_f16 v[76:79], v[160:163], v[140:143], v[76:79]
	v_mfma_f32_16x16x32_f16 v[80:83], v[164:167], v[140:143], v[80:83]
	s_add_u32 m0, s28, 0x9000
	s_nop 0
	global_load_lds_dwordx4 v10, s[6:7]
	v_mfma_f32_16x16x32_f16 v[84:87], v[168:171], v[140:143], v[84:87]
	s_waitcnt lgkmcnt(11)
	v_mfma_f32_16x16x32_f16 v[88:91], v[156:159], v[144:147], v[88:91]
	v_mfma_f32_16x16x32_f16 v[92:95], v[160:163], v[144:147], v[92:95]
	v_mfma_f32_16x16x32_f16 v[96:99], v[164:167], v[144:147], v[96:99]
	v_mfma_f32_16x16x32_f16 v[100:103], v[168:171], v[144:147], v[100:103]
	s_waitcnt lgkmcnt(10)
	v_mfma_f32_16x16x32_f16 v[104:107], v[156:159], v[148:151], v[104:107]
	v_mfma_f32_16x16x32_f16 v[108:111], v[160:163], v[148:151], v[108:111]
	s_add_u32 m0, s28, 0xb000
	s_nop 0
	global_load_lds_dwordx4 v11, s[6:7]
	s_add_u32 s6, s6, s20
	s_addc_u32 s7, s7, 0
	v_mfma_f32_16x16x32_f16 v[112:115], v[164:167], v[148:151], v[112:115]
	v_mfma_f32_16x16x32_f16 v[116:119], v[168:171], v[148:151], v[116:119]
	s_waitcnt lgkmcnt(9)
	v_mfma_f32_16x16x32_f16 v[120:123], v[156:159], v[152:155], v[120:123]
	v_mfma_f32_16x16x32_f16 v[124:127], v[160:163], v[152:155], v[124:127]
	v_mfma_f32_16x16x32_f16 v[128:131], v[164:167], v[152:155], v[128:131]
	v_mfma_f32_16x16x32_f16 v[132:135], v[168:171], v[152:155], v[132:135]
	s_waitcnt vmcnt(7) lgkmcnt(0)
	s_barrier
	s_waitcnt lgkmcnt(6)
	ds_read_b128 v[136:139], v19
	ds_read_b128 v[156:159], v21
	ds_read_b128 v[160:163], v21 offset:2048
	ds_read_b128 v[164:167], v21 offset:4096
	ds_read_b128 v[168:171], v21 offset:6144
	ds_read_b128 v[140:143], v19 offset:2048
	ds_read_b128 v[144:147], v19 offset:4096
	ds_read_b128 v[148:151], v19 offset:6144
	ds_read_b128 v[152:155], v19 offset:8192
	v_mfma_f32_16x16x32_f16 v[56:59], v[192:195], v[172:175], v[56:59]
	s_add_u32 m0, s28, 0xd000
	s_nop 0
	global_load_lds_dwordx4 v10, s[4:5]
	s_waitcnt lgkmcnt(15)
	v_mfma_f32_16x16x32_f16 v[60:63], v[196:199], v[172:175], v[60:63]
	s_waitcnt lgkmcnt(14)
	v_mfma_f32_16x16x32_f16 v[64:67], v[200:203], v[172:175], v[64:67]
	s_waitcnt lgkmcnt(13)
	v_mfma_f32_16x16x32_f16 v[68:71], v[204:207], v[172:175], v[68:71]
	s_waitcnt lgkmcnt(12)
	v_mfma_f32_16x16x32_f16 v[72:75], v[192:195], v[176:179], v[72:75]
	v_mfma_f32_16x16x32_f16 v[76:79], v[196:199], v[176:179], v[76:79]
	s_add_u32 m0, s28, 0xf000
	s_nop 0
	global_load_lds_dwordx4 v11, s[4:5]
	v_mfma_f32_16x16x32_f16 v[80:83], v[200:203], v[176:179], v[80:83]
	v_mfma_f32_16x16x32_f16 v[84:87], v[204:207], v[176:179], v[84:87]
	s_waitcnt lgkmcnt(11)
	v_mfma_f32_16x16x32_f16 v[88:91], v[192:195], v[180:183], v[88:91]
	v_mfma_f32_16x16x32_f16 v[92:95], v[196:199], v[180:183], v[92:95]
	v_mfma_f32_16x16x32_f16 v[96:99], v[200:203], v[180:183], v[96:99]
	s_add_u32 m0, s28, 0x11000
	s_nop 0
	global_load_lds_dwordx4 v12, s[4:5]
	v_mfma_f32_16x16x32_f16 v[100:103], v[204:207], v[180:183], v[100:103]
	s_waitcnt lgkmcnt(10)
	v_mfma_f32_16x16x32_f16 v[104:107], v[192:195], v[184:187], v[104:107]
	v_mfma_f32_16x16x32_f16 v[108:111], v[196:199], v[184:187], v[108:111]
	v_mfma_f32_16x16x32_f16 v[112:115], v[200:203], v[184:187], v[112:115]
	v_mfma_f32_16x16x32_f16 v[116:119], v[204:207], v[184:187], v[116:119]
	s_add_u32 m0, s28, 0x13000
	s_nop 0
	global_load_lds_dwordx4 v13, s[4:5]
	s_waitcnt lgkmcnt(9)
	v_mfma_f32_16x16x32_f16 v[120:123], v[192:195], v[188:191], v[120:123]
	v_mfma_f32_16x16x32_f16 v[124:127], v[196:199], v[188:191], v[124:127]
	v_mfma_f32_16x16x32_f16 v[128:131], v[200:203], v[188:191], v[128:131]
	v_mfma_f32_16x16x32_f16 v[132:135], v[204:207], v[188:191], v[132:135]
	s_waitcnt lgkmcnt(6)
	ds_read_b128 v[172:175], v20
	ds_read_b128 v[192:195], v22
	ds_read_b128 v[196:199], v22 offset:2048
	ds_read_b128 v[200:203], v22 offset:4096
	ds_read_b128 v[204:207], v22 offset:6144
	ds_read_b128 v[176:179], v20 offset:2048
	ds_read_b128 v[180:183], v20 offset:4096
	ds_read_b128 v[184:187], v20 offset:6144
	ds_read_b128 v[188:191], v20 offset:8192
	v_mfma_f32_16x16x32_f16 v[56:59], v[156:159], v[136:139], v[56:59]
	s_add_u32 m0, s28, 0x15000
	s_nop 0
	global_load_lds_dwordx4 v14, s[4:5]
	s_add_u32 s4, s4, s20
	s_addc_u32 s5, s5, 0
	s_waitcnt lgkmcnt(15)
	v_mfma_f32_16x16x32_f16 v[60:63], v[160:163], v[136:139], v[60:63]
	s_waitcnt lgkmcnt(14)
	v_mfma_f32_16x16x32_f16 v[64:67], v[164:167], v[136:139], v[64:67]
	s_waitcnt lgkmcnt(13)
	v_mfma_f32_16x16x32_f16 v[68:71], v[168:171], v[136:139], v[68:71]
	s_waitcnt lgkmcnt(12)
	v_mfma_f32_16x16x32_f16 v[72:75], v[156:159], v[140:143], v[72:75]
	v_mfma_f32_16x16x32_f16 v[76:79], v[160:163], v[140:143], v[76:79]
	v_mfma_f32_16x16x32_f16 v[80:83], v[164:167], v[140:143], v[80:83]
	s_add_u32 m0, s28, 0x16000
	s_nop 0
	global_load_lds_dwordx4 v10, s[6:7]
	v_mfma_f32_16x16x32_f16 v[84:87], v[168:171], v[140:143], v[84:87]
	s_waitcnt lgkmcnt(11)
	v_mfma_f32_16x16x32_f16 v[88:91], v[156:159], v[144:147], v[88:91]
	v_mfma_f32_16x16x32_f16 v[92:95], v[160:163], v[144:147], v[92:95]
	v_mfma_f32_16x16x32_f16 v[96:99], v[164:167], v[144:147], v[96:99]
	v_mfma_f32_16x16x32_f16 v[100:103], v[168:171], v[144:147], v[100:103]
	s_waitcnt lgkmcnt(10)
	v_mfma_f32_16x16x32_f16 v[104:107], v[156:159], v[148:151], v[104:107]
	v_mfma_f32_16x16x32_f16 v[108:111], v[160:163], v[148:151], v[108:111]
	s_add_u32 m0, s28, 0x18000
	s_nop 0
	global_load_lds_dwordx4 v11, s[6:7]
	s_add_u32 s6, s6, s20
	s_addc_u32 s7, s7, 0
	v_mfma_f32_16x16x32_f16 v[112:115], v[164:167], v[148:151], v[112:115]
	v_mfma_f32_16x16x32_f16 v[116:119], v[168:171], v[148:151], v[116:119]
	s_waitcnt lgkmcnt(9)
	v_mfma_f32_16x16x32_f16 v[120:123], v[156:159], v[152:155], v[120:123]
	v_mfma_f32_16x16x32_f16 v[124:127], v[160:163], v[152:155], v[124:127]
	v_mfma_f32_16x16x32_f16 v[128:131], v[164:167], v[152:155], v[128:131]
	v_mfma_f32_16x16x32_f16 v[132:135], v[168:171], v[152:155], v[132:135]
	s_waitcnt vmcnt(7) lgkmcnt(0)
	s_barrier
	s_waitcnt lgkmcnt(6)
	ds_read_b128 v[136:139], v15
	ds_read_b128 v[156:159], v17
	ds_read_b128 v[160:163], v17 offset:2048
	ds_read_b128 v[164:167], v17 offset:4096
	ds_read_b128 v[168:171], v17 offset:6144
	ds_read_b128 v[140:143], v15 offset:2048
	ds_read_b128 v[144:147], v15 offset:4096
	ds_read_b128 v[148:151], v15 offset:6144
	ds_read_b128 v[152:155], v15 offset:8192
	v_mfma_f32_16x16x32_f16 v[56:59], v[192:195], v[172:175], v[56:59]
	s_add_u32 m0, s28, 0x1a000
	s_nop 0
	global_load_lds_dwordx4 v10, s[4:5]
	s_waitcnt lgkmcnt(15)
	v_mfma_f32_16x16x32_f16 v[60:63], v[196:199], v[172:175], v[60:63]
	s_waitcnt lgkmcnt(14)
	v_mfma_f32_16x16x32_f16 v[64:67], v[200:203], v[172:175], v[64:67]
	s_waitcnt lgkmcnt(13)
	v_mfma_f32_16x16x32_f16 v[68:71], v[204:207], v[172:175], v[68:71]
	s_waitcnt lgkmcnt(12)
	v_mfma_f32_16x16x32_f16 v[72:75], v[192:195], v[176:179], v[72:75]
	v_mfma_f32_16x16x32_f16 v[76:79], v[196:199], v[176:179], v[76:79]
	s_add_u32 m0, s28, 0x1c000
	s_nop 0
	global_load_lds_dwordx4 v11, s[4:5]
	v_mfma_f32_16x16x32_f16 v[80:83], v[200:203], v[176:179], v[80:83]
	v_mfma_f32_16x16x32_f16 v[84:87], v[204:207], v[176:179], v[84:87]
	s_waitcnt lgkmcnt(11)
	v_mfma_f32_16x16x32_f16 v[88:91], v[192:195], v[180:183], v[88:91]
	v_mfma_f32_16x16x32_f16 v[92:95], v[196:199], v[180:183], v[92:95]
	v_mfma_f32_16x16x32_f16 v[96:99], v[200:203], v[180:183], v[96:99]
	s_add_u32 m0, s28, 0x1e000
	s_nop 0
	global_load_lds_dwordx4 v12, s[4:5]
	v_mfma_f32_16x16x32_f16 v[100:103], v[204:207], v[180:183], v[100:103]
	s_waitcnt lgkmcnt(10)
	v_mfma_f32_16x16x32_f16 v[104:107], v[192:195], v[184:187], v[104:107]
	v_mfma_f32_16x16x32_f16 v[108:111], v[196:199], v[184:187], v[108:111]
	v_mfma_f32_16x16x32_f16 v[112:115], v[200:203], v[184:187], v[112:115]
	v_mfma_f32_16x16x32_f16 v[116:119], v[204:207], v[184:187], v[116:119]
	s_add_u32 m0, s28, 0x20000
	s_nop 0
	global_load_lds_dwordx4 v13, s[4:5]
	s_waitcnt lgkmcnt(9)
	v_mfma_f32_16x16x32_f16 v[120:123], v[192:195], v[188:191], v[120:123]
	v_mfma_f32_16x16x32_f16 v[124:127], v[196:199], v[188:191], v[124:127]
	v_mfma_f32_16x16x32_f16 v[128:131], v[200:203], v[188:191], v[128:131]
	v_mfma_f32_16x16x32_f16 v[132:135], v[204:207], v[188:191], v[132:135]
	s_waitcnt lgkmcnt(6)
	ds_read_b128 v[172:175], v16
	ds_read_b128 v[192:195], v18
	ds_read_b128 v[196:199], v18 offset:2048
	ds_read_b128 v[200:203], v18 offset:4096
	ds_read_b128 v[204:207], v18 offset:6144
	ds_read_b128 v[176:179], v16 offset:2048
	ds_read_b128 v[180:183], v16 offset:4096
	ds_read_b128 v[184:187], v16 offset:6144
	ds_read_b128 v[188:191], v16 offset:8192
	v_mfma_f32_16x16x32_f16 v[56:59], v[156:159], v[136:139], v[56:59]
	s_add_u32 m0, s28, 0x22000
	s_nop 0
	global_load_lds_dwordx4 v14, s[4:5]
	s_add_u32 s4, s4, s20
	s_addc_u32 s5, s5, 0
	s_waitcnt lgkmcnt(15)
	v_mfma_f32_16x16x32_f16 v[60:63], v[160:163], v[136:139], v[60:63]
	s_waitcnt lgkmcnt(14)
	v_mfma_f32_16x16x32_f16 v[64:67], v[164:167], v[136:139], v[64:67]
	s_waitcnt lgkmcnt(13)
	v_mfma_f32_16x16x32_f16 v[68:71], v[168:171], v[136:139], v[68:71]
	s_waitcnt lgkmcnt(12)
	v_mfma_f32_16x16x32_f16 v[72:75], v[156:159], v[140:143], v[72:75]
	v_mfma_f32_16x16x32_f16 v[76:79], v[160:163], v[140:143], v[76:79]
	v_mfma_f32_16x16x32_f16 v[80:83], v[164:167], v[140:143], v[80:83]
	s_add_u32 m0, s28, 0x23000
	s_nop 0
	global_load_lds_dwordx4 v10, s[6:7]
	v_mfma_f32_16x16x32_f16 v[84:87], v[168:171], v[140:143], v[84:87]
	s_waitcnt lgkmcnt(11)
	v_mfma_f32_16x16x32_f16 v[88:91], v[156:159], v[144:147], v[88:91]
	v_mfma_f32_16x16x32_f16 v[92:95], v[160:163], v[144:147], v[92:95]
	v_mfma_f32_16x16x32_f16 v[96:99], v[164:167], v[144:147], v[96:99]
	v_mfma_f32_16x16x32_f16 v[100:103], v[168:171], v[144:147], v[100:103]
	s_waitcnt lgkmcnt(10)
	v_mfma_f32_16x16x32_f16 v[104:107], v[156:159], v[148:151], v[104:107]
	v_mfma_f32_16x16x32_f16 v[108:111], v[160:163], v[148:151], v[108:111]
	s_add_u32 m0, s28, 0x25000
	s_nop 0
	global_load_lds_dwordx4 v11, s[6:7]
	s_add_u32 s6, s6, s20
	s_addc_u32 s7, s7, 0
	v_mfma_f32_16x16x32_f16 v[112:115], v[164:167], v[148:151], v[112:115]
	v_mfma_f32_16x16x32_f16 v[116:119], v[168:171], v[148:151], v[116:119]
	s_waitcnt lgkmcnt(9)
	v_mfma_f32_16x16x32_f16 v[120:123], v[156:159], v[152:155], v[120:123]
	v_mfma_f32_16x16x32_f16 v[124:127], v[160:163], v[152:155], v[124:127]
	v_mfma_f32_16x16x32_f16 v[128:131], v[164:167], v[152:155], v[128:131]
	v_mfma_f32_16x16x32_f16 v[132:135], v[168:171], v[152:155], v[132:135]
	s_waitcnt vmcnt(7) lgkmcnt(0)
	s_barrier
	s_waitcnt lgkmcnt(6)
	ds_read_b128 v[136:139], v15 offset:53248
	ds_read_b128 v[156:159], v17 offset:53248
	ds_read_b128 v[160:163], v17 offset:55296
	ds_read_b128 v[164:167], v17 offset:57344
	ds_read_b128 v[168:171], v17 offset:59392
	ds_read_b128 v[140:143], v15 offset:55296
	ds_read_b128 v[144:147], v15 offset:57344
	ds_read_b128 v[148:151], v15 offset:59392
	ds_read_b128 v[152:155], v15 offset:61440
	v_mfma_f32_16x16x32_f16 v[56:59], v[192:195], v[172:175], v[56:59]
	s_add_u32 m0, s28, 0x0
	s_nop 0
	global_load_lds_dwordx4 v10, s[4:5]
	s_waitcnt lgkmcnt(15)
	v_mfma_f32_16x16x32_f16 v[60:63], v[196:199], v[172:175], v[60:63]
	s_waitcnt lgkmcnt(14)
	v_mfma_f32_16x16x32_f16 v[64:67], v[200:203], v[172:175], v[64:67]
	s_waitcnt lgkmcnt(13)
	v_mfma_f32_16x16x32_f16 v[68:71], v[204:207], v[172:175], v[68:71]
	s_waitcnt lgkmcnt(12)
	v_mfma_f32_16x16x32_f16 v[72:75], v[192:195], v[176:179], v[72:75]
	v_mfma_f32_16x16x32_f16 v[76:79], v[196:199], v[176:179], v[76:79]
	s_add_u32 m0, s28, 0x2000
	s_nop 0
	global_load_lds_dwordx4 v11, s[4:5]
	v_mfma_f32_16x16x32_f16 v[80:83], v[200:203], v[176:179], v[80:83]
	v_mfma_f32_16x16x32_f16 v[84:87], v[204:207], v[176:179], v[84:87]
	s_waitcnt lgkmcnt(11)
	v_mfma_f32_16x16x32_f16 v[88:91], v[192:195], v[180:183], v[88:91]
	v_mfma_f32_16x16x32_f16 v[92:95], v[196:199], v[180:183], v[92:95]
	v_mfma_f32_16x16x32_f16 v[96:99], v[200:203], v[180:183], v[96:99]
	s_add_u32 m0, s28, 0x4000
	s_nop 0
	global_load_lds_dwordx4 v12, s[4:5]
	v_mfma_f32_16x16x32_f16 v[100:103], v[204:207], v[180:183], v[100:103]
	s_waitcnt lgkmcnt(10)
	v_mfma_f32_16x16x32_f16 v[104:107], v[192:195], v[184:187], v[104:107]
	v_mfma_f32_16x16x32_f16 v[108:111], v[196:199], v[184:187], v[108:111]
	v_mfma_f32_16x16x32_f16 v[112:115], v[200:203], v[184:187], v[112:115]
	v_mfma_f32_16x16x32_f16 v[116:119], v[204:207], v[184:187], v[116:119]
	s_add_u32 m0, s28, 0x6000
	s_nop 0
	global_load_lds_dwordx4 v13, s[4:5]
	s_waitcnt lgkmcnt(9)
	v_mfma_f32_16x16x32_f16 v[120:123], v[192:195], v[188:191], v[120:123]
	v_mfma_f32_16x16x32_f16 v[124:127], v[196:199], v[188:191], v[124:127]
	v_mfma_f32_16x16x32_f16 v[128:131], v[200:203], v[188:191], v[128:131]
	v_mfma_f32_16x16x32_f16 v[132:135], v[204:207], v[188:191], v[132:135]
	s_waitcnt lgkmcnt(6)
	ds_read_b128 v[172:175], v16 offset:53248
	ds_read_b128 v[192:195], v18 offset:53248
	ds_read_b128 v[196:199], v18 offset:55296
	ds_read_b128 v[200:203], v18 offset:57344
	ds_read_b128 v[204:207], v18 offset:59392
	ds_read_b128 v[176:179], v16 offset:55296
	ds_read_b128 v[180:183], v16 offset:57344
	ds_read_b128 v[184:187], v16 offset:59392
	ds_read_b128 v[188:191], v16 offset:61440
	v_mfma_f32_16x16x32_f16 v[56:59], v[156:159], v[136:139], v[56:59]
	s_add_u32 m0, s28, 0x8000
	s_nop 0
	global_load_lds_dwordx4 v14, s[4:5]
	s_add_u32 s4, s4, s20
	s_addc_u32 s5, s5, 0
	s_waitcnt lgkmcnt(15)
	v_mfma_f32_16x16x32_f16 v[60:63], v[160:163], v[136:139], v[60:63]
	s_waitcnt lgkmcnt(14)
	v_mfma_f32_16x16x32_f16 v[64:67], v[164:167], v[136:139], v[64:67]
	s_waitcnt lgkmcnt(13)
	v_mfma_f32_16x16x32_f16 v[68:71], v[168:171], v[136:139], v[68:71]
	s_waitcnt lgkmcnt(12)
	v_mfma_f32_16x16x32_f16 v[72:75], v[156:159], v[140:143], v[72:75]
	v_mfma_f32_16x16x32_f16 v[76:79], v[160:163], v[140:143], v[76:79]
	v_mfma_f32_16x16x32_f16 v[80:83], v[164:167], v[140:143], v[80:83]
	s_add_u32 m0, s28, 0x9000
	s_nop 0
	global_load_lds_dwordx4 v10, s[6:7]
	v_mfma_f32_16x16x32_f16 v[84:87], v[168:171], v[140:143], v[84:87]
	s_waitcnt lgkmcnt(11)
	v_mfma_f32_16x16x32_f16 v[88:91], v[156:159], v[144:147], v[88:91]
	v_mfma_f32_16x16x32_f16 v[92:95], v[160:163], v[144:147], v[92:95]
	v_mfma_f32_16x16x32_f16 v[96:99], v[164:167], v[144:147], v[96:99]
	v_mfma_f32_16x16x32_f16 v[100:103], v[168:171], v[144:147], v[100:103]
	s_waitcnt lgkmcnt(10)
	v_mfma_f32_16x16x32_f16 v[104:107], v[156:159], v[148:151], v[104:107]
	v_mfma_f32_16x16x32_f16 v[108:111], v[160:163], v[148:151], v[108:111]
	s_add_u32 m0, s28, 0xb000
	s_nop 0
	global_load_lds_dwordx4 v11, s[6:7]
	s_add_u32 s6, s6, s20
	s_addc_u32 s7, s7, 0
	v_mfma_f32_16x16x32_f16 v[112:115], v[164:167], v[148:151], v[112:115]
	v_mfma_f32_16x16x32_f16 v[116:119], v[168:171], v[148:151], v[116:119]
	s_waitcnt lgkmcnt(9)
	v_mfma_f32_16x16x32_f16 v[120:123], v[156:159], v[152:155], v[120:123]
	v_mfma_f32_16x16x32_f16 v[124:127], v[160:163], v[152:155], v[124:127]
	v_mfma_f32_16x16x32_f16 v[128:131], v[164:167], v[152:155], v[128:131]
	v_mfma_f32_16x16x32_f16 v[132:135], v[168:171], v[152:155], v[132:135]
	s_waitcnt vmcnt(7) lgkmcnt(0)
	s_barrier
	s_waitcnt lgkmcnt(6)
	ds_read_b128 v[136:139], v19
	ds_read_b128 v[156:159], v21
	ds_read_b128 v[160:163], v21 offset:2048
	ds_read_b128 v[164:167], v21 offset:4096
	ds_read_b128 v[168:171], v21 offset:6144
	ds_read_b128 v[140:143], v19 offset:2048
	ds_read_b128 v[144:147], v19 offset:4096
	ds_read_b128 v[148:151], v19 offset:6144
	ds_read_b128 v[152:155], v19 offset:8192
	v_mfma_f32_16x16x32_f16 v[56:59], v[192:195], v[172:175], v[56:59]
	s_add_u32 m0, s28, 0xd000
	s_nop 0
	global_load_lds_dwordx4 v10, s[4:5]
	s_waitcnt lgkmcnt(15)
	v_mfma_f32_16x16x32_f16 v[60:63], v[196:199], v[172:175], v[60:63]
	s_waitcnt lgkmcnt(14)
	v_mfma_f32_16x16x32_f16 v[64:67], v[200:203], v[172:175], v[64:67]
	s_waitcnt lgkmcnt(13)
	v_mfma_f32_16x16x32_f16 v[68:71], v[204:207], v[172:175], v[68:71]
	s_waitcnt lgkmcnt(12)
	v_mfma_f32_16x16x32_f16 v[72:75], v[192:195], v[176:179], v[72:75]
	v_mfma_f32_16x16x32_f16 v[76:79], v[196:199], v[176:179], v[76:79]
	s_add_u32 m0, s28, 0xf000
	s_nop 0
	global_load_lds_dwordx4 v11, s[4:5]
	v_mfma_f32_16x16x32_f16 v[80:83], v[200:203], v[176:179], v[80:83]
	v_mfma_f32_16x16x32_f16 v[84:87], v[204:207], v[176:179], v[84:87]
	s_waitcnt lgkmcnt(11)
	v_mfma_f32_16x16x32_f16 v[88:91], v[192:195], v[180:183], v[88:91]
	v_mfma_f32_16x16x32_f16 v[92:95], v[196:199], v[180:183], v[92:95]
	v_mfma_f32_16x16x32_f16 v[96:99], v[200:203], v[180:183], v[96:99]
	s_add_u32 m0, s28, 0x11000
	s_nop 0
	global_load_lds_dwordx4 v12, s[4:5]
	v_mfma_f32_16x16x32_f16 v[100:103], v[204:207], v[180:183], v[100:103]
	s_waitcnt lgkmcnt(10)
	v_mfma_f32_16x16x32_f16 v[104:107], v[192:195], v[184:187], v[104:107]
	v_mfma_f32_16x16x32_f16 v[108:111], v[196:199], v[184:187], v[108:111]
	v_mfma_f32_16x16x32_f16 v[112:115], v[200:203], v[184:187], v[112:115]
	v_mfma_f32_16x16x32_f16 v[116:119], v[204:207], v[184:187], v[116:119]
	s_add_u32 m0, s28, 0x13000
	s_nop 0
	global_load_lds_dwordx4 v13, s[4:5]
	s_waitcnt lgkmcnt(9)
	v_mfma_f32_16x16x32_f16 v[120:123], v[192:195], v[188:191], v[120:123]
	v_mfma_f32_16x16x32_f16 v[124:127], v[196:199], v[188:191], v[124:127]
	v_mfma_f32_16x16x32_f16 v[128:131], v[200:203], v[188:191], v[128:131]
	v_mfma_f32_16x16x32_f16 v[132:135], v[204:207], v[188:191], v[132:135]
	s_waitcnt lgkmcnt(6)
	ds_read_b128 v[172:175], v20
	ds_read_b128 v[192:195], v22
	ds_read_b128 v[196:199], v22 offset:2048
	ds_read_b128 v[200:203], v22 offset:4096
	ds_read_b128 v[204:207], v22 offset:6144
	ds_read_b128 v[176:179], v20 offset:2048
	ds_read_b128 v[180:183], v20 offset:4096
	ds_read_b128 v[184:187], v20 offset:6144
	ds_read_b128 v[188:191], v20 offset:8192
	v_mfma_f32_16x16x32_f16 v[56:59], v[156:159], v[136:139], v[56:59]
	s_add_u32 m0, s28, 0x15000
	s_nop 0
	global_load_lds_dwordx4 v14, s[4:5]
	s_add_u32 s4, s4, s20
	s_addc_u32 s5, s5, 0
	s_waitcnt lgkmcnt(15)
	v_mfma_f32_16x16x32_f16 v[60:63], v[160:163], v[136:139], v[60:63]
	s_waitcnt lgkmcnt(14)
	v_mfma_f32_16x16x32_f16 v[64:67], v[164:167], v[136:139], v[64:67]
	s_waitcnt lgkmcnt(13)
	v_mfma_f32_16x16x32_f16 v[68:71], v[168:171], v[136:139], v[68:71]
	s_waitcnt lgkmcnt(12)
	v_mfma_f32_16x16x32_f16 v[72:75], v[156:159], v[140:143], v[72:75]
	v_mfma_f32_16x16x32_f16 v[76:79], v[160:163], v[140:143], v[76:79]
	v_mfma_f32_16x16x32_f16 v[80:83], v[164:167], v[140:143], v[80:83]
	s_add_u32 m0, s28, 0x16000
	s_nop 0
	global_load_lds_dwordx4 v10, s[6:7]
	v_mfma_f32_16x16x32_f16 v[84:87], v[168:171], v[140:143], v[84:87]
	s_waitcnt lgkmcnt(11)
	v_mfma_f32_16x16x32_f16 v[88:91], v[156:159], v[144:147], v[88:91]
	v_mfma_f32_16x16x32_f16 v[92:95], v[160:163], v[144:147], v[92:95]
	v_mfma_f32_16x16x32_f16 v[96:99], v[164:167], v[144:147], v[96:99]
	v_mfma_f32_16x16x32_f16 v[100:103], v[168:171], v[144:147], v[100:103]
	s_waitcnt lgkmcnt(10)
	v_mfma_f32_16x16x32_f16 v[104:107], v[156:159], v[148:151], v[104:107]
	v_mfma_f32_16x16x32_f16 v[108:111], v[160:163], v[148:151], v[108:111]
	s_add_u32 m0, s28, 0x18000
	s_nop 0
	global_load_lds_dwordx4 v11, s[6:7]
	s_add_u32 s6, s6, s20
	s_addc_u32 s7, s7, 0
	v_mfma_f32_16x16x32_f16 v[112:115], v[164:167], v[148:151], v[112:115]
	v_mfma_f32_16x16x32_f16 v[116:119], v[168:171], v[148:151], v[116:119]
	s_waitcnt lgkmcnt(9)
	v_mfma_f32_16x16x32_f16 v[120:123], v[156:159], v[152:155], v[120:123]
	v_mfma_f32_16x16x32_f16 v[124:127], v[160:163], v[152:155], v[124:127]
	v_mfma_f32_16x16x32_f16 v[128:131], v[164:167], v[152:155], v[128:131]
	v_mfma_f32_16x16x32_f16 v[132:135], v[168:171], v[152:155], v[132:135]
	s_waitcnt vmcnt(7) lgkmcnt(0)
	s_barrier
	s_waitcnt lgkmcnt(6)
	ds_read_b128 v[136:139], v15
	ds_read_b128 v[156:159], v17
	ds_read_b128 v[160:163], v17 offset:2048
	ds_read_b128 v[164:167], v17 offset:4096
	ds_read_b128 v[168:171], v17 offset:6144
	ds_read_b128 v[140:143], v15 offset:2048
	ds_read_b128 v[144:147], v15 offset:4096
	ds_read_b128 v[148:151], v15 offset:6144
	ds_read_b128 v[152:155], v15 offset:8192
	v_mfma_f32_16x16x32_f16 v[56:59], v[192:195], v[172:175], v[56:59]
	s_add_u32 m0, s28, 0x1a000
	s_nop 0
	global_load_lds_dwordx4 v10, s[4:5]
	s_waitcnt lgkmcnt(15)
	v_mfma_f32_16x16x32_f16 v[60:63], v[196:199], v[172:175], v[60:63]
	s_waitcnt lgkmcnt(14)
	v_mfma_f32_16x16x32_f16 v[64:67], v[200:203], v[172:175], v[64:67]
	s_waitcnt lgkmcnt(13)
	v_mfma_f32_16x16x32_f16 v[68:71], v[204:207], v[172:175], v[68:71]
	s_waitcnt lgkmcnt(12)
	v_mfma_f32_16x16x32_f16 v[72:75], v[192:195], v[176:179], v[72:75]
	v_mfma_f32_16x16x32_f16 v[76:79], v[196:199], v[176:179], v[76:79]
	s_add_u32 m0, s28, 0x1c000
	s_nop 0
	global_load_lds_dwordx4 v11, s[4:5]
	v_mfma_f32_16x16x32_f16 v[80:83], v[200:203], v[176:179], v[80:83]
	v_mfma_f32_16x16x32_f16 v[84:87], v[204:207], v[176:179], v[84:87]
	s_waitcnt lgkmcnt(11)
	v_mfma_f32_16x16x32_f16 v[88:91], v[192:195], v[180:183], v[88:91]
	v_mfma_f32_16x16x32_f16 v[92:95], v[196:199], v[180:183], v[92:95]
	v_mfma_f32_16x16x32_f16 v[96:99], v[200:203], v[180:183], v[96:99]
	s_add_u32 m0, s28, 0x1e000
	s_nop 0
	global_load_lds_dwordx4 v12, s[4:5]
	v_mfma_f32_16x16x32_f16 v[100:103], v[204:207], v[180:183], v[100:103]
	s_waitcnt lgkmcnt(10)
	v_mfma_f32_16x16x32_f16 v[104:107], v[192:195], v[184:187], v[104:107]
	v_mfma_f32_16x16x32_f16 v[108:111], v[196:199], v[184:187], v[108:111]
	v_mfma_f32_16x16x32_f16 v[112:115], v[200:203], v[184:187], v[112:115]
	v_mfma_f32_16x16x32_f16 v[116:119], v[204:207], v[184:187], v[116:119]
	s_add_u32 m0, s28, 0x20000
	s_nop 0
	global_load_lds_dwordx4 v13, s[4:5]
	s_waitcnt lgkmcnt(9)
	v_mfma_f32_16x16x32_f16 v[120:123], v[192:195], v[188:191], v[120:123]
	v_mfma_f32_16x16x32_f16 v[124:127], v[196:199], v[188:191], v[124:127]
	v_mfma_f32_16x16x32_f16 v[128:131], v[200:203], v[188:191], v[128:131]
	v_mfma_f32_16x16x32_f16 v[132:135], v[204:207], v[188:191], v[132:135]
	s_waitcnt lgkmcnt(6)
	ds_read_b128 v[172:175], v16
	ds_read_b128 v[192:195], v18
	ds_read_b128 v[196:199], v18 offset:2048
	ds_read_b128 v[200:203], v18 offset:4096
	ds_read_b128 v[204:207], v18 offset:6144
	ds_read_b128 v[176:179], v16 offset:2048
	ds_read_b128 v[180:183], v16 offset:4096
	ds_read_b128 v[184:187], v16 offset:6144
	ds_read_b128 v[188:191], v16 offset:8192
	v_mfma_f32_16x16x32_f16 v[56:59], v[156:159], v[136:139], v[56:59]
	s_add_u32 m0, s28, 0x22000
	s_nop 0
	global_load_lds_dwordx4 v14, s[4:5]
	s_add_u32 s4, s4, s20
	s_addc_u32 s5, s5, 0
	s_waitcnt lgkmcnt(15)
	v_mfma_f32_16x16x32_f16 v[60:63], v[160:163], v[136:139], v[60:63]
	s_waitcnt lgkmcnt(14)
	v_mfma_f32_16x16x32_f16 v[64:67], v[164:167], v[136:139], v[64:67]
	s_waitcnt lgkmcnt(13)
	v_mfma_f32_16x16x32_f16 v[68:71], v[168:171], v[136:139], v[68:71]
	s_waitcnt lgkmcnt(12)
	v_mfma_f32_16x16x32_f16 v[72:75], v[156:159], v[140:143], v[72:75]
	v_mfma_f32_16x16x32_f16 v[76:79], v[160:163], v[140:143], v[76:79]
	v_mfma_f32_16x16x32_f16 v[80:83], v[164:167], v[140:143], v[80:83]
	s_add_u32 m0, s28, 0x23000
	s_nop 0
	global_load_lds_dwordx4 v10, s[6:7]
	v_mfma_f32_16x16x32_f16 v[84:87], v[168:171], v[140:143], v[84:87]
	s_waitcnt lgkmcnt(11)
	v_mfma_f32_16x16x32_f16 v[88:91], v[156:159], v[144:147], v[88:91]
	v_mfma_f32_16x16x32_f16 v[92:95], v[160:163], v[144:147], v[92:95]
	v_mfma_f32_16x16x32_f16 v[96:99], v[164:167], v[144:147], v[96:99]
	v_mfma_f32_16x16x32_f16 v[100:103], v[168:171], v[144:147], v[100:103]
	s_waitcnt lgkmcnt(10)
	v_mfma_f32_16x16x32_f16 v[104:107], v[156:159], v[148:151], v[104:107]
	v_mfma_f32_16x16x32_f16 v[108:111], v[160:163], v[148:151], v[108:111]
	s_add_u32 m0, s28, 0x25000
	s_nop 0
	global_load_lds_dwordx4 v11, s[6:7]
	s_add_u32 s6, s6, s20
	s_addc_u32 s7, s7, 0
	v_mfma_f32_16x16x32_f16 v[112:115], v[164:167], v[148:151], v[112:115]
	v_mfma_f32_16x16x32_f16 v[116:119], v[168:171], v[148:151], v[116:119]
	s_waitcnt lgkmcnt(9)
	v_mfma_f32_16x16x32_f16 v[120:123], v[156:159], v[152:155], v[120:123]
	v_mfma_f32_16x16x32_f16 v[124:127], v[160:163], v[152:155], v[124:127]
	v_mfma_f32_16x16x32_f16 v[128:131], v[164:167], v[152:155], v[128:131]
	v_mfma_f32_16x16x32_f16 v[132:135], v[168:171], v[152:155], v[132:135]
	s_waitcnt vmcnt(7) lgkmcnt(0)
	s_barrier
	s_waitcnt lgkmcnt(6)
	ds_read_b128 v[136:139], v15 offset:53248
	ds_read_b128 v[156:159], v17 offset:53248
	ds_read_b128 v[160:163], v17 offset:55296
	ds_read_b128 v[164:167], v17 offset:57344
	ds_read_b128 v[168:171], v17 offset:59392
	ds_read_b128 v[140:143], v15 offset:55296
	ds_read_b128 v[144:147], v15 offset:57344
	ds_read_b128 v[148:151], v15 offset:59392
	ds_read_b128 v[152:155], v15 offset:61440
	v_mfma_f32_16x16x32_f16 v[56:59], v[192:195], v[172:175], v[56:59]
	s_add_u32 m0, s28, 0x0
	s_nop 0
	global_load_lds_dwordx4 v10, s[4:5]
	s_waitcnt lgkmcnt(15)
	v_mfma_f32_16x16x32_f16 v[60:63], v[196:199], v[172:175], v[60:63]
	s_waitcnt lgkmcnt(14)
	v_mfma_f32_16x16x32_f16 v[64:67], v[200:203], v[172:175], v[64:67]
	s_waitcnt lgkmcnt(13)
	v_mfma_f32_16x16x32_f16 v[68:71], v[204:207], v[172:175], v[68:71]
	s_waitcnt lgkmcnt(12)
	v_mfma_f32_16x16x32_f16 v[72:75], v[192:195], v[176:179], v[72:75]
	v_mfma_f32_16x16x32_f16 v[76:79], v[196:199], v[176:179], v[76:79]
	s_add_u32 m0, s28, 0x2000
	s_nop 0
	global_load_lds_dwordx4 v11, s[4:5]
	v_mfma_f32_16x16x32_f16 v[80:83], v[200:203], v[176:179], v[80:83]
	v_mfma_f32_16x16x32_f16 v[84:87], v[204:207], v[176:179], v[84:87]
	s_waitcnt lgkmcnt(11)
	v_mfma_f32_16x16x32_f16 v[88:91], v[192:195], v[180:183], v[88:91]
	v_mfma_f32_16x16x32_f16 v[92:95], v[196:199], v[180:183], v[92:95]
	v_mfma_f32_16x16x32_f16 v[96:99], v[200:203], v[180:183], v[96:99]
	s_add_u32 m0, s28, 0x4000
	s_nop 0
	global_load_lds_dwordx4 v12, s[4:5]
	v_mfma_f32_16x16x32_f16 v[100:103], v[204:207], v[180:183], v[100:103]
	s_waitcnt lgkmcnt(10)
	v_mfma_f32_16x16x32_f16 v[104:107], v[192:195], v[184:187], v[104:107]
	v_mfma_f32_16x16x32_f16 v[108:111], v[196:199], v[184:187], v[108:111]
	v_mfma_f32_16x16x32_f16 v[112:115], v[200:203], v[184:187], v[112:115]
	v_mfma_f32_16x16x32_f16 v[116:119], v[204:207], v[184:187], v[116:119]
	s_add_u32 m0, s28, 0x6000
	s_nop 0
	global_load_lds_dwordx4 v13, s[4:5]
	s_waitcnt lgkmcnt(9)
	v_mfma_f32_16x16x32_f16 v[120:123], v[192:195], v[188:191], v[120:123]
	v_mfma_f32_16x16x32_f16 v[124:127], v[196:199], v[188:191], v[124:127]
	v_mfma_f32_16x16x32_f16 v[128:131], v[200:203], v[188:191], v[128:131]
	v_mfma_f32_16x16x32_f16 v[132:135], v[204:207], v[188:191], v[132:135]
	s_waitcnt lgkmcnt(6)
	ds_read_b128 v[172:175], v16 offset:53248
	ds_read_b128 v[192:195], v18 offset:53248
	ds_read_b128 v[196:199], v18 offset:55296
	ds_read_b128 v[200:203], v18 offset:57344
	ds_read_b128 v[204:207], v18 offset:59392
	ds_read_b128 v[176:179], v16 offset:55296
	ds_read_b128 v[180:183], v16 offset:57344
	ds_read_b128 v[184:187], v16 offset:59392
	ds_read_b128 v[188:191], v16 offset:61440
	v_mfma_f32_16x16x32_f16 v[56:59], v[156:159], v[136:139], v[56:59]
	s_add_u32 m0, s28, 0x8000
	s_nop 0
	global_load_lds_dwordx4 v14, s[4:5]
	s_add_u32 s4, s4, s20
	s_addc_u32 s5, s5, 0
	s_waitcnt lgkmcnt(15)
	v_mfma_f32_16x16x32_f16 v[60:63], v[160:163], v[136:139], v[60:63]
	s_waitcnt lgkmcnt(14)
	v_mfma_f32_16x16x32_f16 v[64:67], v[164:167], v[136:139], v[64:67]
	s_waitcnt lgkmcnt(13)
	v_mfma_f32_16x16x32_f16 v[68:71], v[168:171], v[136:139], v[68:71]
	s_waitcnt lgkmcnt(12)
	v_mfma_f32_16x16x32_f16 v[72:75], v[156:159], v[140:143], v[72:75]
	v_mfma_f32_16x16x32_f16 v[76:79], v[160:163], v[140:143], v[76:79]
	v_mfma_f32_16x16x32_f16 v[80:83], v[164:167], v[140:143], v[80:83]
	s_add_u32 m0, s28, 0x9000
	s_nop 0
	global_load_lds_dwordx4 v10, s[6:7]
	v_mfma_f32_16x16x32_f16 v[84:87], v[168:171], v[140:143], v[84:87]
	s_waitcnt lgkmcnt(11)
	v_mfma_f32_16x16x32_f16 v[88:91], v[156:159], v[144:147], v[88:91]
	v_mfma_f32_16x16x32_f16 v[92:95], v[160:163], v[144:147], v[92:95]
	v_mfma_f32_16x16x32_f16 v[96:99], v[164:167], v[144:147], v[96:99]
	v_mfma_f32_16x16x32_f16 v[100:103], v[168:171], v[144:147], v[100:103]
	s_waitcnt lgkmcnt(10)
	v_mfma_f32_16x16x32_f16 v[104:107], v[156:159], v[148:151], v[104:107]
	v_mfma_f32_16x16x32_f16 v[108:111], v[160:163], v[148:151], v[108:111]
	s_add_u32 m0, s28, 0xb000
	s_nop 0
	global_load_lds_dwordx4 v11, s[6:7]
	s_add_u32 s6, s6, s20
	s_addc_u32 s7, s7, 0
	v_mfma_f32_16x16x32_f16 v[112:115], v[164:167], v[148:151], v[112:115]
	v_mfma_f32_16x16x32_f16 v[116:119], v[168:171], v[148:151], v[116:119]
	s_waitcnt lgkmcnt(9)
	v_mfma_f32_16x16x32_f16 v[120:123], v[156:159], v[152:155], v[120:123]
	v_mfma_f32_16x16x32_f16 v[124:127], v[160:163], v[152:155], v[124:127]
	v_mfma_f32_16x16x32_f16 v[128:131], v[164:167], v[152:155], v[128:131]
	v_mfma_f32_16x16x32_f16 v[132:135], v[168:171], v[152:155], v[132:135]
	s_waitcnt vmcnt(7) lgkmcnt(0)
	s_barrier
	s_waitcnt lgkmcnt(6)
	ds_read_b128 v[136:139], v19
	ds_read_b128 v[156:159], v21
	ds_read_b128 v[160:163], v21 offset:2048
	ds_read_b128 v[164:167], v21 offset:4096
	ds_read_b128 v[168:171], v21 offset:6144
	ds_read_b128 v[140:143], v19 offset:2048
	ds_read_b128 v[144:147], v19 offset:4096
	ds_read_b128 v[148:151], v19 offset:6144
	ds_read_b128 v[152:155], v19 offset:8192
	v_mfma_f32_16x16x32_f16 v[56:59], v[192:195], v[172:175], v[56:59]
	s_add_u32 m0, s28, 0xd000
	s_nop 0
	global_load_lds_dwordx4 v10, s[4:5]
	s_waitcnt lgkmcnt(15)
	v_mfma_f32_16x16x32_f16 v[60:63], v[196:199], v[172:175], v[60:63]
	s_waitcnt lgkmcnt(14)
	v_mfma_f32_16x16x32_f16 v[64:67], v[200:203], v[172:175], v[64:67]
	s_waitcnt lgkmcnt(13)
	v_mfma_f32_16x16x32_f16 v[68:71], v[204:207], v[172:175], v[68:71]
	s_waitcnt lgkmcnt(12)
	v_mfma_f32_16x16x32_f16 v[72:75], v[192:195], v[176:179], v[72:75]
	v_mfma_f32_16x16x32_f16 v[76:79], v[196:199], v[176:179], v[76:79]
	s_add_u32 m0, s28, 0xf000
	s_nop 0
	global_load_lds_dwordx4 v11, s[4:5]
	v_mfma_f32_16x16x32_f16 v[80:83], v[200:203], v[176:179], v[80:83]
	v_mfma_f32_16x16x32_f16 v[84:87], v[204:207], v[176:179], v[84:87]
	s_waitcnt lgkmcnt(11)
	v_mfma_f32_16x16x32_f16 v[88:91], v[192:195], v[180:183], v[88:91]
	v_mfma_f32_16x16x32_f16 v[92:95], v[196:199], v[180:183], v[92:95]
	v_mfma_f32_16x16x32_f16 v[96:99], v[200:203], v[180:183], v[96:99]
	s_add_u32 m0, s28, 0x11000
	s_nop 0
	global_load_lds_dwordx4 v12, s[4:5]
	v_mfma_f32_16x16x32_f16 v[100:103], v[204:207], v[180:183], v[100:103]
	s_waitcnt lgkmcnt(10)
	v_mfma_f32_16x16x32_f16 v[104:107], v[192:195], v[184:187], v[104:107]
	v_mfma_f32_16x16x32_f16 v[108:111], v[196:199], v[184:187], v[108:111]
	v_mfma_f32_16x16x32_f16 v[112:115], v[200:203], v[184:187], v[112:115]
	v_mfma_f32_16x16x32_f16 v[116:119], v[204:207], v[184:187], v[116:119]
	s_add_u32 m0, s28, 0x13000
	s_nop 0
	global_load_lds_dwordx4 v13, s[4:5]
	s_waitcnt lgkmcnt(9)
	v_mfma_f32_16x16x32_f16 v[120:123], v[192:195], v[188:191], v[120:123]
	v_mfma_f32_16x16x32_f16 v[124:127], v[196:199], v[188:191], v[124:127]
	v_mfma_f32_16x16x32_f16 v[128:131], v[200:203], v[188:191], v[128:131]
	v_mfma_f32_16x16x32_f16 v[132:135], v[204:207], v[188:191], v[132:135]
	s_waitcnt lgkmcnt(6)
	ds_read_b128 v[172:175], v20
	ds_read_b128 v[192:195], v22
	ds_read_b128 v[196:199], v22 offset:2048
	ds_read_b128 v[200:203], v22 offset:4096
	ds_read_b128 v[204:207], v22 offset:6144
	ds_read_b128 v[176:179], v20 offset:2048
	ds_read_b128 v[180:183], v20 offset:4096
	ds_read_b128 v[184:187], v20 offset:6144
	ds_read_b128 v[188:191], v20 offset:8192
	v_mfma_f32_16x16x32_f16 v[56:59], v[156:159], v[136:139], v[56:59]
	s_add_u32 m0, s28, 0x15000
	s_nop 0
	global_load_lds_dwordx4 v14, s[4:5]
	s_add_u32 s4, s4, s20
	s_addc_u32 s5, s5, 0
	s_waitcnt lgkmcnt(15)
	v_mfma_f32_16x16x32_f16 v[60:63], v[160:163], v[136:139], v[60:63]
	s_waitcnt lgkmcnt(14)
	v_mfma_f32_16x16x32_f16 v[64:67], v[164:167], v[136:139], v[64:67]
	s_waitcnt lgkmcnt(13)
	v_mfma_f32_16x16x32_f16 v[68:71], v[168:171], v[136:139], v[68:71]
	s_waitcnt lgkmcnt(12)
	v_mfma_f32_16x16x32_f16 v[72:75], v[156:159], v[140:143], v[72:75]
	v_mfma_f32_16x16x32_f16 v[76:79], v[160:163], v[140:143], v[76:79]
	v_mfma_f32_16x16x32_f16 v[80:83], v[164:167], v[140:143], v[80:83]
	s_add_u32 m0, s28, 0x16000
	s_nop 0
	global_load_lds_dwordx4 v10, s[6:7]
	v_mfma_f32_16x16x32_f16 v[84:87], v[168:171], v[140:143], v[84:87]
	s_waitcnt lgkmcnt(11)
	v_mfma_f32_16x16x32_f16 v[88:91], v[156:159], v[144:147], v[88:91]
	v_mfma_f32_16x16x32_f16 v[92:95], v[160:163], v[144:147], v[92:95]
	v_mfma_f32_16x16x32_f16 v[96:99], v[164:167], v[144:147], v[96:99]
	v_mfma_f32_16x16x32_f16 v[100:103], v[168:171], v[144:147], v[100:103]
	s_waitcnt lgkmcnt(10)
	v_mfma_f32_16x16x32_f16 v[104:107], v[156:159], v[148:151], v[104:107]
	v_mfma_f32_16x16x32_f16 v[108:111], v[160:163], v[148:151], v[108:111]
	s_add_u32 m0, s28, 0x18000
	s_nop 0
	global_load_lds_dwordx4 v11, s[6:7]
	s_add_u32 s6, s6, s20
	s_addc_u32 s7, s7, 0
	v_mfma_f32_16x16x32_f16 v[112:115], v[164:167], v[148:151], v[112:115]
	v_mfma_f32_16x16x32_f16 v[116:119], v[168:171], v[148:151], v[116:119]
	s_waitcnt lgkmcnt(9)
	v_mfma_f32_16x16x32_f16 v[120:123], v[156:159], v[152:155], v[120:123]
	v_mfma_f32_16x16x32_f16 v[124:127], v[160:163], v[152:155], v[124:127]
	v_mfma_f32_16x16x32_f16 v[128:131], v[164:167], v[152:155], v[128:131]
	v_mfma_f32_16x16x32_f16 v[132:135], v[168:171], v[152:155], v[132:135]
	s_waitcnt vmcnt(7) lgkmcnt(0)
	s_barrier
	s_waitcnt lgkmcnt(6)
	ds_read_b128 v[136:139], v15
	ds_read_b128 v[156:159], v17
	ds_read_b128 v[160:163], v17 offset:2048
	ds_read_b128 v[164:167], v17 offset:4096
	ds_read_b128 v[168:171], v17 offset:6144
	ds_read_b128 v[140:143], v15 offset:2048
	ds_read_b128 v[144:147], v15 offset:4096
	ds_read_b128 v[148:151], v15 offset:6144
	ds_read_b128 v[152:155], v15 offset:8192
	v_mfma_f32_16x16x32_f16 v[56:59], v[192:195], v[172:175], v[56:59]
	s_add_u32 m0, s28, 0x1a000
	s_nop 0
	global_load_lds_dwordx4 v10, s[4:5]
	s_waitcnt lgkmcnt(15)
	v_mfma_f32_16x16x32_f16 v[60:63], v[196:199], v[172:175], v[60:63]
	s_waitcnt lgkmcnt(14)
	v_mfma_f32_16x16x32_f16 v[64:67], v[200:203], v[172:175], v[64:67]
	s_waitcnt lgkmcnt(13)
	v_mfma_f32_16x16x32_f16 v[68:71], v[204:207], v[172:175], v[68:71]
	s_waitcnt lgkmcnt(12)
	v_mfma_f32_16x16x32_f16 v[72:75], v[192:195], v[176:179], v[72:75]
	v_mfma_f32_16x16x32_f16 v[76:79], v[196:199], v[176:179], v[76:79]
	s_add_u32 m0, s28, 0x1c000
	s_nop 0
	global_load_lds_dwordx4 v11, s[4:5]
	v_mfma_f32_16x16x32_f16 v[80:83], v[200:203], v[176:179], v[80:83]
	v_mfma_f32_16x16x32_f16 v[84:87], v[204:207], v[176:179], v[84:87]
	s_waitcnt lgkmcnt(11)
	v_mfma_f32_16x16x32_f16 v[88:91], v[192:195], v[180:183], v[88:91]
	v_mfma_f32_16x16x32_f16 v[92:95], v[196:199], v[180:183], v[92:95]
	v_mfma_f32_16x16x32_f16 v[96:99], v[200:203], v[180:183], v[96:99]
	s_add_u32 m0, s28, 0x1e000
	s_nop 0
	global_load_lds_dwordx4 v12, s[4:5]
	v_mfma_f32_16x16x32_f16 v[100:103], v[204:207], v[180:183], v[100:103]
	s_waitcnt lgkmcnt(10)
	v_mfma_f32_16x16x32_f16 v[104:107], v[192:195], v[184:187], v[104:107]
	v_mfma_f32_16x16x32_f16 v[108:111], v[196:199], v[184:187], v[108:111]
	v_mfma_f32_16x16x32_f16 v[112:115], v[200:203], v[184:187], v[112:115]
	v_mfma_f32_16x16x32_f16 v[116:119], v[204:207], v[184:187], v[116:119]
	s_add_u32 m0, s28, 0x20000
	s_nop 0
	global_load_lds_dwordx4 v13, s[4:5]
	s_waitcnt lgkmcnt(9)
	v_mfma_f32_16x16x32_f16 v[120:123], v[192:195], v[188:191], v[120:123]
	v_mfma_f32_16x16x32_f16 v[124:127], v[196:199], v[188:191], v[124:127]
	v_mfma_f32_16x16x32_f16 v[128:131], v[200:203], v[188:191], v[128:131]
	v_mfma_f32_16x16x32_f16 v[132:135], v[204:207], v[188:191], v[132:135]
	s_waitcnt lgkmcnt(6)
	ds_read_b128 v[172:175], v16
	ds_read_b128 v[192:195], v18
	ds_read_b128 v[196:199], v18 offset:2048
	ds_read_b128 v[200:203], v18 offset:4096
	ds_read_b128 v[204:207], v18 offset:6144
	ds_read_b128 v[176:179], v16 offset:2048
	ds_read_b128 v[180:183], v16 offset:4096
	ds_read_b128 v[184:187], v16 offset:6144
	ds_read_b128 v[188:191], v16 offset:8192
	v_mfma_f32_16x16x32_f16 v[56:59], v[156:159], v[136:139], v[56:59]
	s_add_u32 m0, s28, 0x22000
	s_nop 0
	global_load_lds_dwordx4 v14, s[4:5]
	s_add_u32 s4, s4, s20
	s_addc_u32 s5, s5, 0
	s_waitcnt lgkmcnt(15)
	v_mfma_f32_16x16x32_f16 v[60:63], v[160:163], v[136:139], v[60:63]
	s_waitcnt lgkmcnt(14)
	v_mfma_f32_16x16x32_f16 v[64:67], v[164:167], v[136:139], v[64:67]
	s_waitcnt lgkmcnt(13)
	v_mfma_f32_16x16x32_f16 v[68:71], v[168:171], v[136:139], v[68:71]
	s_waitcnt lgkmcnt(12)
	v_mfma_f32_16x16x32_f16 v[72:75], v[156:159], v[140:143], v[72:75]
	v_mfma_f32_16x16x32_f16 v[76:79], v[160:163], v[140:143], v[76:79]
	v_mfma_f32_16x16x32_f16 v[80:83], v[164:167], v[140:143], v[80:83]
	s_add_u32 m0, s28, 0x23000
	s_nop 0
	global_load_lds_dwordx4 v10, s[6:7]
	v_mfma_f32_16x16x32_f16 v[84:87], v[168:171], v[140:143], v[84:87]
	s_waitcnt lgkmcnt(11)
	v_mfma_f32_16x16x32_f16 v[88:91], v[156:159], v[144:147], v[88:91]
	v_mfma_f32_16x16x32_f16 v[92:95], v[160:163], v[144:147], v[92:95]
	v_mfma_f32_16x16x32_f16 v[96:99], v[164:167], v[144:147], v[96:99]
	v_mfma_f32_16x16x32_f16 v[100:103], v[168:171], v[144:147], v[100:103]
	s_waitcnt lgkmcnt(10)
	v_mfma_f32_16x16x32_f16 v[104:107], v[156:159], v[148:151], v[104:107]
	v_mfma_f32_16x16x32_f16 v[108:111], v[160:163], v[148:151], v[108:111]
	s_add_u32 m0, s28, 0x25000
	s_nop 0
	global_load_lds_dwordx4 v11, s[6:7]
	s_add_u32 s6, s6, s20
	s_addc_u32 s7, s7, 0
	v_mfma_f32_16x16x32_f16 v[112:115], v[164:167], v[148:151], v[112:115]
	v_mfma_f32_16x16x32_f16 v[116:119], v[168:171], v[148:151], v[116:119]
	s_waitcnt lgkmcnt(9)
	v_mfma_f32_16x16x32_f16 v[120:123], v[156:159], v[152:155], v[120:123]
	v_mfma_f32_16x16x32_f16 v[124:127], v[160:163], v[152:155], v[124:127]
	v_mfma_f32_16x16x32_f16 v[128:131], v[164:167], v[152:155], v[128:131]
	v_mfma_f32_16x16x32_f16 v[132:135], v[168:171], v[152:155], v[132:135]
	s_waitcnt vmcnt(7) lgkmcnt(0)
	s_barrier
	s_waitcnt lgkmcnt(6)
	ds_read_b128 v[136:139], v15 offset:53248
	ds_read_b128 v[156:159], v17 offset:53248
	ds_read_b128 v[160:163], v17 offset:55296
	ds_read_b128 v[164:167], v17 offset:57344
	ds_read_b128 v[168:171], v17 offset:59392
	ds_read_b128 v[140:143], v15 offset:55296
	ds_read_b128 v[144:147], v15 offset:57344
	ds_read_b128 v[148:151], v15 offset:59392
	ds_read_b128 v[152:155], v15 offset:61440
	v_mfma_f32_16x16x32_f16 v[56:59], v[192:195], v[172:175], v[56:59]
	s_add_u32 m0, s28, 0x0
	s_nop 0
	global_load_lds_dwordx4 v10, s[4:5]
	s_waitcnt lgkmcnt(15)
	v_mfma_f32_16x16x32_f16 v[60:63], v[196:199], v[172:175], v[60:63]
	s_waitcnt lgkmcnt(14)
	v_mfma_f32_16x16x32_f16 v[64:67], v[200:203], v[172:175], v[64:67]
	s_waitcnt lgkmcnt(13)
	v_mfma_f32_16x16x32_f16 v[68:71], v[204:207], v[172:175], v[68:71]
	s_waitcnt lgkmcnt(12)
	v_mfma_f32_16x16x32_f16 v[72:75], v[192:195], v[176:179], v[72:75]
	v_mfma_f32_16x16x32_f16 v[76:79], v[196:199], v[176:179], v[76:79]
	s_add_u32 m0, s28, 0x2000
	s_nop 0
	global_load_lds_dwordx4 v11, s[4:5]
	v_mfma_f32_16x16x32_f16 v[80:83], v[200:203], v[176:179], v[80:83]
	v_mfma_f32_16x16x32_f16 v[84:87], v[204:207], v[176:179], v[84:87]
	s_waitcnt lgkmcnt(11)
	v_mfma_f32_16x16x32_f16 v[88:91], v[192:195], v[180:183], v[88:91]
	v_mfma_f32_16x16x32_f16 v[92:95], v[196:199], v[180:183], v[92:95]
	v_mfma_f32_16x16x32_f16 v[96:99], v[200:203], v[180:183], v[96:99]
	s_add_u32 m0, s28, 0x4000
	s_nop 0
	global_load_lds_dwordx4 v12, s[4:5]
	v_mfma_f32_16x16x32_f16 v[100:103], v[204:207], v[180:183], v[100:103]
	s_waitcnt lgkmcnt(10)
	v_mfma_f32_16x16x32_f16 v[104:107], v[192:195], v[184:187], v[104:107]
	v_mfma_f32_16x16x32_f16 v[108:111], v[196:199], v[184:187], v[108:111]
	v_mfma_f32_16x16x32_f16 v[112:115], v[200:203], v[184:187], v[112:115]
	v_mfma_f32_16x16x32_f16 v[116:119], v[204:207], v[184:187], v[116:119]
	s_add_u32 m0, s28, 0x6000
	s_nop 0
	global_load_lds_dwordx4 v13, s[4:5]
	s_waitcnt lgkmcnt(9)
	v_mfma_f32_16x16x32_f16 v[120:123], v[192:195], v[188:191], v[120:123]
	v_mfma_f32_16x16x32_f16 v[124:127], v[196:199], v[188:191], v[124:127]
	v_mfma_f32_16x16x32_f16 v[128:131], v[200:203], v[188:191], v[128:131]
	v_mfma_f32_16x16x32_f16 v[132:135], v[204:207], v[188:191], v[132:135]
	s_waitcnt lgkmcnt(6)
	ds_read_b128 v[172:175], v16 offset:53248
	ds_read_b128 v[192:195], v18 offset:53248
	ds_read_b128 v[196:199], v18 offset:55296
	ds_read_b128 v[200:203], v18 offset:57344
	ds_read_b128 v[204:207], v18 offset:59392
	ds_read_b128 v[176:179], v16 offset:55296
	ds_read_b128 v[180:183], v16 offset:57344
	ds_read_b128 v[184:187], v16 offset:59392
	ds_read_b128 v[188:191], v16 offset:61440
	v_mfma_f32_16x16x32_f16 v[56:59], v[156:159], v[136:139], v[56:59]
	s_add_u32 m0, s28, 0x8000
	s_nop 0
	global_load_lds_dwordx4 v14, s[4:5]
	s_add_u32 s4, s4, s20
	s_addc_u32 s5, s5, 0
	s_waitcnt lgkmcnt(15)
	v_mfma_f32_16x16x32_f16 v[60:63], v[160:163], v[136:139], v[60:63]
	s_waitcnt lgkmcnt(14)
	v_mfma_f32_16x16x32_f16 v[64:67], v[164:167], v[136:139], v[64:67]
	s_waitcnt lgkmcnt(13)
	v_mfma_f32_16x16x32_f16 v[68:71], v[168:171], v[136:139], v[68:71]
	s_waitcnt lgkmcnt(12)
	v_mfma_f32_16x16x32_f16 v[72:75], v[156:159], v[140:143], v[72:75]
	v_mfma_f32_16x16x32_f16 v[76:79], v[160:163], v[140:143], v[76:79]
	v_mfma_f32_16x16x32_f16 v[80:83], v[164:167], v[140:143], v[80:83]
	s_add_u32 m0, s28, 0x9000
	s_nop 0
	global_load_lds_dwordx4 v10, s[6:7]
	v_mfma_f32_16x16x32_f16 v[84:87], v[168:171], v[140:143], v[84:87]
	s_waitcnt lgkmcnt(11)
	v_mfma_f32_16x16x32_f16 v[88:91], v[156:159], v[144:147], v[88:91]
	v_mfma_f32_16x16x32_f16 v[92:95], v[160:163], v[144:147], v[92:95]
	v_mfma_f32_16x16x32_f16 v[96:99], v[164:167], v[144:147], v[96:99]
	v_mfma_f32_16x16x32_f16 v[100:103], v[168:171], v[144:147], v[100:103]
	s_waitcnt lgkmcnt(10)
	v_mfma_f32_16x16x32_f16 v[104:107], v[156:159], v[148:151], v[104:107]
	v_mfma_f32_16x16x32_f16 v[108:111], v[160:163], v[148:151], v[108:111]
	s_add_u32 m0, s28, 0xb000
	s_nop 0
	global_load_lds_dwordx4 v11, s[6:7]
	s_add_u32 s6, s6, s20
	s_addc_u32 s7, s7, 0
	v_mfma_f32_16x16x32_f16 v[112:115], v[164:167], v[148:151], v[112:115]
	v_mfma_f32_16x16x32_f16 v[116:119], v[168:171], v[148:151], v[116:119]
	s_waitcnt lgkmcnt(9)
	v_mfma_f32_16x16x32_f16 v[120:123], v[156:159], v[152:155], v[120:123]
	v_mfma_f32_16x16x32_f16 v[124:127], v[160:163], v[152:155], v[124:127]
	v_mfma_f32_16x16x32_f16 v[128:131], v[164:167], v[152:155], v[128:131]
	v_mfma_f32_16x16x32_f16 v[132:135], v[168:171], v[152:155], v[132:135]
	s_waitcnt vmcnt(7) lgkmcnt(0)
	s_barrier
	s_waitcnt lgkmcnt(6)
	ds_read_b128 v[136:139], v19
	ds_read_b128 v[156:159], v21
	ds_read_b128 v[160:163], v21 offset:2048
	ds_read_b128 v[164:167], v21 offset:4096
	ds_read_b128 v[168:171], v21 offset:6144
	ds_read_b128 v[140:143], v19 offset:2048
	ds_read_b128 v[144:147], v19 offset:4096
	ds_read_b128 v[148:151], v19 offset:6144
	ds_read_b128 v[152:155], v19 offset:8192
	v_mfma_f32_16x16x32_f16 v[56:59], v[192:195], v[172:175], v[56:59]
	s_waitcnt lgkmcnt(15)
	v_mfma_f32_16x16x32_f16 v[60:63], v[196:199], v[172:175], v[60:63]
	s_waitcnt lgkmcnt(14)
	v_mfma_f32_16x16x32_f16 v[64:67], v[200:203], v[172:175], v[64:67]
	s_waitcnt lgkmcnt(13)
	v_mfma_f32_16x16x32_f16 v[68:71], v[204:207], v[172:175], v[68:71]
	s_waitcnt lgkmcnt(12)
	v_mfma_f32_16x16x32_f16 v[72:75], v[192:195], v[176:179], v[72:75]
	v_mfma_f32_16x16x32_f16 v[76:79], v[196:199], v[176:179], v[76:79]
	v_mfma_f32_16x16x32_f16 v[80:83], v[200:203], v[176:179], v[80:83]
	v_mfma_f32_16x16x32_f16 v[84:87], v[204:207], v[176:179], v[84:87]
	s_waitcnt lgkmcnt(11)
	v_mfma_f32_16x16x32_f16 v[88:91], v[192:195], v[180:183], v[88:91]
	v_mfma_f32_16x16x32_f16 v[92:95], v[196:199], v[180:183], v[92:95]
	v_mfma_f32_16x16x32_f16 v[96:99], v[200:203], v[180:183], v[96:99]
	v_mfma_f32_16x16x32_f16 v[100:103], v[204:207], v[180:183], v[100:103]
	s_waitcnt lgkmcnt(10)
	v_mfma_f32_16x16x32_f16 v[104:107], v[192:195], v[184:187], v[104:107]
	v_mfma_f32_16x16x32_f16 v[108:111], v[196:199], v[184:187], v[108:111]
	v_mfma_f32_16x16x32_f16 v[112:115], v[200:203], v[184:187], v[112:115]
	v_mfma_f32_16x16x32_f16 v[116:119], v[204:207], v[184:187], v[116:119]
	s_waitcnt lgkmcnt(9)
	v_mfma_f32_16x16x32_f16 v[120:123], v[192:195], v[188:191], v[120:123]
	v_mfma_f32_16x16x32_f16 v[124:127], v[196:199], v[188:191], v[124:127]
	v_mfma_f32_16x16x32_f16 v[128:131], v[200:203], v[188:191], v[128:131]
	v_mfma_f32_16x16x32_f16 v[132:135], v[204:207], v[188:191], v[132:135]
	s_waitcnt lgkmcnt(6)
	ds_read_b128 v[172:175], v20
	ds_read_b128 v[192:195], v22
	ds_read_b128 v[196:199], v22 offset:2048
	ds_read_b128 v[200:203], v22 offset:4096
	ds_read_b128 v[204:207], v22 offset:6144
	ds_read_b128 v[176:179], v20 offset:2048
	ds_read_b128 v[180:183], v20 offset:4096
	ds_read_b128 v[184:187], v20 offset:6144
	ds_read_b128 v[188:191], v20 offset:8192
	v_mfma_f32_16x16x32_f16 v[56:59], v[156:159], v[136:139], v[56:59]
	s_waitcnt lgkmcnt(15)
	v_mfma_f32_16x16x32_f16 v[60:63], v[160:163], v[136:139], v[60:63]
	s_waitcnt lgkmcnt(14)
	v_mfma_f32_16x16x32_f16 v[64:67], v[164:167], v[136:139], v[64:67]
	s_waitcnt lgkmcnt(13)
	v_mfma_f32_16x16x32_f16 v[68:71], v[168:171], v[136:139], v[68:71]
	s_waitcnt lgkmcnt(12)
	v_mfma_f32_16x16x32_f16 v[72:75], v[156:159], v[140:143], v[72:75]
	v_mfma_f32_16x16x32_f16 v[76:79], v[160:163], v[140:143], v[76:79]
	v_mfma_f32_16x16x32_f16 v[80:83], v[164:167], v[140:143], v[80:83]
	v_mfma_f32_16x16x32_f16 v[84:87], v[168:171], v[140:143], v[84:87]
	s_waitcnt lgkmcnt(11)
	v_mfma_f32_16x16x32_f16 v[88:91], v[156:159], v[144:147], v[88:91]
	v_mfma_f32_16x16x32_f16 v[92:95], v[160:163], v[144:147], v[92:95]
	v_mfma_f32_16x16x32_f16 v[96:99], v[164:167], v[144:147], v[96:99]
	v_mfma_f32_16x16x32_f16 v[100:103], v[168:171], v[144:147], v[100:103]
	s_waitcnt lgkmcnt(10)
	v_mfma_f32_16x16x32_f16 v[104:107], v[156:159], v[148:151], v[104:107]
	v_mfma_f32_16x16x32_f16 v[108:111], v[160:163], v[148:151], v[108:111]
	v_mfma_f32_16x16x32_f16 v[112:115], v[164:167], v[148:151], v[112:115]
	v_mfma_f32_16x16x32_f16 v[116:119], v[168:171], v[148:151], v[116:119]
	s_waitcnt lgkmcnt(9)
	v_mfma_f32_16x16x32_f16 v[120:123], v[156:159], v[152:155], v[120:123]
	v_mfma_f32_16x16x32_f16 v[124:127], v[160:163], v[152:155], v[124:127]
	v_mfma_f32_16x16x32_f16 v[128:131], v[164:167], v[152:155], v[128:131]
	v_mfma_f32_16x16x32_f16 v[132:135], v[168:171], v[152:155], v[132:135]
	s_waitcnt vmcnt(0) lgkmcnt(0)
	s_barrier
	s_waitcnt lgkmcnt(6)
	ds_read_b128 v[136:139], v15
	ds_read_b128 v[156:159], v17
	ds_read_b128 v[160:163], v17 offset:2048
	ds_read_b128 v[164:167], v17 offset:4096
	ds_read_b128 v[168:171], v17 offset:6144
	ds_read_b128 v[140:143], v15 offset:2048
	ds_read_b128 v[144:147], v15 offset:4096
	ds_read_b128 v[148:151], v15 offset:6144
	ds_read_b128 v[152:155], v15 offset:8192
	v_mfma_f32_16x16x32_f16 v[56:59], v[192:195], v[172:175], v[56:59]
	s_waitcnt lgkmcnt(15)
	v_mfma_f32_16x16x32_f16 v[60:63], v[196:199], v[172:175], v[60:63]
	s_waitcnt lgkmcnt(14)
	v_mfma_f32_16x16x32_f16 v[64:67], v[200:203], v[172:175], v[64:67]
	s_waitcnt lgkmcnt(13)
	v_mfma_f32_16x16x32_f16 v[68:71], v[204:207], v[172:175], v[68:71]
	s_waitcnt lgkmcnt(12)
	v_mfma_f32_16x16x32_f16 v[72:75], v[192:195], v[176:179], v[72:75]
	v_mfma_f32_16x16x32_f16 v[76:79], v[196:199], v[176:179], v[76:79]
	v_mfma_f32_16x16x32_f16 v[80:83], v[200:203], v[176:179], v[80:83]
	v_mfma_f32_16x16x32_f16 v[84:87], v[204:207], v[176:179], v[84:87]
	s_waitcnt lgkmcnt(11)
	v_mfma_f32_16x16x32_f16 v[88:91], v[192:195], v[180:183], v[88:91]
	v_mfma_f32_16x16x32_f16 v[92:95], v[196:199], v[180:183], v[92:95]
	v_mfma_f32_16x16x32_f16 v[96:99], v[200:203], v[180:183], v[96:99]
	v_mfma_f32_16x16x32_f16 v[100:103], v[204:207], v[180:183], v[100:103]
	s_waitcnt lgkmcnt(10)
	v_mfma_f32_16x16x32_f16 v[104:107], v[192:195], v[184:187], v[104:107]
	v_mfma_f32_16x16x32_f16 v[108:111], v[196:199], v[184:187], v[108:111]
	v_mfma_f32_16x16x32_f16 v[112:115], v[200:203], v[184:187], v[112:115]
	v_mfma_f32_16x16x32_f16 v[116:119], v[204:207], v[184:187], v[116:119]
	s_waitcnt lgkmcnt(9)
	v_mfma_f32_16x16x32_f16 v[120:123], v[192:195], v[188:191], v[120:123]
	v_mfma_f32_16x16x32_f16 v[124:127], v[196:199], v[188:191], v[124:127]
	v_mfma_f32_16x16x32_f16 v[128:131], v[200:203], v[188:191], v[128:131]
	v_mfma_f32_16x16x32_f16 v[132:135], v[204:207], v[188:191], v[132:135]
	s_waitcnt lgkmcnt(6)
	ds_read_b128 v[172:175], v16
	ds_read_b128 v[192:195], v18
	ds_read_b128 v[196:199], v18 offset:2048
	ds_read_b128 v[200:203], v18 offset:4096
	ds_read_b128 v[204:207], v18 offset:6144
	ds_read_b128 v[176:179], v16 offset:2048
	ds_read_b128 v[180:183], v16 offset:4096
	ds_read_b128 v[184:187], v16 offset:6144
	ds_read_b128 v[188:191], v16 offset:8192
	v_mfma_f32_16x16x32_f16 v[56:59], v[156:159], v[136:139], v[56:59]
	s_waitcnt lgkmcnt(15)
	v_mfma_f32_16x16x32_f16 v[60:63], v[160:163], v[136:139], v[60:63]
	s_waitcnt lgkmcnt(14)
	v_mfma_f32_16x16x32_f16 v[64:67], v[164:167], v[136:139], v[64:67]
	s_waitcnt lgkmcnt(13)
	v_mfma_f32_16x16x32_f16 v[68:71], v[168:171], v[136:139], v[68:71]
	s_waitcnt lgkmcnt(12)
	v_mfma_f32_16x16x32_f16 v[72:75], v[156:159], v[140:143], v[72:75]
	v_mfma_f32_16x16x32_f16 v[76:79], v[160:163], v[140:143], v[76:79]
	v_mfma_f32_16x16x32_f16 v[80:83], v[164:167], v[140:143], v[80:83]
	v_mfma_f32_16x16x32_f16 v[84:87], v[168:171], v[140:143], v[84:87]
	s_waitcnt lgkmcnt(11)
	v_mfma_f32_16x16x32_f16 v[88:91], v[156:159], v[144:147], v[88:91]
	v_mfma_f32_16x16x32_f16 v[92:95], v[160:163], v[144:147], v[92:95]
	v_mfma_f32_16x16x32_f16 v[96:99], v[164:167], v[144:147], v[96:99]
	v_mfma_f32_16x16x32_f16 v[100:103], v[168:171], v[144:147], v[100:103]
	s_waitcnt lgkmcnt(10)
	v_mfma_f32_16x16x32_f16 v[104:107], v[156:159], v[148:151], v[104:107]
	v_mfma_f32_16x16x32_f16 v[108:111], v[160:163], v[148:151], v[108:111]
	v_mfma_f32_16x16x32_f16 v[112:115], v[164:167], v[148:151], v[112:115]
	v_mfma_f32_16x16x32_f16 v[116:119], v[168:171], v[148:151], v[116:119]
	s_waitcnt lgkmcnt(9)
	v_mfma_f32_16x16x32_f16 v[120:123], v[156:159], v[152:155], v[120:123]
	v_mfma_f32_16x16x32_f16 v[124:127], v[160:163], v[152:155], v[124:127]
	v_mfma_f32_16x16x32_f16 v[128:131], v[164:167], v[152:155], v[128:131]
	v_mfma_f32_16x16x32_f16 v[132:135], v[168:171], v[152:155], v[132:135]
	s_waitcnt lgkmcnt(7)
	v_mfma_f32_16x16x32_f16 v[56:59], v[192:195], v[172:175], v[56:59]
	s_waitcnt lgkmcnt(6)
	v_mfma_f32_16x16x32_f16 v[60:63], v[196:199], v[172:175], v[60:63]
	s_waitcnt lgkmcnt(5)
	v_mfma_f32_16x16x32_f16 v[64:67], v[200:203], v[172:175], v[64:67]
	s_waitcnt lgkmcnt(4)
	v_mfma_f32_16x16x32_f16 v[68:71], v[204:207], v[172:175], v[68:71]
	s_waitcnt lgkmcnt(3)
	v_mfma_f32_16x16x32_f16 v[72:75], v[192:195], v[176:179], v[72:75]
	v_mfma_f32_16x16x32_f16 v[76:79], v[196:199], v[176:179], v[76:79]
	v_mfma_f32_16x16x32_f16 v[80:83], v[200:203], v[176:179], v[80:83]
	v_mfma_f32_16x16x32_f16 v[84:87], v[204:207], v[176:179], v[84:87]
	s_waitcnt lgkmcnt(2)
	v_mfma_f32_16x16x32_f16 v[88:91], v[192:195], v[180:183], v[88:91]
	v_mfma_f32_16x16x32_f16 v[92:95], v[196:199], v[180:183], v[92:95]
	v_mfma_f32_16x16x32_f16 v[96:99], v[200:203], v[180:183], v[96:99]
	v_mfma_f32_16x16x32_f16 v[100:103], v[204:207], v[180:183], v[100:103]
	s_waitcnt lgkmcnt(1)
	v_mfma_f32_16x16x32_f16 v[104:107], v[192:195], v[184:187], v[104:107]
	v_mfma_f32_16x16x32_f16 v[108:111], v[196:199], v[184:187], v[108:111]
	v_mfma_f32_16x16x32_f16 v[112:115], v[200:203], v[184:187], v[112:115]
	v_mfma_f32_16x16x32_f16 v[116:119], v[204:207], v[184:187], v[116:119]
	s_waitcnt lgkmcnt(0)
	v_mfma_f32_16x16x32_f16 v[120:123], v[192:195], v[188:191], v[120:123]
	v_mfma_f32_16x16x32_f16 v[124:127], v[196:199], v[188:191], v[124:127]
	v_mfma_f32_16x16x32_f16 v[128:131], v[200:203], v[188:191], v[128:131]
	v_mfma_f32_16x16x32_f16 v[132:135], v[204:207], v[188:191], v[132:135]
	s_nop 7
	s_nop 1
	v_mov_b32_e32 v213, s19
	v_pk_add_f32 v[56:57], v[56:57], v[24:25]
	v_pk_add_f32 v[58:59], v[58:59], v[26:27]
	v_pk_add_f32 v[60:61], v[60:61], v[28:29]
	v_pk_add_f32 v[62:63], v[62:63], v[30:31]
	v_pk_add_f32 v[64:65], v[64:65], v[32:33]
	v_pk_add_f32 v[66:67], v[66:67], v[34:35]
	v_pk_add_f32 v[68:69], v[68:69], v[36:37]
	v_pk_add_f32 v[70:71], v[70:71], v[38:39]
	v_pk_mul_f32 v[208:209], v[56:57], v[56:57]
	v_pk_fma_f32 v[208:209], v[58:59], v[58:59], v[208:209]
	v_pk_fma_f32 v[208:209], v[60:61], v[60:61], v[208:209]
	v_pk_fma_f32 v[208:209], v[62:63], v[62:63], v[208:209]
	v_pk_fma_f32 v[208:209], v[64:65], v[64:65], v[208:209]
	v_pk_fma_f32 v[208:209], v[66:67], v[66:67], v[208:209]
	v_pk_fma_f32 v[208:209], v[68:69], v[68:69], v[208:209]
	v_pk_fma_f32 v[208:209], v[70:71], v[70:71], v[208:209]
	v_add_f32_e32 v208, v208, v209
	v_mov_b32_e32 v209, v208
	s_nop 1
	v_permlane16_swap_b32_e32 v208, v209
	v_add_f32_e32 v208, v208, v209
	v_mov_b32_e32 v209, v208
	s_nop 1
	v_permlane32_swap_b32_e32 v208, v209
	v_add_f32_e32 v208, v208, v209
	v_mov_b32_e32 v210, 0x358637bd
	v_fmac_f32_e32 v210, 0x3c800000, v208
	v_rsq_f32_e32 v210, v210
	s_add_u32 s24, s29, 0
	s_lshr_b32 s8, s24, 1
	s_lshl_b32 s8, s8, 12
	s_and_b32 s24, s24, 1
	s_lshl_b32 s24, s24, 8
	s_add_u32 s8, s8, s24
	v_mul_f32_e32 v210, v213, v210
	v_add_u32_e32 v212, s8, v23
	v_pk_mul_f32 v[56:57], v[56:57], v[210:211] op_sel_hi:[1,0]
	v_pk_mul_f32 v[58:59], v[58:59], v[210:211] op_sel_hi:[1,0]
	v_pk_mul_f32 v[56:57], v[56:57], v[40:41]
	v_pk_mul_f32 v[58:59], v[58:59], v[42:43]
	v_cvt_pk_f16_f32 v56, v56, v57
	v_cvt_pk_f16_f32 v57, v58, v59
	global_store_dwordx2 v212, v[56:57], s[22:23] offset:0
	v_pk_mul_f32 v[60:61], v[60:61], v[210:211] op_sel_hi:[1,0]
	v_pk_mul_f32 v[62:63], v[62:63], v[210:211] op_sel_hi:[1,0]
	v_pk_mul_f32 v[60:61], v[60:61], v[44:45]
	v_pk_mul_f32 v[62:63], v[62:63], v[46:47]
	v_cvt_pk_f16_f32 v60, v60, v61
	v_cvt_pk_f16_f32 v61, v62, v63
	global_store_dwordx2 v212, v[60:61], s[22:23] offset:1024
	v_pk_mul_f32 v[64:65], v[64:65], v[210:211] op_sel_hi:[1,0]
	v_pk_mul_f32 v[66:67], v[66:67], v[210:211] op_sel_hi:[1,0]
	v_pk_mul_f32 v[64:65], v[64:65], v[48:49]
	v_pk_mul_f32 v[66:67], v[66:67], v[50:51]
	v_cvt_pk_f16_f32 v64, v64, v65
	v_cvt_pk_f16_f32 v65, v66, v67
	global_store_dwordx2 v212, v[64:65], s[22:23] offset:2048
	v_pk_mul_f32 v[68:69], v[68:69], v[210:211] op_sel_hi:[1,0]
	v_pk_mul_f32 v[70:71], v[70:71], v[210:211] op_sel_hi:[1,0]
	v_pk_mul_f32 v[68:69], v[68:69], v[52:53]
	v_pk_mul_f32 v[70:71], v[70:71], v[54:55]
	v_cvt_pk_f16_f32 v68, v68, v69
	v_cvt_pk_f16_f32 v69, v70, v71
	global_store_dwordx2 v212, v[68:69], s[22:23] offset:3072
	v_pk_add_f32 v[72:73], v[72:73], v[24:25]
	v_pk_add_f32 v[74:75], v[74:75], v[26:27]
	v_pk_add_f32 v[76:77], v[76:77], v[28:29]
	v_pk_add_f32 v[78:79], v[78:79], v[30:31]
	v_pk_add_f32 v[80:81], v[80:81], v[32:33]
	v_pk_add_f32 v[82:83], v[82:83], v[34:35]
	v_pk_add_f32 v[84:85], v[84:85], v[36:37]
	v_pk_add_f32 v[86:87], v[86:87], v[38:39]
	v_pk_mul_f32 v[208:209], v[72:73], v[72:73]
	v_pk_fma_f32 v[208:209], v[74:75], v[74:75], v[208:209]
	v_pk_fma_f32 v[208:209], v[76:77], v[76:77], v[208:209]
	v_pk_fma_f32 v[208:209], v[78:79], v[78:79], v[208:209]
	v_pk_fma_f32 v[208:209], v[80:81], v[80:81], v[208:209]
	v_pk_fma_f32 v[208:209], v[82:83], v[82:83], v[208:209]
	v_pk_fma_f32 v[208:209], v[84:85], v[84:85], v[208:209]
	v_pk_fma_f32 v[208:209], v[86:87], v[86:87], v[208:209]
	v_add_f32_e32 v208, v208, v209
	v_mov_b32_e32 v209, v208
	s_nop 1
	v_permlane16_swap_b32_e32 v208, v209
	v_add_f32_e32 v208, v208, v209
	v_mov_b32_e32 v209, v208
	s_nop 1
	v_permlane32_swap_b32_e32 v208, v209
	v_add_f32_e32 v208, v208, v209
	v_mov_b32_e32 v210, 0x358637bd
	v_fmac_f32_e32 v210, 0x3c800000, v208
	v_rsq_f32_e32 v210, v210
	s_add_u32 s24, s29, 1
	s_lshr_b32 s8, s24, 1
	s_lshl_b32 s8, s8, 12
	s_and_b32 s24, s24, 1
	s_lshl_b32 s24, s24, 8
	s_add_u32 s8, s8, s24
	v_mul_f32_e32 v210, v213, v210
	v_add_u32_e32 v212, s8, v23
	v_pk_mul_f32 v[72:73], v[72:73], v[210:211] op_sel_hi:[1,0]
	v_pk_mul_f32 v[74:75], v[74:75], v[210:211] op_sel_hi:[1,0]
	v_pk_mul_f32 v[72:73], v[72:73], v[40:41]
	v_pk_mul_f32 v[74:75], v[74:75], v[42:43]
	v_cvt_pk_f16_f32 v72, v72, v73
	v_cvt_pk_f16_f32 v73, v74, v75
	global_store_dwordx2 v212, v[72:73], s[22:23] offset:0
	v_pk_mul_f32 v[76:77], v[76:77], v[210:211] op_sel_hi:[1,0]
	v_pk_mul_f32 v[78:79], v[78:79], v[210:211] op_sel_hi:[1,0]
	v_pk_mul_f32 v[76:77], v[76:77], v[44:45]
	v_pk_mul_f32 v[78:79], v[78:79], v[46:47]
	v_cvt_pk_f16_f32 v76, v76, v77
	v_cvt_pk_f16_f32 v77, v78, v79
	global_store_dwordx2 v212, v[76:77], s[22:23] offset:1024
	v_pk_mul_f32 v[80:81], v[80:81], v[210:211] op_sel_hi:[1,0]
	v_pk_mul_f32 v[82:83], v[82:83], v[210:211] op_sel_hi:[1,0]
	v_pk_mul_f32 v[80:81], v[80:81], v[48:49]
	v_pk_mul_f32 v[82:83], v[82:83], v[50:51]
	v_cvt_pk_f16_f32 v80, v80, v81
	v_cvt_pk_f16_f32 v81, v82, v83
	global_store_dwordx2 v212, v[80:81], s[22:23] offset:2048
	v_pk_mul_f32 v[84:85], v[84:85], v[210:211] op_sel_hi:[1,0]
	v_pk_mul_f32 v[86:87], v[86:87], v[210:211] op_sel_hi:[1,0]
	v_pk_mul_f32 v[84:85], v[84:85], v[52:53]
	v_pk_mul_f32 v[86:87], v[86:87], v[54:55]
	v_cvt_pk_f16_f32 v84, v84, v85
	v_cvt_pk_f16_f32 v85, v86, v87
	global_store_dwordx2 v212, v[84:85], s[22:23] offset:3072
	v_pk_add_f32 v[88:89], v[88:89], v[24:25]
	v_pk_add_f32 v[90:91], v[90:91], v[26:27]
	v_pk_add_f32 v[92:93], v[92:93], v[28:29]
	v_pk_add_f32 v[94:95], v[94:95], v[30:31]
	v_pk_add_f32 v[96:97], v[96:97], v[32:33]
	v_pk_add_f32 v[98:99], v[98:99], v[34:35]
	v_pk_add_f32 v[100:101], v[100:101], v[36:37]
	v_pk_add_f32 v[102:103], v[102:103], v[38:39]
	v_pk_mul_f32 v[208:209], v[88:89], v[88:89]
	v_pk_fma_f32 v[208:209], v[90:91], v[90:91], v[208:209]
	v_pk_fma_f32 v[208:209], v[92:93], v[92:93], v[208:209]
	v_pk_fma_f32 v[208:209], v[94:95], v[94:95], v[208:209]
	v_pk_fma_f32 v[208:209], v[96:97], v[96:97], v[208:209]
	v_pk_fma_f32 v[208:209], v[98:99], v[98:99], v[208:209]
	v_pk_fma_f32 v[208:209], v[100:101], v[100:101], v[208:209]
	v_pk_fma_f32 v[208:209], v[102:103], v[102:103], v[208:209]
	v_add_f32_e32 v208, v208, v209
	v_mov_b32_e32 v209, v208
	s_nop 1
	v_permlane16_swap_b32_e32 v208, v209
	v_add_f32_e32 v208, v208, v209
	v_mov_b32_e32 v209, v208
	s_nop 1
	v_permlane32_swap_b32_e32 v208, v209
	v_add_f32_e32 v208, v208, v209
	v_mov_b32_e32 v210, 0x358637bd
	v_fmac_f32_e32 v210, 0x3c800000, v208
	v_rsq_f32_e32 v210, v210
	s_add_u32 s24, s29, 2
	s_lshr_b32 s8, s24, 1
	s_lshl_b32 s8, s8, 12
	s_and_b32 s24, s24, 1
	s_lshl_b32 s24, s24, 8
	s_add_u32 s8, s8, s24
	v_mul_f32_e32 v210, v213, v210
	v_add_u32_e32 v212, s8, v23
	v_pk_mul_f32 v[88:89], v[88:89], v[210:211] op_sel_hi:[1,0]
	v_pk_mul_f32 v[90:91], v[90:91], v[210:211] op_sel_hi:[1,0]
	v_pk_mul_f32 v[88:89], v[88:89], v[40:41]
	v_pk_mul_f32 v[90:91], v[90:91], v[42:43]
	v_cvt_pk_f16_f32 v88, v88, v89
	v_cvt_pk_f16_f32 v89, v90, v91
	global_store_dwordx2 v212, v[88:89], s[22:23] offset:0
	v_pk_mul_f32 v[92:93], v[92:93], v[210:211] op_sel_hi:[1,0]
	v_pk_mul_f32 v[94:95], v[94:95], v[210:211] op_sel_hi:[1,0]
	v_pk_mul_f32 v[92:93], v[92:93], v[44:45]
	v_pk_mul_f32 v[94:95], v[94:95], v[46:47]
	v_cvt_pk_f16_f32 v92, v92, v93
	v_cvt_pk_f16_f32 v93, v94, v95
	global_store_dwordx2 v212, v[92:93], s[22:23] offset:1024
	v_pk_mul_f32 v[96:97], v[96:97], v[210:211] op_sel_hi:[1,0]
	v_pk_mul_f32 v[98:99], v[98:99], v[210:211] op_sel_hi:[1,0]
	v_pk_mul_f32 v[96:97], v[96:97], v[48:49]
	v_pk_mul_f32 v[98:99], v[98:99], v[50:51]
	v_cvt_pk_f16_f32 v96, v96, v97
	v_cvt_pk_f16_f32 v97, v98, v99
	global_store_dwordx2 v212, v[96:97], s[22:23] offset:2048
	v_pk_mul_f32 v[100:101], v[100:101], v[210:211] op_sel_hi:[1,0]
	v_pk_mul_f32 v[102:103], v[102:103], v[210:211] op_sel_hi:[1,0]
	v_pk_mul_f32 v[100:101], v[100:101], v[52:53]
	v_pk_mul_f32 v[102:103], v[102:103], v[54:55]
	v_cvt_pk_f16_f32 v100, v100, v101
	v_cvt_pk_f16_f32 v101, v102, v103
	global_store_dwordx2 v212, v[100:101], s[22:23] offset:3072
	v_pk_add_f32 v[104:105], v[104:105], v[24:25]
	v_pk_add_f32 v[106:107], v[106:107], v[26:27]
	v_pk_add_f32 v[108:109], v[108:109], v[28:29]
	v_pk_add_f32 v[110:111], v[110:111], v[30:31]
	v_pk_add_f32 v[112:113], v[112:113], v[32:33]
	v_pk_add_f32 v[114:115], v[114:115], v[34:35]
	v_pk_add_f32 v[116:117], v[116:117], v[36:37]
	v_pk_add_f32 v[118:119], v[118:119], v[38:39]
	v_pk_mul_f32 v[208:209], v[104:105], v[104:105]
	v_pk_fma_f32 v[208:209], v[106:107], v[106:107], v[208:209]
	v_pk_fma_f32 v[208:209], v[108:109], v[108:109], v[208:209]
	v_pk_fma_f32 v[208:209], v[110:111], v[110:111], v[208:209]
	v_pk_fma_f32 v[208:209], v[112:113], v[112:113], v[208:209]
	v_pk_fma_f32 v[208:209], v[114:115], v[114:115], v[208:209]
	v_pk_fma_f32 v[208:209], v[116:117], v[116:117], v[208:209]
	v_pk_fma_f32 v[208:209], v[118:119], v[118:119], v[208:209]
	v_add_f32_e32 v208, v208, v209
	v_mov_b32_e32 v209, v208
	s_nop 1
	v_permlane16_swap_b32_e32 v208, v209
	v_add_f32_e32 v208, v208, v209
	v_mov_b32_e32 v209, v208
	s_nop 1
	v_permlane32_swap_b32_e32 v208, v209
	v_add_f32_e32 v208, v208, v209
	v_mov_b32_e32 v210, 0x358637bd
	v_fmac_f32_e32 v210, 0x3c800000, v208
	v_rsq_f32_e32 v210, v210
	s_add_u32 s24, s29, 3
	s_lshr_b32 s8, s24, 1
	s_lshl_b32 s8, s8, 12
	s_and_b32 s24, s24, 1
	s_lshl_b32 s24, s24, 8
	s_add_u32 s8, s8, s24
	v_mul_f32_e32 v210, v213, v210
	v_add_u32_e32 v212, s8, v23
	v_pk_mul_f32 v[104:105], v[104:105], v[210:211] op_sel_hi:[1,0]
	v_pk_mul_f32 v[106:107], v[106:107], v[210:211] op_sel_hi:[1,0]
	v_pk_mul_f32 v[104:105], v[104:105], v[40:41]
	v_pk_mul_f32 v[106:107], v[106:107], v[42:43]
	v_cvt_pk_f16_f32 v104, v104, v105
	v_cvt_pk_f16_f32 v105, v106, v107
	global_store_dwordx2 v212, v[104:105], s[22:23] offset:0
	v_pk_mul_f32 v[108:109], v[108:109], v[210:211] op_sel_hi:[1,0]
	v_pk_mul_f32 v[110:111], v[110:111], v[210:211] op_sel_hi:[1,0]
	v_pk_mul_f32 v[108:109], v[108:109], v[44:45]
	v_pk_mul_f32 v[110:111], v[110:111], v[46:47]
	v_cvt_pk_f16_f32 v108, v108, v109
	v_cvt_pk_f16_f32 v109, v110, v111
	global_store_dwordx2 v212, v[108:109], s[22:23] offset:1024
	v_pk_mul_f32 v[112:113], v[112:113], v[210:211] op_sel_hi:[1,0]
	v_pk_mul_f32 v[114:115], v[114:115], v[210:211] op_sel_hi:[1,0]
	v_pk_mul_f32 v[112:113], v[112:113], v[48:49]
	v_pk_mul_f32 v[114:115], v[114:115], v[50:51]
	v_cvt_pk_f16_f32 v112, v112, v113
	v_cvt_pk_f16_f32 v113, v114, v115
	global_store_dwordx2 v212, v[112:113], s[22:23] offset:2048
	v_pk_mul_f32 v[116:117], v[116:117], v[210:211] op_sel_hi:[1,0]
	v_pk_mul_f32 v[118:119], v[118:119], v[210:211] op_sel_hi:[1,0]
	v_pk_mul_f32 v[116:117], v[116:117], v[52:53]
	v_pk_mul_f32 v[118:119], v[118:119], v[54:55]
	v_cvt_pk_f16_f32 v116, v116, v117
	v_cvt_pk_f16_f32 v117, v118, v119
	global_store_dwordx2 v212, v[116:117], s[22:23] offset:3072
	v_pk_add_f32 v[120:121], v[120:121], v[24:25]
	v_pk_add_f32 v[122:123], v[122:123], v[26:27]
	v_pk_add_f32 v[124:125], v[124:125], v[28:29]
	v_pk_add_f32 v[126:127], v[126:127], v[30:31]
	v_pk_add_f32 v[128:129], v[128:129], v[32:33]
	v_pk_add_f32 v[130:131], v[130:131], v[34:35]
	v_pk_add_f32 v[132:133], v[132:133], v[36:37]
	v_pk_add_f32 v[134:135], v[134:135], v[38:39]
	v_pk_mul_f32 v[208:209], v[120:121], v[120:121]
	v_pk_fma_f32 v[208:209], v[122:123], v[122:123], v[208:209]
	v_pk_fma_f32 v[208:209], v[124:125], v[124:125], v[208:209]
	v_pk_fma_f32 v[208:209], v[126:127], v[126:127], v[208:209]
	v_pk_fma_f32 v[208:209], v[128:129], v[128:129], v[208:209]
	v_pk_fma_f32 v[208:209], v[130:131], v[130:131], v[208:209]
	v_pk_fma_f32 v[208:209], v[132:133], v[132:133], v[208:209]
	v_pk_fma_f32 v[208:209], v[134:135], v[134:135], v[208:209]
	v_add_f32_e32 v208, v208, v209
	v_mov_b32_e32 v209, v208
	s_nop 1
	v_permlane16_swap_b32_e32 v208, v209
	v_add_f32_e32 v208, v208, v209
	v_mov_b32_e32 v209, v208
	s_nop 1
	v_permlane32_swap_b32_e32 v208, v209
	v_add_f32_e32 v208, v208, v209
	v_mov_b32_e32 v210, 0x358637bd
	v_fmac_f32_e32 v210, 0x3c800000, v208
	v_rsq_f32_e32 v210, v210
	s_add_u32 s24, s29, 4
	s_lshr_b32 s8, s24, 1
	s_lshl_b32 s8, s8, 12
	s_and_b32 s24, s24, 1
	s_lshl_b32 s24, s24, 8
	s_add_u32 s8, s8, s24
	v_mul_f32_e32 v210, v213, v210
	v_add_u32_e32 v212, s8, v23
	v_pk_mul_f32 v[120:121], v[120:121], v[210:211] op_sel_hi:[1,0]
	v_pk_mul_f32 v[122:123], v[122:123], v[210:211] op_sel_hi:[1,0]
	v_pk_mul_f32 v[120:121], v[120:121], v[40:41]
	v_pk_mul_f32 v[122:123], v[122:123], v[42:43]
	v_cvt_pk_f16_f32 v120, v120, v121
	v_cvt_pk_f16_f32 v121, v122, v123
	global_store_dwordx2 v212, v[120:121], s[22:23] offset:0
	v_pk_mul_f32 v[124:125], v[124:125], v[210:211] op_sel_hi:[1,0]
	v_pk_mul_f32 v[126:127], v[126:127], v[210:211] op_sel_hi:[1,0]
	v_pk_mul_f32 v[124:125], v[124:125], v[44:45]
	v_pk_mul_f32 v[126:127], v[126:127], v[46:47]
	v_cvt_pk_f16_f32 v124, v124, v125
	v_cvt_pk_f16_f32 v125, v126, v127
	global_store_dwordx2 v212, v[124:125], s[22:23] offset:1024
	v_pk_mul_f32 v[128:129], v[128:129], v[210:211] op_sel_hi:[1,0]
	v_pk_mul_f32 v[130:131], v[130:131], v[210:211] op_sel_hi:[1,0]
	v_pk_mul_f32 v[128:129], v[128:129], v[48:49]
	v_pk_mul_f32 v[130:131], v[130:131], v[50:51]
	v_cvt_pk_f16_f32 v128, v128, v129
	v_cvt_pk_f16_f32 v129, v130, v131
	global_store_dwordx2 v212, v[128:129], s[22:23] offset:2048
	v_pk_mul_f32 v[132:133], v[132:133], v[210:211] op_sel_hi:[1,0]
	v_pk_mul_f32 v[134:135], v[134:135], v[210:211] op_sel_hi:[1,0]
	v_pk_mul_f32 v[132:133], v[132:133], v[52:53]
	v_pk_mul_f32 v[134:135], v[134:135], v[54:55]
	v_cvt_pk_f16_f32 v132, v132, v133
	v_cvt_pk_f16_f32 v133, v134, v135
	global_store_dwordx2 v212, v[132:133], s[22:23] offset:3072
	s_branch .Lpf_done
.Lpf_vKB:
	s_lshl_b32 s25, s25, 6
	s_add_u32 s25, s25, 32
	s_add_u32 s29, s10, s25
	s_lshr_b32 s29, s29, 4
	v_add_u32_e32 v5, s25, v3
	v_lshlrev_b32_e32 v5, 7, v5
	v_add_u32_e32 v15, v5, v6
	v_add_u32_e32 v16, v5, v7
	v_add_u32_e32 v5, 0x9000, v9
	v_add_u32_e32 v17, v5, v6
	v_add_u32_e32 v18, v5, v7
	v_add_u32_e32 v19, 0x1a000, v15
	v_add_u32_e32 v20, 0x1a000, v16
	v_add_u32_e32 v21, 0x1a000, v17
	v_add_u32_e32 v22, 0x1a000, v18
	v_lshlrev_b32_e32 v5, 4, v4
	global_load_dwordx4 v[24:27], v5, s[14:15] offset:0
	global_load_dwordx4 v[28:31], v5, s[14:15] offset:64
	global_load_dwordx4 v[32:35], v5, s[14:15] offset:128
	global_load_dwordx4 v[36:39], v5, s[14:15] offset:192
	global_load_dwordx4 v[40:43], v5, s[16:17] offset:0
	global_load_dwordx4 v[44:47], v5, s[16:17] offset:64
	global_load_dwordx4 v[48:51], v5, s[16:17] offset:128
	global_load_dwordx4 v[52:55], v5, s[16:17] offset:192
	s_add_u32 m0, s28, 0x0
	s_nop 0
	global_load_lds_dwordx4 v10, s[4:5]
	s_add_u32 m0, s28, 0x2000
	s_nop 0
	global_load_lds_dwordx4 v11, s[4:5]
	s_add_u32 m0, s28, 0x4000
	s_nop 0
	global_load_lds_dwordx4 v12, s[4:5]
	s_add_u32 m0, s28, 0x6000
	s_nop 0
	global_load_lds_dwordx4 v13, s[4:5]
	s_add_u32 s4, s4, s20
	s_addc_u32 s5, s5, 0
	s_add_u32 m0, s28, 0x9000
	s_nop 0
	global_load_lds_dwordx4 v10, s[6:7]
	s_add_u32 m0, s28, 0xb000
	s_nop 0
	global_load_lds_dwordx4 v11, s[6:7]
	s_add_u32 s6, s6, s20
	s_addc_u32 s7, s7, 0
	s_add_u32 m0, s28, 0xd000
	s_nop 0
	global_load_lds_dwordx4 v10, s[4:5]
	s_add_u32 m0, s28, 0xf000
	s_nop 0
	global_load_lds_dwordx4 v11, s[4:5]
	s_add_u32 m0, s28, 0x11000
	s_nop 0
	global_load_lds_dwordx4 v12, s[4:5]
	s_add_u32 m0, s28, 0x13000
	s_nop 0
	global_load_lds_dwordx4 v13, s[4:5]
	s_add_u32 s4, s4, s20
	s_addc_u32 s5, s5, 0
	s_add_u32 m0, s28, 0x16000
	s_nop 0
	global_load_lds_dwordx4 v10, s[6:7]
	s_add_u32 m0, s28, 0x18000
	s_nop 0
	global_load_lds_dwordx4 v11, s[6:7]
	s_add_u32 s6, s6, s20
	s_addc_u32 s7, s7, 0
	s_waitcnt vmcnt(6) lgkmcnt(0)
	s_barrier
	s_waitcnt lgkmcnt(7)
	ds_read_b128 v[136:139], v15
	ds_read_b128 v[156:159], v17
	ds_read_b128 v[160:163], v17 offset:2048
	ds_read_b128 v[164:167], v17 offset:4096
	ds_read_b128 v[168:171], v17 offset:6144
	ds_read_b128 v[140:143], v15 offset:2048
	ds_read_b128 v[144:147], v15 offset:4096
	ds_read_b128 v[148:151], v15 offset:6144
	s_waitcnt lgkmcnt(7)
	ds_read_b128 v[172:175], v16
	ds_read_b128 v[192:195], v18
	ds_read_b128 v[196:199], v18 offset:2048
	ds_read_b128 v[200:203], v18 offset:4096
	ds_read_b128 v[204:207], v18 offset:6144
	ds_read_b128 v[176:179], v16 offset:2048
	ds_read_b128 v[180:183], v16 offset:4096
	ds_read_b128 v[184:187], v16 offset:6144
	s_waitcnt lgkmcnt(14)
	v_mfma_f32_16x16x32_f16 v[56:59], v[156:159], v[136:139], 0
	s_add_u32 m0, s28, 0x1a000
	s_nop 0
	global_load_lds_dwordx4 v10, s[4:5]
	s_waitcnt lgkmcnt(13)
	v_mfma_f32_16x16x32_f16 v[60:63], v[160:163], v[136:139], 0
	s_waitcnt lgkmcnt(12)
	v_mfma_f32_16x16x32_f16 v[64:67], v[164:167], v[136:139], 0
	s_add_u32 m0, s28, 0x1c000
	s_nop 0
	global_load_lds_dwordx4 v11, s[4:5]
	s_waitcnt lgkmcnt(11)
	v_mfma_f32_16x16x32_f16 v[68:71], v[168:171], v[136:139], 0
	s_waitcnt lgkmcnt(10)
	v_mfma_f32_16x16x32_f16 v[72:75], v[156:159], v[140:143], 0
	v_mfma_f32_16x16x32_f16 v[76:79], v[160:163], v[140:143], 0
	s_add_u32 m0, s28, 0x1e000
	s_nop 0
	global_load_lds_dwordx4 v12, s[4:5]
	v_mfma_f32_16x16x32_f16 v[80:83], v[164:167], v[140:143], 0
	v_mfma_f32_16x16x32_f16 v[84:87], v[168:171], v[140:143], 0
	s_waitcnt lgkmcnt(9)
	v_mfma_f32_16x16x32_f16 v[88:91], v[156:159], v[144:147], 0
	s_add_u32 m0, s28, 0x20000
	s_nop 0
	global_load_lds_dwordx4 v13, s[4:5]
	s_add_u32 s4, s4, s20
	s_addc_u32 s5, s5, 0
	v_mfma_f32_16x16x32_f16 v[92:95], v[160:163], v[144:147], 0
	v_mfma_f32_16x16x32_f16 v[96:99], v[164:167], v[144:147], 0
	s_add_u32 m0, s28, 0x23000
	s_nop 0
	global_load_lds_dwordx4 v10, s[6:7]
	v_mfma_f32_16x16x32_f16 v[100:103], v[168:171], v[144:147], 0
	s_waitcnt lgkmcnt(8)
	v_mfma_f32_16x16x32_f16 v[104:107], v[156:159], v[148:151], 0
	v_mfma_f32_16x16x32_f16 v[108:111], v[160:163], v[148:151], 0
	s_add_u32 m0, s28, 0x25000
	s_nop 0
	global_load_lds_dwordx4 v11, s[6:7]
	s_add_u32 s6, s6, s20
	s_addc_u32 s7, s7, 0
	v_mfma_f32_16x16x32_f16 v[112:115], v[164:167], v[148:151], 0
	v_mfma_f32_16x16x32_f16 v[116:119], v[168:171], v[148:151], 0
	s_waitcnt vmcnt(6) lgkmcnt(0)
	s_barrier
	s_waitcnt lgkmcnt(7)
	ds_read_b128 v[136:139], v15 offset:53248
	ds_read_b128 v[156:159], v17 offset:53248
	ds_read_b128 v[160:163], v17 offset:55296
	ds_read_b128 v[164:167], v17 offset:57344
	ds_read_b128 v[168:171], v17 offset:59392
	ds_read_b128 v[140:143], v15 offset:55296
	ds_read_b128 v[144:147], v15 offset:57344
	ds_read_b128 v[148:151], v15 offset:59392
	s_waitcnt lgkmcnt(14)
	v_mfma_f32_16x16x32_f16 v[56:59], v[192:195], v[172:175], v[56:59]
	s_add_u32 m0, s28, 0x0
	s_nop 0
	global_load_lds_dwordx4 v10, s[4:5]
	s_waitcnt lgkmcnt(13)
	v_mfma_f32_16x16x32_f16 v[60:63], v[196:199], v[172:175], v[60:63]
	s_waitcnt lgkmcnt(12)
	v_mfma_f32_16x16x32_f16 v[64:67], v[200:203], v[172:175], v[64:67]
	s_waitcnt lgkmcnt(11)
	v_mfma_f32_16x16x32_f16 v[68:71], v[204:207], v[172:175], v[68:71]
	s_waitcnt lgkmcnt(10)
	v_mfma_f32_16x16x32_f16 v[72:75], v[192:195], v[176:179], v[72:75]
	v_mfma_f32_16x16x32_f16 v[76:79], v[196:199], v[176:179], v[76:79]
	s_add_u32 m0, s28, 0x2000
	s_nop 0
	global_load_lds_dwordx4 v11, s[4:5]
	v_mfma_f32_16x16x32_f16 v[80:83], v[200:203], v[176:179], v[80:83]
	v_mfma_f32_16x16x32_f16 v[84:87], v[204:207], v[176:179], v[84:87]
	s_waitcnt lgkmcnt(9)
	v_mfma_f32_16x16x32_f16 v[88:91], v[192:195], v[180:183], v[88:91]
	v_mfma_f32_16x16x32_f16 v[92:95], v[196:199], v[180:183], v[92:95]
	v_mfma_f32_16x16x32_f16 v[96:99], v[200:203], v[180:183], v[96:99]
	s_add_u32 m0, s28, 0x4000
	s_nop 0
	global_load_lds_dwordx4 v12, s[4:5]
	v_mfma_f32_16x16x32_f16 v[100:103], v[204:207], v[180:183], v[100:103]
	s_waitcnt lgkmcnt(8)
	v_mfma_f32_16x16x32_f16 v[104:107], v[192:195], v[184:187], v[104:107]
	v_mfma_f32_16x16x32_f16 v[108:111], v[196:199], v[184:187], v[108:111]
	v_mfma_f32_16x16x32_f16 v[112:115], v[200:203], v[184:187], v[112:115]
	v_mfma_f32_16x16x32_f16 v[116:119], v[204:207], v[184:187], v[116:119]
	s_waitcnt lgkmcnt(7)
	ds_read_b128 v[172:175], v16 offset:53248
	ds_read_b128 v[192:195], v18 offset:53248
	ds_read_b128 v[196:199], v18 offset:55296
	ds_read_b128 v[200:203], v18 offset:57344
	ds_read_b128 v[204:207], v18 offset:59392
	ds_read_b128 v[176:179], v16 offset:55296
	ds_read_b128 v[180:183], v16 offset:57344
	ds_read_b128 v[184:187], v16 offset:59392
	s_waitcnt lgkmcnt(14)
	v_mfma_f32_16x16x32_f16 v[56:59], v[156:159], v[136:139], v[56:59]
	s_add_u32 m0, s28, 0x6000
	s_nop 0
	global_load_lds_dwordx4 v13, s[4:5]
	s_add_u32 s4, s4, s20
	s_addc_u32 s5, s5, 0
	s_waitcnt lgkmcnt(13)
	v_mfma_f32_16x16x32_f16 v[60:63], v[160:163], v[136:139], v[60:63]
	s_waitcnt lgkmcnt(12)
	v_mfma_f32_16x16x32_f16 v[64:67], v[164:167], v[136:139], v[64:67]
	s_waitcnt lgkmcnt(11)
	v_mfma_f32_16x16x32_f16 v[68:71], v[168:171], v[136:139], v[68:71]
	s_waitcnt lgkmcnt(10)
	v_mfma_f32_16x16x32_f16 v[72:75], v[156:159], v[140:143], v[72:75]
	v_mfma_f32_16x16x32_f16 v[76:79], v[160:163], v[140:143], v[76:79]
	s_add_u32 m0, s28, 0x9000
	s_nop 0
	global_load_lds_dwordx4 v10, s[6:7]
	v_mfma_f32_16x16x32_f16 v[80:83], v[164:167], v[140:143], v[80:83]
	v_mfma_f32_16x16x32_f16 v[84:87], v[168:171], v[140:143], v[84:87]
	s_waitcnt lgkmcnt(9)
	v_mfma_f32_16x16x32_f16 v[88:91], v[156:159], v[144:147], v[88:91]
	v_mfma_f32_16x16x32_f16 v[92:95], v[160:163], v[144:147], v[92:95]
	v_mfma_f32_16x16x32_f16 v[96:99], v[164:167], v[144:147], v[96:99]
	s_add_u32 m0, s28, 0xb000
	s_nop 0
	global_load_lds_dwordx4 v11, s[6:7]
	s_add_u32 s6, s6, s20
	s_addc_u32 s7, s7, 0
	v_mfma_f32_16x16x32_f16 v[100:103], v[168:171], v[144:147], v[100:103]
	s_waitcnt lgkmcnt(8)
	v_mfma_f32_16x16x32_f16 v[104:107], v[156:159], v[148:151], v[104:107]
	v_mfma_f32_16x16x32_f16 v[108:111], v[160:163], v[148:151], v[108:111]
	v_mfma_f32_16x16x32_f16 v[112:115], v[164:167], v[148:151], v[112:115]
	v_mfma_f32_16x16x32_f16 v[116:119], v[168:171], v[148:151], v[116:119]
	s_waitcnt vmcnt(6) lgkmcnt(0)
	s_barrier
	s_waitcnt lgkmcnt(7)
	ds_read_b128 v[136:139], v19
	ds_read_b128 v[156:159], v21
	ds_read_b128 v[160:163], v21 offset:2048
	ds_read_b128 v[164:167], v21 offset:4096
	ds_read_b128 v[168:171], v21 offset:6144
	ds_read_b128 v[140:143], v19 offset:2048
	ds_read_b128 v[144:147], v19 offset:4096
	ds_read_b128 v[148:151], v19 offset:6144
	s_waitcnt lgkmcnt(14)
	v_mfma_f32_16x16x32_f16 v[56:59], v[192:195], v[172:175], v[56:59]
	s_add_u32 m0, s28, 0xd000
	s_nop 0
	global_load_lds_dwordx4 v10, s[4:5]
	s_waitcnt lgkmcnt(13)
	v_mfma_f32_16x16x32_f16 v[60:63], v[196:199], v[172:175], v[60:63]
	s_waitcnt lgkmcnt(12)
	v_mfma_f32_16x16x32_f16 v[64:67], v[200:203], v[172:175], v[64:67]
	s_waitcnt lgkmcnt(11)
	v_mfma_f32_16x16x32_f16 v[68:71], v[204:207], v[172:175], v[68:71]
	s_waitcnt lgkmcnt(10)
	v_mfma_f32_16x16x32_f16 v[72:75], v[192:195], v[176:179], v[72:75]
	v_mfma_f32_16x16x32_f16 v[76:79], v[196:199], v[176:179], v[76:79]
	s_add_u32 m0, s28, 0xf000
	s_nop 0
	global_load_lds_dwordx4 v11, s[4:5]
	v_mfma_f32_16x16x32_f16 v[80:83], v[200:203], v[176:179], v[80:83]
	v_mfma_f32_16x16x32_f16 v[84:87], v[204:207], v[176:179], v[84:87]
	s_waitcnt lgkmcnt(9)
	v_mfma_f32_16x16x32_f16 v[88:91], v[192:195], v[180:183], v[88:91]
	v_mfma_f32_16x16x32_f16 v[92:95], v[196:199], v[180:183], v[92:95]
	v_mfma_f32_16x16x32_f16 v[96:99], v[200:203], v[180:183], v[96:99]
	s_add_u32 m0, s28, 0x11000
	s_nop 0
	global_load_lds_dwordx4 v12, s[4:5]
	v_mfma_f32_16x16x32_f16 v[100:103], v[204:207], v[180:183], v[100:103]
	s_waitcnt lgkmcnt(8)
	v_mfma_f32_16x16x32_f16 v[104:107], v[192:195], v[184:187], v[104:107]
	v_mfma_f32_16x16x32_f16 v[108:111], v[196:199], v[184:187], v[108:111]
	v_mfma_f32_16x16x32_f16 v[112:115], v[200:203], v[184:187], v[112:115]
	v_mfma_f32_16x16x32_f16 v[116:119], v[204:207], v[184:187], v[116:119]
	s_waitcnt lgkmcnt(7)
	ds_read_b128 v[172:175], v20
	ds_read_b128 v[192:195], v22
	ds_read_b128 v[196:199], v22 offset:2048
	ds_read_b128 v[200:203], v22 offset:4096
	ds_read_b128 v[204:207], v22 offset:6144
	ds_read_b128 v[176:179], v20 offset:2048
	ds_read_b128 v[180:183], v20 offset:4096
	ds_read_b128 v[184:187], v20 offset:6144
	s_waitcnt lgkmcnt(14)
	v_mfma_f32_16x16x32_f16 v[56:59], v[156:159], v[136:139], v[56:59]
	s_add_u32 m0, s28, 0x13000
	s_nop 0
	global_load_lds_dwordx4 v13, s[4:5]
	s_add_u32 s4, s4, s20
	s_addc_u32 s5, s5, 0
	s_waitcnt lgkmcnt(13)
	v_mfma_f32_16x16x32_f16 v[60:63], v[160:163], v[136:139], v[60:63]
	s_waitcnt lgkmcnt(12)
	v_mfma_f32_16x16x32_f16 v[64:67], v[164:167], v[136:139], v[64:67]
	s_waitcnt lgkmcnt(11)
	v_mfma_f32_16x16x32_f16 v[68:71], v[168:171], v[136:139], v[68:71]
	s_waitcnt lgkmcnt(10)
	v_mfma_f32_16x16x32_f16 v[72:75], v[156:159], v[140:143], v[72:75]
	v_mfma_f32_16x16x32_f16 v[76:79], v[160:163], v[140:143], v[76:79]
	s_add_u32 m0, s28, 0x16000
	s_nop 0
	global_load_lds_dwordx4 v10, s[6:7]
	v_mfma_f32_16x16x32_f16 v[80:83], v[164:167], v[140:143], v[80:83]
	v_mfma_f32_16x16x32_f16 v[84:87], v[168:171], v[140:143], v[84:87]
	s_waitcnt lgkmcnt(9)
	v_mfma_f32_16x16x32_f16 v[88:91], v[156:159], v[144:147], v[88:91]
	v_mfma_f32_16x16x32_f16 v[92:95], v[160:163], v[144:147], v[92:95]
	v_mfma_f32_16x16x32_f16 v[96:99], v[164:167], v[144:147], v[96:99]
	s_add_u32 m0, s28, 0x18000
	s_nop 0
	global_load_lds_dwordx4 v11, s[6:7]
	s_add_u32 s6, s6, s20
	s_addc_u32 s7, s7, 0
	v_mfma_f32_16x16x32_f16 v[100:103], v[168:171], v[144:147], v[100:103]
	s_waitcnt lgkmcnt(8)
	v_mfma_f32_16x16x32_f16 v[104:107], v[156:159], v[148:151], v[104:107]
	v_mfma_f32_16x16x32_f16 v[108:111], v[160:163], v[148:151], v[108:111]
	v_mfma_f32_16x16x32_f16 v[112:115], v[164:167], v[148:151], v[112:115]
	v_mfma_f32_16x16x32_f16 v[116:119], v[168:171], v[148:151], v[116:119]
	s_waitcnt vmcnt(6) lgkmcnt(0)
	s_barrier
	s_waitcnt lgkmcnt(7)
	ds_read_b128 v[136:139], v15
	ds_read_b128 v[156:159], v17
	ds_read_b128 v[160:163], v17 offset:2048
	ds_read_b128 v[164:167], v17 offset:4096
	ds_read_b128 v[168:171], v17 offset:6144
	ds_read_b128 v[140:143], v15 offset:2048
	ds_read_b128 v[144:147], v15 offset:4096
	ds_read_b128 v[148:151], v15 offset:6144
	s_waitcnt lgkmcnt(14)
	v_mfma_f32_16x16x32_f16 v[56:59], v[192:195], v[172:175], v[56:59]
	s_add_u32 m0, s28, 0x1a000
	s_nop 0
	global_load_lds_dwordx4 v10, s[4:5]
	s_waitcnt lgkmcnt(13)
	v_mfma_f32_16x16x32_f16 v[60:63], v[196:199], v[172:175], v[60:63]
	s_waitcnt lgkmcnt(12)
	v_mfma_f32_16x16x32_f16 v[64:67], v[200:203], v[172:175], v[64:67]
	s_waitcnt lgkmcnt(11)
	v_mfma_f32_16x16x32_f16 v[68:71], v[204:207], v[172:175], v[68:71]
	s_waitcnt lgkmcnt(10)
	v_mfma_f32_16x16x32_f16 v[72:75], v[192:195], v[176:179], v[72:75]
	v_mfma_f32_16x16x32_f16 v[76:79], v[196:199], v[176:179], v[76:79]
	s_add_u32 m0, s28, 0x1c000
	s_nop 0
	global_load_lds_dwordx4 v11, s[4:5]
	v_mfma_f32_16x16x32_f16 v[80:83], v[200:203], v[176:179], v[80:83]
	v_mfma_f32_16x16x32_f16 v[84:87], v[204:207], v[176:179], v[84:87]
	s_waitcnt lgkmcnt(9)
	v_mfma_f32_16x16x32_f16 v[88:91], v[192:195], v[180:183], v[88:91]
	v_mfma_f32_16x16x32_f16 v[92:95], v[196:199], v[180:183], v[92:95]
	v_mfma_f32_16x16x32_f16 v[96:99], v[200:203], v[180:183], v[96:99]
	s_add_u32 m0, s28, 0x1e000
	s_nop 0
	global_load_lds_dwordx4 v12, s[4:5]
	v_mfma_f32_16x16x32_f16 v[100:103], v[204:207], v[180:183], v[100:103]
	s_waitcnt lgkmcnt(8)
	v_mfma_f32_16x16x32_f16 v[104:107], v[192:195], v[184:187], v[104:107]
	v_mfma_f32_16x16x32_f16 v[108:111], v[196:199], v[184:187], v[108:111]
	v_mfma_f32_16x16x32_f16 v[112:115], v[200:203], v[184:187], v[112:115]
	v_mfma_f32_16x16x32_f16 v[116:119], v[204:207], v[184:187], v[116:119]
	s_waitcnt lgkmcnt(7)
	ds_read_b128 v[172:175], v16
	ds_read_b128 v[192:195], v18
	ds_read_b128 v[196:199], v18 offset:2048
	ds_read_b128 v[200:203], v18 offset:4096
	ds_read_b128 v[204:207], v18 offset:6144
	ds_read_b128 v[176:179], v16 offset:2048
	ds_read_b128 v[180:183], v16 offset:4096
	ds_read_b128 v[184:187], v16 offset:6144
	s_waitcnt lgkmcnt(14)
	v_mfma_f32_16x16x32_f16 v[56:59], v[156:159], v[136:139], v[56:59]
	s_add_u32 m0, s28, 0x20000
	s_nop 0
	global_load_lds_dwordx4 v13, s[4:5]
	s_add_u32 s4, s4, s20
	s_addc_u32 s5, s5, 0
	s_waitcnt lgkmcnt(13)
	v_mfma_f32_16x16x32_f16 v[60:63], v[160:163], v[136:139], v[60:63]
	s_waitcnt lgkmcnt(12)
	v_mfma_f32_16x16x32_f16 v[64:67], v[164:167], v[136:139], v[64:67]
	s_waitcnt lgkmcnt(11)
	v_mfma_f32_16x16x32_f16 v[68:71], v[168:171], v[136:139], v[68:71]
	s_waitcnt lgkmcnt(10)
	v_mfma_f32_16x16x32_f16 v[72:75], v[156:159], v[140:143], v[72:75]
	v_mfma_f32_16x16x32_f16 v[76:79], v[160:163], v[140:143], v[76:79]
	s_add_u32 m0, s28, 0x23000
	s_nop 0
	global_load_lds_dwordx4 v10, s[6:7]
	v_mfma_f32_16x16x32_f16 v[80:83], v[164:167], v[140:143], v[80:83]
	v_mfma_f32_16x16x32_f16 v[84:87], v[168:171], v[140:143], v[84:87]
	s_waitcnt lgkmcnt(9)
	v_mfma_f32_16x16x32_f16 v[88:91], v[156:159], v[144:147], v[88:91]
	v_mfma_f32_16x16x32_f16 v[92:95], v[160:163], v[144:147], v[92:95]
	v_mfma_f32_16x16x32_f16 v[96:99], v[164:167], v[144:147], v[96:99]
	s_add_u32 m0, s28, 0x25000
	s_nop 0
	global_load_lds_dwordx4 v11, s[6:7]
	s_add_u32 s6, s6, s20
	s_addc_u32 s7, s7, 0
	v_mfma_f32_16x16x32_f16 v[100:103], v[168:171], v[144:147], v[100:103]
	s_waitcnt lgkmcnt(8)
	v_mfma_f32_16x16x32_f16 v[104:107], v[156:159], v[148:151], v[104:107]
	v_mfma_f32_16x16x32_f16 v[108:111], v[160:163], v[148:151], v[108:111]
	v_mfma_f32_16x16x32_f16 v[112:115], v[164:167], v[148:151], v[112:115]
	v_mfma_f32_16x16x32_f16 v[116:119], v[168:171], v[148:151], v[116:119]
	s_waitcnt vmcnt(6) lgkmcnt(0)
	s_barrier
	s_waitcnt lgkmcnt(7)
	ds_read_b128 v[136:139], v15 offset:53248
	ds_read_b128 v[156:159], v17 offset:53248
	ds_read_b128 v[160:163], v17 offset:55296
	ds_read_b128 v[164:167], v17 offset:57344
	ds_read_b128 v[168:171], v17 offset:59392
	ds_read_b128 v[140:143], v15 offset:55296
	ds_read_b128 v[144:147], v15 offset:57344
	ds_read_b128 v[148:151], v15 offset:59392
	s_waitcnt lgkmcnt(14)
	v_mfma_f32_16x16x32_f16 v[56:59], v[192:195], v[172:175], v[56:59]
	s_add_u32 m0, s28, 0x0
	s_nop 0
	global_load_lds_dwordx4 v10, s[4:5]
	s_waitcnt lgkmcnt(13)
	v_mfma_f32_16x16x32_f16 v[60:63], v[196:199], v[172:175], v[60:63]
	s_waitcnt lgkmcnt(12)
	v_mfma_f32_16x16x32_f16 v[64:67], v[200:203], v[172:175], v[64:67]
	s_waitcnt lgkmcnt(11)
	v_mfma_f32_16x16x32_f16 v[68:71], v[204:207], v[172:175], v[68:71]
	s_waitcnt lgkmcnt(10)
	v_mfma_f32_16x16x32_f16 v[72:75], v[192:195], v[176:179], v[72:75]
	v_mfma_f32_16x16x32_f16 v[76:79], v[196:199], v[176:179], v[76:79]
	s_add_u32 m0, s28, 0x2000
	s_nop 0
	global_load_lds_dwordx4 v11, s[4:5]
	v_mfma_f32_16x16x32_f16 v[80:83], v[200:203], v[176:179], v[80:83]
	v_mfma_f32_16x16x32_f16 v[84:87], v[204:207], v[176:179], v[84:87]
	s_waitcnt lgkmcnt(9)
	v_mfma_f32_16x16x32_f16 v[88:91], v[192:195], v[180:183], v[88:91]
	v_mfma_f32_16x16x32_f16 v[92:95], v[196:199], v[180:183], v[92:95]
	v_mfma_f32_16x16x32_f16 v[96:99], v[200:203], v[180:183], v[96:99]
	s_add_u32 m0, s28, 0x4000
	s_nop 0
	global_load_lds_dwordx4 v12, s[4:5]
	v_mfma_f32_16x16x32_f16 v[100:103], v[204:207], v[180:183], v[100:103]
	s_waitcnt lgkmcnt(8)
	v_mfma_f32_16x16x32_f16 v[104:107], v[192:195], v[184:187], v[104:107]
	v_mfma_f32_16x16x32_f16 v[108:111], v[196:199], v[184:187], v[108:111]
	v_mfma_f32_16x16x32_f16 v[112:115], v[200:203], v[184:187], v[112:115]
	v_mfma_f32_16x16x32_f16 v[116:119], v[204:207], v[184:187], v[116:119]
	s_waitcnt lgkmcnt(7)
	ds_read_b128 v[172:175], v16 offset:53248
	ds_read_b128 v[192:195], v18 offset:53248
	ds_read_b128 v[196:199], v18 offset:55296
	ds_read_b128 v[200:203], v18 offset:57344
	ds_read_b128 v[204:207], v18 offset:59392
	ds_read_b128 v[176:179], v16 offset:55296
	ds_read_b128 v[180:183], v16 offset:57344
	ds_read_b128 v[184:187], v16 offset:59392
	s_waitcnt lgkmcnt(14)
	v_mfma_f32_16x16x32_f16 v[56:59], v[156:159], v[136:139], v[56:59]
	s_add_u32 m0, s28, 0x6000
	s_nop 0
	global_load_lds_dwordx4 v13, s[4:5]
	s_add_u32 s4, s4, s20
	s_addc_u32 s5, s5, 0
	s_waitcnt lgkmcnt(13)
	v_mfma_f32_16x16x32_f16 v[60:63], v[160:163], v[136:139], v[60:63]
	s_waitcnt lgkmcnt(12)
	v_mfma_f32_16x16x32_f16 v[64:67], v[164:167], v[136:139], v[64:67]
	s_waitcnt lgkmcnt(11)
	v_mfma_f32_16x16x32_f16 v[68:71], v[168:171], v[136:139], v[68:71]
	s_waitcnt lgkmcnt(10)
	v_mfma_f32_16x16x32_f16 v[72:75], v[156:159], v[140:143], v[72:75]
	v_mfma_f32_16x16x32_f16 v[76:79], v[160:163], v[140:143], v[76:79]
	s_add_u32 m0, s28, 0x9000
	s_nop 0
	global_load_lds_dwordx4 v10, s[6:7]
	v_mfma_f32_16x16x32_f16 v[80:83], v[164:167], v[140:143], v[80:83]
	v_mfma_f32_16x16x32_f16 v[84:87], v[168:171], v[140:143], v[84:87]
	s_waitcnt lgkmcnt(9)
	v_mfma_f32_16x16x32_f16 v[88:91], v[156:159], v[144:147], v[88:91]
	v_mfma_f32_16x16x32_f16 v[92:95], v[160:163], v[144:147], v[92:95]
	v_mfma_f32_16x16x32_f16 v[96:99], v[164:167], v[144:147], v[96:99]
	s_add_u32 m0, s28, 0xb000
	s_nop 0
	global_load_lds_dwordx4 v11, s[6:7]
	s_add_u32 s6, s6, s20
	s_addc_u32 s7, s7, 0
	v_mfma_f32_16x16x32_f16 v[100:103], v[168:171], v[144:147], v[100:103]
	s_waitcnt lgkmcnt(8)
	v_mfma_f32_16x16x32_f16 v[104:107], v[156:159], v[148:151], v[104:107]
	v_mfma_f32_16x16x32_f16 v[108:111], v[160:163], v[148:151], v[108:111]
	v_mfma_f32_16x16x32_f16 v[112:115], v[164:167], v[148:151], v[112:115]
	v_mfma_f32_16x16x32_f16 v[116:119], v[168:171], v[148:151], v[116:119]
	s_waitcnt vmcnt(6) lgkmcnt(0)
	s_barrier
	s_waitcnt lgkmcnt(7)
	ds_read_b128 v[136:139], v19
	ds_read_b128 v[156:159], v21
	ds_read_b128 v[160:163], v21 offset:2048
	ds_read_b128 v[164:167], v21 offset:4096
	ds_read_b128 v[168:171], v21 offset:6144
	ds_read_b128 v[140:143], v19 offset:2048
	ds_read_b128 v[144:147], v19 offset:4096
	ds_read_b128 v[148:151], v19 offset:6144
	s_waitcnt lgkmcnt(14)
	v_mfma_f32_16x16x32_f16 v[56:59], v[192:195], v[172:175], v[56:59]
	s_add_u32 m0, s28, 0xd000
	s_nop 0
	global_load_lds_dwordx4 v10, s[4:5]
	s_waitcnt lgkmcnt(13)
	v_mfma_f32_16x16x32_f16 v[60:63], v[196:199], v[172:175], v[60:63]
	s_waitcnt lgkmcnt(12)
	v_mfma_f32_16x16x32_f16 v[64:67], v[200:203], v[172:175], v[64:67]
	s_waitcnt lgkmcnt(11)
	v_mfma_f32_16x16x32_f16 v[68:71], v[204:207], v[172:175], v[68:71]
	s_waitcnt lgkmcnt(10)
	v_mfma_f32_16x16x32_f16 v[72:75], v[192:195], v[176:179], v[72:75]
	v_mfma_f32_16x16x32_f16 v[76:79], v[196:199], v[176:179], v[76:79]
	s_add_u32 m0, s28, 0xf000
	s_nop 0
	global_load_lds_dwordx4 v11, s[4:5]
	v_mfma_f32_16x16x32_f16 v[80:83], v[200:203], v[176:179], v[80:83]
	v_mfma_f32_16x16x32_f16 v[84:87], v[204:207], v[176:179], v[84:87]
	s_waitcnt lgkmcnt(9)
	v_mfma_f32_16x16x32_f16 v[88:91], v[192:195], v[180:183], v[88:91]
	v_mfma_f32_16x16x32_f16 v[92:95], v[196:199], v[180:183], v[92:95]
	v_mfma_f32_16x16x32_f16 v[96:99], v[200:203], v[180:183], v[96:99]
	s_add_u32 m0, s28, 0x11000
	s_nop 0
	global_load_lds_dwordx4 v12, s[4:5]
	v_mfma_f32_16x16x32_f16 v[100:103], v[204:207], v[180:183], v[100:103]
	s_waitcnt lgkmcnt(8)
	v_mfma_f32_16x16x32_f16 v[104:107], v[192:195], v[184:187], v[104:107]
	v_mfma_f32_16x16x32_f16 v[108:111], v[196:199], v[184:187], v[108:111]
	v_mfma_f32_16x16x32_f16 v[112:115], v[200:203], v[184:187], v[112:115]
	v_mfma_f32_16x16x32_f16 v[116:119], v[204:207], v[184:187], v[116:119]
	s_waitcnt lgkmcnt(7)
	ds_read_b128 v[172:175], v20
	ds_read_b128 v[192:195], v22
	ds_read_b128 v[196:199], v22 offset:2048
	ds_read_b128 v[200:203], v22 offset:4096
	ds_read_b128 v[204:207], v22 offset:6144
	ds_read_b128 v[176:179], v20 offset:2048
	ds_read_b128 v[180:183], v20 offset:4096
	ds_read_b128 v[184:187], v20 offset:6144
	s_waitcnt lgkmcnt(14)
	v_mfma_f32_16x16x32_f16 v[56:59], v[156:159], v[136:139], v[56:59]
	s_add_u32 m0, s28, 0x13000
	s_nop 0
	global_load_lds_dwordx4 v13, s[4:5]
	s_add_u32 s4, s4, s20
	s_addc_u32 s5, s5, 0
	s_waitcnt lgkmcnt(13)
	v_mfma_f32_16x16x32_f16 v[60:63], v[160:163], v[136:139], v[60:63]
	s_waitcnt lgkmcnt(12)
	v_mfma_f32_16x16x32_f16 v[64:67], v[164:167], v[136:139], v[64:67]
	s_waitcnt lgkmcnt(11)
	v_mfma_f32_16x16x32_f16 v[68:71], v[168:171], v[136:139], v[68:71]
	s_waitcnt lgkmcnt(10)
	v_mfma_f32_16x16x32_f16 v[72:75], v[156:159], v[140:143], v[72:75]
	v_mfma_f32_16x16x32_f16 v[76:79], v[160:163], v[140:143], v[76:79]
	s_add_u32 m0, s28, 0x16000
	s_nop 0
	global_load_lds_dwordx4 v10, s[6:7]
	v_mfma_f32_16x16x32_f16 v[80:83], v[164:167], v[140:143], v[80:83]
	v_mfma_f32_16x16x32_f16 v[84:87], v[168:171], v[140:143], v[84:87]
	s_waitcnt lgkmcnt(9)
	v_mfma_f32_16x16x32_f16 v[88:91], v[156:159], v[144:147], v[88:91]
	v_mfma_f32_16x16x32_f16 v[92:95], v[160:163], v[144:147], v[92:95]
	v_mfma_f32_16x16x32_f16 v[96:99], v[164:167], v[144:147], v[96:99]
	s_add_u32 m0, s28, 0x18000
	s_nop 0
	global_load_lds_dwordx4 v11, s[6:7]
	s_add_u32 s6, s6, s20
	s_addc_u32 s7, s7, 0
	v_mfma_f32_16x16x32_f16 v[100:103], v[168:171], v[144:147], v[100:103]
	s_waitcnt lgkmcnt(8)
	v_mfma_f32_16x16x32_f16 v[104:107], v[156:159], v[148:151], v[104:107]
	v_mfma_f32_16x16x32_f16 v[108:111], v[160:163], v[148:151], v[108:111]
	v_mfma_f32_16x16x32_f16 v[112:115], v[164:167], v[148:151], v[112:115]
	v_mfma_f32_16x16x32_f16 v[116:119], v[168:171], v[148:151], v[116:119]
	s_waitcnt vmcnt(6) lgkmcnt(0)
	s_barrier
	s_waitcnt lgkmcnt(7)
	ds_read_b128 v[136:139], v15
	ds_read_b128 v[156:159], v17
	ds_read_b128 v[160:163], v17 offset:2048
	ds_read_b128 v[164:167], v17 offset:4096
	ds_read_b128 v[168:171], v17 offset:6144
	ds_read_b128 v[140:143], v15 offset:2048
	ds_read_b128 v[144:147], v15 offset:4096
	ds_read_b128 v[148:151], v15 offset:6144
	s_waitcnt lgkmcnt(14)
	v_mfma_f32_16x16x32_f16 v[56:59], v[192:195], v[172:175], v[56:59]
	s_add_u32 m0, s28, 0x1a000
	s_nop 0
	global_load_lds_dwordx4 v10, s[4:5]
	s_waitcnt lgkmcnt(13)
	v_mfma_f32_16x16x32_f16 v[60:63], v[196:199], v[172:175], v[60:63]
	s_waitcnt lgkmcnt(12)
	v_mfma_f32_16x16x32_f16 v[64:67], v[200:203], v[172:175], v[64:67]
	s_waitcnt lgkmcnt(11)
	v_mfma_f32_16x16x32_f16 v[68:71], v[204:207], v[172:175], v[68:71]
	s_waitcnt lgkmcnt(10)
	v_mfma_f32_16x16x32_f16 v[72:75], v[192:195], v[176:179], v[72:75]
	v_mfma_f32_16x16x32_f16 v[76:79], v[196:199], v[176:179], v[76:79]
	s_add_u32 m0, s28, 0x1c000
	s_nop 0
	global_load_lds_dwordx4 v11, s[4:5]
	v_mfma_f32_16x16x32_f16 v[80:83], v[200:203], v[176:179], v[80:83]
	v_mfma_f32_16x16x32_f16 v[84:87], v[204:207], v[176:179], v[84:87]
	s_waitcnt lgkmcnt(9)
	v_mfma_f32_16x16x32_f16 v[88:91], v[192:195], v[180:183], v[88:91]
	v_mfma_f32_16x16x32_f16 v[92:95], v[196:199], v[180:183], v[92:95]
	v_mfma_f32_16x16x32_f16 v[96:99], v[200:203], v[180:183], v[96:99]
	s_add_u32 m0, s28, 0x1e000
	s_nop 0
	global_load_lds_dwordx4 v12, s[4:5]
	v_mfma_f32_16x16x32_f16 v[100:103], v[204:207], v[180:183], v[100:103]
	s_waitcnt lgkmcnt(8)
	v_mfma_f32_16x16x32_f16 v[104:107], v[192:195], v[184:187], v[104:107]
	v_mfma_f32_16x16x32_f16 v[108:111], v[196:199], v[184:187], v[108:111]
	v_mfma_f32_16x16x32_f16 v[112:115], v[200:203], v[184:187], v[112:115]
	v_mfma_f32_16x16x32_f16 v[116:119], v[204:207], v[184:187], v[116:119]
	s_waitcnt lgkmcnt(7)
	ds_read_b128 v[172:175], v16
	ds_read_b128 v[192:195], v18
	ds_read_b128 v[196:199], v18 offset:2048
	ds_read_b128 v[200:203], v18 offset:4096
	ds_read_b128 v[204:207], v18 offset:6144
	ds_read_b128 v[176:179], v16 offset:2048
	ds_read_b128 v[180:183], v16 offset:4096
	ds_read_b128 v[184:187], v16 offset:6144
	s_waitcnt lgkmcnt(14)
	v_mfma_f32_16x16x32_f16 v[56:59], v[156:159], v[136:139], v[56:59]
	s_add_u32 m0, s28, 0x20000
	s_nop 0
	global_load_lds_dwordx4 v13, s[4:5]
	s_add_u32 s4, s4, s20
	s_addc_u32 s5, s5, 0
	s_waitcnt lgkmcnt(13)
	v_mfma_f32_16x16x32_f16 v[60:63], v[160:163], v[136:139], v[60:63]
	s_waitcnt lgkmcnt(12)
	v_mfma_f32_16x16x32_f16 v[64:67], v[164:167], v[136:139], v[64:67]
	s_waitcnt lgkmcnt(11)
	v_mfma_f32_16x16x32_f16 v[68:71], v[168:171], v[136:139], v[68:71]
	s_waitcnt lgkmcnt(10)
	v_mfma_f32_16x16x32_f16 v[72:75], v[156:159], v[140:143], v[72:75]
	v_mfma_f32_16x16x32_f16 v[76:79], v[160:163], v[140:143], v[76:79]
	s_add_u32 m0, s28, 0x23000
	s_nop 0
	global_load_lds_dwordx4 v10, s[6:7]
	v_mfma_f32_16x16x32_f16 v[80:83], v[164:167], v[140:143], v[80:83]
	v_mfma_f32_16x16x32_f16 v[84:87], v[168:171], v[140:143], v[84:87]
	s_waitcnt lgkmcnt(9)
	v_mfma_f32_16x16x32_f16 v[88:91], v[156:159], v[144:147], v[88:91]
	v_mfma_f32_16x16x32_f16 v[92:95], v[160:163], v[144:147], v[92:95]
	v_mfma_f32_16x16x32_f16 v[96:99], v[164:167], v[144:147], v[96:99]
	s_add_u32 m0, s28, 0x25000
	s_nop 0
	global_load_lds_dwordx4 v11, s[6:7]
	s_add_u32 s6, s6, s20
	s_addc_u32 s7, s7, 0
	v_mfma_f32_16x16x32_f16 v[100:103], v[168:171], v[144:147], v[100:103]
	s_waitcnt lgkmcnt(8)
	v_mfma_f32_16x16x32_f16 v[104:107], v[156:159], v[148:151], v[104:107]
	v_mfma_f32_16x16x32_f16 v[108:111], v[160:163], v[148:151], v[108:111]
	v_mfma_f32_16x16x32_f16 v[112:115], v[164:167], v[148:151], v[112:115]
	v_mfma_f32_16x16x32_f16 v[116:119], v[168:171], v[148:151], v[116:119]
	s_waitcnt vmcnt(6) lgkmcnt(0)
	s_barrier
	s_waitcnt lgkmcnt(7)
	ds_read_b128 v[136:139], v15 offset:53248
	ds_read_b128 v[156:159], v17 offset:53248
	ds_read_b128 v[160:163], v17 offset:55296
	ds_read_b128 v[164:167], v17 offset:57344
	ds_read_b128 v[168:171], v17 offset:59392
	ds_read_b128 v[140:143], v15 offset:55296
	ds_read_b128 v[144:147], v15 offset:57344
	ds_read_b128 v[148:151], v15 offset:59392
	s_waitcnt lgkmcnt(14)
	v_mfma_f32_16x16x32_f16 v[56:59], v[192:195], v[172:175], v[56:59]
	s_add_u32 m0, s28, 0x0
	s_nop 0
	global_load_lds_dwordx4 v10, s[4:5]
	s_waitcnt lgkmcnt(13)
	v_mfma_f32_16x16x32_f16 v[60:63], v[196:199], v[172:175], v[60:63]
	s_waitcnt lgkmcnt(12)
	v_mfma_f32_16x16x32_f16 v[64:67], v[200:203], v[172:175], v[64:67]
	s_waitcnt lgkmcnt(11)
	v_mfma_f32_16x16x32_f16 v[68:71], v[204:207], v[172:175], v[68:71]
	s_waitcnt lgkmcnt(10)
	v_mfma_f32_16x16x32_f16 v[72:75], v[192:195], v[176:179], v[72:75]
	v_mfma_f32_16x16x32_f16 v[76:79], v[196:199], v[176:179], v[76:79]
	s_add_u32 m0, s28, 0x2000
	s_nop 0
	global_load_lds_dwordx4 v11, s[4:5]
	v_mfma_f32_16x16x32_f16 v[80:83], v[200:203], v[176:179], v[80:83]
	v_mfma_f32_16x16x32_f16 v[84:87], v[204:207], v[176:179], v[84:87]
	s_waitcnt lgkmcnt(9)
	v_mfma_f32_16x16x32_f16 v[88:91], v[192:195], v[180:183], v[88:91]
	v_mfma_f32_16x16x32_f16 v[92:95], v[196:199], v[180:183], v[92:95]
	v_mfma_f32_16x16x32_f16 v[96:99], v[200:203], v[180:183], v[96:99]
	s_add_u32 m0, s28, 0x4000
	s_nop 0
	global_load_lds_dwordx4 v12, s[4:5]
	v_mfma_f32_16x16x32_f16 v[100:103], v[204:207], v[180:183], v[100:103]
	s_waitcnt lgkmcnt(8)
	v_mfma_f32_16x16x32_f16 v[104:107], v[192:195], v[184:187], v[104:107]
	v_mfma_f32_16x16x32_f16 v[108:111], v[196:199], v[184:187], v[108:111]
	v_mfma_f32_16x16x32_f16 v[112:115], v[200:203], v[184:187], v[112:115]
	v_mfma_f32_16x16x32_f16 v[116:119], v[204:207], v[184:187], v[116:119]
	s_waitcnt lgkmcnt(7)
	ds_read_b128 v[172:175], v16 offset:53248
	ds_read_b128 v[192:195], v18 offset:53248
	ds_read_b128 v[196:199], v18 offset:55296
	ds_read_b128 v[200:203], v18 offset:57344
	ds_read_b128 v[204:207], v18 offset:59392
	ds_read_b128 v[176:179], v16 offset:55296
	ds_read_b128 v[180:183], v16 offset:57344
	ds_read_b128 v[184:187], v16 offset:59392
	s_waitcnt lgkmcnt(14)
	v_mfma_f32_16x16x32_f16 v[56:59], v[156:159], v[136:139], v[56:59]
	s_add_u32 m0, s28, 0x6000
	s_nop 0
	global_load_lds_dwordx4 v13, s[4:5]
	s_add_u32 s4, s4, s20
	s_addc_u32 s5, s5, 0
	s_waitcnt lgkmcnt(13)
	v_mfma_f32_16x16x32_f16 v[60:63], v[160:163], v[136:139], v[60:63]
	s_waitcnt lgkmcnt(12)
	v_mfma_f32_16x16x32_f16 v[64:67], v[164:167], v[136:139], v[64:67]
	s_waitcnt lgkmcnt(11)
	v_mfma_f32_16x16x32_f16 v[68:71], v[168:171], v[136:139], v[68:71]
	s_waitcnt lgkmcnt(10)
	v_mfma_f32_16x16x32_f16 v[72:75], v[156:159], v[140:143], v[72:75]
	v_mfma_f32_16x16x32_f16 v[76:79], v[160:163], v[140:143], v[76:79]
	s_add_u32 m0, s28, 0x9000
	s_nop 0
	global_load_lds_dwordx4 v10, s[6:7]
	v_mfma_f32_16x16x32_f16 v[80:83], v[164:167], v[140:143], v[80:83]
	v_mfma_f32_16x16x32_f16 v[84:87], v[168:171], v[140:143], v[84:87]
	s_waitcnt lgkmcnt(9)
	v_mfma_f32_16x16x32_f16 v[88:91], v[156:159], v[144:147], v[88:91]
	v_mfma_f32_16x16x32_f16 v[92:95], v[160:163], v[144:147], v[92:95]
	v_mfma_f32_16x16x32_f16 v[96:99], v[164:167], v[144:147], v[96:99]
	s_add_u32 m0, s28, 0xb000
	s_nop 0
	global_load_lds_dwordx4 v11, s[6:7]
	s_add_u32 s6, s6, s20
	s_addc_u32 s7, s7, 0
	v_mfma_f32_16x16x32_f16 v[100:103], v[168:171], v[144:147], v[100:103]
	s_waitcnt lgkmcnt(8)
	v_mfma_f32_16x16x32_f16 v[104:107], v[156:159], v[148:151], v[104:107]
	v_mfma_f32_16x16x32_f16 v[108:111], v[160:163], v[148:151], v[108:111]
	v_mfma_f32_16x16x32_f16 v[112:115], v[164:167], v[148:151], v[112:115]
	v_mfma_f32_16x16x32_f16 v[116:119], v[168:171], v[148:151], v[116:119]
	s_waitcnt vmcnt(6) lgkmcnt(0)
	s_barrier
	s_waitcnt lgkmcnt(7)
	ds_read_b128 v[136:139], v19
	ds_read_b128 v[156:159], v21
	ds_read_b128 v[160:163], v21 offset:2048
	ds_read_b128 v[164:167], v21 offset:4096
	ds_read_b128 v[168:171], v21 offset:6144
	ds_read_b128 v[140:143], v19 offset:2048
	ds_read_b128 v[144:147], v19 offset:4096
	ds_read_b128 v[148:151], v19 offset:6144
	s_waitcnt lgkmcnt(14)
	v_mfma_f32_16x16x32_f16 v[56:59], v[192:195], v[172:175], v[56:59]
	s_add_u32 m0, s28, 0xd000
	s_nop 0
	global_load_lds_dwordx4 v10, s[4:5]
	s_waitcnt lgkmcnt(13)
	v_mfma_f32_16x16x32_f16 v[60:63], v[196:199], v[172:175], v[60:63]
	s_waitcnt lgkmcnt(12)
	v_mfma_f32_16x16x32_f16 v[64:67], v[200:203], v[172:175], v[64:67]
	s_waitcnt lgkmcnt(11)
	v_mfma_f32_16x16x32_f16 v[68:71], v[204:207], v[172:175], v[68:71]
	s_waitcnt lgkmcnt(10)
	v_mfma_f32_16x16x32_f16 v[72:75], v[192:195], v[176:179], v[72:75]
	v_mfma_f32_16x16x32_f16 v[76:79], v[196:199], v[176:179], v[76:79]
	s_add_u32 m0, s28, 0xf000
	s_nop 0
	global_load_lds_dwordx4 v11, s[4:5]
	v_mfma_f32_16x16x32_f16 v[80:83], v[200:203], v[176:179], v[80:83]
	v_mfma_f32_16x16x32_f16 v[84:87], v[204:207], v[176:179], v[84:87]
	s_waitcnt lgkmcnt(9)
	v_mfma_f32_16x16x32_f16 v[88:91], v[192:195], v[180:183], v[88:91]
	v_mfma_f32_16x16x32_f16 v[92:95], v[196:199], v[180:183], v[92:95]
	v_mfma_f32_16x16x32_f16 v[96:99], v[200:203], v[180:183], v[96:99]
	s_add_u32 m0, s28, 0x11000
	s_nop 0
	global_load_lds_dwordx4 v12, s[4:5]
	v_mfma_f32_16x16x32_f16 v[100:103], v[204:207], v[180:183], v[100:103]
	s_waitcnt lgkmcnt(8)
	v_mfma_f32_16x16x32_f16 v[104:107], v[192:195], v[184:187], v[104:107]
	v_mfma_f32_16x16x32_f16 v[108:111], v[196:199], v[184:187], v[108:111]
	v_mfma_f32_16x16x32_f16 v[112:115], v[200:203], v[184:187], v[112:115]
	v_mfma_f32_16x16x32_f16 v[116:119], v[204:207], v[184:187], v[116:119]
	s_waitcnt lgkmcnt(7)
	ds_read_b128 v[172:175], v20
	ds_read_b128 v[192:195], v22
	ds_read_b128 v[196:199], v22 offset:2048
	ds_read_b128 v[200:203], v22 offset:4096
	ds_read_b128 v[204:207], v22 offset:6144
	ds_read_b128 v[176:179], v20 offset:2048
	ds_read_b128 v[180:183], v20 offset:4096
	ds_read_b128 v[184:187], v20 offset:6144
	s_waitcnt lgkmcnt(14)
	v_mfma_f32_16x16x32_f16 v[56:59], v[156:159], v[136:139], v[56:59]
	s_add_u32 m0, s28, 0x13000
	s_nop 0
	global_load_lds_dwordx4 v13, s[4:5]
	s_add_u32 s4, s4, s20
	s_addc_u32 s5, s5, 0
	s_waitcnt lgkmcnt(13)
	v_mfma_f32_16x16x32_f16 v[60:63], v[160:163], v[136:139], v[60:63]
	s_waitcnt lgkmcnt(12)
	v_mfma_f32_16x16x32_f16 v[64:67], v[164:167], v[136:139], v[64:67]
	s_waitcnt lgkmcnt(11)
	v_mfma_f32_16x16x32_f16 v[68:71], v[168:171], v[136:139], v[68:71]
	s_waitcnt lgkmcnt(10)
	v_mfma_f32_16x16x32_f16 v[72:75], v[156:159], v[140:143], v[72:75]
	v_mfma_f32_16x16x32_f16 v[76:79], v[160:163], v[140:143], v[76:79]
	s_add_u32 m0, s28, 0x16000
	s_nop 0
	global_load_lds_dwordx4 v10, s[6:7]
	v_mfma_f32_16x16x32_f16 v[80:83], v[164:167], v[140:143], v[80:83]
	v_mfma_f32_16x16x32_f16 v[84:87], v[168:171], v[140:143], v[84:87]
	s_waitcnt lgkmcnt(9)
	v_mfma_f32_16x16x32_f16 v[88:91], v[156:159], v[144:147], v[88:91]
	v_mfma_f32_16x16x32_f16 v[92:95], v[160:163], v[144:147], v[92:95]
	v_mfma_f32_16x16x32_f16 v[96:99], v[164:167], v[144:147], v[96:99]
	s_add_u32 m0, s28, 0x18000
	s_nop 0
	global_load_lds_dwordx4 v11, s[6:7]
	s_add_u32 s6, s6, s20
	s_addc_u32 s7, s7, 0
	v_mfma_f32_16x16x32_f16 v[100:103], v[168:171], v[144:147], v[100:103]
	s_waitcnt lgkmcnt(8)
	v_mfma_f32_16x16x32_f16 v[104:107], v[156:159], v[148:151], v[104:107]
	v_mfma_f32_16x16x32_f16 v[108:111], v[160:163], v[148:151], v[108:111]
	v_mfma_f32_16x16x32_f16 v[112:115], v[164:167], v[148:151], v[112:115]
	v_mfma_f32_16x16x32_f16 v[116:119], v[168:171], v[148:151], v[116:119]
	s_waitcnt vmcnt(6) lgkmcnt(0)
	s_barrier
	s_waitcnt lgkmcnt(7)
	ds_read_b128 v[136:139], v15
	ds_read_b128 v[156:159], v17
	ds_read_b128 v[160:163], v17 offset:2048
	ds_read_b128 v[164:167], v17 offset:4096
	ds_read_b128 v[168:171], v17 offset:6144
	ds_read_b128 v[140:143], v15 offset:2048
	ds_read_b128 v[144:147], v15 offset:4096
	ds_read_b128 v[148:151], v15 offset:6144
	s_waitcnt lgkmcnt(14)
	v_mfma_f32_16x16x32_f16 v[56:59], v[192:195], v[172:175], v[56:59]
	s_add_u32 m0, s28, 0x1a000
	s_nop 0
	global_load_lds_dwordx4 v10, s[4:5]
	s_waitcnt lgkmcnt(13)
	v_mfma_f32_16x16x32_f16 v[60:63], v[196:199], v[172:175], v[60:63]
	s_waitcnt lgkmcnt(12)
	v_mfma_f32_16x16x32_f16 v[64:67], v[200:203], v[172:175], v[64:67]
	s_waitcnt lgkmcnt(11)
	v_mfma_f32_16x16x32_f16 v[68:71], v[204:207], v[172:175], v[68:71]
	s_waitcnt lgkmcnt(10)
	v_mfma_f32_16x16x32_f16 v[72:75], v[192:195], v[176:179], v[72:75]
	v_mfma_f32_16x16x32_f16 v[76:79], v[196:199], v[176:179], v[76:79]
	s_add_u32 m0, s28, 0x1c000
	s_nop 0
	global_load_lds_dwordx4 v11, s[4:5]
	v_mfma_f32_16x16x32_f16 v[80:83], v[200:203], v[176:179], v[80:83]
	v_mfma_f32_16x16x32_f16 v[84:87], v[204:207], v[176:179], v[84:87]
	s_waitcnt lgkmcnt(9)
	v_mfma_f32_16x16x32_f16 v[88:91], v[192:195], v[180:183], v[88:91]
	v_mfma_f32_16x16x32_f16 v[92:95], v[196:199], v[180:183], v[92:95]
	v_mfma_f32_16x16x32_f16 v[96:99], v[200:203], v[180:183], v[96:99]
	s_add_u32 m0, s28, 0x1e000
	s_nop 0
	global_load_lds_dwordx4 v12, s[4:5]
	v_mfma_f32_16x16x32_f16 v[100:103], v[204:207], v[180:183], v[100:103]
	s_waitcnt lgkmcnt(8)
	v_mfma_f32_16x16x32_f16 v[104:107], v[192:195], v[184:187], v[104:107]
	v_mfma_f32_16x16x32_f16 v[108:111], v[196:199], v[184:187], v[108:111]
	v_mfma_f32_16x16x32_f16 v[112:115], v[200:203], v[184:187], v[112:115]
	v_mfma_f32_16x16x32_f16 v[116:119], v[204:207], v[184:187], v[116:119]
	s_waitcnt lgkmcnt(7)
	ds_read_b128 v[172:175], v16
	ds_read_b128 v[192:195], v18
	ds_read_b128 v[196:199], v18 offset:2048
	ds_read_b128 v[200:203], v18 offset:4096
	ds_read_b128 v[204:207], v18 offset:6144
	ds_read_b128 v[176:179], v16 offset:2048
	ds_read_b128 v[180:183], v16 offset:4096
	ds_read_b128 v[184:187], v16 offset:6144
	s_waitcnt lgkmcnt(14)
	v_mfma_f32_16x16x32_f16 v[56:59], v[156:159], v[136:139], v[56:59]
	s_add_u32 m0, s28, 0x20000
	s_nop 0
	global_load_lds_dwordx4 v13, s[4:5]
	s_add_u32 s4, s4, s20
	s_addc_u32 s5, s5, 0
	s_waitcnt lgkmcnt(13)
	v_mfma_f32_16x16x32_f16 v[60:63], v[160:163], v[136:139], v[60:63]
	s_waitcnt lgkmcnt(12)
	v_mfma_f32_16x16x32_f16 v[64:67], v[164:167], v[136:139], v[64:67]
	s_waitcnt lgkmcnt(11)
	v_mfma_f32_16x16x32_f16 v[68:71], v[168:171], v[136:139], v[68:71]
	s_waitcnt lgkmcnt(10)
	v_mfma_f32_16x16x32_f16 v[72:75], v[156:159], v[140:143], v[72:75]
	v_mfma_f32_16x16x32_f16 v[76:79], v[160:163], v[140:143], v[76:79]
	s_add_u32 m0, s28, 0x23000
	s_nop 0
	global_load_lds_dwordx4 v10, s[6:7]
	v_mfma_f32_16x16x32_f16 v[80:83], v[164:167], v[140:143], v[80:83]
	v_mfma_f32_16x16x32_f16 v[84:87], v[168:171], v[140:143], v[84:87]
	s_waitcnt lgkmcnt(9)
	v_mfma_f32_16x16x32_f16 v[88:91], v[156:159], v[144:147], v[88:91]
	v_mfma_f32_16x16x32_f16 v[92:95], v[160:163], v[144:147], v[92:95]
	v_mfma_f32_16x16x32_f16 v[96:99], v[164:167], v[144:147], v[96:99]
	s_add_u32 m0, s28, 0x25000
	s_nop 0
	global_load_lds_dwordx4 v11, s[6:7]
	s_add_u32 s6, s6, s20
	s_addc_u32 s7, s7, 0
	v_mfma_f32_16x16x32_f16 v[100:103], v[168:171], v[144:147], v[100:103]
	s_waitcnt lgkmcnt(8)
	v_mfma_f32_16x16x32_f16 v[104:107], v[156:159], v[148:151], v[104:107]
	v_mfma_f32_16x16x32_f16 v[108:111], v[160:163], v[148:151], v[108:111]
	v_mfma_f32_16x16x32_f16 v[112:115], v[164:167], v[148:151], v[112:115]
	v_mfma_f32_16x16x32_f16 v[116:119], v[168:171], v[148:151], v[116:119]
	s_waitcnt vmcnt(6) lgkmcnt(0)
	s_barrier
	s_waitcnt lgkmcnt(7)
	ds_read_b128 v[136:139], v15 offset:53248
	ds_read_b128 v[156:159], v17 offset:53248
	ds_read_b128 v[160:163], v17 offset:55296
	ds_read_b128 v[164:167], v17 offset:57344
	ds_read_b128 v[168:171], v17 offset:59392
	ds_read_b128 v[140:143], v15 offset:55296
	ds_read_b128 v[144:147], v15 offset:57344
	ds_read_b128 v[148:151], v15 offset:59392
	s_waitcnt lgkmcnt(14)
	v_mfma_f32_16x16x32_f16 v[56:59], v[192:195], v[172:175], v[56:59]
	s_add_u32 m0, s28, 0x0
	s_nop 0
	global_load_lds_dwordx4 v10, s[4:5]
	s_waitcnt lgkmcnt(13)
	v_mfma_f32_16x16x32_f16 v[60:63], v[196:199], v[172:175], v[60:63]
	s_waitcnt lgkmcnt(12)
	v_mfma_f32_16x16x32_f16 v[64:67], v[200:203], v[172:175], v[64:67]
	s_waitcnt lgkmcnt(11)
	v_mfma_f32_16x16x32_f16 v[68:71], v[204:207], v[172:175], v[68:71]
	s_waitcnt lgkmcnt(10)
	v_mfma_f32_16x16x32_f16 v[72:75], v[192:195], v[176:179], v[72:75]
	v_mfma_f32_16x16x32_f16 v[76:79], v[196:199], v[176:179], v[76:79]
	s_add_u32 m0, s28, 0x2000
	s_nop 0
	global_load_lds_dwordx4 v11, s[4:5]
	v_mfma_f32_16x16x32_f16 v[80:83], v[200:203], v[176:179], v[80:83]
	v_mfma_f32_16x16x32_f16 v[84:87], v[204:207], v[176:179], v[84:87]
	s_waitcnt lgkmcnt(9)
	v_mfma_f32_16x16x32_f16 v[88:91], v[192:195], v[180:183], v[88:91]
	v_mfma_f32_16x16x32_f16 v[92:95], v[196:199], v[180:183], v[92:95]
	v_mfma_f32_16x16x32_f16 v[96:99], v[200:203], v[180:183], v[96:99]
	s_add_u32 m0, s28, 0x4000
	s_nop 0
	global_load_lds_dwordx4 v12, s[4:5]
	v_mfma_f32_16x16x32_f16 v[100:103], v[204:207], v[180:183], v[100:103]
	s_waitcnt lgkmcnt(8)
	v_mfma_f32_16x16x32_f16 v[104:107], v[192:195], v[184:187], v[104:107]
	v_mfma_f32_16x16x32_f16 v[108:111], v[196:199], v[184:187], v[108:111]
	v_mfma_f32_16x16x32_f16 v[112:115], v[200:203], v[184:187], v[112:115]
	v_mfma_f32_16x16x32_f16 v[116:119], v[204:207], v[184:187], v[116:119]
	s_waitcnt lgkmcnt(7)
	ds_read_b128 v[172:175], v16 offset:53248
	ds_read_b128 v[192:195], v18 offset:53248
	ds_read_b128 v[196:199], v18 offset:55296
	ds_read_b128 v[200:203], v18 offset:57344
	ds_read_b128 v[204:207], v18 offset:59392
	ds_read_b128 v[176:179], v16 offset:55296
	ds_read_b128 v[180:183], v16 offset:57344
	ds_read_b128 v[184:187], v16 offset:59392
	s_waitcnt lgkmcnt(14)
	v_mfma_f32_16x16x32_f16 v[56:59], v[156:159], v[136:139], v[56:59]
	s_add_u32 m0, s28, 0x6000
	s_nop 0
	global_load_lds_dwordx4 v13, s[4:5]
	s_add_u32 s4, s4, s20
	s_addc_u32 s5, s5, 0
	s_waitcnt lgkmcnt(13)
	v_mfma_f32_16x16x32_f16 v[60:63], v[160:163], v[136:139], v[60:63]
	s_waitcnt lgkmcnt(12)
	v_mfma_f32_16x16x32_f16 v[64:67], v[164:167], v[136:139], v[64:67]
	s_waitcnt lgkmcnt(11)
	v_mfma_f32_16x16x32_f16 v[68:71], v[168:171], v[136:139], v[68:71]
	s_waitcnt lgkmcnt(10)
	v_mfma_f32_16x16x32_f16 v[72:75], v[156:159], v[140:143], v[72:75]
	v_mfma_f32_16x16x32_f16 v[76:79], v[160:163], v[140:143], v[76:79]
	s_add_u32 m0, s28, 0x9000
	s_nop 0
	global_load_lds_dwordx4 v10, s[6:7]
	v_mfma_f32_16x16x32_f16 v[80:83], v[164:167], v[140:143], v[80:83]
	v_mfma_f32_16x16x32_f16 v[84:87], v[168:171], v[140:143], v[84:87]
	s_waitcnt lgkmcnt(9)
	v_mfma_f32_16x16x32_f16 v[88:91], v[156:159], v[144:147], v[88:91]
	v_mfma_f32_16x16x32_f16 v[92:95], v[160:163], v[144:147], v[92:95]
	v_mfma_f32_16x16x32_f16 v[96:99], v[164:167], v[144:147], v[96:99]
	s_add_u32 m0, s28, 0xb000
	s_nop 0
	global_load_lds_dwordx4 v11, s[6:7]
	s_add_u32 s6, s6, s20
	s_addc_u32 s7, s7, 0
	v_mfma_f32_16x16x32_f16 v[100:103], v[168:171], v[144:147], v[100:103]
	s_waitcnt lgkmcnt(8)
	v_mfma_f32_16x16x32_f16 v[104:107], v[156:159], v[148:151], v[104:107]
	v_mfma_f32_16x16x32_f16 v[108:111], v[160:163], v[148:151], v[108:111]
	v_mfma_f32_16x16x32_f16 v[112:115], v[164:167], v[148:151], v[112:115]
	v_mfma_f32_16x16x32_f16 v[116:119], v[168:171], v[148:151], v[116:119]
	s_waitcnt vmcnt(6) lgkmcnt(0)
	s_barrier
	s_waitcnt lgkmcnt(7)
	ds_read_b128 v[136:139], v19
	ds_read_b128 v[156:159], v21
	ds_read_b128 v[160:163], v21 offset:2048
	ds_read_b128 v[164:167], v21 offset:4096
	ds_read_b128 v[168:171], v21 offset:6144
	ds_read_b128 v[140:143], v19 offset:2048
	ds_read_b128 v[144:147], v19 offset:4096
	ds_read_b128 v[148:151], v19 offset:6144
	s_waitcnt lgkmcnt(14)
	v_mfma_f32_16x16x32_f16 v[56:59], v[192:195], v[172:175], v[56:59]
	s_add_u32 m0, s28, 0xd000
	s_nop 0
	global_load_lds_dwordx4 v10, s[4:5]
	s_waitcnt lgkmcnt(13)
	v_mfma_f32_16x16x32_f16 v[60:63], v[196:199], v[172:175], v[60:63]
	s_waitcnt lgkmcnt(12)
	v_mfma_f32_16x16x32_f16 v[64:67], v[200:203], v[172:175], v[64:67]
	s_waitcnt lgkmcnt(11)
	v_mfma_f32_16x16x32_f16 v[68:71], v[204:207], v[172:175], v[68:71]
	s_waitcnt lgkmcnt(10)
	v_mfma_f32_16x16x32_f16 v[72:75], v[192:195], v[176:179], v[72:75]
	v_mfma_f32_16x16x32_f16 v[76:79], v[196:199], v[176:179], v[76:79]
	s_add_u32 m0, s28, 0xf000
	s_nop 0
	global_load_lds_dwordx4 v11, s[4:5]
	v_mfma_f32_16x16x32_f16 v[80:83], v[200:203], v[176:179], v[80:83]
	v_mfma_f32_16x16x32_f16 v[84:87], v[204:207], v[176:179], v[84:87]
	s_waitcnt lgkmcnt(9)
	v_mfma_f32_16x16x32_f16 v[88:91], v[192:195], v[180:183], v[88:91]
	v_mfma_f32_16x16x32_f16 v[92:95], v[196:199], v[180:183], v[92:95]
	v_mfma_f32_16x16x32_f16 v[96:99], v[200:203], v[180:183], v[96:99]
	s_add_u32 m0, s28, 0x11000
	s_nop 0
	global_load_lds_dwordx4 v12, s[4:5]
	v_mfma_f32_16x16x32_f16 v[100:103], v[204:207], v[180:183], v[100:103]
	s_waitcnt lgkmcnt(8)
	v_mfma_f32_16x16x32_f16 v[104:107], v[192:195], v[184:187], v[104:107]
	v_mfma_f32_16x16x32_f16 v[108:111], v[196:199], v[184:187], v[108:111]
	v_mfma_f32_16x16x32_f16 v[112:115], v[200:203], v[184:187], v[112:115]
	v_mfma_f32_16x16x32_f16 v[116:119], v[204:207], v[184:187], v[116:119]
	s_waitcnt lgkmcnt(7)
	ds_read_b128 v[172:175], v20
	ds_read_b128 v[192:195], v22
	ds_read_b128 v[196:199], v22 offset:2048
	ds_read_b128 v[200:203], v22 offset:4096
	ds_read_b128 v[204:207], v22 offset:6144
	ds_read_b128 v[176:179], v20 offset:2048
	ds_read_b128 v[180:183], v20 offset:4096
	ds_read_b128 v[184:187], v20 offset:6144
	s_waitcnt lgkmcnt(14)
	v_mfma_f32_16x16x32_f16 v[56:59], v[156:159], v[136:139], v[56:59]
	s_add_u32 m0, s28, 0x13000
	s_nop 0
	global_load_lds_dwordx4 v13, s[4:5]
	s_add_u32 s4, s4, s20
	s_addc_u32 s5, s5, 0
	s_waitcnt lgkmcnt(13)
	v_mfma_f32_16x16x32_f16 v[60:63], v[160:163], v[136:139], v[60:63]
	s_waitcnt lgkmcnt(12)
	v_mfma_f32_16x16x32_f16 v[64:67], v[164:167], v[136:139], v[64:67]
	s_waitcnt lgkmcnt(11)
	v_mfma_f32_16x16x32_f16 v[68:71], v[168:171], v[136:139], v[68:71]
	s_waitcnt lgkmcnt(10)
	v_mfma_f32_16x16x32_f16 v[72:75], v[156:159], v[140:143], v[72:75]
	v_mfma_f32_16x16x32_f16 v[76:79], v[160:163], v[140:143], v[76:79]
	s_add_u32 m0, s28, 0x16000
	s_nop 0
	global_load_lds_dwordx4 v10, s[6:7]
	v_mfma_f32_16x16x32_f16 v[80:83], v[164:167], v[140:143], v[80:83]
	v_mfma_f32_16x16x32_f16 v[84:87], v[168:171], v[140:143], v[84:87]
	s_waitcnt lgkmcnt(9)
	v_mfma_f32_16x16x32_f16 v[88:91], v[156:159], v[144:147], v[88:91]
	v_mfma_f32_16x16x32_f16 v[92:95], v[160:163], v[144:147], v[92:95]
	v_mfma_f32_16x16x32_f16 v[96:99], v[164:167], v[144:147], v[96:99]
	s_add_u32 m0, s28, 0x18000
	s_nop 0
	global_load_lds_dwordx4 v11, s[6:7]
	s_add_u32 s6, s6, s20
	s_addc_u32 s7, s7, 0
	v_mfma_f32_16x16x32_f16 v[100:103], v[168:171], v[144:147], v[100:103]
	s_waitcnt lgkmcnt(8)
	v_mfma_f32_16x16x32_f16 v[104:107], v[156:159], v[148:151], v[104:107]
	v_mfma_f32_16x16x32_f16 v[108:111], v[160:163], v[148:151], v[108:111]
	v_mfma_f32_16x16x32_f16 v[112:115], v[164:167], v[148:151], v[112:115]
	v_mfma_f32_16x16x32_f16 v[116:119], v[168:171], v[148:151], v[116:119]
	s_waitcnt vmcnt(6) lgkmcnt(0)
	s_barrier
	s_waitcnt lgkmcnt(7)
	ds_read_b128 v[136:139], v15
	ds_read_b128 v[156:159], v17
	ds_read_b128 v[160:163], v17 offset:2048
	ds_read_b128 v[164:167], v17 offset:4096
	ds_read_b128 v[168:171], v17 offset:6144
	ds_read_b128 v[140:143], v15 offset:2048
	ds_read_b128 v[144:147], v15 offset:4096
	ds_read_b128 v[148:151], v15 offset:6144
	s_waitcnt lgkmcnt(14)
	v_mfma_f32_16x16x32_f16 v[56:59], v[192:195], v[172:175], v[56:59]
	s_add_u32 m0, s28, 0x1a000
	s_nop 0
	global_load_lds_dwordx4 v10, s[4:5]
	s_waitcnt lgkmcnt(13)
	v_mfma_f32_16x16x32_f16 v[60:63], v[196:199], v[172:175], v[60:63]
	s_waitcnt lgkmcnt(12)
	v_mfma_f32_16x16x32_f16 v[64:67], v[200:203], v[172:175], v[64:67]
	s_waitcnt lgkmcnt(11)
	v_mfma_f32_16x16x32_f16 v[68:71], v[204:207], v[172:175], v[68:71]
	s_waitcnt lgkmcnt(10)
	v_mfma_f32_16x16x32_f16 v[72:75], v[192:195], v[176:179], v[72:75]
	v_mfma_f32_16x16x32_f16 v[76:79], v[196:199], v[176:179], v[76:79]
	s_add_u32 m0, s28, 0x1c000
	s_nop 0
	global_load_lds_dwordx4 v11, s[4:5]
	v_mfma_f32_16x16x32_f16 v[80:83], v[200:203], v[176:179], v[80:83]
	v_mfma_f32_16x16x32_f16 v[84:87], v[204:207], v[176:179], v[84:87]
	s_waitcnt lgkmcnt(9)
	v_mfma_f32_16x16x32_f16 v[88:91], v[192:195], v[180:183], v[88:91]
	v_mfma_f32_16x16x32_f16 v[92:95], v[196:199], v[180:183], v[92:95]
	v_mfma_f32_16x16x32_f16 v[96:99], v[200:203], v[180:183], v[96:99]
	s_add_u32 m0, s28, 0x1e000
	s_nop 0
	global_load_lds_dwordx4 v12, s[4:5]
	v_mfma_f32_16x16x32_f16 v[100:103], v[204:207], v[180:183], v[100:103]
	s_waitcnt lgkmcnt(8)
	v_mfma_f32_16x16x32_f16 v[104:107], v[192:195], v[184:187], v[104:107]
	v_mfma_f32_16x16x32_f16 v[108:111], v[196:199], v[184:187], v[108:111]
	v_mfma_f32_16x16x32_f16 v[112:115], v[200:203], v[184:187], v[112:115]
	v_mfma_f32_16x16x32_f16 v[116:119], v[204:207], v[184:187], v[116:119]
	s_waitcnt lgkmcnt(7)
	ds_read_b128 v[172:175], v16
	ds_read_b128 v[192:195], v18
	ds_read_b128 v[196:199], v18 offset:2048
	ds_read_b128 v[200:203], v18 offset:4096
	ds_read_b128 v[204:207], v18 offset:6144
	ds_read_b128 v[176:179], v16 offset:2048
	ds_read_b128 v[180:183], v16 offset:4096
	ds_read_b128 v[184:187], v16 offset:6144
	s_waitcnt lgkmcnt(14)
	v_mfma_f32_16x16x32_f16 v[56:59], v[156:159], v[136:139], v[56:59]
	s_add_u32 m0, s28, 0x20000
	s_nop 0
	global_load_lds_dwordx4 v13, s[4:5]
	s_add_u32 s4, s4, s20
	s_addc_u32 s5, s5, 0
	s_waitcnt lgkmcnt(13)
	v_mfma_f32_16x16x32_f16 v[60:63], v[160:163], v[136:139], v[60:63]
	s_waitcnt lgkmcnt(12)
	v_mfma_f32_16x16x32_f16 v[64:67], v[164:167], v[136:139], v[64:67]
	s_waitcnt lgkmcnt(11)
	v_mfma_f32_16x16x32_f16 v[68:71], v[168:171], v[136:139], v[68:71]
	s_waitcnt lgkmcnt(10)
	v_mfma_f32_16x16x32_f16 v[72:75], v[156:159], v[140:143], v[72:75]
	v_mfma_f32_16x16x32_f16 v[76:79], v[160:163], v[140:143], v[76:79]
	s_add_u32 m0, s28, 0x23000
	s_nop 0
	global_load_lds_dwordx4 v10, s[6:7]
	v_mfma_f32_16x16x32_f16 v[80:83], v[164:167], v[140:143], v[80:83]
	v_mfma_f32_16x16x32_f16 v[84:87], v[168:171], v[140:143], v[84:87]
	s_waitcnt lgkmcnt(9)
	v_mfma_f32_16x16x32_f16 v[88:91], v[156:159], v[144:147], v[88:91]
	v_mfma_f32_16x16x32_f16 v[92:95], v[160:163], v[144:147], v[92:95]
	v_mfma_f32_16x16x32_f16 v[96:99], v[164:167], v[144:147], v[96:99]
	s_add_u32 m0, s28, 0x25000
	s_nop 0
	global_load_lds_dwordx4 v11, s[6:7]
	s_add_u32 s6, s6, s20
	s_addc_u32 s7, s7, 0
	v_mfma_f32_16x16x32_f16 v[100:103], v[168:171], v[144:147], v[100:103]
	s_waitcnt lgkmcnt(8)
	v_mfma_f32_16x16x32_f16 v[104:107], v[156:159], v[148:151], v[104:107]
	v_mfma_f32_16x16x32_f16 v[108:111], v[160:163], v[148:151], v[108:111]
	v_mfma_f32_16x16x32_f16 v[112:115], v[164:167], v[148:151], v[112:115]
	v_mfma_f32_16x16x32_f16 v[116:119], v[168:171], v[148:151], v[116:119]
	s_waitcnt vmcnt(6) lgkmcnt(0)
	s_barrier
	s_waitcnt lgkmcnt(7)
	ds_read_b128 v[136:139], v15 offset:53248
	ds_read_b128 v[156:159], v17 offset:53248
	ds_read_b128 v[160:163], v17 offset:55296
	ds_read_b128 v[164:167], v17 offset:57344
	ds_read_b128 v[168:171], v17 offset:59392
	ds_read_b128 v[140:143], v15 offset:55296
	ds_read_b128 v[144:147], v15 offset:57344
	ds_read_b128 v[148:151], v15 offset:59392
	s_waitcnt lgkmcnt(14)
	v_mfma_f32_16x16x32_f16 v[56:59], v[192:195], v[172:175], v[56:59]
	s_add_u32 m0, s28, 0x0
	s_nop 0
	global_load_lds_dwordx4 v10, s[4:5]
	s_waitcnt lgkmcnt(13)
	v_mfma_f32_16x16x32_f16 v[60:63], v[196:199], v[172:175], v[60:63]
	s_waitcnt lgkmcnt(12)
	v_mfma_f32_16x16x32_f16 v[64:67], v[200:203], v[172:175], v[64:67]
	s_waitcnt lgkmcnt(11)
	v_mfma_f32_16x16x32_f16 v[68:71], v[204:207], v[172:175], v[68:71]
	s_waitcnt lgkmcnt(10)
	v_mfma_f32_16x16x32_f16 v[72:75], v[192:195], v[176:179], v[72:75]
	v_mfma_f32_16x16x32_f16 v[76:79], v[196:199], v[176:179], v[76:79]
	s_add_u32 m0, s28, 0x2000
	s_nop 0
	global_load_lds_dwordx4 v11, s[4:5]
	v_mfma_f32_16x16x32_f16 v[80:83], v[200:203], v[176:179], v[80:83]
	v_mfma_f32_16x16x32_f16 v[84:87], v[204:207], v[176:179], v[84:87]
	s_waitcnt lgkmcnt(9)
	v_mfma_f32_16x16x32_f16 v[88:91], v[192:195], v[180:183], v[88:91]
	v_mfma_f32_16x16x32_f16 v[92:95], v[196:199], v[180:183], v[92:95]
	v_mfma_f32_16x16x32_f16 v[96:99], v[200:203], v[180:183], v[96:99]
	s_add_u32 m0, s28, 0x4000
	s_nop 0
	global_load_lds_dwordx4 v12, s[4:5]
	v_mfma_f32_16x16x32_f16 v[100:103], v[204:207], v[180:183], v[100:103]
	s_waitcnt lgkmcnt(8)
	v_mfma_f32_16x16x32_f16 v[104:107], v[192:195], v[184:187], v[104:107]
	v_mfma_f32_16x16x32_f16 v[108:111], v[196:199], v[184:187], v[108:111]
	v_mfma_f32_16x16x32_f16 v[112:115], v[200:203], v[184:187], v[112:115]
	v_mfma_f32_16x16x32_f16 v[116:119], v[204:207], v[184:187], v[116:119]
	s_waitcnt lgkmcnt(7)
	ds_read_b128 v[172:175], v16 offset:53248
	ds_read_b128 v[192:195], v18 offset:53248
	ds_read_b128 v[196:199], v18 offset:55296
	ds_read_b128 v[200:203], v18 offset:57344
	ds_read_b128 v[204:207], v18 offset:59392
	ds_read_b128 v[176:179], v16 offset:55296
	ds_read_b128 v[180:183], v16 offset:57344
	ds_read_b128 v[184:187], v16 offset:59392
	s_waitcnt lgkmcnt(14)
	v_mfma_f32_16x16x32_f16 v[56:59], v[156:159], v[136:139], v[56:59]
	s_add_u32 m0, s28, 0x6000
	s_nop 0
	global_load_lds_dwordx4 v13, s[4:5]
	s_add_u32 s4, s4, s20
	s_addc_u32 s5, s5, 0
	s_waitcnt lgkmcnt(13)
	v_mfma_f32_16x16x32_f16 v[60:63], v[160:163], v[136:139], v[60:63]
	s_waitcnt lgkmcnt(12)
	v_mfma_f32_16x16x32_f16 v[64:67], v[164:167], v[136:139], v[64:67]
	s_waitcnt lgkmcnt(11)
	v_mfma_f32_16x16x32_f16 v[68:71], v[168:171], v[136:139], v[68:71]
	s_waitcnt lgkmcnt(10)
	v_mfma_f32_16x16x32_f16 v[72:75], v[156:159], v[140:143], v[72:75]
	v_mfma_f32_16x16x32_f16 v[76:79], v[160:163], v[140:143], v[76:79]
	s_add_u32 m0, s28, 0x9000
	s_nop 0
	global_load_lds_dwordx4 v10, s[6:7]
	v_mfma_f32_16x16x32_f16 v[80:83], v[164:167], v[140:143], v[80:83]
	v_mfma_f32_16x16x32_f16 v[84:87], v[168:171], v[140:143], v[84:87]
	s_waitcnt lgkmcnt(9)
	v_mfma_f32_16x16x32_f16 v[88:91], v[156:159], v[144:147], v[88:91]
	v_mfma_f32_16x16x32_f16 v[92:95], v[160:163], v[144:147], v[92:95]
	v_mfma_f32_16x16x32_f16 v[96:99], v[164:167], v[144:147], v[96:99]
	s_add_u32 m0, s28, 0xb000
	s_nop 0
	global_load_lds_dwordx4 v11, s[6:7]
	s_add_u32 s6, s6, s20
	s_addc_u32 s7, s7, 0
	v_mfma_f32_16x16x32_f16 v[100:103], v[168:171], v[144:147], v[100:103]
	s_waitcnt lgkmcnt(8)
	v_mfma_f32_16x16x32_f16 v[104:107], v[156:159], v[148:151], v[104:107]
	v_mfma_f32_16x16x32_f16 v[108:111], v[160:163], v[148:151], v[108:111]
	v_mfma_f32_16x16x32_f16 v[112:115], v[164:167], v[148:151], v[112:115]
	v_mfma_f32_16x16x32_f16 v[116:119], v[168:171], v[148:151], v[116:119]
	s_waitcnt vmcnt(6) lgkmcnt(0)
	s_barrier
	s_waitcnt lgkmcnt(7)
	ds_read_b128 v[136:139], v19
	ds_read_b128 v[156:159], v21
	ds_read_b128 v[160:163], v21 offset:2048
	ds_read_b128 v[164:167], v21 offset:4096
	ds_read_b128 v[168:171], v21 offset:6144
	ds_read_b128 v[140:143], v19 offset:2048
	ds_read_b128 v[144:147], v19 offset:4096
	ds_read_b128 v[148:151], v19 offset:6144
	s_waitcnt lgkmcnt(14)
	v_mfma_f32_16x16x32_f16 v[56:59], v[192:195], v[172:175], v[56:59]
	s_waitcnt lgkmcnt(13)
	v_mfma_f32_16x16x32_f16 v[60:63], v[196:199], v[172:175], v[60:63]
	s_waitcnt lgkmcnt(12)
	v_mfma_f32_16x16x32_f16 v[64:67], v[200:203], v[172:175], v[64:67]
	s_waitcnt lgkmcnt(11)
	v_mfma_f32_16x16x32_f16 v[68:71], v[204:207], v[172:175], v[68:71]
	s_waitcnt lgkmcnt(10)
	v_mfma_f32_16x16x32_f16 v[72:75], v[192:195], v[176:179], v[72:75]
	v_mfma_f32_16x16x32_f16 v[76:79], v[196:199], v[176:179], v[76:79]
	v_mfma_f32_16x16x32_f16 v[80:83], v[200:203], v[176:179], v[80:83]
	v_mfma_f32_16x16x32_f16 v[84:87], v[204:207], v[176:179], v[84:87]
	s_waitcnt lgkmcnt(9)
	v_mfma_f32_16x16x32_f16 v[88:91], v[192:195], v[180:183], v[88:91]
	v_mfma_f32_16x16x32_f16 v[92:95], v[196:199], v[180:183], v[92:95]
	v_mfma_f32_16x16x32_f16 v[96:99], v[200:203], v[180:183], v[96:99]
	v_mfma_f32_16x16x32_f16 v[100:103], v[204:207], v[180:183], v[100:103]
	s_waitcnt lgkmcnt(8)
	v_mfma_f32_16x16x32_f16 v[104:107], v[192:195], v[184:187], v[104:107]
	v_mfma_f32_16x16x32_f16 v[108:111], v[196:199], v[184:187], v[108:111]
	v_mfma_f32_16x16x32_f16 v[112:115], v[200:203], v[184:187], v[112:115]
	v_mfma_f32_16x16x32_f16 v[116:119], v[204:207], v[184:187], v[116:119]
	s_waitcnt lgkmcnt(7)
	ds_read_b128 v[172:175], v20
	ds_read_b128 v[192:195], v22
	ds_read_b128 v[196:199], v22 offset:2048
	ds_read_b128 v[200:203], v22 offset:4096
	ds_read_b128 v[204:207], v22 offset:6144
	ds_read_b128 v[176:179], v20 offset:2048
	ds_read_b128 v[180:183], v20 offset:4096
	ds_read_b128 v[184:187], v20 offset:6144
	s_waitcnt lgkmcnt(14)
	v_mfma_f32_16x16x32_f16 v[56:59], v[156:159], v[136:139], v[56:59]
	s_waitcnt lgkmcnt(13)
	v_mfma_f32_16x16x32_f16 v[60:63], v[160:163], v[136:139], v[60:63]
	s_waitcnt lgkmcnt(12)
	v_mfma_f32_16x16x32_f16 v[64:67], v[164:167], v[136:139], v[64:67]
	s_waitcnt lgkmcnt(11)
	v_mfma_f32_16x16x32_f16 v[68:71], v[168:171], v[136:139], v[68:71]
	s_waitcnt lgkmcnt(10)
	v_mfma_f32_16x16x32_f16 v[72:75], v[156:159], v[140:143], v[72:75]
	v_mfma_f32_16x16x32_f16 v[76:79], v[160:163], v[140:143], v[76:79]
	v_mfma_f32_16x16x32_f16 v[80:83], v[164:167], v[140:143], v[80:83]
	v_mfma_f32_16x16x32_f16 v[84:87], v[168:171], v[140:143], v[84:87]
	s_waitcnt lgkmcnt(9)
	v_mfma_f32_16x16x32_f16 v[88:91], v[156:159], v[144:147], v[88:91]
	v_mfma_f32_16x16x32_f16 v[92:95], v[160:163], v[144:147], v[92:95]
	v_mfma_f32_16x16x32_f16 v[96:99], v[164:167], v[144:147], v[96:99]
	v_mfma_f32_16x16x32_f16 v[100:103], v[168:171], v[144:147], v[100:103]
	s_waitcnt lgkmcnt(8)
	v_mfma_f32_16x16x32_f16 v[104:107], v[156:159], v[148:151], v[104:107]
	v_mfma_f32_16x16x32_f16 v[108:111], v[160:163], v[148:151], v[108:111]
	v_mfma_f32_16x16x32_f16 v[112:115], v[164:167], v[148:151], v[112:115]
	v_mfma_f32_16x16x32_f16 v[116:119], v[168:171], v[148:151], v[116:119]
	s_waitcnt vmcnt(0) lgkmcnt(0)
	s_barrier
	s_waitcnt lgkmcnt(7)
	ds_read_b128 v[136:139], v15
	ds_read_b128 v[156:159], v17
	ds_read_b128 v[160:163], v17 offset:2048
	ds_read_b128 v[164:167], v17 offset:4096
	ds_read_b128 v[168:171], v17 offset:6144
	ds_read_b128 v[140:143], v15 offset:2048
	ds_read_b128 v[144:147], v15 offset:4096
	ds_read_b128 v[148:151], v15 offset:6144
	s_waitcnt lgkmcnt(14)
	v_mfma_f32_16x16x32_f16 v[56:59], v[192:195], v[172:175], v[56:59]
	s_waitcnt lgkmcnt(13)
	v_mfma_f32_16x16x32_f16 v[60:63], v[196:199], v[172:175], v[60:63]
	s_waitcnt lgkmcnt(12)
	v_mfma_f32_16x16x32_f16 v[64:67], v[200:203], v[172:175], v[64:67]
	s_waitcnt lgkmcnt(11)
	v_mfma_f32_16x16x32_f16 v[68:71], v[204:207], v[172:175], v[68:71]
	s_waitcnt lgkmcnt(10)
	v_mfma_f32_16x16x32_f16 v[72:75], v[192:195], v[176:179], v[72:75]
	v_mfma_f32_16x16x32_f16 v[76:79], v[196:199], v[176:179], v[76:79]
	v_mfma_f32_16x16x32_f16 v[80:83], v[200:203], v[176:179], v[80:83]
	v_mfma_f32_16x16x32_f16 v[84:87], v[204:207], v[176:179], v[84:87]
	s_waitcnt lgkmcnt(9)
	v_mfma_f32_16x16x32_f16 v[88:91], v[192:195], v[180:183], v[88:91]
	v_mfma_f32_16x16x32_f16 v[92:95], v[196:199], v[180:183], v[92:95]
	v_mfma_f32_16x16x32_f16 v[96:99], v[200:203], v[180:183], v[96:99]
	v_mfma_f32_16x16x32_f16 v[100:103], v[204:207], v[180:183], v[100:103]
	s_waitcnt lgkmcnt(8)
	v_mfma_f32_16x16x32_f16 v[104:107], v[192:195], v[184:187], v[104:107]
	v_mfma_f32_16x16x32_f16 v[108:111], v[196:199], v[184:187], v[108:111]
	v_mfma_f32_16x16x32_f16 v[112:115], v[200:203], v[184:187], v[112:115]
	v_mfma_f32_16x16x32_f16 v[116:119], v[204:207], v[184:187], v[116:119]
	s_waitcnt lgkmcnt(7)
	ds_read_b128 v[172:175], v16
	ds_read_b128 v[192:195], v18
	ds_read_b128 v[196:199], v18 offset:2048
	ds_read_b128 v[200:203], v18 offset:4096
	ds_read_b128 v[204:207], v18 offset:6144
	ds_read_b128 v[176:179], v16 offset:2048
	ds_read_b128 v[180:183], v16 offset:4096
	ds_read_b128 v[184:187], v16 offset:6144
	s_waitcnt lgkmcnt(14)
	v_mfma_f32_16x16x32_f16 v[56:59], v[156:159], v[136:139], v[56:59]
	s_waitcnt lgkmcnt(13)
	v_mfma_f32_16x16x32_f16 v[60:63], v[160:163], v[136:139], v[60:63]
	s_waitcnt lgkmcnt(12)
	v_mfma_f32_16x16x32_f16 v[64:67], v[164:167], v[136:139], v[64:67]
	s_waitcnt lgkmcnt(11)
	v_mfma_f32_16x16x32_f16 v[68:71], v[168:171], v[136:139], v[68:71]
	s_waitcnt lgkmcnt(10)
	v_mfma_f32_16x16x32_f16 v[72:75], v[156:159], v[140:143], v[72:75]
	v_mfma_f32_16x16x32_f16 v[76:79], v[160:163], v[140:143], v[76:79]
	v_mfma_f32_16x16x32_f16 v[80:83], v[164:167], v[140:143], v[80:83]
	v_mfma_f32_16x16x32_f16 v[84:87], v[168:171], v[140:143], v[84:87]
	s_waitcnt lgkmcnt(9)
	v_mfma_f32_16x16x32_f16 v[88:91], v[156:159], v[144:147], v[88:91]
	v_mfma_f32_16x16x32_f16 v[92:95], v[160:163], v[144:147], v[92:95]
	v_mfma_f32_16x16x32_f16 v[96:99], v[164:167], v[144:147], v[96:99]
	v_mfma_f32_16x16x32_f16 v[100:103], v[168:171], v[144:147], v[100:103]
	s_waitcnt lgkmcnt(8)
	v_mfma_f32_16x16x32_f16 v[104:107], v[156:159], v[148:151], v[104:107]
	v_mfma_f32_16x16x32_f16 v[108:111], v[160:163], v[148:151], v[108:111]
	v_mfma_f32_16x16x32_f16 v[112:115], v[164:167], v[148:151], v[112:115]
	v_mfma_f32_16x16x32_f16 v[116:119], v[168:171], v[148:151], v[116:119]
	s_waitcnt lgkmcnt(6)
	v_mfma_f32_16x16x32_f16 v[56:59], v[192:195], v[172:175], v[56:59]
	s_waitcnt lgkmcnt(5)
	v_mfma_f32_16x16x32_f16 v[60:63], v[196:199], v[172:175], v[60:63]
	s_waitcnt lgkmcnt(4)
	v_mfma_f32_16x16x32_f16 v[64:67], v[200:203], v[172:175], v[64:67]
	s_waitcnt lgkmcnt(3)
	v_mfma_f32_16x16x32_f16 v[68:71], v[204:207], v[172:175], v[68:71]
	s_waitcnt lgkmcnt(2)
	v_mfma_f32_16x16x32_f16 v[72:75], v[192:195], v[176:179], v[72:75]
	v_mfma_f32_16x16x32_f16 v[76:79], v[196:199], v[176:179], v[76:79]
	v_mfma_f32_16x16x32_f16 v[80:83], v[200:203], v[176:179], v[80:83]
	v_mfma_f32_16x16x32_f16 v[84:87], v[204:207], v[176:179], v[84:87]
	s_waitcnt lgkmcnt(1)
	v_mfma_f32_16x16x32_f16 v[88:91], v[192:195], v[180:183], v[88:91]
	v_mfma_f32_16x16x32_f16 v[92:95], v[196:199], v[180:183], v[92:95]
	v_mfma_f32_16x16x32_f16 v[96:99], v[200:203], v[180:183], v[96:99]
	v_mfma_f32_16x16x32_f16 v[100:103], v[204:207], v[180:183], v[100:103]
	s_waitcnt lgkmcnt(0)
	v_mfma_f32_16x16x32_f16 v[104:107], v[192:195], v[184:187], v[104:107]
	v_mfma_f32_16x16x32_f16 v[108:111], v[196:199], v[184:187], v[108:111]
	v_mfma_f32_16x16x32_f16 v[112:115], v[200:203], v[184:187], v[112:115]
	v_mfma_f32_16x16x32_f16 v[116:119], v[204:207], v[184:187], v[116:119]
	s_nop 7
	s_nop 1
	v_mov_b32_e32 v213, s19
	v_pk_add_f32 v[56:57], v[56:57], v[24:25]
	v_pk_add_f32 v[58:59], v[58:59], v[26:27]
	v_pk_add_f32 v[60:61], v[60:61], v[28:29]
	v_pk_add_f32 v[62:63], v[62:63], v[30:31]
	v_pk_add_f32 v[64:65], v[64:65], v[32:33]
	v_pk_add_f32 v[66:67], v[66:67], v[34:35]
	v_pk_add_f32 v[68:69], v[68:69], v[36:37]
	v_pk_add_f32 v[70:71], v[70:71], v[38:39]
	v_pk_mul_f32 v[208:209], v[56:57], v[56:57]
	v_pk_fma_f32 v[208:209], v[58:59], v[58:59], v[208:209]
	v_pk_fma_f32 v[208:209], v[60:61], v[60:61], v[208:209]
	v_pk_fma_f32 v[208:209], v[62:63], v[62:63], v[208:209]
	v_pk_fma_f32 v[208:209], v[64:65], v[64:65], v[208:209]
	v_pk_fma_f32 v[208:209], v[66:67], v[66:67], v[208:209]
	v_pk_fma_f32 v[208:209], v[68:69], v[68:69], v[208:209]
	v_pk_fma_f32 v[208:209], v[70:71], v[70:71], v[208:209]
	v_add_f32_e32 v208, v208, v209
	v_mov_b32_e32 v209, v208
	s_nop 1
	v_permlane16_swap_b32_e32 v208, v209
	v_add_f32_e32 v208, v208, v209
	v_mov_b32_e32 v209, v208
	s_nop 1
	v_permlane32_swap_b32_e32 v208, v209
	v_add_f32_e32 v208, v208, v209
	v_mov_b32_e32 v210, 0x358637bd
	v_fmac_f32_e32 v210, 0x3c800000, v208
	v_rsq_f32_e32 v210, v210
	s_add_u32 s24, s29, 0
	s_lshr_b32 s8, s24, 1
	s_lshl_b32 s8, s8, 12
	s_and_b32 s24, s24, 1
	s_lshl_b32 s24, s24, 8
	s_add_u32 s8, s8, s24
	v_mul_f32_e32 v210, v213, v210
	v_add_u32_e32 v212, s8, v23
	v_pk_mul_f32 v[56:57], v[56:57], v[210:211] op_sel_hi:[1,0]
	v_pk_mul_f32 v[58:59], v[58:59], v[210:211] op_sel_hi:[1,0]
	v_pk_mul_f32 v[56:57], v[56:57], v[40:41]
	v_pk_mul_f32 v[58:59], v[58:59], v[42:43]
	v_cvt_pk_f16_f32 v56, v56, v57
	v_cvt_pk_f16_f32 v57, v58, v59
	global_store_dwordx2 v212, v[56:57], s[22:23] offset:0
	v_pk_mul_f32 v[60:61], v[60:61], v[210:211] op_sel_hi:[1,0]
	v_pk_mul_f32 v[62:63], v[62:63], v[210:211] op_sel_hi:[1,0]
	v_pk_mul_f32 v[60:61], v[60:61], v[44:45]
	v_pk_mul_f32 v[62:63], v[62:63], v[46:47]
	v_cvt_pk_f16_f32 v60, v60, v61
	v_cvt_pk_f16_f32 v61, v62, v63
	global_store_dwordx2 v212, v[60:61], s[22:23] offset:1024
	v_pk_mul_f32 v[64:65], v[64:65], v[210:211] op_sel_hi:[1,0]
	v_pk_mul_f32 v[66:67], v[66:67], v[210:211] op_sel_hi:[1,0]
	v_pk_mul_f32 v[64:65], v[64:65], v[48:49]
	v_pk_mul_f32 v[66:67], v[66:67], v[50:51]
	v_cvt_pk_f16_f32 v64, v64, v65
	v_cvt_pk_f16_f32 v65, v66, v67
	global_store_dwordx2 v212, v[64:65], s[22:23] offset:2048
	v_pk_mul_f32 v[68:69], v[68:69], v[210:211] op_sel_hi:[1,0]
	v_pk_mul_f32 v[70:71], v[70:71], v[210:211] op_sel_hi:[1,0]
	v_pk_mul_f32 v[68:69], v[68:69], v[52:53]
	v_pk_mul_f32 v[70:71], v[70:71], v[54:55]
	v_cvt_pk_f16_f32 v68, v68, v69
	v_cvt_pk_f16_f32 v69, v70, v71
	global_store_dwordx2 v212, v[68:69], s[22:23] offset:3072
	v_pk_add_f32 v[72:73], v[72:73], v[24:25]
	v_pk_add_f32 v[74:75], v[74:75], v[26:27]
	v_pk_add_f32 v[76:77], v[76:77], v[28:29]
	v_pk_add_f32 v[78:79], v[78:79], v[30:31]
	v_pk_add_f32 v[80:81], v[80:81], v[32:33]
	v_pk_add_f32 v[82:83], v[82:83], v[34:35]
	v_pk_add_f32 v[84:85], v[84:85], v[36:37]
	v_pk_add_f32 v[86:87], v[86:87], v[38:39]
	v_pk_mul_f32 v[208:209], v[72:73], v[72:73]
	v_pk_fma_f32 v[208:209], v[74:75], v[74:75], v[208:209]
	v_pk_fma_f32 v[208:209], v[76:77], v[76:77], v[208:209]
	v_pk_fma_f32 v[208:209], v[78:79], v[78:79], v[208:209]
	v_pk_fma_f32 v[208:209], v[80:81], v[80:81], v[208:209]
	v_pk_fma_f32 v[208:209], v[82:83], v[82:83], v[208:209]
	v_pk_fma_f32 v[208:209], v[84:85], v[84:85], v[208:209]
	v_pk_fma_f32 v[208:209], v[86:87], v[86:87], v[208:209]
	v_add_f32_e32 v208, v208, v209
	v_mov_b32_e32 v209, v208
	s_nop 1
	v_permlane16_swap_b32_e32 v208, v209
	v_add_f32_e32 v208, v208, v209
	v_mov_b32_e32 v209, v208
	s_nop 1
	v_permlane32_swap_b32_e32 v208, v209
	v_add_f32_e32 v208, v208, v209
	v_mov_b32_e32 v210, 0x358637bd
	v_fmac_f32_e32 v210, 0x3c800000, v208
	v_rsq_f32_e32 v210, v210
	s_add_u32 s24, s29, 1
	s_lshr_b32 s8, s24, 1
	s_lshl_b32 s8, s8, 12
	s_and_b32 s24, s24, 1
	s_lshl_b32 s24, s24, 8
	s_add_u32 s8, s8, s24
	v_mul_f32_e32 v210, v213, v210
	v_add_u32_e32 v212, s8, v23
	v_pk_mul_f32 v[72:73], v[72:73], v[210:211] op_sel_hi:[1,0]
	v_pk_mul_f32 v[74:75], v[74:75], v[210:211] op_sel_hi:[1,0]
	v_pk_mul_f32 v[72:73], v[72:73], v[40:41]
	v_pk_mul_f32 v[74:75], v[74:75], v[42:43]
	v_cvt_pk_f16_f32 v72, v72, v73
	v_cvt_pk_f16_f32 v73, v74, v75
	global_store_dwordx2 v212, v[72:73], s[22:23] offset:0
	v_pk_mul_f32 v[76:77], v[76:77], v[210:211] op_sel_hi:[1,0]
	v_pk_mul_f32 v[78:79], v[78:79], v[210:211] op_sel_hi:[1,0]
	v_pk_mul_f32 v[76:77], v[76:77], v[44:45]
	v_pk_mul_f32 v[78:79], v[78:79], v[46:47]
	v_cvt_pk_f16_f32 v76, v76, v77
	v_cvt_pk_f16_f32 v77, v78, v79
	global_store_dwordx2 v212, v[76:77], s[22:23] offset:1024
	v_pk_mul_f32 v[80:81], v[80:81], v[210:211] op_sel_hi:[1,0]
	v_pk_mul_f32 v[82:83], v[82:83], v[210:211] op_sel_hi:[1,0]
	v_pk_mul_f32 v[80:81], v[80:81], v[48:49]
	v_pk_mul_f32 v[82:83], v[82:83], v[50:51]
	v_cvt_pk_f16_f32 v80, v80, v81
	v_cvt_pk_f16_f32 v81, v82, v83
	global_store_dwordx2 v212, v[80:81], s[22:23] offset:2048
	v_pk_mul_f32 v[84:85], v[84:85], v[210:211] op_sel_hi:[1,0]
	v_pk_mul_f32 v[86:87], v[86:87], v[210:211] op_sel_hi:[1,0]
	v_pk_mul_f32 v[84:85], v[84:85], v[52:53]
	v_pk_mul_f32 v[86:87], v[86:87], v[54:55]
	v_cvt_pk_f16_f32 v84, v84, v85
	v_cvt_pk_f16_f32 v85, v86, v87
	global_store_dwordx2 v212, v[84:85], s[22:23] offset:3072
	v_pk_add_f32 v[88:89], v[88:89], v[24:25]
	v_pk_add_f32 v[90:91], v[90:91], v[26:27]
	v_pk_add_f32 v[92:93], v[92:93], v[28:29]
	v_pk_add_f32 v[94:95], v[94:95], v[30:31]
	v_pk_add_f32 v[96:97], v[96:97], v[32:33]
	v_pk_add_f32 v[98:99], v[98:99], v[34:35]
	v_pk_add_f32 v[100:101], v[100:101], v[36:37]
	v_pk_add_f32 v[102:103], v[102:103], v[38:39]
	v_pk_mul_f32 v[208:209], v[88:89], v[88:89]
	v_pk_fma_f32 v[208:209], v[90:91], v[90:91], v[208:209]
	v_pk_fma_f32 v[208:209], v[92:93], v[92:93], v[208:209]
	v_pk_fma_f32 v[208:209], v[94:95], v[94:95], v[208:209]
	v_pk_fma_f32 v[208:209], v[96:97], v[96:97], v[208:209]
	v_pk_fma_f32 v[208:209], v[98:99], v[98:99], v[208:209]
	v_pk_fma_f32 v[208:209], v[100:101], v[100:101], v[208:209]
	v_pk_fma_f32 v[208:209], v[102:103], v[102:103], v[208:209]
	v_add_f32_e32 v208, v208, v209
	v_mov_b32_e32 v209, v208
	s_nop 1
	v_permlane16_swap_b32_e32 v208, v209
	v_add_f32_e32 v208, v208, v209
	v_mov_b32_e32 v209, v208
	s_nop 1
	v_permlane32_swap_b32_e32 v208, v209
	v_add_f32_e32 v208, v208, v209
	v_mov_b32_e32 v210, 0x358637bd
	v_fmac_f32_e32 v210, 0x3c800000, v208
	v_rsq_f32_e32 v210, v210
	s_add_u32 s24, s29, 2
	s_lshr_b32 s8, s24, 1
	s_lshl_b32 s8, s8, 12
	s_and_b32 s24, s24, 1
	s_lshl_b32 s24, s24, 8
	s_add_u32 s8, s8, s24
	v_mul_f32_e32 v210, v213, v210
	v_add_u32_e32 v212, s8, v23
	v_pk_mul_f32 v[88:89], v[88:89], v[210:211] op_sel_hi:[1,0]
	v_pk_mul_f32 v[90:91], v[90:91], v[210:211] op_sel_hi:[1,0]
	v_pk_mul_f32 v[88:89], v[88:89], v[40:41]
	v_pk_mul_f32 v[90:91], v[90:91], v[42:43]
	v_cvt_pk_f16_f32 v88, v88, v89
	v_cvt_pk_f16_f32 v89, v90, v91
	global_store_dwordx2 v212, v[88:89], s[22:23] offset:0
	v_pk_mul_f32 v[92:93], v[92:93], v[210:211] op_sel_hi:[1,0]
	v_pk_mul_f32 v[94:95], v[94:95], v[210:211] op_sel_hi:[1,0]
	v_pk_mul_f32 v[92:93], v[92:93], v[44:45]
	v_pk_mul_f32 v[94:95], v[94:95], v[46:47]
	v_cvt_pk_f16_f32 v92, v92, v93
	v_cvt_pk_f16_f32 v93, v94, v95
	global_store_dwordx2 v212, v[92:93], s[22:23] offset:1024
	v_pk_mul_f32 v[96:97], v[96:97], v[210:211] op_sel_hi:[1,0]
	v_pk_mul_f32 v[98:99], v[98:99], v[210:211] op_sel_hi:[1,0]
	v_pk_mul_f32 v[96:97], v[96:97], v[48:49]
	v_pk_mul_f32 v[98:99], v[98:99], v[50:51]
	v_cvt_pk_f16_f32 v96, v96, v97
	v_cvt_pk_f16_f32 v97, v98, v99
	global_store_dwordx2 v212, v[96:97], s[22:23] offset:2048
	v_pk_mul_f32 v[100:101], v[100:101], v[210:211] op_sel_hi:[1,0]
	v_pk_mul_f32 v[102:103], v[102:103], v[210:211] op_sel_hi:[1,0]
	v_pk_mul_f32 v[100:101], v[100:101], v[52:53]
	v_pk_mul_f32 v[102:103], v[102:103], v[54:55]
	v_cvt_pk_f16_f32 v100, v100, v101
	v_cvt_pk_f16_f32 v101, v102, v103
	global_store_dwordx2 v212, v[100:101], s[22:23] offset:3072
	v_pk_add_f32 v[104:105], v[104:105], v[24:25]
	v_pk_add_f32 v[106:107], v[106:107], v[26:27]
	v_pk_add_f32 v[108:109], v[108:109], v[28:29]
	v_pk_add_f32 v[110:111], v[110:111], v[30:31]
	v_pk_add_f32 v[112:113], v[112:113], v[32:33]
	v_pk_add_f32 v[114:115], v[114:115], v[34:35]
	v_pk_add_f32 v[116:117], v[116:117], v[36:37]
	v_pk_add_f32 v[118:119], v[118:119], v[38:39]
	v_pk_mul_f32 v[208:209], v[104:105], v[104:105]
	v_pk_fma_f32 v[208:209], v[106:107], v[106:107], v[208:209]
	v_pk_fma_f32 v[208:209], v[108:109], v[108:109], v[208:209]
	v_pk_fma_f32 v[208:209], v[110:111], v[110:111], v[208:209]
	v_pk_fma_f32 v[208:209], v[112:113], v[112:113], v[208:209]
	v_pk_fma_f32 v[208:209], v[114:115], v[114:115], v[208:209]
	v_pk_fma_f32 v[208:209], v[116:117], v[116:117], v[208:209]
	v_pk_fma_f32 v[208:209], v[118:119], v[118:119], v[208:209]
	v_add_f32_e32 v208, v208, v209
	v_mov_b32_e32 v209, v208
	s_nop 1
	v_permlane16_swap_b32_e32 v208, v209
	v_add_f32_e32 v208, v208, v209
	v_mov_b32_e32 v209, v208
	s_nop 1
	v_permlane32_swap_b32_e32 v208, v209
	v_add_f32_e32 v208, v208, v209
	v_mov_b32_e32 v210, 0x358637bd
	v_fmac_f32_e32 v210, 0x3c800000, v208
	v_rsq_f32_e32 v210, v210
	s_add_u32 s24, s29, 3
	s_lshr_b32 s8, s24, 1
	s_lshl_b32 s8, s8, 12
	s_and_b32 s24, s24, 1
	s_lshl_b32 s24, s24, 8
	s_add_u32 s8, s8, s24
	v_mul_f32_e32 v210, v213, v210
	v_add_u32_e32 v212, s8, v23
	v_pk_mul_f32 v[104:105], v[104:105], v[210:211] op_sel_hi:[1,0]
	v_pk_mul_f32 v[106:107], v[106:107], v[210:211] op_sel_hi:[1,0]
	v_pk_mul_f32 v[104:105], v[104:105], v[40:41]
	v_pk_mul_f32 v[106:107], v[106:107], v[42:43]
	v_cvt_pk_f16_f32 v104, v104, v105
	v_cvt_pk_f16_f32 v105, v106, v107
	global_store_dwordx2 v212, v[104:105], s[22:23] offset:0
	v_pk_mul_f32 v[108:109], v[108:109], v[210:211] op_sel_hi:[1,0]
	v_pk_mul_f32 v[110:111], v[110:111], v[210:211] op_sel_hi:[1,0]
	v_pk_mul_f32 v[108:109], v[108:109], v[44:45]
	v_pk_mul_f32 v[110:111], v[110:111], v[46:47]
	v_cvt_pk_f16_f32 v108, v108, v109
	v_cvt_pk_f16_f32 v109, v110, v111
	global_store_dwordx2 v212, v[108:109], s[22:23] offset:1024
	v_pk_mul_f32 v[112:113], v[112:113], v[210:211] op_sel_hi:[1,0]
	v_pk_mul_f32 v[114:115], v[114:115], v[210:211] op_sel_hi:[1,0]
	v_pk_mul_f32 v[112:113], v[112:113], v[48:49]
	v_pk_mul_f32 v[114:115], v[114:115], v[50:51]
	v_cvt_pk_f16_f32 v112, v112, v113
	v_cvt_pk_f16_f32 v113, v114, v115
	global_store_dwordx2 v212, v[112:113], s[22:23] offset:2048
	v_pk_mul_f32 v[116:117], v[116:117], v[210:211] op_sel_hi:[1,0]
	v_pk_mul_f32 v[118:119], v[118:119], v[210:211] op_sel_hi:[1,0]
	v_pk_mul_f32 v[116:117], v[116:117], v[52:53]
	v_pk_mul_f32 v[118:119], v[118:119], v[54:55]
	v_cvt_pk_f16_f32 v116, v116, v117
	v_cvt_pk_f16_f32 v117, v118, v119
	global_store_dwordx2 v212, v[116:117], s[22:23] offset:3072
	s_branch .Lpf_done
.Lpf_vVA:
	s_mul_i32 s25, s25, 0x50
	s_add_u32 s29, s10, s25
	s_lshr_b32 s29, s29, 4
	v_add_u32_e32 v5, s25, v3
	v_lshlrev_b32_e32 v5, 7, v5
	v_add_u32_e32 v15, v5, v6
	v_add_u32_e32 v16, v5, v7
	v_add_u32_e32 v5, 0x9000, v9
	v_add_u32_e32 v17, v5, v6
	v_add_u32_e32 v18, v5, v7
	v_add_u32_e32 v19, 0x1a000, v15
	v_add_u32_e32 v20, 0x1a000, v16
	v_add_u32_e32 v21, 0x1a000, v17
	v_add_u32_e32 v22, 0x1a000, v18
	v_lshlrev_b32_e32 v5, 2, v3
	global_load_dword v24, v5, s[14:15] offset:0
	global_load_dword v26, v5, s[14:15] offset:64
	global_load_dword v28, v5, s[14:15] offset:128
	global_load_dword v30, v5, s[14:15] offset:192
	s_add_u32 m0, s28, 0x0
	s_nop 0
	global_load_lds_dwordx4 v10, s[4:5]
	s_add_u32 m0, s28, 0x2000
	s_nop 0
	global_load_lds_dwordx4 v11, s[4:5]
	s_add_u32 m0, s28, 0x4000
	s_nop 0
	global_load_lds_dwordx4 v12, s[4:5]
	s_add_u32 m0, s28, 0x6000
	s_nop 0
	global_load_lds_dwordx4 v13, s[4:5]
	s_add_u32 m0, s28, 0x8000
	s_nop 0
	global_load_lds_dwordx4 v14, s[4:5]
	s_add_u32 s4, s4, s20
	s_addc_u32 s5, s5, 0
	s_add_u32 m0, s28, 0x9000
	s_nop 0
	global_load_lds_dwordx4 v10, s[6:7]
	s_add_u32 m0, s28, 0xb000
	s_nop 0
	global_load_lds_dwordx4 v11, s[6:7]
	s_add_u32 s6, s6, s20
	s_addc_u32 s7, s7, 0
	s_add_u32 m0, s28, 0xd000
	s_nop 0
	global_load_lds_dwordx4 v10, s[4:5]
	s_add_u32 m0, s28, 0xf000
	s_nop 0
	global_load_lds_dwordx4 v11, s[4:5]
	s_add_u32 m0, s28, 0x11000
	s_nop 0
	global_load_lds_dwordx4 v12, s[4:5]
	s_add_u32 m0, s28, 0x13000
	s_nop 0
	global_load_lds_dwordx4 v13, s[4:5]
	s_add_u32 m0, s28, 0x15000
	s_nop 0
	global_load_lds_dwordx4 v14, s[4:5]
	s_add_u32 s4, s4, s20
	s_addc_u32 s5, s5, 0
	s_add_u32 m0, s28, 0x16000
	s_nop 0
	global_load_lds_dwordx4 v10, s[6:7]
	s_add_u32 m0, s28, 0x18000
	s_nop 0
	global_load_lds_dwordx4 v11, s[6:7]
	s_add_u32 s6, s6, s20
	s_addc_u32 s7, s7, 0
	s_waitcnt vmcnt(7) lgkmcnt(0)
	s_barrier
	s_waitcnt lgkmcnt(6)
	ds_read_b128 v[136:139], v15
	ds_read_b128 v[156:159], v17
	ds_read_b128 v[160:163], v17 offset:2048
	ds_read_b128 v[164:167], v17 offset:4096
	ds_read_b128 v[168:171], v17 offset:6144
	ds_read_b128 v[140:143], v15 offset:2048
	ds_read_b128 v[144:147], v15 offset:4096
	ds_read_b128 v[148:151], v15 offset:6144
	ds_read_b128 v[152:155], v15 offset:8192
	s_waitcnt lgkmcnt(6)
	ds_read_b128 v[172:175], v16
	ds_read_b128 v[192:195], v18
	ds_read_b128 v[196:199], v18 offset:2048
	ds_read_b128 v[200:203], v18 offset:4096
	ds_read_b128 v[204:207], v18 offset:6144
	ds_read_b128 v[176:179], v16 offset:2048
	ds_read_b128 v[180:183], v16 offset:4096
	ds_read_b128 v[184:187], v16 offset:6144
	ds_read_b128 v[188:191], v16 offset:8192
	v_mfma_f32_16x16x32_f16 v[56:59], v[136:139], v[156:159], 0
	s_add_u32 m0, s28, 0x1a000
	s_nop 0
	global_load_lds_dwordx4 v10, s[4:5]
	s_waitcnt lgkmcnt(15)
	v_mfma_f32_16x16x32_f16 v[60:63], v[136:139], v[160:163], 0
	s_waitcnt lgkmcnt(14)
	v_mfma_f32_16x16x32_f16 v[64:67], v[136:139], v[164:167], 0
	s_add_u32 m0, s28, 0x1c000
	s_nop 0
	global_load_lds_dwordx4 v11, s[4:5]
	s_waitcnt lgkmcnt(13)
	v_mfma_f32_16x16x32_f16 v[68:71], v[136:139], v[168:171], 0
	s_waitcnt lgkmcnt(12)
	v_mfma_f32_16x16x32_f16 v[72:75], v[140:143], v[156:159], 0
	v_mfma_f32_16x16x32_f16 v[76:79], v[140:143], v[160:163], 0
	s_add_u32 m0, s28, 0x1e000
	s_nop 0
	global_load_lds_dwordx4 v12, s[4:5]
	v_mfma_f32_16x16x32_f16 v[80:83], v[140:143], v[164:167], 0
	v_mfma_f32_16x16x32_f16 v[84:87], v[140:143], v[168:171], 0
	s_waitcnt lgkmcnt(11)
	v_mfma_f32_16x16x32_f16 v[88:91], v[144:147], v[156:159], 0
	s_add_u32 m0, s28, 0x20000
	s_nop 0
	global_load_lds_dwordx4 v13, s[4:5]
	v_mfma_f32_16x16x32_f16 v[92:95], v[144:147], v[160:163], 0
	v_mfma_f32_16x16x32_f16 v[96:99], v[144:147], v[164:167], 0
	v_mfma_f32_16x16x32_f16 v[100:103], v[144:147], v[168:171], 0
	s_add_u32 m0, s28, 0x22000
	s_nop 0
	global_load_lds_dwordx4 v14, s[4:5]
	s_add_u32 s4, s4, s20
	s_addc_u32 s5, s5, 0
	s_waitcnt lgkmcnt(10)
	v_mfma_f32_16x16x32_f16 v[104:107], v[148:151], v[156:159], 0
	v_mfma_f32_16x16x32_f16 v[108:111], v[148:151], v[160:163], 0
	v_mfma_f32_16x16x32_f16 v[112:115], v[148:151], v[164:167], 0
	s_add_u32 m0, s28, 0x23000
	s_nop 0
	global_load_lds_dwordx4 v10, s[6:7]
	v_mfma_f32_16x16x32_f16 v[116:119], v[148:151], v[168:171], 0
	s_waitcnt lgkmcnt(9)
	v_mfma_f32_16x16x32_f16 v[120:123], v[152:155], v[156:159], 0
	v_mfma_f32_16x16x32_f16 v[124:127], v[152:155], v[160:163], 0
	s_add_u32 m0, s28, 0x25000
	s_nop 0
	global_load_lds_dwordx4 v11, s[6:7]
	s_add_u32 s6, s6, s20
	s_addc_u32 s7, s7, 0
	v_mfma_f32_16x16x32_f16 v[128:131], v[152:155], v[164:167], 0
	v_mfma_f32_16x16x32_f16 v[132:135], v[152:155], v[168:171], 0
	s_waitcnt vmcnt(7) lgkmcnt(0)
	s_barrier
	s_waitcnt lgkmcnt(6)
	ds_read_b128 v[136:139], v15 offset:53248
	ds_read_b128 v[156:159], v17 offset:53248
	ds_read_b128 v[160:163], v17 offset:55296
	ds_read_b128 v[164:167], v17 offset:57344
	ds_read_b128 v[168:171], v17 offset:59392
	ds_read_b128 v[140:143], v15 offset:55296
	ds_read_b128 v[144:147], v15 offset:57344
	ds_read_b128 v[148:151], v15 offset:59392
	ds_read_b128 v[152:155], v15 offset:61440
	v_mfma_f32_16x16x32_f16 v[56:59], v[172:175], v[192:195], v[56:59]
	s_add_u32 m0, s28, 0x0
	s_nop 0
	global_load_lds_dwordx4 v10, s[4:5]
	s_waitcnt lgkmcnt(15)
	v_mfma_f32_16x16x32_f16 v[60:63], v[172:175], v[196:199], v[60:63]
	s_waitcnt lgkmcnt(14)
	v_mfma_f32_16x16x32_f16 v[64:67], v[172:175], v[200:203], v[64:67]
	s_waitcnt lgkmcnt(13)
	v_mfma_f32_16x16x32_f16 v[68:71], v[172:175], v[204:207], v[68:71]
	s_waitcnt lgkmcnt(12)
	v_mfma_f32_16x16x32_f16 v[72:75], v[176:179], v[192:195], v[72:75]
	v_mfma_f32_16x16x32_f16 v[76:79], v[176:179], v[196:199], v[76:79]
	s_add_u32 m0, s28, 0x2000
	s_nop 0
	global_load_lds_dwordx4 v11, s[4:5]
	v_mfma_f32_16x16x32_f16 v[80:83], v[176:179], v[200:203], v[80:83]
	v_mfma_f32_16x16x32_f16 v[84:87], v[176:179], v[204:207], v[84:87]
	s_waitcnt lgkmcnt(11)
	v_mfma_f32_16x16x32_f16 v[88:91], v[180:183], v[192:195], v[88:91]
	v_mfma_f32_16x16x32_f16 v[92:95], v[180:183], v[196:199], v[92:95]
	v_mfma_f32_16x16x32_f16 v[96:99], v[180:183], v[200:203], v[96:99]
	s_add_u32 m0, s28, 0x4000
	s_nop 0
	global_load_lds_dwordx4 v12, s[4:5]
	v_mfma_f32_16x16x32_f16 v[100:103], v[180:183], v[204:207], v[100:103]
	s_waitcnt lgkmcnt(10)
	v_mfma_f32_16x16x32_f16 v[104:107], v[184:187], v[192:195], v[104:107]
	v_mfma_f32_16x16x32_f16 v[108:111], v[184:187], v[196:199], v[108:111]
	v_mfma_f32_16x16x32_f16 v[112:115], v[184:187], v[200:203], v[112:115]
	v_mfma_f32_16x16x32_f16 v[116:119], v[184:187], v[204:207], v[116:119]
	s_add_u32 m0, s28, 0x6000
	s_nop 0
	global_load_lds_dwordx4 v13, s[4:5]
	s_waitcnt lgkmcnt(9)
	v_mfma_f32_16x16x32_f16 v[120:123], v[188:191], v[192:195], v[120:123]
	v_mfma_f32_16x16x32_f16 v[124:127], v[188:191], v[196:199], v[124:127]
	v_mfma_f32_16x16x32_f16 v[128:131], v[188:191], v[200:203], v[128:131]
	v_mfma_f32_16x16x32_f16 v[132:135], v[188:191], v[204:207], v[132:135]
	s_waitcnt lgkmcnt(6)
	ds_read_b128 v[172:175], v16 offset:53248
	ds_read_b128 v[192:195], v18 offset:53248
	ds_read_b128 v[196:199], v18 offset:55296
	ds_read_b128 v[200:203], v18 offset:57344
	ds_read_b128 v[204:207], v18 offset:59392
	ds_read_b128 v[176:179], v16 offset:55296
	ds_read_b128 v[180:183], v16 offset:57344
	ds_read_b128 v[184:187], v16 offset:59392
	ds_read_b128 v[188:191], v16 offset:61440
	v_mfma_f32_16x16x32_f16 v[56:59], v[136:139], v[156:159], v[56:59]
	s_add_u32 m0, s28, 0x8000
	s_nop 0
	global_load_lds_dwordx4 v14, s[4:5]
	s_add_u32 s4, s4, s20
	s_addc_u32 s5, s5, 0
	s_waitcnt lgkmcnt(15)
	v_mfma_f32_16x16x32_f16 v[60:63], v[136:139], v[160:163], v[60:63]
	s_waitcnt lgkmcnt(14)
	v_mfma_f32_16x16x32_f16 v[64:67], v[136:139], v[164:167], v[64:67]
	s_waitcnt lgkmcnt(13)
	v_mfma_f32_16x16x32_f16 v[68:71], v[136:139], v[168:171], v[68:71]
	s_waitcnt lgkmcnt(12)
	v_mfma_f32_16x16x32_f16 v[72:75], v[140:143], v[156:159], v[72:75]
	v_mfma_f32_16x16x32_f16 v[76:79], v[140:143], v[160:163], v[76:79]
	v_mfma_f32_16x16x32_f16 v[80:83], v[140:143], v[164:167], v[80:83]
	s_add_u32 m0, s28, 0x9000
	s_nop 0
	global_load_lds_dwordx4 v10, s[6:7]
	v_mfma_f32_16x16x32_f16 v[84:87], v[140:143], v[168:171], v[84:87]
	s_waitcnt lgkmcnt(11)
	v_mfma_f32_16x16x32_f16 v[88:91], v[144:147], v[156:159], v[88:91]
	v_mfma_f32_16x16x32_f16 v[92:95], v[144:147], v[160:163], v[92:95]
	v_mfma_f32_16x16x32_f16 v[96:99], v[144:147], v[164:167], v[96:99]
	v_mfma_f32_16x16x32_f16 v[100:103], v[144:147], v[168:171], v[100:103]
	s_waitcnt lgkmcnt(10)
	v_mfma_f32_16x16x32_f16 v[104:107], v[148:151], v[156:159], v[104:107]
	v_mfma_f32_16x16x32_f16 v[108:111], v[148:151], v[160:163], v[108:111]
	s_add_u32 m0, s28, 0xb000
	s_nop 0
	global_load_lds_dwordx4 v11, s[6:7]
	s_add_u32 s6, s6, s20
	s_addc_u32 s7, s7, 0
	v_mfma_f32_16x16x32_f16 v[112:115], v[148:151], v[164:167], v[112:115]
	v_mfma_f32_16x16x32_f16 v[116:119], v[148:151], v[168:171], v[116:119]
	s_waitcnt lgkmcnt(9)
	v_mfma_f32_16x16x32_f16 v[120:123], v[152:155], v[156:159], v[120:123]
	v_mfma_f32_16x16x32_f16 v[124:127], v[152:155], v[160:163], v[124:127]
	v_mfma_f32_16x16x32_f16 v[128:131], v[152:155], v[164:167], v[128:131]
	v_mfma_f32_16x16x32_f16 v[132:135], v[152:155], v[168:171], v[132:135]
	s_waitcnt vmcnt(7) lgkmcnt(0)
	s_barrier
	s_waitcnt lgkmcnt(6)
	ds_read_b128 v[136:139], v19
	ds_read_b128 v[156:159], v21
	ds_read_b128 v[160:163], v21 offset:2048
	ds_read_b128 v[164:167], v21 offset:4096
	ds_read_b128 v[168:171], v21 offset:6144
	ds_read_b128 v[140:143], v19 offset:2048
	ds_read_b128 v[144:147], v19 offset:4096
	ds_read_b128 v[148:151], v19 offset:6144
	ds_read_b128 v[152:155], v19 offset:8192
	v_mfma_f32_16x16x32_f16 v[56:59], v[172:175], v[192:195], v[56:59]
	s_add_u32 m0, s28, 0xd000
	s_nop 0
	global_load_lds_dwordx4 v10, s[4:5]
	s_waitcnt lgkmcnt(15)
	v_mfma_f32_16x16x32_f16 v[60:63], v[172:175], v[196:199], v[60:63]
	s_waitcnt lgkmcnt(14)
	v_mfma_f32_16x16x32_f16 v[64:67], v[172:175], v[200:203], v[64:67]
	s_waitcnt lgkmcnt(13)
	v_mfma_f32_16x16x32_f16 v[68:71], v[172:175], v[204:207], v[68:71]
	s_waitcnt lgkmcnt(12)
	v_mfma_f32_16x16x32_f16 v[72:75], v[176:179], v[192:195], v[72:75]
	v_mfma_f32_16x16x32_f16 v[76:79], v[176:179], v[196:199], v[76:79]
	s_add_u32 m0, s28, 0xf000
	s_nop 0
	global_load_lds_dwordx4 v11, s[4:5]
	v_mfma_f32_16x16x32_f16 v[80:83], v[176:179], v[200:203], v[80:83]
	v_mfma_f32_16x16x32_f16 v[84:87], v[176:179], v[204:207], v[84:87]
	s_waitcnt lgkmcnt(11)
	v_mfma_f32_16x16x32_f16 v[88:91], v[180:183], v[192:195], v[88:91]
	v_mfma_f32_16x16x32_f16 v[92:95], v[180:183], v[196:199], v[92:95]
	v_mfma_f32_16x16x32_f16 v[96:99], v[180:183], v[200:203], v[96:99]
	s_add_u32 m0, s28, 0x11000
	s_nop 0
	global_load_lds_dwordx4 v12, s[4:5]
	v_mfma_f32_16x16x32_f16 v[100:103], v[180:183], v[204:207], v[100:103]
	s_waitcnt lgkmcnt(10)
	v_mfma_f32_16x16x32_f16 v[104:107], v[184:187], v[192:195], v[104:107]
	v_mfma_f32_16x16x32_f16 v[108:111], v[184:187], v[196:199], v[108:111]
	v_mfma_f32_16x16x32_f16 v[112:115], v[184:187], v[200:203], v[112:115]
	v_mfma_f32_16x16x32_f16 v[116:119], v[184:187], v[204:207], v[116:119]
	s_add_u32 m0, s28, 0x13000
	s_nop 0
	global_load_lds_dwordx4 v13, s[4:5]
	s_waitcnt lgkmcnt(9)
	v_mfma_f32_16x16x32_f16 v[120:123], v[188:191], v[192:195], v[120:123]
	v_mfma_f32_16x16x32_f16 v[124:127], v[188:191], v[196:199], v[124:127]
	v_mfma_f32_16x16x32_f16 v[128:131], v[188:191], v[200:203], v[128:131]
	v_mfma_f32_16x16x32_f16 v[132:135], v[188:191], v[204:207], v[132:135]
	s_waitcnt lgkmcnt(6)
	ds_read_b128 v[172:175], v20
	ds_read_b128 v[192:195], v22
	ds_read_b128 v[196:199], v22 offset:2048
	ds_read_b128 v[200:203], v22 offset:4096
	ds_read_b128 v[204:207], v22 offset:6144
	ds_read_b128 v[176:179], v20 offset:2048
	ds_read_b128 v[180:183], v20 offset:4096
	ds_read_b128 v[184:187], v20 offset:6144
	ds_read_b128 v[188:191], v20 offset:8192
	v_mfma_f32_16x16x32_f16 v[56:59], v[136:139], v[156:159], v[56:59]
	s_add_u32 m0, s28, 0x15000
	s_nop 0
	global_load_lds_dwordx4 v14, s[4:5]
	s_add_u32 s4, s4, s20
	s_addc_u32 s5, s5, 0
	s_waitcnt lgkmcnt(15)
	v_mfma_f32_16x16x32_f16 v[60:63], v[136:139], v[160:163], v[60:63]
	s_waitcnt lgkmcnt(14)
	v_mfma_f32_16x16x32_f16 v[64:67], v[136:139], v[164:167], v[64:67]
	s_waitcnt lgkmcnt(13)
	v_mfma_f32_16x16x32_f16 v[68:71], v[136:139], v[168:171], v[68:71]
	s_waitcnt lgkmcnt(12)
	v_mfma_f32_16x16x32_f16 v[72:75], v[140:143], v[156:159], v[72:75]
	v_mfma_f32_16x16x32_f16 v[76:79], v[140:143], v[160:163], v[76:79]
	v_mfma_f32_16x16x32_f16 v[80:83], v[140:143], v[164:167], v[80:83]
	s_add_u32 m0, s28, 0x16000
	s_nop 0
	global_load_lds_dwordx4 v10, s[6:7]
	v_mfma_f32_16x16x32_f16 v[84:87], v[140:143], v[168:171], v[84:87]
	s_waitcnt lgkmcnt(11)
	v_mfma_f32_16x16x32_f16 v[88:91], v[144:147], v[156:159], v[88:91]
	v_mfma_f32_16x16x32_f16 v[92:95], v[144:147], v[160:163], v[92:95]
	v_mfma_f32_16x16x32_f16 v[96:99], v[144:147], v[164:167], v[96:99]
	v_mfma_f32_16x16x32_f16 v[100:103], v[144:147], v[168:171], v[100:103]
	s_waitcnt lgkmcnt(10)
	v_mfma_f32_16x16x32_f16 v[104:107], v[148:151], v[156:159], v[104:107]
	v_mfma_f32_16x16x32_f16 v[108:111], v[148:151], v[160:163], v[108:111]
	s_add_u32 m0, s28, 0x18000
	s_nop 0
	global_load_lds_dwordx4 v11, s[6:7]
	s_add_u32 s6, s6, s20
	s_addc_u32 s7, s7, 0
	v_mfma_f32_16x16x32_f16 v[112:115], v[148:151], v[164:167], v[112:115]
	v_mfma_f32_16x16x32_f16 v[116:119], v[148:151], v[168:171], v[116:119]
	s_waitcnt lgkmcnt(9)
	v_mfma_f32_16x16x32_f16 v[120:123], v[152:155], v[156:159], v[120:123]
	v_mfma_f32_16x16x32_f16 v[124:127], v[152:155], v[160:163], v[124:127]
	v_mfma_f32_16x16x32_f16 v[128:131], v[152:155], v[164:167], v[128:131]
	v_mfma_f32_16x16x32_f16 v[132:135], v[152:155], v[168:171], v[132:135]
	s_waitcnt vmcnt(7) lgkmcnt(0)
	s_barrier
	s_waitcnt lgkmcnt(6)
	ds_read_b128 v[136:139], v15
	ds_read_b128 v[156:159], v17
	ds_read_b128 v[160:163], v17 offset:2048
	ds_read_b128 v[164:167], v17 offset:4096
	ds_read_b128 v[168:171], v17 offset:6144
	ds_read_b128 v[140:143], v15 offset:2048
	ds_read_b128 v[144:147], v15 offset:4096
	ds_read_b128 v[148:151], v15 offset:6144
	ds_read_b128 v[152:155], v15 offset:8192
	v_mfma_f32_16x16x32_f16 v[56:59], v[172:175], v[192:195], v[56:59]
	s_add_u32 m0, s28, 0x1a000
	s_nop 0
	global_load_lds_dwordx4 v10, s[4:5]
	s_waitcnt lgkmcnt(15)
	v_mfma_f32_16x16x32_f16 v[60:63], v[172:175], v[196:199], v[60:63]
	s_waitcnt lgkmcnt(14)
	v_mfma_f32_16x16x32_f16 v[64:67], v[172:175], v[200:203], v[64:67]
	s_waitcnt lgkmcnt(13)
	v_mfma_f32_16x16x32_f16 v[68:71], v[172:175], v[204:207], v[68:71]
	s_waitcnt lgkmcnt(12)
	v_mfma_f32_16x16x32_f16 v[72:75], v[176:179], v[192:195], v[72:75]
	v_mfma_f32_16x16x32_f16 v[76:79], v[176:179], v[196:199], v[76:79]
	s_add_u32 m0, s28, 0x1c000
	s_nop 0
	global_load_lds_dwordx4 v11, s[4:5]
	v_mfma_f32_16x16x32_f16 v[80:83], v[176:179], v[200:203], v[80:83]
	v_mfma_f32_16x16x32_f16 v[84:87], v[176:179], v[204:207], v[84:87]
	s_waitcnt lgkmcnt(11)
	v_mfma_f32_16x16x32_f16 v[88:91], v[180:183], v[192:195], v[88:91]
	v_mfma_f32_16x16x32_f16 v[92:95], v[180:183], v[196:199], v[92:95]
	v_mfma_f32_16x16x32_f16 v[96:99], v[180:183], v[200:203], v[96:99]
	s_add_u32 m0, s28, 0x1e000
	s_nop 0
	global_load_lds_dwordx4 v12, s[4:5]
	v_mfma_f32_16x16x32_f16 v[100:103], v[180:183], v[204:207], v[100:103]
	s_waitcnt lgkmcnt(10)
	v_mfma_f32_16x16x32_f16 v[104:107], v[184:187], v[192:195], v[104:107]
	v_mfma_f32_16x16x32_f16 v[108:111], v[184:187], v[196:199], v[108:111]
	v_mfma_f32_16x16x32_f16 v[112:115], v[184:187], v[200:203], v[112:115]
	v_mfma_f32_16x16x32_f16 v[116:119], v[184:187], v[204:207], v[116:119]
	s_add_u32 m0, s28, 0x20000
	s_nop 0
	global_load_lds_dwordx4 v13, s[4:5]
	s_waitcnt lgkmcnt(9)
	v_mfma_f32_16x16x32_f16 v[120:123], v[188:191], v[192:195], v[120:123]
	v_mfma_f32_16x16x32_f16 v[124:127], v[188:191], v[196:199], v[124:127]
	v_mfma_f32_16x16x32_f16 v[128:131], v[188:191], v[200:203], v[128:131]
	v_mfma_f32_16x16x32_f16 v[132:135], v[188:191], v[204:207], v[132:135]
	s_waitcnt lgkmcnt(6)
	ds_read_b128 v[172:175], v16
	ds_read_b128 v[192:195], v18
	ds_read_b128 v[196:199], v18 offset:2048
	ds_read_b128 v[200:203], v18 offset:4096
	ds_read_b128 v[204:207], v18 offset:6144
	ds_read_b128 v[176:179], v16 offset:2048
	ds_read_b128 v[180:183], v16 offset:4096
	ds_read_b128 v[184:187], v16 offset:6144
	ds_read_b128 v[188:191], v16 offset:8192
	v_mfma_f32_16x16x32_f16 v[56:59], v[136:139], v[156:159], v[56:59]
	s_add_u32 m0, s28, 0x22000
	s_nop 0
	global_load_lds_dwordx4 v14, s[4:5]
	s_add_u32 s4, s4, s20
	s_addc_u32 s5, s5, 0
	s_waitcnt lgkmcnt(15)
	v_mfma_f32_16x16x32_f16 v[60:63], v[136:139], v[160:163], v[60:63]
	s_waitcnt lgkmcnt(14)
	v_mfma_f32_16x16x32_f16 v[64:67], v[136:139], v[164:167], v[64:67]
	s_waitcnt lgkmcnt(13)
	v_mfma_f32_16x16x32_f16 v[68:71], v[136:139], v[168:171], v[68:71]
	s_waitcnt lgkmcnt(12)
	v_mfma_f32_16x16x32_f16 v[72:75], v[140:143], v[156:159], v[72:75]
	v_mfma_f32_16x16x32_f16 v[76:79], v[140:143], v[160:163], v[76:79]
	v_mfma_f32_16x16x32_f16 v[80:83], v[140:143], v[164:167], v[80:83]
	s_add_u32 m0, s28, 0x23000
	s_nop 0
	global_load_lds_dwordx4 v10, s[6:7]
	v_mfma_f32_16x16x32_f16 v[84:87], v[140:143], v[168:171], v[84:87]
	s_waitcnt lgkmcnt(11)
	v_mfma_f32_16x16x32_f16 v[88:91], v[144:147], v[156:159], v[88:91]
	v_mfma_f32_16x16x32_f16 v[92:95], v[144:147], v[160:163], v[92:95]
	v_mfma_f32_16x16x32_f16 v[96:99], v[144:147], v[164:167], v[96:99]
	v_mfma_f32_16x16x32_f16 v[100:103], v[144:147], v[168:171], v[100:103]
	s_waitcnt lgkmcnt(10)
	v_mfma_f32_16x16x32_f16 v[104:107], v[148:151], v[156:159], v[104:107]
	v_mfma_f32_16x16x32_f16 v[108:111], v[148:151], v[160:163], v[108:111]
	s_add_u32 m0, s28, 0x25000
	s_nop 0
	global_load_lds_dwordx4 v11, s[6:7]
	s_add_u32 s6, s6, s20
	s_addc_u32 s7, s7, 0
	v_mfma_f32_16x16x32_f16 v[112:115], v[148:151], v[164:167], v[112:115]
	v_mfma_f32_16x16x32_f16 v[116:119], v[148:151], v[168:171], v[116:119]
	s_waitcnt lgkmcnt(9)
	v_mfma_f32_16x16x32_f16 v[120:123], v[152:155], v[156:159], v[120:123]
	v_mfma_f32_16x16x32_f16 v[124:127], v[152:155], v[160:163], v[124:127]
	v_mfma_f32_16x16x32_f16 v[128:131], v[152:155], v[164:167], v[128:131]
	v_mfma_f32_16x16x32_f16 v[132:135], v[152:155], v[168:171], v[132:135]
	s_waitcnt vmcnt(7) lgkmcnt(0)
	s_barrier
	s_waitcnt lgkmcnt(6)
	ds_read_b128 v[136:139], v15 offset:53248
	ds_read_b128 v[156:159], v17 offset:53248
	ds_read_b128 v[160:163], v17 offset:55296
	ds_read_b128 v[164:167], v17 offset:57344
	ds_read_b128 v[168:171], v17 offset:59392
	ds_read_b128 v[140:143], v15 offset:55296
	ds_read_b128 v[144:147], v15 offset:57344
	ds_read_b128 v[148:151], v15 offset:59392
	ds_read_b128 v[152:155], v15 offset:61440
	v_mfma_f32_16x16x32_f16 v[56:59], v[172:175], v[192:195], v[56:59]
	s_add_u32 m0, s28, 0x0
	s_nop 0
	global_load_lds_dwordx4 v10, s[4:5]
	s_waitcnt lgkmcnt(15)
	v_mfma_f32_16x16x32_f16 v[60:63], v[172:175], v[196:199], v[60:63]
	s_waitcnt lgkmcnt(14)
	v_mfma_f32_16x16x32_f16 v[64:67], v[172:175], v[200:203], v[64:67]
	s_waitcnt lgkmcnt(13)
	v_mfma_f32_16x16x32_f16 v[68:71], v[172:175], v[204:207], v[68:71]
	s_waitcnt lgkmcnt(12)
	v_mfma_f32_16x16x32_f16 v[72:75], v[176:179], v[192:195], v[72:75]
	v_mfma_f32_16x16x32_f16 v[76:79], v[176:179], v[196:199], v[76:79]
	s_add_u32 m0, s28, 0x2000
	s_nop 0
	global_load_lds_dwordx4 v11, s[4:5]
	v_mfma_f32_16x16x32_f16 v[80:83], v[176:179], v[200:203], v[80:83]
	v_mfma_f32_16x16x32_f16 v[84:87], v[176:179], v[204:207], v[84:87]
	s_waitcnt lgkmcnt(11)
	v_mfma_f32_16x16x32_f16 v[88:91], v[180:183], v[192:195], v[88:91]
	v_mfma_f32_16x16x32_f16 v[92:95], v[180:183], v[196:199], v[92:95]
	v_mfma_f32_16x16x32_f16 v[96:99], v[180:183], v[200:203], v[96:99]
	s_add_u32 m0, s28, 0x4000
	s_nop 0
	global_load_lds_dwordx4 v12, s[4:5]
	v_mfma_f32_16x16x32_f16 v[100:103], v[180:183], v[204:207], v[100:103]
	s_waitcnt lgkmcnt(10)
	v_mfma_f32_16x16x32_f16 v[104:107], v[184:187], v[192:195], v[104:107]
	v_mfma_f32_16x16x32_f16 v[108:111], v[184:187], v[196:199], v[108:111]
	v_mfma_f32_16x16x32_f16 v[112:115], v[184:187], v[200:203], v[112:115]
	v_mfma_f32_16x16x32_f16 v[116:119], v[184:187], v[204:207], v[116:119]
	s_add_u32 m0, s28, 0x6000
	s_nop 0
	global_load_lds_dwordx4 v13, s[4:5]
	s_waitcnt lgkmcnt(9)
	v_mfma_f32_16x16x32_f16 v[120:123], v[188:191], v[192:195], v[120:123]
	v_mfma_f32_16x16x32_f16 v[124:127], v[188:191], v[196:199], v[124:127]
	v_mfma_f32_16x16x32_f16 v[128:131], v[188:191], v[200:203], v[128:131]
	v_mfma_f32_16x16x32_f16 v[132:135], v[188:191], v[204:207], v[132:135]
	s_waitcnt lgkmcnt(6)
	ds_read_b128 v[172:175], v16 offset:53248
	ds_read_b128 v[192:195], v18 offset:53248
	ds_read_b128 v[196:199], v18 offset:55296
	ds_read_b128 v[200:203], v18 offset:57344
	ds_read_b128 v[204:207], v18 offset:59392
	ds_read_b128 v[176:179], v16 offset:55296
	ds_read_b128 v[180:183], v16 offset:57344
	ds_read_b128 v[184:187], v16 offset:59392
	ds_read_b128 v[188:191], v16 offset:61440
	v_mfma_f32_16x16x32_f16 v[56:59], v[136:139], v[156:159], v[56:59]
	s_add_u32 m0, s28, 0x8000
	s_nop 0
	global_load_lds_dwordx4 v14, s[4:5]
	s_add_u32 s4, s4, s20
	s_addc_u32 s5, s5, 0
	s_waitcnt lgkmcnt(15)
	v_mfma_f32_16x16x32_f16 v[60:63], v[136:139], v[160:163], v[60:63]
	s_waitcnt lgkmcnt(14)
	v_mfma_f32_16x16x32_f16 v[64:67], v[136:139], v[164:167], v[64:67]
	s_waitcnt lgkmcnt(13)
	v_mfma_f32_16x16x32_f16 v[68:71], v[136:139], v[168:171], v[68:71]
	s_waitcnt lgkmcnt(12)
	v_mfma_f32_16x16x32_f16 v[72:75], v[140:143], v[156:159], v[72:75]
	v_mfma_f32_16x16x32_f16 v[76:79], v[140:143], v[160:163], v[76:79]
	v_mfma_f32_16x16x32_f16 v[80:83], v[140:143], v[164:167], v[80:83]
	s_add_u32 m0, s28, 0x9000
	s_nop 0
	global_load_lds_dwordx4 v10, s[6:7]
	v_mfma_f32_16x16x32_f16 v[84:87], v[140:143], v[168:171], v[84:87]
	s_waitcnt lgkmcnt(11)
	v_mfma_f32_16x16x32_f16 v[88:91], v[144:147], v[156:159], v[88:91]
	v_mfma_f32_16x16x32_f16 v[92:95], v[144:147], v[160:163], v[92:95]
	v_mfma_f32_16x16x32_f16 v[96:99], v[144:147], v[164:167], v[96:99]
	v_mfma_f32_16x16x32_f16 v[100:103], v[144:147], v[168:171], v[100:103]
	s_waitcnt lgkmcnt(10)
	v_mfma_f32_16x16x32_f16 v[104:107], v[148:151], v[156:159], v[104:107]
	v_mfma_f32_16x16x32_f16 v[108:111], v[148:151], v[160:163], v[108:111]
	s_add_u32 m0, s28, 0xb000
	s_nop 0
	global_load_lds_dwordx4 v11, s[6:7]
	s_add_u32 s6, s6, s20
	s_addc_u32 s7, s7, 0
	v_mfma_f32_16x16x32_f16 v[112:115], v[148:151], v[164:167], v[112:115]
	v_mfma_f32_16x16x32_f16 v[116:119], v[148:151], v[168:171], v[116:119]
	s_waitcnt lgkmcnt(9)
	v_mfma_f32_16x16x32_f16 v[120:123], v[152:155], v[156:159], v[120:123]
	v_mfma_f32_16x16x32_f16 v[124:127], v[152:155], v[160:163], v[124:127]
	v_mfma_f32_16x16x32_f16 v[128:131], v[152:155], v[164:167], v[128:131]
	v_mfma_f32_16x16x32_f16 v[132:135], v[152:155], v[168:171], v[132:135]
	s_waitcnt vmcnt(7) lgkmcnt(0)
	s_barrier
	s_waitcnt lgkmcnt(6)
	ds_read_b128 v[136:139], v19
	ds_read_b128 v[156:159], v21
	ds_read_b128 v[160:163], v21 offset:2048
	ds_read_b128 v[164:167], v21 offset:4096
	ds_read_b128 v[168:171], v21 offset:6144
	ds_read_b128 v[140:143], v19 offset:2048
	ds_read_b128 v[144:147], v19 offset:4096
	ds_read_b128 v[148:151], v19 offset:6144
	ds_read_b128 v[152:155], v19 offset:8192
	v_mfma_f32_16x16x32_f16 v[56:59], v[172:175], v[192:195], v[56:59]
	s_add_u32 m0, s28, 0xd000
	s_nop 0
	global_load_lds_dwordx4 v10, s[4:5]
	s_waitcnt lgkmcnt(15)
	v_mfma_f32_16x16x32_f16 v[60:63], v[172:175], v[196:199], v[60:63]
	s_waitcnt lgkmcnt(14)
	v_mfma_f32_16x16x32_f16 v[64:67], v[172:175], v[200:203], v[64:67]
	s_waitcnt lgkmcnt(13)
	v_mfma_f32_16x16x32_f16 v[68:71], v[172:175], v[204:207], v[68:71]
	s_waitcnt lgkmcnt(12)
	v_mfma_f32_16x16x32_f16 v[72:75], v[176:179], v[192:195], v[72:75]
	v_mfma_f32_16x16x32_f16 v[76:79], v[176:179], v[196:199], v[76:79]
	s_add_u32 m0, s28, 0xf000
	s_nop 0
	global_load_lds_dwordx4 v11, s[4:5]
	v_mfma_f32_16x16x32_f16 v[80:83], v[176:179], v[200:203], v[80:83]
	v_mfma_f32_16x16x32_f16 v[84:87], v[176:179], v[204:207], v[84:87]
	s_waitcnt lgkmcnt(11)
	v_mfma_f32_16x16x32_f16 v[88:91], v[180:183], v[192:195], v[88:91]
	v_mfma_f32_16x16x32_f16 v[92:95], v[180:183], v[196:199], v[92:95]
	v_mfma_f32_16x16x32_f16 v[96:99], v[180:183], v[200:203], v[96:99]
	s_add_u32 m0, s28, 0x11000
	s_nop 0
	global_load_lds_dwordx4 v12, s[4:5]
	v_mfma_f32_16x16x32_f16 v[100:103], v[180:183], v[204:207], v[100:103]
	s_waitcnt lgkmcnt(10)
	v_mfma_f32_16x16x32_f16 v[104:107], v[184:187], v[192:195], v[104:107]
	v_mfma_f32_16x16x32_f16 v[108:111], v[184:187], v[196:199], v[108:111]
	v_mfma_f32_16x16x32_f16 v[112:115], v[184:187], v[200:203], v[112:115]
	v_mfma_f32_16x16x32_f16 v[116:119], v[184:187], v[204:207], v[116:119]
	s_add_u32 m0, s28, 0x13000
	s_nop 0
	global_load_lds_dwordx4 v13, s[4:5]
	s_waitcnt lgkmcnt(9)
	v_mfma_f32_16x16x32_f16 v[120:123], v[188:191], v[192:195], v[120:123]
	v_mfma_f32_16x16x32_f16 v[124:127], v[188:191], v[196:199], v[124:127]
	v_mfma_f32_16x16x32_f16 v[128:131], v[188:191], v[200:203], v[128:131]
	v_mfma_f32_16x16x32_f16 v[132:135], v[188:191], v[204:207], v[132:135]
	s_waitcnt lgkmcnt(6)
	ds_read_b128 v[172:175], v20
	ds_read_b128 v[192:195], v22
	ds_read_b128 v[196:199], v22 offset:2048
	ds_read_b128 v[200:203], v22 offset:4096
	ds_read_b128 v[204:207], v22 offset:6144
	ds_read_b128 v[176:179], v20 offset:2048
	ds_read_b128 v[180:183], v20 offset:4096
	ds_read_b128 v[184:187], v20 offset:6144
	ds_read_b128 v[188:191], v20 offset:8192
	v_mfma_f32_16x16x32_f16 v[56:59], v[136:139], v[156:159], v[56:59]
	s_add_u32 m0, s28, 0x15000
	s_nop 0
	global_load_lds_dwordx4 v14, s[4:5]
	s_add_u32 s4, s4, s20
	s_addc_u32 s5, s5, 0
	s_waitcnt lgkmcnt(15)
	v_mfma_f32_16x16x32_f16 v[60:63], v[136:139], v[160:163], v[60:63]
	s_waitcnt lgkmcnt(14)
	v_mfma_f32_16x16x32_f16 v[64:67], v[136:139], v[164:167], v[64:67]
	s_waitcnt lgkmcnt(13)
	v_mfma_f32_16x16x32_f16 v[68:71], v[136:139], v[168:171], v[68:71]
	s_waitcnt lgkmcnt(12)
	v_mfma_f32_16x16x32_f16 v[72:75], v[140:143], v[156:159], v[72:75]
	v_mfma_f32_16x16x32_f16 v[76:79], v[140:143], v[160:163], v[76:79]
	v_mfma_f32_16x16x32_f16 v[80:83], v[140:143], v[164:167], v[80:83]
	s_add_u32 m0, s28, 0x16000
	s_nop 0
	global_load_lds_dwordx4 v10, s[6:7]
	v_mfma_f32_16x16x32_f16 v[84:87], v[140:143], v[168:171], v[84:87]
	s_waitcnt lgkmcnt(11)
	v_mfma_f32_16x16x32_f16 v[88:91], v[144:147], v[156:159], v[88:91]
	v_mfma_f32_16x16x32_f16 v[92:95], v[144:147], v[160:163], v[92:95]
	v_mfma_f32_16x16x32_f16 v[96:99], v[144:147], v[164:167], v[96:99]
	v_mfma_f32_16x16x32_f16 v[100:103], v[144:147], v[168:171], v[100:103]
	s_waitcnt lgkmcnt(10)
	v_mfma_f32_16x16x32_f16 v[104:107], v[148:151], v[156:159], v[104:107]
	v_mfma_f32_16x16x32_f16 v[108:111], v[148:151], v[160:163], v[108:111]
	s_add_u32 m0, s28, 0x18000
	s_nop 0
	global_load_lds_dwordx4 v11, s[6:7]
	s_add_u32 s6, s6, s20
	s_addc_u32 s7, s7, 0
	v_mfma_f32_16x16x32_f16 v[112:115], v[148:151], v[164:167], v[112:115]
	v_mfma_f32_16x16x32_f16 v[116:119], v[148:151], v[168:171], v[116:119]
	s_waitcnt lgkmcnt(9)
	v_mfma_f32_16x16x32_f16 v[120:123], v[152:155], v[156:159], v[120:123]
	v_mfma_f32_16x16x32_f16 v[124:127], v[152:155], v[160:163], v[124:127]
	v_mfma_f32_16x16x32_f16 v[128:131], v[152:155], v[164:167], v[128:131]
	v_mfma_f32_16x16x32_f16 v[132:135], v[152:155], v[168:171], v[132:135]
	s_waitcnt vmcnt(7) lgkmcnt(0)
	s_barrier
	s_waitcnt lgkmcnt(6)
	ds_read_b128 v[136:139], v15
	ds_read_b128 v[156:159], v17
	ds_read_b128 v[160:163], v17 offset:2048
	ds_read_b128 v[164:167], v17 offset:4096
	ds_read_b128 v[168:171], v17 offset:6144
	ds_read_b128 v[140:143], v15 offset:2048
	ds_read_b128 v[144:147], v15 offset:4096
	ds_read_b128 v[148:151], v15 offset:6144
	ds_read_b128 v[152:155], v15 offset:8192
	v_mfma_f32_16x16x32_f16 v[56:59], v[172:175], v[192:195], v[56:59]
	s_add_u32 m0, s28, 0x1a000
	s_nop 0
	global_load_lds_dwordx4 v10, s[4:5]
	s_waitcnt lgkmcnt(15)
	v_mfma_f32_16x16x32_f16 v[60:63], v[172:175], v[196:199], v[60:63]
	s_waitcnt lgkmcnt(14)
	v_mfma_f32_16x16x32_f16 v[64:67], v[172:175], v[200:203], v[64:67]
	s_waitcnt lgkmcnt(13)
	v_mfma_f32_16x16x32_f16 v[68:71], v[172:175], v[204:207], v[68:71]
	s_waitcnt lgkmcnt(12)
	v_mfma_f32_16x16x32_f16 v[72:75], v[176:179], v[192:195], v[72:75]
	v_mfma_f32_16x16x32_f16 v[76:79], v[176:179], v[196:199], v[76:79]
	s_add_u32 m0, s28, 0x1c000
	s_nop 0
	global_load_lds_dwordx4 v11, s[4:5]
	v_mfma_f32_16x16x32_f16 v[80:83], v[176:179], v[200:203], v[80:83]
	v_mfma_f32_16x16x32_f16 v[84:87], v[176:179], v[204:207], v[84:87]
	s_waitcnt lgkmcnt(11)
	v_mfma_f32_16x16x32_f16 v[88:91], v[180:183], v[192:195], v[88:91]
	v_mfma_f32_16x16x32_f16 v[92:95], v[180:183], v[196:199], v[92:95]
	v_mfma_f32_16x16x32_f16 v[96:99], v[180:183], v[200:203], v[96:99]
	s_add_u32 m0, s28, 0x1e000
	s_nop 0
	global_load_lds_dwordx4 v12, s[4:5]
	v_mfma_f32_16x16x32_f16 v[100:103], v[180:183], v[204:207], v[100:103]
	s_waitcnt lgkmcnt(10)
	v_mfma_f32_16x16x32_f16 v[104:107], v[184:187], v[192:195], v[104:107]
	v_mfma_f32_16x16x32_f16 v[108:111], v[184:187], v[196:199], v[108:111]
	v_mfma_f32_16x16x32_f16 v[112:115], v[184:187], v[200:203], v[112:115]
	v_mfma_f32_16x16x32_f16 v[116:119], v[184:187], v[204:207], v[116:119]
	s_add_u32 m0, s28, 0x20000
	s_nop 0
	global_load_lds_dwordx4 v13, s[4:5]
	s_waitcnt lgkmcnt(9)
	v_mfma_f32_16x16x32_f16 v[120:123], v[188:191], v[192:195], v[120:123]
	v_mfma_f32_16x16x32_f16 v[124:127], v[188:191], v[196:199], v[124:127]
	v_mfma_f32_16x16x32_f16 v[128:131], v[188:191], v[200:203], v[128:131]
	v_mfma_f32_16x16x32_f16 v[132:135], v[188:191], v[204:207], v[132:135]
	s_waitcnt lgkmcnt(6)
	ds_read_b128 v[172:175], v16
	ds_read_b128 v[192:195], v18
	ds_read_b128 v[196:199], v18 offset:2048
	ds_read_b128 v[200:203], v18 offset:4096
	ds_read_b128 v[204:207], v18 offset:6144
	ds_read_b128 v[176:179], v16 offset:2048
	ds_read_b128 v[180:183], v16 offset:4096
	ds_read_b128 v[184:187], v16 offset:6144
	ds_read_b128 v[188:191], v16 offset:8192
	v_mfma_f32_16x16x32_f16 v[56:59], v[136:139], v[156:159], v[56:59]
	s_add_u32 m0, s28, 0x22000
	s_nop 0
	global_load_lds_dwordx4 v14, s[4:5]
	s_add_u32 s4, s4, s20
	s_addc_u32 s5, s5, 0
	s_waitcnt lgkmcnt(15)
	v_mfma_f32_16x16x32_f16 v[60:63], v[136:139], v[160:163], v[60:63]
	s_waitcnt lgkmcnt(14)
	v_mfma_f32_16x16x32_f16 v[64:67], v[136:139], v[164:167], v[64:67]
	s_waitcnt lgkmcnt(13)
	v_mfma_f32_16x16x32_f16 v[68:71], v[136:139], v[168:171], v[68:71]
	s_waitcnt lgkmcnt(12)
	v_mfma_f32_16x16x32_f16 v[72:75], v[140:143], v[156:159], v[72:75]
	v_mfma_f32_16x16x32_f16 v[76:79], v[140:143], v[160:163], v[76:79]
	v_mfma_f32_16x16x32_f16 v[80:83], v[140:143], v[164:167], v[80:83]
	s_add_u32 m0, s28, 0x23000
	s_nop 0
	global_load_lds_dwordx4 v10, s[6:7]
	v_mfma_f32_16x16x32_f16 v[84:87], v[140:143], v[168:171], v[84:87]
	s_waitcnt lgkmcnt(11)
	v_mfma_f32_16x16x32_f16 v[88:91], v[144:147], v[156:159], v[88:91]
	v_mfma_f32_16x16x32_f16 v[92:95], v[144:147], v[160:163], v[92:95]
	v_mfma_f32_16x16x32_f16 v[96:99], v[144:147], v[164:167], v[96:99]
	v_mfma_f32_16x16x32_f16 v[100:103], v[144:147], v[168:171], v[100:103]
	s_waitcnt lgkmcnt(10)
	v_mfma_f32_16x16x32_f16 v[104:107], v[148:151], v[156:159], v[104:107]
	v_mfma_f32_16x16x32_f16 v[108:111], v[148:151], v[160:163], v[108:111]
	s_add_u32 m0, s28, 0x25000
	s_nop 0
	global_load_lds_dwordx4 v11, s[6:7]
	s_add_u32 s6, s6, s20
	s_addc_u32 s7, s7, 0
	v_mfma_f32_16x16x32_f16 v[112:115], v[148:151], v[164:167], v[112:115]
	v_mfma_f32_16x16x32_f16 v[116:119], v[148:151], v[168:171], v[116:119]
	s_waitcnt lgkmcnt(9)
	v_mfma_f32_16x16x32_f16 v[120:123], v[152:155], v[156:159], v[120:123]
	v_mfma_f32_16x16x32_f16 v[124:127], v[152:155], v[160:163], v[124:127]
	v_mfma_f32_16x16x32_f16 v[128:131], v[152:155], v[164:167], v[128:131]
	v_mfma_f32_16x16x32_f16 v[132:135], v[152:155], v[168:171], v[132:135]
	s_waitcnt vmcnt(7) lgkmcnt(0)
	s_barrier
	s_waitcnt lgkmcnt(6)
	ds_read_b128 v[136:139], v15 offset:53248
	ds_read_b128 v[156:159], v17 offset:53248
	ds_read_b128 v[160:163], v17 offset:55296
	ds_read_b128 v[164:167], v17 offset:57344
	ds_read_b128 v[168:171], v17 offset:59392
	ds_read_b128 v[140:143], v15 offset:55296
	ds_read_b128 v[144:147], v15 offset:57344
	ds_read_b128 v[148:151], v15 offset:59392
	ds_read_b128 v[152:155], v15 offset:61440
	v_mfma_f32_16x16x32_f16 v[56:59], v[172:175], v[192:195], v[56:59]
	s_add_u32 m0, s28, 0x0
	s_nop 0
	global_load_lds_dwordx4 v10, s[4:5]
	s_waitcnt lgkmcnt(15)
	v_mfma_f32_16x16x32_f16 v[60:63], v[172:175], v[196:199], v[60:63]
	s_waitcnt lgkmcnt(14)
	v_mfma_f32_16x16x32_f16 v[64:67], v[172:175], v[200:203], v[64:67]
	s_waitcnt lgkmcnt(13)
	v_mfma_f32_16x16x32_f16 v[68:71], v[172:175], v[204:207], v[68:71]
	s_waitcnt lgkmcnt(12)
	v_mfma_f32_16x16x32_f16 v[72:75], v[176:179], v[192:195], v[72:75]
	v_mfma_f32_16x16x32_f16 v[76:79], v[176:179], v[196:199], v[76:79]
	s_add_u32 m0, s28, 0x2000
	s_nop 0
	global_load_lds_dwordx4 v11, s[4:5]
	v_mfma_f32_16x16x32_f16 v[80:83], v[176:179], v[200:203], v[80:83]
	v_mfma_f32_16x16x32_f16 v[84:87], v[176:179], v[204:207], v[84:87]
	s_waitcnt lgkmcnt(11)
	v_mfma_f32_16x16x32_f16 v[88:91], v[180:183], v[192:195], v[88:91]
	v_mfma_f32_16x16x32_f16 v[92:95], v[180:183], v[196:199], v[92:95]
	v_mfma_f32_16x16x32_f16 v[96:99], v[180:183], v[200:203], v[96:99]
	s_add_u32 m0, s28, 0x4000
	s_nop 0
	global_load_lds_dwordx4 v12, s[4:5]
	v_mfma_f32_16x16x32_f16 v[100:103], v[180:183], v[204:207], v[100:103]
	s_waitcnt lgkmcnt(10)
	v_mfma_f32_16x16x32_f16 v[104:107], v[184:187], v[192:195], v[104:107]
	v_mfma_f32_16x16x32_f16 v[108:111], v[184:187], v[196:199], v[108:111]
	v_mfma_f32_16x16x32_f16 v[112:115], v[184:187], v[200:203], v[112:115]
	v_mfma_f32_16x16x32_f16 v[116:119], v[184:187], v[204:207], v[116:119]
	s_add_u32 m0, s28, 0x6000
	s_nop 0
	global_load_lds_dwordx4 v13, s[4:5]
	s_waitcnt lgkmcnt(9)
	v_mfma_f32_16x16x32_f16 v[120:123], v[188:191], v[192:195], v[120:123]
	v_mfma_f32_16x16x32_f16 v[124:127], v[188:191], v[196:199], v[124:127]
	v_mfma_f32_16x16x32_f16 v[128:131], v[188:191], v[200:203], v[128:131]
	v_mfma_f32_16x16x32_f16 v[132:135], v[188:191], v[204:207], v[132:135]
	s_waitcnt lgkmcnt(6)
	ds_read_b128 v[172:175], v16 offset:53248
	ds_read_b128 v[192:195], v18 offset:53248
	ds_read_b128 v[196:199], v18 offset:55296
	ds_read_b128 v[200:203], v18 offset:57344
	ds_read_b128 v[204:207], v18 offset:59392
	ds_read_b128 v[176:179], v16 offset:55296
	ds_read_b128 v[180:183], v16 offset:57344
	ds_read_b128 v[184:187], v16 offset:59392
	ds_read_b128 v[188:191], v16 offset:61440
	v_mfma_f32_16x16x32_f16 v[56:59], v[136:139], v[156:159], v[56:59]
	s_add_u32 m0, s28, 0x8000
	s_nop 0
	global_load_lds_dwordx4 v14, s[4:5]
	s_add_u32 s4, s4, s20
	s_addc_u32 s5, s5, 0
	s_waitcnt lgkmcnt(15)
	v_mfma_f32_16x16x32_f16 v[60:63], v[136:139], v[160:163], v[60:63]
	s_waitcnt lgkmcnt(14)
	v_mfma_f32_16x16x32_f16 v[64:67], v[136:139], v[164:167], v[64:67]
	s_waitcnt lgkmcnt(13)
	v_mfma_f32_16x16x32_f16 v[68:71], v[136:139], v[168:171], v[68:71]
	s_waitcnt lgkmcnt(12)
	v_mfma_f32_16x16x32_f16 v[72:75], v[140:143], v[156:159], v[72:75]
	v_mfma_f32_16x16x32_f16 v[76:79], v[140:143], v[160:163], v[76:79]
	v_mfma_f32_16x16x32_f16 v[80:83], v[140:143], v[164:167], v[80:83]
	s_add_u32 m0, s28, 0x9000
	s_nop 0
	global_load_lds_dwordx4 v10, s[6:7]
	v_mfma_f32_16x16x32_f16 v[84:87], v[140:143], v[168:171], v[84:87]
	s_waitcnt lgkmcnt(11)
	v_mfma_f32_16x16x32_f16 v[88:91], v[144:147], v[156:159], v[88:91]
	v_mfma_f32_16x16x32_f16 v[92:95], v[144:147], v[160:163], v[92:95]
	v_mfma_f32_16x16x32_f16 v[96:99], v[144:147], v[164:167], v[96:99]
	v_mfma_f32_16x16x32_f16 v[100:103], v[144:147], v[168:171], v[100:103]
	s_waitcnt lgkmcnt(10)
	v_mfma_f32_16x16x32_f16 v[104:107], v[148:151], v[156:159], v[104:107]
	v_mfma_f32_16x16x32_f16 v[108:111], v[148:151], v[160:163], v[108:111]
	s_add_u32 m0, s28, 0xb000
	s_nop 0
	global_load_lds_dwordx4 v11, s[6:7]
	s_add_u32 s6, s6, s20
	s_addc_u32 s7, s7, 0
	v_mfma_f32_16x16x32_f16 v[112:115], v[148:151], v[164:167], v[112:115]
	v_mfma_f32_16x16x32_f16 v[116:119], v[148:151], v[168:171], v[116:119]
	s_waitcnt lgkmcnt(9)
	v_mfma_f32_16x16x32_f16 v[120:123], v[152:155], v[156:159], v[120:123]
	v_mfma_f32_16x16x32_f16 v[124:127], v[152:155], v[160:163], v[124:127]
	v_mfma_f32_16x16x32_f16 v[128:131], v[152:155], v[164:167], v[128:131]
	v_mfma_f32_16x16x32_f16 v[132:135], v[152:155], v[168:171], v[132:135]
	s_waitcnt vmcnt(7) lgkmcnt(0)
	s_barrier
	s_waitcnt lgkmcnt(6)
	ds_read_b128 v[136:139], v19
	ds_read_b128 v[156:159], v21
	ds_read_b128 v[160:163], v21 offset:2048
	ds_read_b128 v[164:167], v21 offset:4096
	ds_read_b128 v[168:171], v21 offset:6144
	ds_read_b128 v[140:143], v19 offset:2048
	ds_read_b128 v[144:147], v19 offset:4096
	ds_read_b128 v[148:151], v19 offset:6144
	ds_read_b128 v[152:155], v19 offset:8192
	v_mfma_f32_16x16x32_f16 v[56:59], v[172:175], v[192:195], v[56:59]
	s_add_u32 m0, s28, 0xd000
	s_nop 0
	global_load_lds_dwordx4 v10, s[4:5]
	s_waitcnt lgkmcnt(15)
	v_mfma_f32_16x16x32_f16 v[60:63], v[172:175], v[196:199], v[60:63]
	s_waitcnt lgkmcnt(14)
	v_mfma_f32_16x16x32_f16 v[64:67], v[172:175], v[200:203], v[64:67]
	s_waitcnt lgkmcnt(13)
	v_mfma_f32_16x16x32_f16 v[68:71], v[172:175], v[204:207], v[68:71]
	s_waitcnt lgkmcnt(12)
	v_mfma_f32_16x16x32_f16 v[72:75], v[176:179], v[192:195], v[72:75]
	v_mfma_f32_16x16x32_f16 v[76:79], v[176:179], v[196:199], v[76:79]
	s_add_u32 m0, s28, 0xf000
	s_nop 0
	global_load_lds_dwordx4 v11, s[4:5]
	v_mfma_f32_16x16x32_f16 v[80:83], v[176:179], v[200:203], v[80:83]
	v_mfma_f32_16x16x32_f16 v[84:87], v[176:179], v[204:207], v[84:87]
	s_waitcnt lgkmcnt(11)
	v_mfma_f32_16x16x32_f16 v[88:91], v[180:183], v[192:195], v[88:91]
	v_mfma_f32_16x16x32_f16 v[92:95], v[180:183], v[196:199], v[92:95]
	v_mfma_f32_16x16x32_f16 v[96:99], v[180:183], v[200:203], v[96:99]
	s_add_u32 m0, s28, 0x11000
	s_nop 0
	global_load_lds_dwordx4 v12, s[4:5]
	v_mfma_f32_16x16x32_f16 v[100:103], v[180:183], v[204:207], v[100:103]
	s_waitcnt lgkmcnt(10)
	v_mfma_f32_16x16x32_f16 v[104:107], v[184:187], v[192:195], v[104:107]
	v_mfma_f32_16x16x32_f16 v[108:111], v[184:187], v[196:199], v[108:111]
	v_mfma_f32_16x16x32_f16 v[112:115], v[184:187], v[200:203], v[112:115]
	v_mfma_f32_16x16x32_f16 v[116:119], v[184:187], v[204:207], v[116:119]
	s_add_u32 m0, s28, 0x13000
	s_nop 0
	global_load_lds_dwordx4 v13, s[4:5]
	s_waitcnt lgkmcnt(9)
	v_mfma_f32_16x16x32_f16 v[120:123], v[188:191], v[192:195], v[120:123]
	v_mfma_f32_16x16x32_f16 v[124:127], v[188:191], v[196:199], v[124:127]
	v_mfma_f32_16x16x32_f16 v[128:131], v[188:191], v[200:203], v[128:131]
	v_mfma_f32_16x16x32_f16 v[132:135], v[188:191], v[204:207], v[132:135]
	s_waitcnt lgkmcnt(6)
	ds_read_b128 v[172:175], v20
	ds_read_b128 v[192:195], v22
	ds_read_b128 v[196:199], v22 offset:2048
	ds_read_b128 v[200:203], v22 offset:4096
	ds_read_b128 v[204:207], v22 offset:6144
	ds_read_b128 v[176:179], v20 offset:2048
	ds_read_b128 v[180:183], v20 offset:4096
	ds_read_b128 v[184:187], v20 offset:6144
	ds_read_b128 v[188:191], v20 offset:8192
	v_mfma_f32_16x16x32_f16 v[56:59], v[136:139], v[156:159], v[56:59]
	s_add_u32 m0, s28, 0x15000
	s_nop 0
	global_load_lds_dwordx4 v14, s[4:5]
	s_add_u32 s4, s4, s20
	s_addc_u32 s5, s5, 0
	s_waitcnt lgkmcnt(15)
	v_mfma_f32_16x16x32_f16 v[60:63], v[136:139], v[160:163], v[60:63]
	s_waitcnt lgkmcnt(14)
	v_mfma_f32_16x16x32_f16 v[64:67], v[136:139], v[164:167], v[64:67]
	s_waitcnt lgkmcnt(13)
	v_mfma_f32_16x16x32_f16 v[68:71], v[136:139], v[168:171], v[68:71]
	s_waitcnt lgkmcnt(12)
	v_mfma_f32_16x16x32_f16 v[72:75], v[140:143], v[156:159], v[72:75]
	v_mfma_f32_16x16x32_f16 v[76:79], v[140:143], v[160:163], v[76:79]
	v_mfma_f32_16x16x32_f16 v[80:83], v[140:143], v[164:167], v[80:83]
	s_add_u32 m0, s28, 0x16000
	s_nop 0
	global_load_lds_dwordx4 v10, s[6:7]
	v_mfma_f32_16x16x32_f16 v[84:87], v[140:143], v[168:171], v[84:87]
	s_waitcnt lgkmcnt(11)
	v_mfma_f32_16x16x32_f16 v[88:91], v[144:147], v[156:159], v[88:91]
	v_mfma_f32_16x16x32_f16 v[92:95], v[144:147], v[160:163], v[92:95]
	v_mfma_f32_16x16x32_f16 v[96:99], v[144:147], v[164:167], v[96:99]
	v_mfma_f32_16x16x32_f16 v[100:103], v[144:147], v[168:171], v[100:103]
	s_waitcnt lgkmcnt(10)
	v_mfma_f32_16x16x32_f16 v[104:107], v[148:151], v[156:159], v[104:107]
	v_mfma_f32_16x16x32_f16 v[108:111], v[148:151], v[160:163], v[108:111]
	s_add_u32 m0, s28, 0x18000
	s_nop 0
	global_load_lds_dwordx4 v11, s[6:7]
	s_add_u32 s6, s6, s20
	s_addc_u32 s7, s7, 0
	v_mfma_f32_16x16x32_f16 v[112:115], v[148:151], v[164:167], v[112:115]
	v_mfma_f32_16x16x32_f16 v[116:119], v[148:151], v[168:171], v[116:119]
	s_waitcnt lgkmcnt(9)
	v_mfma_f32_16x16x32_f16 v[120:123], v[152:155], v[156:159], v[120:123]
	v_mfma_f32_16x16x32_f16 v[124:127], v[152:155], v[160:163], v[124:127]
	v_mfma_f32_16x16x32_f16 v[128:131], v[152:155], v[164:167], v[128:131]
	v_mfma_f32_16x16x32_f16 v[132:135], v[152:155], v[168:171], v[132:135]
	s_waitcnt vmcnt(7) lgkmcnt(0)
	s_barrier
	s_waitcnt lgkmcnt(6)
	ds_read_b128 v[136:139], v15
	ds_read_b128 v[156:159], v17
	ds_read_b128 v[160:163], v17 offset:2048
	ds_read_b128 v[164:167], v17 offset:4096
	ds_read_b128 v[168:171], v17 offset:6144
	ds_read_b128 v[140:143], v15 offset:2048
	ds_read_b128 v[144:147], v15 offset:4096
	ds_read_b128 v[148:151], v15 offset:6144
	ds_read_b128 v[152:155], v15 offset:8192
	v_mfma_f32_16x16x32_f16 v[56:59], v[172:175], v[192:195], v[56:59]
	s_add_u32 m0, s28, 0x1a000
	s_nop 0
	global_load_lds_dwordx4 v10, s[4:5]
	s_waitcnt lgkmcnt(15)
	v_mfma_f32_16x16x32_f16 v[60:63], v[172:175], v[196:199], v[60:63]
	s_waitcnt lgkmcnt(14)
	v_mfma_f32_16x16x32_f16 v[64:67], v[172:175], v[200:203], v[64:67]
	s_waitcnt lgkmcnt(13)
	v_mfma_f32_16x16x32_f16 v[68:71], v[172:175], v[204:207], v[68:71]
	s_waitcnt lgkmcnt(12)
	v_mfma_f32_16x16x32_f16 v[72:75], v[176:179], v[192:195], v[72:75]
	v_mfma_f32_16x16x32_f16 v[76:79], v[176:179], v[196:199], v[76:79]
	s_add_u32 m0, s28, 0x1c000
	s_nop 0
	global_load_lds_dwordx4 v11, s[4:5]
	v_mfma_f32_16x16x32_f16 v[80:83], v[176:179], v[200:203], v[80:83]
	v_mfma_f32_16x16x32_f16 v[84:87], v[176:179], v[204:207], v[84:87]
	s_waitcnt lgkmcnt(11)
	v_mfma_f32_16x16x32_f16 v[88:91], v[180:183], v[192:195], v[88:91]
	v_mfma_f32_16x16x32_f16 v[92:95], v[180:183], v[196:199], v[92:95]
	v_mfma_f32_16x16x32_f16 v[96:99], v[180:183], v[200:203], v[96:99]
	s_add_u32 m0, s28, 0x1e000
	s_nop 0
	global_load_lds_dwordx4 v12, s[4:5]
	v_mfma_f32_16x16x32_f16 v[100:103], v[180:183], v[204:207], v[100:103]
	s_waitcnt lgkmcnt(10)
	v_mfma_f32_16x16x32_f16 v[104:107], v[184:187], v[192:195], v[104:107]
	v_mfma_f32_16x16x32_f16 v[108:111], v[184:187], v[196:199], v[108:111]
	v_mfma_f32_16x16x32_f16 v[112:115], v[184:187], v[200:203], v[112:115]
	v_mfma_f32_16x16x32_f16 v[116:119], v[184:187], v[204:207], v[116:119]
	s_add_u32 m0, s28, 0x20000
	s_nop 0
	global_load_lds_dwordx4 v13, s[4:5]
	s_waitcnt lgkmcnt(9)
	v_mfma_f32_16x16x32_f16 v[120:123], v[188:191], v[192:195], v[120:123]
	v_mfma_f32_16x16x32_f16 v[124:127], v[188:191], v[196:199], v[124:127]
	v_mfma_f32_16x16x32_f16 v[128:131], v[188:191], v[200:203], v[128:131]
	v_mfma_f32_16x16x32_f16 v[132:135], v[188:191], v[204:207], v[132:135]
	s_waitcnt lgkmcnt(6)
	ds_read_b128 v[172:175], v16
	ds_read_b128 v[192:195], v18
	ds_read_b128 v[196:199], v18 offset:2048
	ds_read_b128 v[200:203], v18 offset:4096
	ds_read_b128 v[204:207], v18 offset:6144
	ds_read_b128 v[176:179], v16 offset:2048
	ds_read_b128 v[180:183], v16 offset:4096
	ds_read_b128 v[184:187], v16 offset:6144
	ds_read_b128 v[188:191], v16 offset:8192
	v_mfma_f32_16x16x32_f16 v[56:59], v[136:139], v[156:159], v[56:59]
	s_add_u32 m0, s28, 0x22000
	s_nop 0
	global_load_lds_dwordx4 v14, s[4:5]
	s_add_u32 s4, s4, s20
	s_addc_u32 s5, s5, 0
	s_waitcnt lgkmcnt(15)
	v_mfma_f32_16x16x32_f16 v[60:63], v[136:139], v[160:163], v[60:63]
	s_waitcnt lgkmcnt(14)
	v_mfma_f32_16x16x32_f16 v[64:67], v[136:139], v[164:167], v[64:67]
	s_waitcnt lgkmcnt(13)
	v_mfma_f32_16x16x32_f16 v[68:71], v[136:139], v[168:171], v[68:71]
	s_waitcnt lgkmcnt(12)
	v_mfma_f32_16x16x32_f16 v[72:75], v[140:143], v[156:159], v[72:75]
	v_mfma_f32_16x16x32_f16 v[76:79], v[140:143], v[160:163], v[76:79]
	v_mfma_f32_16x16x32_f16 v[80:83], v[140:143], v[164:167], v[80:83]
	s_add_u32 m0, s28, 0x23000
	s_nop 0
	global_load_lds_dwordx4 v10, s[6:7]
	v_mfma_f32_16x16x32_f16 v[84:87], v[140:143], v[168:171], v[84:87]
	s_waitcnt lgkmcnt(11)
	v_mfma_f32_16x16x32_f16 v[88:91], v[144:147], v[156:159], v[88:91]
	v_mfma_f32_16x16x32_f16 v[92:95], v[144:147], v[160:163], v[92:95]
	v_mfma_f32_16x16x32_f16 v[96:99], v[144:147], v[164:167], v[96:99]
	v_mfma_f32_16x16x32_f16 v[100:103], v[144:147], v[168:171], v[100:103]
	s_waitcnt lgkmcnt(10)
	v_mfma_f32_16x16x32_f16 v[104:107], v[148:151], v[156:159], v[104:107]
	v_mfma_f32_16x16x32_f16 v[108:111], v[148:151], v[160:163], v[108:111]
	s_add_u32 m0, s28, 0x25000
	s_nop 0
	global_load_lds_dwordx4 v11, s[6:7]
	s_add_u32 s6, s6, s20
	s_addc_u32 s7, s7, 0
	v_mfma_f32_16x16x32_f16 v[112:115], v[148:151], v[164:167], v[112:115]
	v_mfma_f32_16x16x32_f16 v[116:119], v[148:151], v[168:171], v[116:119]
	s_waitcnt lgkmcnt(9)
	v_mfma_f32_16x16x32_f16 v[120:123], v[152:155], v[156:159], v[120:123]
	v_mfma_f32_16x16x32_f16 v[124:127], v[152:155], v[160:163], v[124:127]
	v_mfma_f32_16x16x32_f16 v[128:131], v[152:155], v[164:167], v[128:131]
	v_mfma_f32_16x16x32_f16 v[132:135], v[152:155], v[168:171], v[132:135]
	s_waitcnt vmcnt(7) lgkmcnt(0)
	s_barrier
	s_waitcnt lgkmcnt(6)
	ds_read_b128 v[136:139], v15 offset:53248
	ds_read_b128 v[156:159], v17 offset:53248
	ds_read_b128 v[160:163], v17 offset:55296
	ds_read_b128 v[164:167], v17 offset:57344
	ds_read_b128 v[168:171], v17 offset:59392
	ds_read_b128 v[140:143], v15 offset:55296
	ds_read_b128 v[144:147], v15 offset:57344
	ds_read_b128 v[148:151], v15 offset:59392
	ds_read_b128 v[152:155], v15 offset:61440
	v_mfma_f32_16x16x32_f16 v[56:59], v[172:175], v[192:195], v[56:59]
	s_add_u32 m0, s28, 0x0
	s_nop 0
	global_load_lds_dwordx4 v10, s[4:5]
	s_waitcnt lgkmcnt(15)
	v_mfma_f32_16x16x32_f16 v[60:63], v[172:175], v[196:199], v[60:63]
	s_waitcnt lgkmcnt(14)
	v_mfma_f32_16x16x32_f16 v[64:67], v[172:175], v[200:203], v[64:67]
	s_waitcnt lgkmcnt(13)
	v_mfma_f32_16x16x32_f16 v[68:71], v[172:175], v[204:207], v[68:71]
	s_waitcnt lgkmcnt(12)
	v_mfma_f32_16x16x32_f16 v[72:75], v[176:179], v[192:195], v[72:75]
	v_mfma_f32_16x16x32_f16 v[76:79], v[176:179], v[196:199], v[76:79]
	s_add_u32 m0, s28, 0x2000
	s_nop 0
	global_load_lds_dwordx4 v11, s[4:5]
	v_mfma_f32_16x16x32_f16 v[80:83], v[176:179], v[200:203], v[80:83]
	v_mfma_f32_16x16x32_f16 v[84:87], v[176:179], v[204:207], v[84:87]
	s_waitcnt lgkmcnt(11)
	v_mfma_f32_16x16x32_f16 v[88:91], v[180:183], v[192:195], v[88:91]
	v_mfma_f32_16x16x32_f16 v[92:95], v[180:183], v[196:199], v[92:95]
	v_mfma_f32_16x16x32_f16 v[96:99], v[180:183], v[200:203], v[96:99]
	s_add_u32 m0, s28, 0x4000
	s_nop 0
	global_load_lds_dwordx4 v12, s[4:5]
	v_mfma_f32_16x16x32_f16 v[100:103], v[180:183], v[204:207], v[100:103]
	s_waitcnt lgkmcnt(10)
	v_mfma_f32_16x16x32_f16 v[104:107], v[184:187], v[192:195], v[104:107]
	v_mfma_f32_16x16x32_f16 v[108:111], v[184:187], v[196:199], v[108:111]
	v_mfma_f32_16x16x32_f16 v[112:115], v[184:187], v[200:203], v[112:115]
	v_mfma_f32_16x16x32_f16 v[116:119], v[184:187], v[204:207], v[116:119]
	s_add_u32 m0, s28, 0x6000
	s_nop 0
	global_load_lds_dwordx4 v13, s[4:5]
	s_waitcnt lgkmcnt(9)
	v_mfma_f32_16x16x32_f16 v[120:123], v[188:191], v[192:195], v[120:123]
	v_mfma_f32_16x16x32_f16 v[124:127], v[188:191], v[196:199], v[124:127]
	v_mfma_f32_16x16x32_f16 v[128:131], v[188:191], v[200:203], v[128:131]
	v_mfma_f32_16x16x32_f16 v[132:135], v[188:191], v[204:207], v[132:135]
	s_waitcnt lgkmcnt(6)
	ds_read_b128 v[172:175], v16 offset:53248
	ds_read_b128 v[192:195], v18 offset:53248
	ds_read_b128 v[196:199], v18 offset:55296
	ds_read_b128 v[200:203], v18 offset:57344
	ds_read_b128 v[204:207], v18 offset:59392
	ds_read_b128 v[176:179], v16 offset:55296
	ds_read_b128 v[180:183], v16 offset:57344
	ds_read_b128 v[184:187], v16 offset:59392
	ds_read_b128 v[188:191], v16 offset:61440
	v_mfma_f32_16x16x32_f16 v[56:59], v[136:139], v[156:159], v[56:59]
	s_add_u32 m0, s28, 0x8000
	s_nop 0
	global_load_lds_dwordx4 v14, s[4:5]
	s_add_u32 s4, s4, s20
	s_addc_u32 s5, s5, 0
	s_waitcnt lgkmcnt(15)
	v_mfma_f32_16x16x32_f16 v[60:63], v[136:139], v[160:163], v[60:63]
	s_waitcnt lgkmcnt(14)
	v_mfma_f32_16x16x32_f16 v[64:67], v[136:139], v[164:167], v[64:67]
	s_waitcnt lgkmcnt(13)
	v_mfma_f32_16x16x32_f16 v[68:71], v[136:139], v[168:171], v[68:71]
	s_waitcnt lgkmcnt(12)
	v_mfma_f32_16x16x32_f16 v[72:75], v[140:143], v[156:159], v[72:75]
	v_mfma_f32_16x16x32_f16 v[76:79], v[140:143], v[160:163], v[76:79]
	v_mfma_f32_16x16x32_f16 v[80:83], v[140:143], v[164:167], v[80:83]
	s_add_u32 m0, s28, 0x9000
	s_nop 0
	global_load_lds_dwordx4 v10, s[6:7]
	v_mfma_f32_16x16x32_f16 v[84:87], v[140:143], v[168:171], v[84:87]
	s_waitcnt lgkmcnt(11)
	v_mfma_f32_16x16x32_f16 v[88:91], v[144:147], v[156:159], v[88:91]
	v_mfma_f32_16x16x32_f16 v[92:95], v[144:147], v[160:163], v[92:95]
	v_mfma_f32_16x16x32_f16 v[96:99], v[144:147], v[164:167], v[96:99]
	v_mfma_f32_16x16x32_f16 v[100:103], v[144:147], v[168:171], v[100:103]
	s_waitcnt lgkmcnt(10)
	v_mfma_f32_16x16x32_f16 v[104:107], v[148:151], v[156:159], v[104:107]
	v_mfma_f32_16x16x32_f16 v[108:111], v[148:151], v[160:163], v[108:111]
	s_add_u32 m0, s28, 0xb000
	s_nop 0
	global_load_lds_dwordx4 v11, s[6:7]
	s_add_u32 s6, s6, s20
	s_addc_u32 s7, s7, 0
	v_mfma_f32_16x16x32_f16 v[112:115], v[148:151], v[164:167], v[112:115]
	v_mfma_f32_16x16x32_f16 v[116:119], v[148:151], v[168:171], v[116:119]
	s_waitcnt lgkmcnt(9)
	v_mfma_f32_16x16x32_f16 v[120:123], v[152:155], v[156:159], v[120:123]
	v_mfma_f32_16x16x32_f16 v[124:127], v[152:155], v[160:163], v[124:127]
	v_mfma_f32_16x16x32_f16 v[128:131], v[152:155], v[164:167], v[128:131]
	v_mfma_f32_16x16x32_f16 v[132:135], v[152:155], v[168:171], v[132:135]
	s_waitcnt vmcnt(7) lgkmcnt(0)
	s_barrier
	s_waitcnt lgkmcnt(6)
	ds_read_b128 v[136:139], v19
	ds_read_b128 v[156:159], v21
	ds_read_b128 v[160:163], v21 offset:2048
	ds_read_b128 v[164:167], v21 offset:4096
	ds_read_b128 v[168:171], v21 offset:6144
	ds_read_b128 v[140:143], v19 offset:2048
	ds_read_b128 v[144:147], v19 offset:4096
	ds_read_b128 v[148:151], v19 offset:6144
	ds_read_b128 v[152:155], v19 offset:8192
	v_mfma_f32_16x16x32_f16 v[56:59], v[172:175], v[192:195], v[56:59]
	s_add_u32 m0, s28, 0xd000
	s_nop 0
	global_load_lds_dwordx4 v10, s[4:5]
	s_waitcnt lgkmcnt(15)
	v_mfma_f32_16x16x32_f16 v[60:63], v[172:175], v[196:199], v[60:63]
	s_waitcnt lgkmcnt(14)
	v_mfma_f32_16x16x32_f16 v[64:67], v[172:175], v[200:203], v[64:67]
	s_waitcnt lgkmcnt(13)
	v_mfma_f32_16x16x32_f16 v[68:71], v[172:175], v[204:207], v[68:71]
	s_waitcnt lgkmcnt(12)
	v_mfma_f32_16x16x32_f16 v[72:75], v[176:179], v[192:195], v[72:75]
	v_mfma_f32_16x16x32_f16 v[76:79], v[176:179], v[196:199], v[76:79]
	s_add_u32 m0, s28, 0xf000
	s_nop 0
	global_load_lds_dwordx4 v11, s[4:5]
	v_mfma_f32_16x16x32_f16 v[80:83], v[176:179], v[200:203], v[80:83]
	v_mfma_f32_16x16x32_f16 v[84:87], v[176:179], v[204:207], v[84:87]
	s_waitcnt lgkmcnt(11)
	v_mfma_f32_16x16x32_f16 v[88:91], v[180:183], v[192:195], v[88:91]
	v_mfma_f32_16x16x32_f16 v[92:95], v[180:183], v[196:199], v[92:95]
	v_mfma_f32_16x16x32_f16 v[96:99], v[180:183], v[200:203], v[96:99]
	s_add_u32 m0, s28, 0x11000
	s_nop 0
	global_load_lds_dwordx4 v12, s[4:5]
	v_mfma_f32_16x16x32_f16 v[100:103], v[180:183], v[204:207], v[100:103]
	s_waitcnt lgkmcnt(10)
	v_mfma_f32_16x16x32_f16 v[104:107], v[184:187], v[192:195], v[104:107]
	v_mfma_f32_16x16x32_f16 v[108:111], v[184:187], v[196:199], v[108:111]
	v_mfma_f32_16x16x32_f16 v[112:115], v[184:187], v[200:203], v[112:115]
	v_mfma_f32_16x16x32_f16 v[116:119], v[184:187], v[204:207], v[116:119]
	s_add_u32 m0, s28, 0x13000
	s_nop 0
	global_load_lds_dwordx4 v13, s[4:5]
	s_waitcnt lgkmcnt(9)
	v_mfma_f32_16x16x32_f16 v[120:123], v[188:191], v[192:195], v[120:123]
	v_mfma_f32_16x16x32_f16 v[124:127], v[188:191], v[196:199], v[124:127]
	v_mfma_f32_16x16x32_f16 v[128:131], v[188:191], v[200:203], v[128:131]
	v_mfma_f32_16x16x32_f16 v[132:135], v[188:191], v[204:207], v[132:135]
	s_waitcnt lgkmcnt(6)
	ds_read_b128 v[172:175], v20
	ds_read_b128 v[192:195], v22
	ds_read_b128 v[196:199], v22 offset:2048
	ds_read_b128 v[200:203], v22 offset:4096
	ds_read_b128 v[204:207], v22 offset:6144
	ds_read_b128 v[176:179], v20 offset:2048
	ds_read_b128 v[180:183], v20 offset:4096
	ds_read_b128 v[184:187], v20 offset:6144
	ds_read_b128 v[188:191], v20 offset:8192
	v_mfma_f32_16x16x32_f16 v[56:59], v[136:139], v[156:159], v[56:59]
	s_add_u32 m0, s28, 0x15000
	s_nop 0
	global_load_lds_dwordx4 v14, s[4:5]
	s_add_u32 s4, s4, s20
	s_addc_u32 s5, s5, 0
	s_waitcnt lgkmcnt(15)
	v_mfma_f32_16x16x32_f16 v[60:63], v[136:139], v[160:163], v[60:63]
	s_waitcnt lgkmcnt(14)
	v_mfma_f32_16x16x32_f16 v[64:67], v[136:139], v[164:167], v[64:67]
	s_waitcnt lgkmcnt(13)
	v_mfma_f32_16x16x32_f16 v[68:71], v[136:139], v[168:171], v[68:71]
	s_waitcnt lgkmcnt(12)
	v_mfma_f32_16x16x32_f16 v[72:75], v[140:143], v[156:159], v[72:75]
	v_mfma_f32_16x16x32_f16 v[76:79], v[140:143], v[160:163], v[76:79]
	v_mfma_f32_16x16x32_f16 v[80:83], v[140:143], v[164:167], v[80:83]
	s_add_u32 m0, s28, 0x16000
	s_nop 0
	global_load_lds_dwordx4 v10, s[6:7]
	v_mfma_f32_16x16x32_f16 v[84:87], v[140:143], v[168:171], v[84:87]
	s_waitcnt lgkmcnt(11)
	v_mfma_f32_16x16x32_f16 v[88:91], v[144:147], v[156:159], v[88:91]
	v_mfma_f32_16x16x32_f16 v[92:95], v[144:147], v[160:163], v[92:95]
	v_mfma_f32_16x16x32_f16 v[96:99], v[144:147], v[164:167], v[96:99]
	v_mfma_f32_16x16x32_f16 v[100:103], v[144:147], v[168:171], v[100:103]
	s_waitcnt lgkmcnt(10)
	v_mfma_f32_16x16x32_f16 v[104:107], v[148:151], v[156:159], v[104:107]
	v_mfma_f32_16x16x32_f16 v[108:111], v[148:151], v[160:163], v[108:111]
	s_add_u32 m0, s28, 0x18000
	s_nop 0
	global_load_lds_dwordx4 v11, s[6:7]
	s_add_u32 s6, s6, s20
	s_addc_u32 s7, s7, 0
	v_mfma_f32_16x16x32_f16 v[112:115], v[148:151], v[164:167], v[112:115]
	v_mfma_f32_16x16x32_f16 v[116:119], v[148:151], v[168:171], v[116:119]
	s_waitcnt lgkmcnt(9)
	v_mfma_f32_16x16x32_f16 v[120:123], v[152:155], v[156:159], v[120:123]
	v_mfma_f32_16x16x32_f16 v[124:127], v[152:155], v[160:163], v[124:127]
	v_mfma_f32_16x16x32_f16 v[128:131], v[152:155], v[164:167], v[128:131]
	v_mfma_f32_16x16x32_f16 v[132:135], v[152:155], v[168:171], v[132:135]
	s_waitcnt vmcnt(7) lgkmcnt(0)
	s_barrier
	s_waitcnt lgkmcnt(6)
	ds_read_b128 v[136:139], v15
	ds_read_b128 v[156:159], v17
	ds_read_b128 v[160:163], v17 offset:2048
	ds_read_b128 v[164:167], v17 offset:4096
	ds_read_b128 v[168:171], v17 offset:6144
	ds_read_b128 v[140:143], v15 offset:2048
	ds_read_b128 v[144:147], v15 offset:4096
	ds_read_b128 v[148:151], v15 offset:6144
	ds_read_b128 v[152:155], v15 offset:8192
	v_mfma_f32_16x16x32_f16 v[56:59], v[172:175], v[192:195], v[56:59]
	s_add_u32 m0, s28, 0x1a000
	s_nop 0
	global_load_lds_dwordx4 v10, s[4:5]
	s_waitcnt lgkmcnt(15)
	v_mfma_f32_16x16x32_f16 v[60:63], v[172:175], v[196:199], v[60:63]
	s_waitcnt lgkmcnt(14)
	v_mfma_f32_16x16x32_f16 v[64:67], v[172:175], v[200:203], v[64:67]
	s_waitcnt lgkmcnt(13)
	v_mfma_f32_16x16x32_f16 v[68:71], v[172:175], v[204:207], v[68:71]
	s_waitcnt lgkmcnt(12)
	v_mfma_f32_16x16x32_f16 v[72:75], v[176:179], v[192:195], v[72:75]
	v_mfma_f32_16x16x32_f16 v[76:79], v[176:179], v[196:199], v[76:79]
	s_add_u32 m0, s28, 0x1c000
	s_nop 0
	global_load_lds_dwordx4 v11, s[4:5]
	v_mfma_f32_16x16x32_f16 v[80:83], v[176:179], v[200:203], v[80:83]
	v_mfma_f32_16x16x32_f16 v[84:87], v[176:179], v[204:207], v[84:87]
	s_waitcnt lgkmcnt(11)
	v_mfma_f32_16x16x32_f16 v[88:91], v[180:183], v[192:195], v[88:91]
	v_mfma_f32_16x16x32_f16 v[92:95], v[180:183], v[196:199], v[92:95]
	v_mfma_f32_16x16x32_f16 v[96:99], v[180:183], v[200:203], v[96:99]
	s_add_u32 m0, s28, 0x1e000
	s_nop 0
	global_load_lds_dwordx4 v12, s[4:5]
	v_mfma_f32_16x16x32_f16 v[100:103], v[180:183], v[204:207], v[100:103]
	s_waitcnt lgkmcnt(10)
	v_mfma_f32_16x16x32_f16 v[104:107], v[184:187], v[192:195], v[104:107]
	v_mfma_f32_16x16x32_f16 v[108:111], v[184:187], v[196:199], v[108:111]
	v_mfma_f32_16x16x32_f16 v[112:115], v[184:187], v[200:203], v[112:115]
	v_mfma_f32_16x16x32_f16 v[116:119], v[184:187], v[204:207], v[116:119]
	s_add_u32 m0, s28, 0x20000
	s_nop 0
	global_load_lds_dwordx4 v13, s[4:5]
	s_waitcnt lgkmcnt(9)
	v_mfma_f32_16x16x32_f16 v[120:123], v[188:191], v[192:195], v[120:123]
	v_mfma_f32_16x16x32_f16 v[124:127], v[188:191], v[196:199], v[124:127]
	v_mfma_f32_16x16x32_f16 v[128:131], v[188:191], v[200:203], v[128:131]
	v_mfma_f32_16x16x32_f16 v[132:135], v[188:191], v[204:207], v[132:135]
	s_waitcnt lgkmcnt(6)
	ds_read_b128 v[172:175], v16
	ds_read_b128 v[192:195], v18
	ds_read_b128 v[196:199], v18 offset:2048
	ds_read_b128 v[200:203], v18 offset:4096
	ds_read_b128 v[204:207], v18 offset:6144
	ds_read_b128 v[176:179], v16 offset:2048
	ds_read_b128 v[180:183], v16 offset:4096
	ds_read_b128 v[184:187], v16 offset:6144
	ds_read_b128 v[188:191], v16 offset:8192
	v_mfma_f32_16x16x32_f16 v[56:59], v[136:139], v[156:159], v[56:59]
	s_add_u32 m0, s28, 0x22000
	s_nop 0
	global_load_lds_dwordx4 v14, s[4:5]
	s_add_u32 s4, s4, s20
	s_addc_u32 s5, s5, 0
	s_waitcnt lgkmcnt(15)
	v_mfma_f32_16x16x32_f16 v[60:63], v[136:139], v[160:163], v[60:63]
	s_waitcnt lgkmcnt(14)
	v_mfma_f32_16x16x32_f16 v[64:67], v[136:139], v[164:167], v[64:67]
	s_waitcnt lgkmcnt(13)
	v_mfma_f32_16x16x32_f16 v[68:71], v[136:139], v[168:171], v[68:71]
	s_waitcnt lgkmcnt(12)
	v_mfma_f32_16x16x32_f16 v[72:75], v[140:143], v[156:159], v[72:75]
	v_mfma_f32_16x16x32_f16 v[76:79], v[140:143], v[160:163], v[76:79]
	v_mfma_f32_16x16x32_f16 v[80:83], v[140:143], v[164:167], v[80:83]
	s_add_u32 m0, s28, 0x23000
	s_nop 0
	global_load_lds_dwordx4 v10, s[6:7]
	v_mfma_f32_16x16x32_f16 v[84:87], v[140:143], v[168:171], v[84:87]
	s_waitcnt lgkmcnt(11)
	v_mfma_f32_16x16x32_f16 v[88:91], v[144:147], v[156:159], v[88:91]
	v_mfma_f32_16x16x32_f16 v[92:95], v[144:147], v[160:163], v[92:95]
	v_mfma_f32_16x16x32_f16 v[96:99], v[144:147], v[164:167], v[96:99]
	v_mfma_f32_16x16x32_f16 v[100:103], v[144:147], v[168:171], v[100:103]
	s_waitcnt lgkmcnt(10)
	v_mfma_f32_16x16x32_f16 v[104:107], v[148:151], v[156:159], v[104:107]
	v_mfma_f32_16x16x32_f16 v[108:111], v[148:151], v[160:163], v[108:111]
	s_add_u32 m0, s28, 0x25000
	s_nop 0
	global_load_lds_dwordx4 v11, s[6:7]
	s_add_u32 s6, s6, s20
	s_addc_u32 s7, s7, 0
	v_mfma_f32_16x16x32_f16 v[112:115], v[148:151], v[164:167], v[112:115]
	v_mfma_f32_16x16x32_f16 v[116:119], v[148:151], v[168:171], v[116:119]
	s_waitcnt lgkmcnt(9)
	v_mfma_f32_16x16x32_f16 v[120:123], v[152:155], v[156:159], v[120:123]
	v_mfma_f32_16x16x32_f16 v[124:127], v[152:155], v[160:163], v[124:127]
	v_mfma_f32_16x16x32_f16 v[128:131], v[152:155], v[164:167], v[128:131]
	v_mfma_f32_16x16x32_f16 v[132:135], v[152:155], v[168:171], v[132:135]
	s_waitcnt vmcnt(7) lgkmcnt(0)
	s_barrier
	s_waitcnt lgkmcnt(6)
	ds_read_b128 v[136:139], v15 offset:53248
	ds_read_b128 v[156:159], v17 offset:53248
	ds_read_b128 v[160:163], v17 offset:55296
	ds_read_b128 v[164:167], v17 offset:57344
	ds_read_b128 v[168:171], v17 offset:59392
	ds_read_b128 v[140:143], v15 offset:55296
	ds_read_b128 v[144:147], v15 offset:57344
	ds_read_b128 v[148:151], v15 offset:59392
	ds_read_b128 v[152:155], v15 offset:61440
	v_mfma_f32_16x16x32_f16 v[56:59], v[172:175], v[192:195], v[56:59]
	s_add_u32 m0, s28, 0x0
	s_nop 0
	global_load_lds_dwordx4 v10, s[4:5]
	s_waitcnt lgkmcnt(15)
	v_mfma_f32_16x16x32_f16 v[60:63], v[172:175], v[196:199], v[60:63]
	s_waitcnt lgkmcnt(14)
	v_mfma_f32_16x16x32_f16 v[64:67], v[172:175], v[200:203], v[64:67]
	s_waitcnt lgkmcnt(13)
	v_mfma_f32_16x16x32_f16 v[68:71], v[172:175], v[204:207], v[68:71]
	s_waitcnt lgkmcnt(12)
	v_mfma_f32_16x16x32_f16 v[72:75], v[176:179], v[192:195], v[72:75]
	v_mfma_f32_16x16x32_f16 v[76:79], v[176:179], v[196:199], v[76:79]
	s_add_u32 m0, s28, 0x2000
	s_nop 0
	global_load_lds_dwordx4 v11, s[4:5]
	v_mfma_f32_16x16x32_f16 v[80:83], v[176:179], v[200:203], v[80:83]
	v_mfma_f32_16x16x32_f16 v[84:87], v[176:179], v[204:207], v[84:87]
	s_waitcnt lgkmcnt(11)
	v_mfma_f32_16x16x32_f16 v[88:91], v[180:183], v[192:195], v[88:91]
	v_mfma_f32_16x16x32_f16 v[92:95], v[180:183], v[196:199], v[92:95]
	v_mfma_f32_16x16x32_f16 v[96:99], v[180:183], v[200:203], v[96:99]
	s_add_u32 m0, s28, 0x4000
	s_nop 0
	global_load_lds_dwordx4 v12, s[4:5]
	v_mfma_f32_16x16x32_f16 v[100:103], v[180:183], v[204:207], v[100:103]
	s_waitcnt lgkmcnt(10)
	v_mfma_f32_16x16x32_f16 v[104:107], v[184:187], v[192:195], v[104:107]
	v_mfma_f32_16x16x32_f16 v[108:111], v[184:187], v[196:199], v[108:111]
	v_mfma_f32_16x16x32_f16 v[112:115], v[184:187], v[200:203], v[112:115]
	v_mfma_f32_16x16x32_f16 v[116:119], v[184:187], v[204:207], v[116:119]
	s_add_u32 m0, s28, 0x6000
	s_nop 0
	global_load_lds_dwordx4 v13, s[4:5]
	s_waitcnt lgkmcnt(9)
	v_mfma_f32_16x16x32_f16 v[120:123], v[188:191], v[192:195], v[120:123]
	v_mfma_f32_16x16x32_f16 v[124:127], v[188:191], v[196:199], v[124:127]
	v_mfma_f32_16x16x32_f16 v[128:131], v[188:191], v[200:203], v[128:131]
	v_mfma_f32_16x16x32_f16 v[132:135], v[188:191], v[204:207], v[132:135]
	s_waitcnt lgkmcnt(6)
	ds_read_b128 v[172:175], v16 offset:53248
	ds_read_b128 v[192:195], v18 offset:53248
	ds_read_b128 v[196:199], v18 offset:55296
	ds_read_b128 v[200:203], v18 offset:57344
	ds_read_b128 v[204:207], v18 offset:59392
	ds_read_b128 v[176:179], v16 offset:55296
	ds_read_b128 v[180:183], v16 offset:57344
	ds_read_b128 v[184:187], v16 offset:59392
	ds_read_b128 v[188:191], v16 offset:61440
	v_mfma_f32_16x16x32_f16 v[56:59], v[136:139], v[156:159], v[56:59]
	s_add_u32 m0, s28, 0x8000
	s_nop 0
	global_load_lds_dwordx4 v14, s[4:5]
	s_add_u32 s4, s4, s20
	s_addc_u32 s5, s5, 0
	s_waitcnt lgkmcnt(15)
	v_mfma_f32_16x16x32_f16 v[60:63], v[136:139], v[160:163], v[60:63]
	s_waitcnt lgkmcnt(14)
	v_mfma_f32_16x16x32_f16 v[64:67], v[136:139], v[164:167], v[64:67]
	s_waitcnt lgkmcnt(13)
	v_mfma_f32_16x16x32_f16 v[68:71], v[136:139], v[168:171], v[68:71]
	s_waitcnt lgkmcnt(12)
	v_mfma_f32_16x16x32_f16 v[72:75], v[140:143], v[156:159], v[72:75]
	v_mfma_f32_16x16x32_f16 v[76:79], v[140:143], v[160:163], v[76:79]
	v_mfma_f32_16x16x32_f16 v[80:83], v[140:143], v[164:167], v[80:83]
	s_add_u32 m0, s28, 0x9000
	s_nop 0
	global_load_lds_dwordx4 v10, s[6:7]
	v_mfma_f32_16x16x32_f16 v[84:87], v[140:143], v[168:171], v[84:87]
	s_waitcnt lgkmcnt(11)
	v_mfma_f32_16x16x32_f16 v[88:91], v[144:147], v[156:159], v[88:91]
	v_mfma_f32_16x16x32_f16 v[92:95], v[144:147], v[160:163], v[92:95]
	v_mfma_f32_16x16x32_f16 v[96:99], v[144:147], v[164:167], v[96:99]
	v_mfma_f32_16x16x32_f16 v[100:103], v[144:147], v[168:171], v[100:103]
	s_waitcnt lgkmcnt(10)
	v_mfma_f32_16x16x32_f16 v[104:107], v[148:151], v[156:159], v[104:107]
	v_mfma_f32_16x16x32_f16 v[108:111], v[148:151], v[160:163], v[108:111]
	s_add_u32 m0, s28, 0xb000
	s_nop 0
	global_load_lds_dwordx4 v11, s[6:7]
	s_add_u32 s6, s6, s20
	s_addc_u32 s7, s7, 0
	v_mfma_f32_16x16x32_f16 v[112:115], v[148:151], v[164:167], v[112:115]
	v_mfma_f32_16x16x32_f16 v[116:119], v[148:151], v[168:171], v[116:119]
	s_waitcnt lgkmcnt(9)
	v_mfma_f32_16x16x32_f16 v[120:123], v[152:155], v[156:159], v[120:123]
	v_mfma_f32_16x16x32_f16 v[124:127], v[152:155], v[160:163], v[124:127]
	v_mfma_f32_16x16x32_f16 v[128:131], v[152:155], v[164:167], v[128:131]
	v_mfma_f32_16x16x32_f16 v[132:135], v[152:155], v[168:171], v[132:135]
	s_waitcnt vmcnt(7) lgkmcnt(0)
	s_barrier
	s_waitcnt lgkmcnt(6)
	ds_read_b128 v[136:139], v19
	ds_read_b128 v[156:159], v21
	ds_read_b128 v[160:163], v21 offset:2048
	ds_read_b128 v[164:167], v21 offset:4096
	ds_read_b128 v[168:171], v21 offset:6144
	ds_read_b128 v[140:143], v19 offset:2048
	ds_read_b128 v[144:147], v19 offset:4096
	ds_read_b128 v[148:151], v19 offset:6144
	ds_read_b128 v[152:155], v19 offset:8192
	v_mfma_f32_16x16x32_f16 v[56:59], v[172:175], v[192:195], v[56:59]
	s_waitcnt lgkmcnt(15)
	v_mfma_f32_16x16x32_f16 v[60:63], v[172:175], v[196:199], v[60:63]
	s_waitcnt lgkmcnt(14)
	v_mfma_f32_16x16x32_f16 v[64:67], v[172:175], v[200:203], v[64:67]
	s_waitcnt lgkmcnt(13)
	v_mfma_f32_16x16x32_f16 v[68:71], v[172:175], v[204:207], v[68:71]
	s_waitcnt lgkmcnt(12)
	v_mfma_f32_16x16x32_f16 v[72:75], v[176:179], v[192:195], v[72:75]
	v_mfma_f32_16x16x32_f16 v[76:79], v[176:179], v[196:199], v[76:79]
	v_mfma_f32_16x16x32_f16 v[80:83], v[176:179], v[200:203], v[80:83]
	v_mfma_f32_16x16x32_f16 v[84:87], v[176:179], v[204:207], v[84:87]
	s_waitcnt lgkmcnt(11)
	v_mfma_f32_16x16x32_f16 v[88:91], v[180:183], v[192:195], v[88:91]
	v_mfma_f32_16x16x32_f16 v[92:95], v[180:183], v[196:199], v[92:95]
	v_mfma_f32_16x16x32_f16 v[96:99], v[180:183], v[200:203], v[96:99]
	v_mfma_f32_16x16x32_f16 v[100:103], v[180:183], v[204:207], v[100:103]
	s_waitcnt lgkmcnt(10)
	v_mfma_f32_16x16x32_f16 v[104:107], v[184:187], v[192:195], v[104:107]
	v_mfma_f32_16x16x32_f16 v[108:111], v[184:187], v[196:199], v[108:111]
	v_mfma_f32_16x16x32_f16 v[112:115], v[184:187], v[200:203], v[112:115]
	v_mfma_f32_16x16x32_f16 v[116:119], v[184:187], v[204:207], v[116:119]
	s_waitcnt lgkmcnt(9)
	v_mfma_f32_16x16x32_f16 v[120:123], v[188:191], v[192:195], v[120:123]
	v_mfma_f32_16x16x32_f16 v[124:127], v[188:191], v[196:199], v[124:127]
	v_mfma_f32_16x16x32_f16 v[128:131], v[188:191], v[200:203], v[128:131]
	v_mfma_f32_16x16x32_f16 v[132:135], v[188:191], v[204:207], v[132:135]
	s_waitcnt lgkmcnt(6)
	ds_read_b128 v[172:175], v20
	ds_read_b128 v[192:195], v22
	ds_read_b128 v[196:199], v22 offset:2048
	ds_read_b128 v[200:203], v22 offset:4096
	ds_read_b128 v[204:207], v22 offset:6144
	ds_read_b128 v[176:179], v20 offset:2048
	ds_read_b128 v[180:183], v20 offset:4096
	ds_read_b128 v[184:187], v20 offset:6144
	ds_read_b128 v[188:191], v20 offset:8192
	v_mfma_f32_16x16x32_f16 v[56:59], v[136:139], v[156:159], v[56:59]
	s_waitcnt lgkmcnt(15)
	v_mfma_f32_16x16x32_f16 v[60:63], v[136:139], v[160:163], v[60:63]
	s_waitcnt lgkmcnt(14)
	v_mfma_f32_16x16x32_f16 v[64:67], v[136:139], v[164:167], v[64:67]
	s_waitcnt lgkmcnt(13)
	v_mfma_f32_16x16x32_f16 v[68:71], v[136:139], v[168:171], v[68:71]
	s_waitcnt lgkmcnt(12)
	v_mfma_f32_16x16x32_f16 v[72:75], v[140:143], v[156:159], v[72:75]
	v_mfma_f32_16x16x32_f16 v[76:79], v[140:143], v[160:163], v[76:79]
	v_mfma_f32_16x16x32_f16 v[80:83], v[140:143], v[164:167], v[80:83]
	v_mfma_f32_16x16x32_f16 v[84:87], v[140:143], v[168:171], v[84:87]
	s_waitcnt lgkmcnt(11)
	v_mfma_f32_16x16x32_f16 v[88:91], v[144:147], v[156:159], v[88:91]
	v_mfma_f32_16x16x32_f16 v[92:95], v[144:147], v[160:163], v[92:95]
	v_mfma_f32_16x16x32_f16 v[96:99], v[144:147], v[164:167], v[96:99]
	v_mfma_f32_16x16x32_f16 v[100:103], v[144:147], v[168:171], v[100:103]
	s_waitcnt lgkmcnt(10)
	v_mfma_f32_16x16x32_f16 v[104:107], v[148:151], v[156:159], v[104:107]
	v_mfma_f32_16x16x32_f16 v[108:111], v[148:151], v[160:163], v[108:111]
	v_mfma_f32_16x16x32_f16 v[112:115], v[148:151], v[164:167], v[112:115]
	v_mfma_f32_16x16x32_f16 v[116:119], v[148:151], v[168:171], v[116:119]
	s_waitcnt lgkmcnt(9)
	v_mfma_f32_16x16x32_f16 v[120:123], v[152:155], v[156:159], v[120:123]
	v_mfma_f32_16x16x32_f16 v[124:127], v[152:155], v[160:163], v[124:127]
	v_mfma_f32_16x16x32_f16 v[128:131], v[152:155], v[164:167], v[128:131]
	v_mfma_f32_16x16x32_f16 v[132:135], v[152:155], v[168:171], v[132:135]
	s_waitcnt vmcnt(0) lgkmcnt(0)
	s_barrier
	s_waitcnt lgkmcnt(6)
	ds_read_b128 v[136:139], v15
	ds_read_b128 v[156:159], v17
	ds_read_b128 v[160:163], v17 offset:2048
	ds_read_b128 v[164:167], v17 offset:4096
	ds_read_b128 v[168:171], v17 offset:6144
	ds_read_b128 v[140:143], v15 offset:2048
	ds_read_b128 v[144:147], v15 offset:4096
	ds_read_b128 v[148:151], v15 offset:6144
	ds_read_b128 v[152:155], v15 offset:8192
	v_mfma_f32_16x16x32_f16 v[56:59], v[172:175], v[192:195], v[56:59]
	s_waitcnt lgkmcnt(15)
	v_mfma_f32_16x16x32_f16 v[60:63], v[172:175], v[196:199], v[60:63]
	s_waitcnt lgkmcnt(14)
	v_mfma_f32_16x16x32_f16 v[64:67], v[172:175], v[200:203], v[64:67]
	s_waitcnt lgkmcnt(13)
	v_mfma_f32_16x16x32_f16 v[68:71], v[172:175], v[204:207], v[68:71]
	s_waitcnt lgkmcnt(12)
	v_mfma_f32_16x16x32_f16 v[72:75], v[176:179], v[192:195], v[72:75]
	v_mfma_f32_16x16x32_f16 v[76:79], v[176:179], v[196:199], v[76:79]
	v_mfma_f32_16x16x32_f16 v[80:83], v[176:179], v[200:203], v[80:83]
	v_mfma_f32_16x16x32_f16 v[84:87], v[176:179], v[204:207], v[84:87]
	s_waitcnt lgkmcnt(11)
	v_mfma_f32_16x16x32_f16 v[88:91], v[180:183], v[192:195], v[88:91]
	v_mfma_f32_16x16x32_f16 v[92:95], v[180:183], v[196:199], v[92:95]
	v_mfma_f32_16x16x32_f16 v[96:99], v[180:183], v[200:203], v[96:99]
	v_mfma_f32_16x16x32_f16 v[100:103], v[180:183], v[204:207], v[100:103]
	s_waitcnt lgkmcnt(10)
	v_mfma_f32_16x16x32_f16 v[104:107], v[184:187], v[192:195], v[104:107]
	v_mfma_f32_16x16x32_f16 v[108:111], v[184:187], v[196:199], v[108:111]
	v_mfma_f32_16x16x32_f16 v[112:115], v[184:187], v[200:203], v[112:115]
	v_mfma_f32_16x16x32_f16 v[116:119], v[184:187], v[204:207], v[116:119]
	s_waitcnt lgkmcnt(9)
	v_mfma_f32_16x16x32_f16 v[120:123], v[188:191], v[192:195], v[120:123]
	v_mfma_f32_16x16x32_f16 v[124:127], v[188:191], v[196:199], v[124:127]
	v_mfma_f32_16x16x32_f16 v[128:131], v[188:191], v[200:203], v[128:131]
	v_mfma_f32_16x16x32_f16 v[132:135], v[188:191], v[204:207], v[132:135]
	s_waitcnt lgkmcnt(6)
	ds_read_b128 v[172:175], v16
	ds_read_b128 v[192:195], v18
	ds_read_b128 v[196:199], v18 offset:2048
	ds_read_b128 v[200:203], v18 offset:4096
	ds_read_b128 v[204:207], v18 offset:6144
	ds_read_b128 v[176:179], v16 offset:2048
	ds_read_b128 v[180:183], v16 offset:4096
	ds_read_b128 v[184:187], v16 offset:6144
	ds_read_b128 v[188:191], v16 offset:8192
	v_mfma_f32_16x16x32_f16 v[56:59], v[136:139], v[156:159], v[56:59]
	s_waitcnt lgkmcnt(15)
	v_mfma_f32_16x16x32_f16 v[60:63], v[136:139], v[160:163], v[60:63]
	s_waitcnt lgkmcnt(14)
	v_mfma_f32_16x16x32_f16 v[64:67], v[136:139], v[164:167], v[64:67]
	s_waitcnt lgkmcnt(13)
	v_mfma_f32_16x16x32_f16 v[68:71], v[136:139], v[168:171], v[68:71]
	s_waitcnt lgkmcnt(12)
	v_mfma_f32_16x16x32_f16 v[72:75], v[140:143], v[156:159], v[72:75]
	v_mfma_f32_16x16x32_f16 v[76:79], v[140:143], v[160:163], v[76:79]
	v_mfma_f32_16x16x32_f16 v[80:83], v[140:143], v[164:167], v[80:83]
	v_mfma_f32_16x16x32_f16 v[84:87], v[140:143], v[168:171], v[84:87]
	s_waitcnt lgkmcnt(11)
	v_mfma_f32_16x16x32_f16 v[88:91], v[144:147], v[156:159], v[88:91]
	v_mfma_f32_16x16x32_f16 v[92:95], v[144:147], v[160:163], v[92:95]
	v_mfma_f32_16x16x32_f16 v[96:99], v[144:147], v[164:167], v[96:99]
	v_mfma_f32_16x16x32_f16 v[100:103], v[144:147], v[168:171], v[100:103]
	s_waitcnt lgkmcnt(10)
	v_mfma_f32_16x16x32_f16 v[104:107], v[148:151], v[156:159], v[104:107]
	v_mfma_f32_16x16x32_f16 v[108:111], v[148:151], v[160:163], v[108:111]
	v_mfma_f32_16x16x32_f16 v[112:115], v[148:151], v[164:167], v[112:115]
	v_mfma_f32_16x16x32_f16 v[116:119], v[148:151], v[168:171], v[116:119]
	s_waitcnt lgkmcnt(9)
	v_mfma_f32_16x16x32_f16 v[120:123], v[152:155], v[156:159], v[120:123]
	v_mfma_f32_16x16x32_f16 v[124:127], v[152:155], v[160:163], v[124:127]
	v_mfma_f32_16x16x32_f16 v[128:131], v[152:155], v[164:167], v[128:131]
	v_mfma_f32_16x16x32_f16 v[132:135], v[152:155], v[168:171], v[132:135]
	s_waitcnt lgkmcnt(7)
	v_mfma_f32_16x16x32_f16 v[56:59], v[172:175], v[192:195], v[56:59]
	s_waitcnt lgkmcnt(6)
	v_mfma_f32_16x16x32_f16 v[60:63], v[172:175], v[196:199], v[60:63]
	s_waitcnt lgkmcnt(5)
	v_mfma_f32_16x16x32_f16 v[64:67], v[172:175], v[200:203], v[64:67]
	s_waitcnt lgkmcnt(4)
	v_mfma_f32_16x16x32_f16 v[68:71], v[172:175], v[204:207], v[68:71]
	s_waitcnt lgkmcnt(3)
	v_mfma_f32_16x16x32_f16 v[72:75], v[176:179], v[192:195], v[72:75]
	v_mfma_f32_16x16x32_f16 v[76:79], v[176:179], v[196:199], v[76:79]
	v_mfma_f32_16x16x32_f16 v[80:83], v[176:179], v[200:203], v[80:83]
	v_mfma_f32_16x16x32_f16 v[84:87], v[176:179], v[204:207], v[84:87]
	s_waitcnt lgkmcnt(2)
	v_mfma_f32_16x16x32_f16 v[88:91], v[180:183], v[192:195], v[88:91]
	v_mfma_f32_16x16x32_f16 v[92:95], v[180:183], v[196:199], v[92:95]
	v_mfma_f32_16x16x32_f16 v[96:99], v[180:183], v[200:203], v[96:99]
	v_mfma_f32_16x16x32_f16 v[100:103], v[180:183], v[204:207], v[100:103]
	s_waitcnt lgkmcnt(1)
	v_mfma_f32_16x16x32_f16 v[104:107], v[184:187], v[192:195], v[104:107]
	v_mfma_f32_16x16x32_f16 v[108:111], v[184:187], v[196:199], v[108:111]
	v_mfma_f32_16x16x32_f16 v[112:115], v[184:187], v[200:203], v[112:115]
	v_mfma_f32_16x16x32_f16 v[116:119], v[184:187], v[204:207], v[116:119]
	s_waitcnt lgkmcnt(0)
	v_mfma_f32_16x16x32_f16 v[120:123], v[188:191], v[192:195], v[120:123]
	v_mfma_f32_16x16x32_f16 v[124:127], v[188:191], v[196:199], v[124:127]
	v_mfma_f32_16x16x32_f16 v[128:131], v[188:191], v[200:203], v[128:131]
	v_mfma_f32_16x16x32_f16 v[132:135], v[188:191], v[204:207], v[132:135]
	s_nop 7
	s_nop 1
	s_add_u32 s24, s29, 0
	s_lshl_b32 s8, s24, 11
	v_add_u32_e32 v212, s8, v23
	v_pk_add_f32 v[56:57], v[56:57], v[24:25] op_sel_hi:[1,0]
	v_pk_add_f32 v[58:59], v[58:59], v[24:25] op_sel_hi:[1,0]
	v_cvt_pk_f16_f32 v56, v56, v57
	v_cvt_pk_f16_f32 v57, v58, v59
	global_store_dwordx2 v212, v[56:57], s[22:23] offset:0
	v_pk_add_f32 v[60:61], v[60:61], v[26:27] op_sel_hi:[1,0]
	v_pk_add_f32 v[62:63], v[62:63], v[26:27] op_sel_hi:[1,0]
	v_cvt_pk_f16_f32 v60, v60, v61
	v_cvt_pk_f16_f32 v61, v62, v63
	global_store_dwordx2 v212, v[60:61], s[22:23] offset:256
	v_pk_add_f32 v[64:65], v[64:65], v[28:29] op_sel_hi:[1,0]
	v_pk_add_f32 v[66:67], v[66:67], v[28:29] op_sel_hi:[1,0]
	v_cvt_pk_f16_f32 v64, v64, v65
	v_cvt_pk_f16_f32 v65, v66, v67
	global_store_dwordx2 v212, v[64:65], s[22:23] offset:1024
	v_pk_add_f32 v[68:69], v[68:69], v[30:31] op_sel_hi:[1,0]
	v_pk_add_f32 v[70:71], v[70:71], v[30:31] op_sel_hi:[1,0]
	v_cvt_pk_f16_f32 v68, v68, v69
	v_cvt_pk_f16_f32 v69, v70, v71
	global_store_dwordx2 v212, v[68:69], s[22:23] offset:1280
	s_add_u32 s24, s29, 1
	s_lshl_b32 s8, s24, 11
	v_add_u32_e32 v212, s8, v23
	v_pk_add_f32 v[72:73], v[72:73], v[24:25] op_sel_hi:[1,0]
	v_pk_add_f32 v[74:75], v[74:75], v[24:25] op_sel_hi:[1,0]
	v_cvt_pk_f16_f32 v72, v72, v73
	v_cvt_pk_f16_f32 v73, v74, v75
	global_store_dwordx2 v212, v[72:73], s[22:23] offset:0
	v_pk_add_f32 v[76:77], v[76:77], v[26:27] op_sel_hi:[1,0]
	v_pk_add_f32 v[78:79], v[78:79], v[26:27] op_sel_hi:[1,0]
	v_cvt_pk_f16_f32 v76, v76, v77
	v_cvt_pk_f16_f32 v77, v78, v79
	global_store_dwordx2 v212, v[76:77], s[22:23] offset:256
	v_pk_add_f32 v[80:81], v[80:81], v[28:29] op_sel_hi:[1,0]
	v_pk_add_f32 v[82:83], v[82:83], v[28:29] op_sel_hi:[1,0]
	v_cvt_pk_f16_f32 v80, v80, v81
	v_cvt_pk_f16_f32 v81, v82, v83
	global_store_dwordx2 v212, v[80:81], s[22:23] offset:1024
	v_pk_add_f32 v[84:85], v[84:85], v[30:31] op_sel_hi:[1,0]
	v_pk_add_f32 v[86:87], v[86:87], v[30:31] op_sel_hi:[1,0]
	v_cvt_pk_f16_f32 v84, v84, v85
	v_cvt_pk_f16_f32 v85, v86, v87
	global_store_dwordx2 v212, v[84:85], s[22:23] offset:1280
	s_add_u32 s24, s29, 2
	s_lshl_b32 s8, s24, 11
	v_add_u32_e32 v212, s8, v23
	v_pk_add_f32 v[88:89], v[88:89], v[24:25] op_sel_hi:[1,0]
	v_pk_add_f32 v[90:91], v[90:91], v[24:25] op_sel_hi:[1,0]
	v_cvt_pk_f16_f32 v88, v88, v89
	v_cvt_pk_f16_f32 v89, v90, v91
	global_store_dwordx2 v212, v[88:89], s[22:23] offset:0
	v_pk_add_f32 v[92:93], v[92:93], v[26:27] op_sel_hi:[1,0]
	v_pk_add_f32 v[94:95], v[94:95], v[26:27] op_sel_hi:[1,0]
	v_cvt_pk_f16_f32 v92, v92, v93
	v_cvt_pk_f16_f32 v93, v94, v95
	global_store_dwordx2 v212, v[92:93], s[22:23] offset:256
	v_pk_add_f32 v[96:97], v[96:97], v[28:29] op_sel_hi:[1,0]
	v_pk_add_f32 v[98:99], v[98:99], v[28:29] op_sel_hi:[1,0]
	v_cvt_pk_f16_f32 v96, v96, v97
	v_cvt_pk_f16_f32 v97, v98, v99
	global_store_dwordx2 v212, v[96:97], s[22:23] offset:1024
	v_pk_add_f32 v[100:101], v[100:101], v[30:31] op_sel_hi:[1,0]
	v_pk_add_f32 v[102:103], v[102:103], v[30:31] op_sel_hi:[1,0]
	v_cvt_pk_f16_f32 v100, v100, v101
	v_cvt_pk_f16_f32 v101, v102, v103
	global_store_dwordx2 v212, v[100:101], s[22:23] offset:1280
	s_add_u32 s24, s29, 3
	s_lshl_b32 s8, s24, 11
	v_add_u32_e32 v212, s8, v23
	v_pk_add_f32 v[104:105], v[104:105], v[24:25] op_sel_hi:[1,0]
	v_pk_add_f32 v[106:107], v[106:107], v[24:25] op_sel_hi:[1,0]
	v_cvt_pk_f16_f32 v104, v104, v105
	v_cvt_pk_f16_f32 v105, v106, v107
	global_store_dwordx2 v212, v[104:105], s[22:23] offset:0
	v_pk_add_f32 v[108:109], v[108:109], v[26:27] op_sel_hi:[1,0]
	v_pk_add_f32 v[110:111], v[110:111], v[26:27] op_sel_hi:[1,0]
	v_cvt_pk_f16_f32 v108, v108, v109
	v_cvt_pk_f16_f32 v109, v110, v111
	global_store_dwordx2 v212, v[108:109], s[22:23] offset:256
	v_pk_add_f32 v[112:113], v[112:113], v[28:29] op_sel_hi:[1,0]
	v_pk_add_f32 v[114:115], v[114:115], v[28:29] op_sel_hi:[1,0]
	v_cvt_pk_f16_f32 v112, v112, v113
	v_cvt_pk_f16_f32 v113, v114, v115
	global_store_dwordx2 v212, v[112:113], s[22:23] offset:1024
	v_pk_add_f32 v[116:117], v[116:117], v[30:31] op_sel_hi:[1,0]
	v_pk_add_f32 v[118:119], v[118:119], v[30:31] op_sel_hi:[1,0]
	v_cvt_pk_f16_f32 v116, v116, v117
	v_cvt_pk_f16_f32 v117, v118, v119
	global_store_dwordx2 v212, v[116:117], s[22:23] offset:1280
	s_add_u32 s24, s29, 4
	s_lshl_b32 s8, s24, 11
	v_add_u32_e32 v212, s8, v23
	v_pk_add_f32 v[120:121], v[120:121], v[24:25] op_sel_hi:[1,0]
	v_pk_add_f32 v[122:123], v[122:123], v[24:25] op_sel_hi:[1,0]
	v_cvt_pk_f16_f32 v120, v120, v121
	v_cvt_pk_f16_f32 v121, v122, v123
	global_store_dwordx2 v212, v[120:121], s[22:23] offset:0
	v_pk_add_f32 v[124:125], v[124:125], v[26:27] op_sel_hi:[1,0]
	v_pk_add_f32 v[126:127], v[126:127], v[26:27] op_sel_hi:[1,0]
	v_cvt_pk_f16_f32 v124, v124, v125
	v_cvt_pk_f16_f32 v125, v126, v127
	global_store_dwordx2 v212, v[124:125], s[22:23] offset:256
	v_pk_add_f32 v[128:129], v[128:129], v[28:29] op_sel_hi:[1,0]
	v_pk_add_f32 v[130:131], v[130:131], v[28:29] op_sel_hi:[1,0]
	v_cvt_pk_f16_f32 v128, v128, v129
	v_cvt_pk_f16_f32 v129, v130, v131
	global_store_dwordx2 v212, v[128:129], s[22:23] offset:1024
	v_pk_add_f32 v[132:133], v[132:133], v[30:31] op_sel_hi:[1,0]
	v_pk_add_f32 v[134:135], v[134:135], v[30:31] op_sel_hi:[1,0]
	v_cvt_pk_f16_f32 v132, v132, v133
	v_cvt_pk_f16_f32 v133, v134, v135
	global_store_dwordx2 v212, v[132:133], s[22:23] offset:1280
	s_branch .Lpf_done
.Lpf_vVB:
	s_lshl_b32 s25, s25, 6
	s_add_u32 s25, s25, 32
	s_add_u32 s29, s10, s25
	s_lshr_b32 s29, s29, 4
	v_add_u32_e32 v5, s25, v3
	v_lshlrev_b32_e32 v5, 7, v5
	v_add_u32_e32 v15, v5, v6
	v_add_u32_e32 v16, v5, v7
	v_add_u32_e32 v5, 0x9000, v9
	v_add_u32_e32 v17, v5, v6
	v_add_u32_e32 v18, v5, v7
	v_add_u32_e32 v19, 0x1a000, v15
	v_add_u32_e32 v20, 0x1a000, v16
	v_add_u32_e32 v21, 0x1a000, v17
	v_add_u32_e32 v22, 0x1a000, v18
	v_lshlrev_b32_e32 v5, 2, v3
	global_load_dword v24, v5, s[14:15] offset:0
	global_load_dword v26, v5, s[14:15] offset:64
	global_load_dword v28, v5, s[14:15] offset:128
	global_load_dword v30, v5, s[14:15] offset:192
	s_add_u32 m0, s28, 0x0
	s_nop 0
	global_load_lds_dwordx4 v10, s[4:5]
	s_add_u32 m0, s28, 0x2000
	s_nop 0
	global_load_lds_dwordx4 v11, s[4:5]
	s_add_u32 m0, s28, 0x4000
	s_nop 0
	global_load_lds_dwordx4 v12, s[4:5]
	s_add_u32 m0, s28, 0x6000
	s_nop 0
	global_load_lds_dwordx4 v13, s[4:5]
	s_add_u32 s4, s4, s20
	s_addc_u32 s5, s5, 0
	s_add_u32 m0, s28, 0x9000
	s_nop 0
	global_load_lds_dwordx4 v10, s[6:7]
	s_add_u32 m0, s28, 0xb000
	s_nop 0
	global_load_lds_dwordx4 v11, s[6:7]
	s_add_u32 s6, s6, s20
	s_addc_u32 s7, s7, 0
	s_add_u32 m0, s28, 0xd000
	s_nop 0
	global_load_lds_dwordx4 v10, s[4:5]
	s_add_u32 m0, s28, 0xf000
	s_nop 0
	global_load_lds_dwordx4 v11, s[4:5]
	s_add_u32 m0, s28, 0x11000
	s_nop 0
	global_load_lds_dwordx4 v12, s[4:5]
	s_add_u32 m0, s28, 0x13000
	s_nop 0
	global_load_lds_dwordx4 v13, s[4:5]
	s_add_u32 s4, s4, s20
	s_addc_u32 s5, s5, 0
	s_add_u32 m0, s28, 0x16000
	s_nop 0
	global_load_lds_dwordx4 v10, s[6:7]
	s_add_u32 m0, s28, 0x18000
	s_nop 0
	global_load_lds_dwordx4 v11, s[6:7]
	s_add_u32 s6, s6, s20
	s_addc_u32 s7, s7, 0
	s_waitcnt vmcnt(6) lgkmcnt(0)
	s_barrier
	s_waitcnt lgkmcnt(7)
	ds_read_b128 v[136:139], v15
	ds_read_b128 v[156:159], v17
	ds_read_b128 v[160:163], v17 offset:2048
	ds_read_b128 v[164:167], v17 offset:4096
	ds_read_b128 v[168:171], v17 offset:6144
	ds_read_b128 v[140:143], v15 offset:2048
	ds_read_b128 v[144:147], v15 offset:4096
	ds_read_b128 v[148:151], v15 offset:6144
	s_waitcnt lgkmcnt(7)
	ds_read_b128 v[172:175], v16
	ds_read_b128 v[192:195], v18
	ds_read_b128 v[196:199], v18 offset:2048
	ds_read_b128 v[200:203], v18 offset:4096
	ds_read_b128 v[204:207], v18 offset:6144
	ds_read_b128 v[176:179], v16 offset:2048
	ds_read_b128 v[180:183], v16 offset:4096
	ds_read_b128 v[184:187], v16 offset:6144
	s_waitcnt lgkmcnt(14)
	v_mfma_f32_16x16x32_f16 v[56:59], v[136:139], v[156:159], 0
	s_add_u32 m0, s28, 0x1a000
	s_nop 0
	global_load_lds_dwordx4 v10, s[4:5]
	s_waitcnt lgkmcnt(13)
	v_mfma_f32_16x16x32_f16 v[60:63], v[136:139], v[160:163], 0
	s_waitcnt lgkmcnt(12)
	v_mfma_f32_16x16x32_f16 v[64:67], v[136:139], v[164:167], 0
	s_add_u32 m0, s28, 0x1c000
	s_nop 0
	global_load_lds_dwordx4 v11, s[4:5]
	s_waitcnt lgkmcnt(11)
	v_mfma_f32_16x16x32_f16 v[68:71], v[136:139], v[168:171], 0
	s_waitcnt lgkmcnt(10)
	v_mfma_f32_16x16x32_f16 v[72:75], v[140:143], v[156:159], 0
	v_mfma_f32_16x16x32_f16 v[76:79], v[140:143], v[160:163], 0
	s_add_u32 m0, s28, 0x1e000
	s_nop 0
	global_load_lds_dwordx4 v12, s[4:5]
	v_mfma_f32_16x16x32_f16 v[80:83], v[140:143], v[164:167], 0
	v_mfma_f32_16x16x32_f16 v[84:87], v[140:143], v[168:171], 0
	s_waitcnt lgkmcnt(9)
	v_mfma_f32_16x16x32_f16 v[88:91], v[144:147], v[156:159], 0
	s_add_u32 m0, s28, 0x20000
	s_nop 0
	global_load_lds_dwordx4 v13, s[4:5]
	s_add_u32 s4, s4, s20
	s_addc_u32 s5, s5, 0
	v_mfma_f32_16x16x32_f16 v[92:95], v[144:147], v[160:163], 0
	v_mfma_f32_16x16x32_f16 v[96:99], v[144:147], v[164:167], 0
	s_add_u32 m0, s28, 0x23000
	s_nop 0
	global_load_lds_dwordx4 v10, s[6:7]
	v_mfma_f32_16x16x32_f16 v[100:103], v[144:147], v[168:171], 0
	s_waitcnt lgkmcnt(8)
	v_mfma_f32_16x16x32_f16 v[104:107], v[148:151], v[156:159], 0
	v_mfma_f32_16x16x32_f16 v[108:111], v[148:151], v[160:163], 0
	s_add_u32 m0, s28, 0x25000
	s_nop 0
	global_load_lds_dwordx4 v11, s[6:7]
	s_add_u32 s6, s6, s20
	s_addc_u32 s7, s7, 0
	v_mfma_f32_16x16x32_f16 v[112:115], v[148:151], v[164:167], 0
	v_mfma_f32_16x16x32_f16 v[116:119], v[148:151], v[168:171], 0
	s_waitcnt vmcnt(6) lgkmcnt(0)
	s_barrier
	s_waitcnt lgkmcnt(7)
	ds_read_b128 v[136:139], v15 offset:53248
	ds_read_b128 v[156:159], v17 offset:53248
	ds_read_b128 v[160:163], v17 offset:55296
	ds_read_b128 v[164:167], v17 offset:57344
	ds_read_b128 v[168:171], v17 offset:59392
	ds_read_b128 v[140:143], v15 offset:55296
	ds_read_b128 v[144:147], v15 offset:57344
	ds_read_b128 v[148:151], v15 offset:59392
	s_waitcnt lgkmcnt(14)
	v_mfma_f32_16x16x32_f16 v[56:59], v[172:175], v[192:195], v[56:59]
	s_add_u32 m0, s28, 0x0
	s_nop 0
	global_load_lds_dwordx4 v10, s[4:5]
	s_waitcnt lgkmcnt(13)
	v_mfma_f32_16x16x32_f16 v[60:63], v[172:175], v[196:199], v[60:63]
	s_waitcnt lgkmcnt(12)
	v_mfma_f32_16x16x32_f16 v[64:67], v[172:175], v[200:203], v[64:67]
	s_waitcnt lgkmcnt(11)
	v_mfma_f32_16x16x32_f16 v[68:71], v[172:175], v[204:207], v[68:71]
	s_waitcnt lgkmcnt(10)
	v_mfma_f32_16x16x32_f16 v[72:75], v[176:179], v[192:195], v[72:75]
	v_mfma_f32_16x16x32_f16 v[76:79], v[176:179], v[196:199], v[76:79]
	s_add_u32 m0, s28, 0x2000
	s_nop 0
	global_load_lds_dwordx4 v11, s[4:5]
	v_mfma_f32_16x16x32_f16 v[80:83], v[176:179], v[200:203], v[80:83]
	v_mfma_f32_16x16x32_f16 v[84:87], v[176:179], v[204:207], v[84:87]
	s_waitcnt lgkmcnt(9)
	v_mfma_f32_16x16x32_f16 v[88:91], v[180:183], v[192:195], v[88:91]
	v_mfma_f32_16x16x32_f16 v[92:95], v[180:183], v[196:199], v[92:95]
	v_mfma_f32_16x16x32_f16 v[96:99], v[180:183], v[200:203], v[96:99]
	s_add_u32 m0, s28, 0x4000
	s_nop 0
	global_load_lds_dwordx4 v12, s[4:5]
	v_mfma_f32_16x16x32_f16 v[100:103], v[180:183], v[204:207], v[100:103]
	s_waitcnt lgkmcnt(8)
	v_mfma_f32_16x16x32_f16 v[104:107], v[184:187], v[192:195], v[104:107]
	v_mfma_f32_16x16x32_f16 v[108:111], v[184:187], v[196:199], v[108:111]
	v_mfma_f32_16x16x32_f16 v[112:115], v[184:187], v[200:203], v[112:115]
	v_mfma_f32_16x16x32_f16 v[116:119], v[184:187], v[204:207], v[116:119]
	s_waitcnt lgkmcnt(7)
	ds_read_b128 v[172:175], v16 offset:53248
	ds_read_b128 v[192:195], v18 offset:53248
	ds_read_b128 v[196:199], v18 offset:55296
	ds_read_b128 v[200:203], v18 offset:57344
	ds_read_b128 v[204:207], v18 offset:59392
	ds_read_b128 v[176:179], v16 offset:55296
	ds_read_b128 v[180:183], v16 offset:57344
	ds_read_b128 v[184:187], v16 offset:59392
	s_waitcnt lgkmcnt(14)
	v_mfma_f32_16x16x32_f16 v[56:59], v[136:139], v[156:159], v[56:59]
	s_add_u32 m0, s28, 0x6000
	s_nop 0
	global_load_lds_dwordx4 v13, s[4:5]
	s_add_u32 s4, s4, s20
	s_addc_u32 s5, s5, 0
	s_waitcnt lgkmcnt(13)
	v_mfma_f32_16x16x32_f16 v[60:63], v[136:139], v[160:163], v[60:63]
	s_waitcnt lgkmcnt(12)
	v_mfma_f32_16x16x32_f16 v[64:67], v[136:139], v[164:167], v[64:67]
	s_waitcnt lgkmcnt(11)
	v_mfma_f32_16x16x32_f16 v[68:71], v[136:139], v[168:171], v[68:71]
	s_waitcnt lgkmcnt(10)
	v_mfma_f32_16x16x32_f16 v[72:75], v[140:143], v[156:159], v[72:75]
	v_mfma_f32_16x16x32_f16 v[76:79], v[140:143], v[160:163], v[76:79]
	s_add_u32 m0, s28, 0x9000
	s_nop 0
	global_load_lds_dwordx4 v10, s[6:7]
	v_mfma_f32_16x16x32_f16 v[80:83], v[140:143], v[164:167], v[80:83]
	v_mfma_f32_16x16x32_f16 v[84:87], v[140:143], v[168:171], v[84:87]
	s_waitcnt lgkmcnt(9)
	v_mfma_f32_16x16x32_f16 v[88:91], v[144:147], v[156:159], v[88:91]
	v_mfma_f32_16x16x32_f16 v[92:95], v[144:147], v[160:163], v[92:95]
	v_mfma_f32_16x16x32_f16 v[96:99], v[144:147], v[164:167], v[96:99]
	s_add_u32 m0, s28, 0xb000
	s_nop 0
	global_load_lds_dwordx4 v11, s[6:7]
	s_add_u32 s6, s6, s20
	s_addc_u32 s7, s7, 0
	v_mfma_f32_16x16x32_f16 v[100:103], v[144:147], v[168:171], v[100:103]
	s_waitcnt lgkmcnt(8)
	v_mfma_f32_16x16x32_f16 v[104:107], v[148:151], v[156:159], v[104:107]
	v_mfma_f32_16x16x32_f16 v[108:111], v[148:151], v[160:163], v[108:111]
	v_mfma_f32_16x16x32_f16 v[112:115], v[148:151], v[164:167], v[112:115]
	v_mfma_f32_16x16x32_f16 v[116:119], v[148:151], v[168:171], v[116:119]
	s_waitcnt vmcnt(6) lgkmcnt(0)
	s_barrier
	s_waitcnt lgkmcnt(7)
	ds_read_b128 v[136:139], v19
	ds_read_b128 v[156:159], v21
	ds_read_b128 v[160:163], v21 offset:2048
	ds_read_b128 v[164:167], v21 offset:4096
	ds_read_b128 v[168:171], v21 offset:6144
	ds_read_b128 v[140:143], v19 offset:2048
	ds_read_b128 v[144:147], v19 offset:4096
	ds_read_b128 v[148:151], v19 offset:6144
	s_waitcnt lgkmcnt(14)
	v_mfma_f32_16x16x32_f16 v[56:59], v[172:175], v[192:195], v[56:59]
	s_add_u32 m0, s28, 0xd000
	s_nop 0
	global_load_lds_dwordx4 v10, s[4:5]
	s_waitcnt lgkmcnt(13)
	v_mfma_f32_16x16x32_f16 v[60:63], v[172:175], v[196:199], v[60:63]
	s_waitcnt lgkmcnt(12)
	v_mfma_f32_16x16x32_f16 v[64:67], v[172:175], v[200:203], v[64:67]
	s_waitcnt lgkmcnt(11)
	v_mfma_f32_16x16x32_f16 v[68:71], v[172:175], v[204:207], v[68:71]
	s_waitcnt lgkmcnt(10)
	v_mfma_f32_16x16x32_f16 v[72:75], v[176:179], v[192:195], v[72:75]
	v_mfma_f32_16x16x32_f16 v[76:79], v[176:179], v[196:199], v[76:79]
	s_add_u32 m0, s28, 0xf000
	s_nop 0
	global_load_lds_dwordx4 v11, s[4:5]
	v_mfma_f32_16x16x32_f16 v[80:83], v[176:179], v[200:203], v[80:83]
	v_mfma_f32_16x16x32_f16 v[84:87], v[176:179], v[204:207], v[84:87]
	s_waitcnt lgkmcnt(9)
	v_mfma_f32_16x16x32_f16 v[88:91], v[180:183], v[192:195], v[88:91]
	v_mfma_f32_16x16x32_f16 v[92:95], v[180:183], v[196:199], v[92:95]
	v_mfma_f32_16x16x32_f16 v[96:99], v[180:183], v[200:203], v[96:99]
	s_add_u32 m0, s28, 0x11000
	s_nop 0
	global_load_lds_dwordx4 v12, s[4:5]
	v_mfma_f32_16x16x32_f16 v[100:103], v[180:183], v[204:207], v[100:103]
	s_waitcnt lgkmcnt(8)
	v_mfma_f32_16x16x32_f16 v[104:107], v[184:187], v[192:195], v[104:107]
	v_mfma_f32_16x16x32_f16 v[108:111], v[184:187], v[196:199], v[108:111]
	v_mfma_f32_16x16x32_f16 v[112:115], v[184:187], v[200:203], v[112:115]
	v_mfma_f32_16x16x32_f16 v[116:119], v[184:187], v[204:207], v[116:119]
	s_waitcnt lgkmcnt(7)
	ds_read_b128 v[172:175], v20
	ds_read_b128 v[192:195], v22
	ds_read_b128 v[196:199], v22 offset:2048
	ds_read_b128 v[200:203], v22 offset:4096
	ds_read_b128 v[204:207], v22 offset:6144
	ds_read_b128 v[176:179], v20 offset:2048
	ds_read_b128 v[180:183], v20 offset:4096
	ds_read_b128 v[184:187], v20 offset:6144
	s_waitcnt lgkmcnt(14)
	v_mfma_f32_16x16x32_f16 v[56:59], v[136:139], v[156:159], v[56:59]
	s_add_u32 m0, s28, 0x13000
	s_nop 0
	global_load_lds_dwordx4 v13, s[4:5]
	s_add_u32 s4, s4, s20
	s_addc_u32 s5, s5, 0
	s_waitcnt lgkmcnt(13)
	v_mfma_f32_16x16x32_f16 v[60:63], v[136:139], v[160:163], v[60:63]
	s_waitcnt lgkmcnt(12)
	v_mfma_f32_16x16x32_f16 v[64:67], v[136:139], v[164:167], v[64:67]
	s_waitcnt lgkmcnt(11)
	v_mfma_f32_16x16x32_f16 v[68:71], v[136:139], v[168:171], v[68:71]
	s_waitcnt lgkmcnt(10)
	v_mfma_f32_16x16x32_f16 v[72:75], v[140:143], v[156:159], v[72:75]
	v_mfma_f32_16x16x32_f16 v[76:79], v[140:143], v[160:163], v[76:79]
	s_add_u32 m0, s28, 0x16000
	s_nop 0
	global_load_lds_dwordx4 v10, s[6:7]
	v_mfma_f32_16x16x32_f16 v[80:83], v[140:143], v[164:167], v[80:83]
	v_mfma_f32_16x16x32_f16 v[84:87], v[140:143], v[168:171], v[84:87]
	s_waitcnt lgkmcnt(9)
	v_mfma_f32_16x16x32_f16 v[88:91], v[144:147], v[156:159], v[88:91]
	v_mfma_f32_16x16x32_f16 v[92:95], v[144:147], v[160:163], v[92:95]
	v_mfma_f32_16x16x32_f16 v[96:99], v[144:147], v[164:167], v[96:99]
	s_add_u32 m0, s28, 0x18000
	s_nop 0
	global_load_lds_dwordx4 v11, s[6:7]
	s_add_u32 s6, s6, s20
	s_addc_u32 s7, s7, 0
	v_mfma_f32_16x16x32_f16 v[100:103], v[144:147], v[168:171], v[100:103]
	s_waitcnt lgkmcnt(8)
	v_mfma_f32_16x16x32_f16 v[104:107], v[148:151], v[156:159], v[104:107]
	v_mfma_f32_16x16x32_f16 v[108:111], v[148:151], v[160:163], v[108:111]
	v_mfma_f32_16x16x32_f16 v[112:115], v[148:151], v[164:167], v[112:115]
	v_mfma_f32_16x16x32_f16 v[116:119], v[148:151], v[168:171], v[116:119]
	s_waitcnt vmcnt(6) lgkmcnt(0)
	s_barrier
	s_waitcnt lgkmcnt(7)
	ds_read_b128 v[136:139], v15
	ds_read_b128 v[156:159], v17
	ds_read_b128 v[160:163], v17 offset:2048
	ds_read_b128 v[164:167], v17 offset:4096
	ds_read_b128 v[168:171], v17 offset:6144
	ds_read_b128 v[140:143], v15 offset:2048
	ds_read_b128 v[144:147], v15 offset:4096
	ds_read_b128 v[148:151], v15 offset:6144
	s_waitcnt lgkmcnt(14)
	v_mfma_f32_16x16x32_f16 v[56:59], v[172:175], v[192:195], v[56:59]
	s_add_u32 m0, s28, 0x1a000
	s_nop 0
	global_load_lds_dwordx4 v10, s[4:5]
	s_waitcnt lgkmcnt(13)
	v_mfma_f32_16x16x32_f16 v[60:63], v[172:175], v[196:199], v[60:63]
	s_waitcnt lgkmcnt(12)
	v_mfma_f32_16x16x32_f16 v[64:67], v[172:175], v[200:203], v[64:67]
	s_waitcnt lgkmcnt(11)
	v_mfma_f32_16x16x32_f16 v[68:71], v[172:175], v[204:207], v[68:71]
	s_waitcnt lgkmcnt(10)
	v_mfma_f32_16x16x32_f16 v[72:75], v[176:179], v[192:195], v[72:75]
	v_mfma_f32_16x16x32_f16 v[76:79], v[176:179], v[196:199], v[76:79]
	s_add_u32 m0, s28, 0x1c000
	s_nop 0
	global_load_lds_dwordx4 v11, s[4:5]
	v_mfma_f32_16x16x32_f16 v[80:83], v[176:179], v[200:203], v[80:83]
	v_mfma_f32_16x16x32_f16 v[84:87], v[176:179], v[204:207], v[84:87]
	s_waitcnt lgkmcnt(9)
	v_mfma_f32_16x16x32_f16 v[88:91], v[180:183], v[192:195], v[88:91]
	v_mfma_f32_16x16x32_f16 v[92:95], v[180:183], v[196:199], v[92:95]
	v_mfma_f32_16x16x32_f16 v[96:99], v[180:183], v[200:203], v[96:99]
	s_add_u32 m0, s28, 0x1e000
	s_nop 0
	global_load_lds_dwordx4 v12, s[4:5]
	v_mfma_f32_16x16x32_f16 v[100:103], v[180:183], v[204:207], v[100:103]
	s_waitcnt lgkmcnt(8)
	v_mfma_f32_16x16x32_f16 v[104:107], v[184:187], v[192:195], v[104:107]
	v_mfma_f32_16x16x32_f16 v[108:111], v[184:187], v[196:199], v[108:111]
	v_mfma_f32_16x16x32_f16 v[112:115], v[184:187], v[200:203], v[112:115]
	v_mfma_f32_16x16x32_f16 v[116:119], v[184:187], v[204:207], v[116:119]
	s_waitcnt lgkmcnt(7)
	ds_read_b128 v[172:175], v16
	ds_read_b128 v[192:195], v18
	ds_read_b128 v[196:199], v18 offset:2048
	ds_read_b128 v[200:203], v18 offset:4096
	ds_read_b128 v[204:207], v18 offset:6144
	ds_read_b128 v[176:179], v16 offset:2048
	ds_read_b128 v[180:183], v16 offset:4096
	ds_read_b128 v[184:187], v16 offset:6144
	s_waitcnt lgkmcnt(14)
	v_mfma_f32_16x16x32_f16 v[56:59], v[136:139], v[156:159], v[56:59]
	s_add_u32 m0, s28, 0x20000
	s_nop 0
	global_load_lds_dwordx4 v13, s[4:5]
	s_add_u32 s4, s4, s20
	s_addc_u32 s5, s5, 0
	s_waitcnt lgkmcnt(13)
	v_mfma_f32_16x16x32_f16 v[60:63], v[136:139], v[160:163], v[60:63]
	s_waitcnt lgkmcnt(12)
	v_mfma_f32_16x16x32_f16 v[64:67], v[136:139], v[164:167], v[64:67]
	s_waitcnt lgkmcnt(11)
	v_mfma_f32_16x16x32_f16 v[68:71], v[136:139], v[168:171], v[68:71]
	s_waitcnt lgkmcnt(10)
	v_mfma_f32_16x16x32_f16 v[72:75], v[140:143], v[156:159], v[72:75]
	v_mfma_f32_16x16x32_f16 v[76:79], v[140:143], v[160:163], v[76:79]
	s_add_u32 m0, s28, 0x23000
	s_nop 0
	global_load_lds_dwordx4 v10, s[6:7]
	v_mfma_f32_16x16x32_f16 v[80:83], v[140:143], v[164:167], v[80:83]
	v_mfma_f32_16x16x32_f16 v[84:87], v[140:143], v[168:171], v[84:87]
	s_waitcnt lgkmcnt(9)
	v_mfma_f32_16x16x32_f16 v[88:91], v[144:147], v[156:159], v[88:91]
	v_mfma_f32_16x16x32_f16 v[92:95], v[144:147], v[160:163], v[92:95]
	v_mfma_f32_16x16x32_f16 v[96:99], v[144:147], v[164:167], v[96:99]
	s_add_u32 m0, s28, 0x25000
	s_nop 0
	global_load_lds_dwordx4 v11, s[6:7]
	s_add_u32 s6, s6, s20
	s_addc_u32 s7, s7, 0
	v_mfma_f32_16x16x32_f16 v[100:103], v[144:147], v[168:171], v[100:103]
	s_waitcnt lgkmcnt(8)
	v_mfma_f32_16x16x32_f16 v[104:107], v[148:151], v[156:159], v[104:107]
	v_mfma_f32_16x16x32_f16 v[108:111], v[148:151], v[160:163], v[108:111]
	v_mfma_f32_16x16x32_f16 v[112:115], v[148:151], v[164:167], v[112:115]
	v_mfma_f32_16x16x32_f16 v[116:119], v[148:151], v[168:171], v[116:119]
	s_waitcnt vmcnt(6) lgkmcnt(0)
	s_barrier
	s_waitcnt lgkmcnt(7)
	ds_read_b128 v[136:139], v15 offset:53248
	ds_read_b128 v[156:159], v17 offset:53248
	ds_read_b128 v[160:163], v17 offset:55296
	ds_read_b128 v[164:167], v17 offset:57344
	ds_read_b128 v[168:171], v17 offset:59392
	ds_read_b128 v[140:143], v15 offset:55296
	ds_read_b128 v[144:147], v15 offset:57344
	ds_read_b128 v[148:151], v15 offset:59392
	s_waitcnt lgkmcnt(14)
	v_mfma_f32_16x16x32_f16 v[56:59], v[172:175], v[192:195], v[56:59]
	s_add_u32 m0, s28, 0x0
	s_nop 0
	global_load_lds_dwordx4 v10, s[4:5]
	s_waitcnt lgkmcnt(13)
	v_mfma_f32_16x16x32_f16 v[60:63], v[172:175], v[196:199], v[60:63]
	s_waitcnt lgkmcnt(12)
	v_mfma_f32_16x16x32_f16 v[64:67], v[172:175], v[200:203], v[64:67]
	s_waitcnt lgkmcnt(11)
	v_mfma_f32_16x16x32_f16 v[68:71], v[172:175], v[204:207], v[68:71]
	s_waitcnt lgkmcnt(10)
	v_mfma_f32_16x16x32_f16 v[72:75], v[176:179], v[192:195], v[72:75]
	v_mfma_f32_16x16x32_f16 v[76:79], v[176:179], v[196:199], v[76:79]
	s_add_u32 m0, s28, 0x2000
	s_nop 0
	global_load_lds_dwordx4 v11, s[4:5]
	v_mfma_f32_16x16x32_f16 v[80:83], v[176:179], v[200:203], v[80:83]
	v_mfma_f32_16x16x32_f16 v[84:87], v[176:179], v[204:207], v[84:87]
	s_waitcnt lgkmcnt(9)
	v_mfma_f32_16x16x32_f16 v[88:91], v[180:183], v[192:195], v[88:91]
	v_mfma_f32_16x16x32_f16 v[92:95], v[180:183], v[196:199], v[92:95]
	v_mfma_f32_16x16x32_f16 v[96:99], v[180:183], v[200:203], v[96:99]
	s_add_u32 m0, s28, 0x4000
	s_nop 0
	global_load_lds_dwordx4 v12, s[4:5]
	v_mfma_f32_16x16x32_f16 v[100:103], v[180:183], v[204:207], v[100:103]
	s_waitcnt lgkmcnt(8)
	v_mfma_f32_16x16x32_f16 v[104:107], v[184:187], v[192:195], v[104:107]
	v_mfma_f32_16x16x32_f16 v[108:111], v[184:187], v[196:199], v[108:111]
	v_mfma_f32_16x16x32_f16 v[112:115], v[184:187], v[200:203], v[112:115]
	v_mfma_f32_16x16x32_f16 v[116:119], v[184:187], v[204:207], v[116:119]
	s_waitcnt lgkmcnt(7)
	ds_read_b128 v[172:175], v16 offset:53248
	ds_read_b128 v[192:195], v18 offset:53248
	ds_read_b128 v[196:199], v18 offset:55296
	ds_read_b128 v[200:203], v18 offset:57344
	ds_read_b128 v[204:207], v18 offset:59392
	ds_read_b128 v[176:179], v16 offset:55296
	ds_read_b128 v[180:183], v16 offset:57344
	ds_read_b128 v[184:187], v16 offset:59392
	s_waitcnt lgkmcnt(14)
	v_mfma_f32_16x16x32_f16 v[56:59], v[136:139], v[156:159], v[56:59]
	s_add_u32 m0, s28, 0x6000
	s_nop 0
	global_load_lds_dwordx4 v13, s[4:5]
	s_add_u32 s4, s4, s20
	s_addc_u32 s5, s5, 0
	s_waitcnt lgkmcnt(13)
	v_mfma_f32_16x16x32_f16 v[60:63], v[136:139], v[160:163], v[60:63]
	s_waitcnt lgkmcnt(12)
	v_mfma_f32_16x16x32_f16 v[64:67], v[136:139], v[164:167], v[64:67]
	s_waitcnt lgkmcnt(11)
	v_mfma_f32_16x16x32_f16 v[68:71], v[136:139], v[168:171], v[68:71]
	s_waitcnt lgkmcnt(10)
	v_mfma_f32_16x16x32_f16 v[72:75], v[140:143], v[156:159], v[72:75]
	v_mfma_f32_16x16x32_f16 v[76:79], v[140:143], v[160:163], v[76:79]
	s_add_u32 m0, s28, 0x9000
	s_nop 0
	global_load_lds_dwordx4 v10, s[6:7]
	v_mfma_f32_16x16x32_f16 v[80:83], v[140:143], v[164:167], v[80:83]
	v_mfma_f32_16x16x32_f16 v[84:87], v[140:143], v[168:171], v[84:87]
	s_waitcnt lgkmcnt(9)
	v_mfma_f32_16x16x32_f16 v[88:91], v[144:147], v[156:159], v[88:91]
	v_mfma_f32_16x16x32_f16 v[92:95], v[144:147], v[160:163], v[92:95]
	v_mfma_f32_16x16x32_f16 v[96:99], v[144:147], v[164:167], v[96:99]
	s_add_u32 m0, s28, 0xb000
	s_nop 0
	global_load_lds_dwordx4 v11, s[6:7]
	s_add_u32 s6, s6, s20
	s_addc_u32 s7, s7, 0
	v_mfma_f32_16x16x32_f16 v[100:103], v[144:147], v[168:171], v[100:103]
	s_waitcnt lgkmcnt(8)
	v_mfma_f32_16x16x32_f16 v[104:107], v[148:151], v[156:159], v[104:107]
	v_mfma_f32_16x16x32_f16 v[108:111], v[148:151], v[160:163], v[108:111]
	v_mfma_f32_16x16x32_f16 v[112:115], v[148:151], v[164:167], v[112:115]
	v_mfma_f32_16x16x32_f16 v[116:119], v[148:151], v[168:171], v[116:119]
	s_waitcnt vmcnt(6) lgkmcnt(0)
	s_barrier
	s_waitcnt lgkmcnt(7)
	ds_read_b128 v[136:139], v19
	ds_read_b128 v[156:159], v21
	ds_read_b128 v[160:163], v21 offset:2048
	ds_read_b128 v[164:167], v21 offset:4096
	ds_read_b128 v[168:171], v21 offset:6144
	ds_read_b128 v[140:143], v19 offset:2048
	ds_read_b128 v[144:147], v19 offset:4096
	ds_read_b128 v[148:151], v19 offset:6144
	s_waitcnt lgkmcnt(14)
	v_mfma_f32_16x16x32_f16 v[56:59], v[172:175], v[192:195], v[56:59]
	s_add_u32 m0, s28, 0xd000
	s_nop 0
	global_load_lds_dwordx4 v10, s[4:5]
	s_waitcnt lgkmcnt(13)
	v_mfma_f32_16x16x32_f16 v[60:63], v[172:175], v[196:199], v[60:63]
	s_waitcnt lgkmcnt(12)
	v_mfma_f32_16x16x32_f16 v[64:67], v[172:175], v[200:203], v[64:67]
	s_waitcnt lgkmcnt(11)
	v_mfma_f32_16x16x32_f16 v[68:71], v[172:175], v[204:207], v[68:71]
	s_waitcnt lgkmcnt(10)
	v_mfma_f32_16x16x32_f16 v[72:75], v[176:179], v[192:195], v[72:75]
	v_mfma_f32_16x16x32_f16 v[76:79], v[176:179], v[196:199], v[76:79]
	s_add_u32 m0, s28, 0xf000
	s_nop 0
	global_load_lds_dwordx4 v11, s[4:5]
	v_mfma_f32_16x16x32_f16 v[80:83], v[176:179], v[200:203], v[80:83]
	v_mfma_f32_16x16x32_f16 v[84:87], v[176:179], v[204:207], v[84:87]
	s_waitcnt lgkmcnt(9)
	v_mfma_f32_16x16x32_f16 v[88:91], v[180:183], v[192:195], v[88:91]
	v_mfma_f32_16x16x32_f16 v[92:95], v[180:183], v[196:199], v[92:95]
	v_mfma_f32_16x16x32_f16 v[96:99], v[180:183], v[200:203], v[96:99]
	s_add_u32 m0, s28, 0x11000
	s_nop 0
	global_load_lds_dwordx4 v12, s[4:5]
	v_mfma_f32_16x16x32_f16 v[100:103], v[180:183], v[204:207], v[100:103]
	s_waitcnt lgkmcnt(8)
	v_mfma_f32_16x16x32_f16 v[104:107], v[184:187], v[192:195], v[104:107]
	v_mfma_f32_16x16x32_f16 v[108:111], v[184:187], v[196:199], v[108:111]
	v_mfma_f32_16x16x32_f16 v[112:115], v[184:187], v[200:203], v[112:115]
	v_mfma_f32_16x16x32_f16 v[116:119], v[184:187], v[204:207], v[116:119]
	s_waitcnt lgkmcnt(7)
	ds_read_b128 v[172:175], v20
	ds_read_b128 v[192:195], v22
	ds_read_b128 v[196:199], v22 offset:2048
	ds_read_b128 v[200:203], v22 offset:4096
	ds_read_b128 v[204:207], v22 offset:6144
	ds_read_b128 v[176:179], v20 offset:2048
	ds_read_b128 v[180:183], v20 offset:4096
	ds_read_b128 v[184:187], v20 offset:6144
	s_waitcnt lgkmcnt(14)
	v_mfma_f32_16x16x32_f16 v[56:59], v[136:139], v[156:159], v[56:59]
	s_add_u32 m0, s28, 0x13000
	s_nop 0
	global_load_lds_dwordx4 v13, s[4:5]
	s_add_u32 s4, s4, s20
	s_addc_u32 s5, s5, 0
	s_waitcnt lgkmcnt(13)
	v_mfma_f32_16x16x32_f16 v[60:63], v[136:139], v[160:163], v[60:63]
	s_waitcnt lgkmcnt(12)
	v_mfma_f32_16x16x32_f16 v[64:67], v[136:139], v[164:167], v[64:67]
	s_waitcnt lgkmcnt(11)
	v_mfma_f32_16x16x32_f16 v[68:71], v[136:139], v[168:171], v[68:71]
	s_waitcnt lgkmcnt(10)
	v_mfma_f32_16x16x32_f16 v[72:75], v[140:143], v[156:159], v[72:75]
	v_mfma_f32_16x16x32_f16 v[76:79], v[140:143], v[160:163], v[76:79]
	s_add_u32 m0, s28, 0x16000
	s_nop 0
	global_load_lds_dwordx4 v10, s[6:7]
	v_mfma_f32_16x16x32_f16 v[80:83], v[140:143], v[164:167], v[80:83]
	v_mfma_f32_16x16x32_f16 v[84:87], v[140:143], v[168:171], v[84:87]
	s_waitcnt lgkmcnt(9)
	v_mfma_f32_16x16x32_f16 v[88:91], v[144:147], v[156:159], v[88:91]
	v_mfma_f32_16x16x32_f16 v[92:95], v[144:147], v[160:163], v[92:95]
	v_mfma_f32_16x16x32_f16 v[96:99], v[144:147], v[164:167], v[96:99]
	s_add_u32 m0, s28, 0x18000
	s_nop 0
	global_load_lds_dwordx4 v11, s[6:7]
	s_add_u32 s6, s6, s20
	s_addc_u32 s7, s7, 0
	v_mfma_f32_16x16x32_f16 v[100:103], v[144:147], v[168:171], v[100:103]
	s_waitcnt lgkmcnt(8)
	v_mfma_f32_16x16x32_f16 v[104:107], v[148:151], v[156:159], v[104:107]
	v_mfma_f32_16x16x32_f16 v[108:111], v[148:151], v[160:163], v[108:111]
	v_mfma_f32_16x16x32_f16 v[112:115], v[148:151], v[164:167], v[112:115]
	v_mfma_f32_16x16x32_f16 v[116:119], v[148:151], v[168:171], v[116:119]
	s_waitcnt vmcnt(6) lgkmcnt(0)
	s_barrier
	s_waitcnt lgkmcnt(7)
	ds_read_b128 v[136:139], v15
	ds_read_b128 v[156:159], v17
	ds_read_b128 v[160:163], v17 offset:2048
	ds_read_b128 v[164:167], v17 offset:4096
	ds_read_b128 v[168:171], v17 offset:6144
	ds_read_b128 v[140:143], v15 offset:2048
	ds_read_b128 v[144:147], v15 offset:4096
	ds_read_b128 v[148:151], v15 offset:6144
	s_waitcnt lgkmcnt(14)
	v_mfma_f32_16x16x32_f16 v[56:59], v[172:175], v[192:195], v[56:59]
	s_add_u32 m0, s28, 0x1a000
	s_nop 0
	global_load_lds_dwordx4 v10, s[4:5]
	s_waitcnt lgkmcnt(13)
	v_mfma_f32_16x16x32_f16 v[60:63], v[172:175], v[196:199], v[60:63]
	s_waitcnt lgkmcnt(12)
	v_mfma_f32_16x16x32_f16 v[64:67], v[172:175], v[200:203], v[64:67]
	s_waitcnt lgkmcnt(11)
	v_mfma_f32_16x16x32_f16 v[68:71], v[172:175], v[204:207], v[68:71]
	s_waitcnt lgkmcnt(10)
	v_mfma_f32_16x16x32_f16 v[72:75], v[176:179], v[192:195], v[72:75]
	v_mfma_f32_16x16x32_f16 v[76:79], v[176:179], v[196:199], v[76:79]
	s_add_u32 m0, s28, 0x1c000
	s_nop 0
	global_load_lds_dwordx4 v11, s[4:5]
	v_mfma_f32_16x16x32_f16 v[80:83], v[176:179], v[200:203], v[80:83]
	v_mfma_f32_16x16x32_f16 v[84:87], v[176:179], v[204:207], v[84:87]
	s_waitcnt lgkmcnt(9)
	v_mfma_f32_16x16x32_f16 v[88:91], v[180:183], v[192:195], v[88:91]
	v_mfma_f32_16x16x32_f16 v[92:95], v[180:183], v[196:199], v[92:95]
	v_mfma_f32_16x16x32_f16 v[96:99], v[180:183], v[200:203], v[96:99]
	s_add_u32 m0, s28, 0x1e000
	s_nop 0
	global_load_lds_dwordx4 v12, s[4:5]
	v_mfma_f32_16x16x32_f16 v[100:103], v[180:183], v[204:207], v[100:103]
	s_waitcnt lgkmcnt(8)
	v_mfma_f32_16x16x32_f16 v[104:107], v[184:187], v[192:195], v[104:107]
	v_mfma_f32_16x16x32_f16 v[108:111], v[184:187], v[196:199], v[108:111]
	v_mfma_f32_16x16x32_f16 v[112:115], v[184:187], v[200:203], v[112:115]
	v_mfma_f32_16x16x32_f16 v[116:119], v[184:187], v[204:207], v[116:119]
	s_waitcnt lgkmcnt(7)
	ds_read_b128 v[172:175], v16
	ds_read_b128 v[192:195], v18
	ds_read_b128 v[196:199], v18 offset:2048
	ds_read_b128 v[200:203], v18 offset:4096
	ds_read_b128 v[204:207], v18 offset:6144
	ds_read_b128 v[176:179], v16 offset:2048
	ds_read_b128 v[180:183], v16 offset:4096
	ds_read_b128 v[184:187], v16 offset:6144
	s_waitcnt lgkmcnt(14)
	v_mfma_f32_16x16x32_f16 v[56:59], v[136:139], v[156:159], v[56:59]
	s_add_u32 m0, s28, 0x20000
	s_nop 0
	global_load_lds_dwordx4 v13, s[4:5]
	s_add_u32 s4, s4, s20
	s_addc_u32 s5, s5, 0
	s_waitcnt lgkmcnt(13)
	v_mfma_f32_16x16x32_f16 v[60:63], v[136:139], v[160:163], v[60:63]
	s_waitcnt lgkmcnt(12)
	v_mfma_f32_16x16x32_f16 v[64:67], v[136:139], v[164:167], v[64:67]
	s_waitcnt lgkmcnt(11)
	v_mfma_f32_16x16x32_f16 v[68:71], v[136:139], v[168:171], v[68:71]
	s_waitcnt lgkmcnt(10)
	v_mfma_f32_16x16x32_f16 v[72:75], v[140:143], v[156:159], v[72:75]
	v_mfma_f32_16x16x32_f16 v[76:79], v[140:143], v[160:163], v[76:79]
	s_add_u32 m0, s28, 0x23000
	s_nop 0
	global_load_lds_dwordx4 v10, s[6:7]
	v_mfma_f32_16x16x32_f16 v[80:83], v[140:143], v[164:167], v[80:83]
	v_mfma_f32_16x16x32_f16 v[84:87], v[140:143], v[168:171], v[84:87]
	s_waitcnt lgkmcnt(9)
	v_mfma_f32_16x16x32_f16 v[88:91], v[144:147], v[156:159], v[88:91]
	v_mfma_f32_16x16x32_f16 v[92:95], v[144:147], v[160:163], v[92:95]
	v_mfma_f32_16x16x32_f16 v[96:99], v[144:147], v[164:167], v[96:99]
	s_add_u32 m0, s28, 0x25000
	s_nop 0
	global_load_lds_dwordx4 v11, s[6:7]
	s_add_u32 s6, s6, s20
	s_addc_u32 s7, s7, 0
	v_mfma_f32_16x16x32_f16 v[100:103], v[144:147], v[168:171], v[100:103]
	s_waitcnt lgkmcnt(8)
	v_mfma_f32_16x16x32_f16 v[104:107], v[148:151], v[156:159], v[104:107]
	v_mfma_f32_16x16x32_f16 v[108:111], v[148:151], v[160:163], v[108:111]
	v_mfma_f32_16x16x32_f16 v[112:115], v[148:151], v[164:167], v[112:115]
	v_mfma_f32_16x16x32_f16 v[116:119], v[148:151], v[168:171], v[116:119]
	s_waitcnt vmcnt(6) lgkmcnt(0)
	s_barrier
	s_waitcnt lgkmcnt(7)
	ds_read_b128 v[136:139], v15 offset:53248
	ds_read_b128 v[156:159], v17 offset:53248
	ds_read_b128 v[160:163], v17 offset:55296
	ds_read_b128 v[164:167], v17 offset:57344
	ds_read_b128 v[168:171], v17 offset:59392
	ds_read_b128 v[140:143], v15 offset:55296
	ds_read_b128 v[144:147], v15 offset:57344
	ds_read_b128 v[148:151], v15 offset:59392
	s_waitcnt lgkmcnt(14)
	v_mfma_f32_16x16x32_f16 v[56:59], v[172:175], v[192:195], v[56:59]
	s_add_u32 m0, s28, 0x0
	s_nop 0
	global_load_lds_dwordx4 v10, s[4:5]
	s_waitcnt lgkmcnt(13)
	v_mfma_f32_16x16x32_f16 v[60:63], v[172:175], v[196:199], v[60:63]
	s_waitcnt lgkmcnt(12)
	v_mfma_f32_16x16x32_f16 v[64:67], v[172:175], v[200:203], v[64:67]
	s_waitcnt lgkmcnt(11)
	v_mfma_f32_16x16x32_f16 v[68:71], v[172:175], v[204:207], v[68:71]
	s_waitcnt lgkmcnt(10)
	v_mfma_f32_16x16x32_f16 v[72:75], v[176:179], v[192:195], v[72:75]
	v_mfma_f32_16x16x32_f16 v[76:79], v[176:179], v[196:199], v[76:79]
	s_add_u32 m0, s28, 0x2000
	s_nop 0
	global_load_lds_dwordx4 v11, s[4:5]
	v_mfma_f32_16x16x32_f16 v[80:83], v[176:179], v[200:203], v[80:83]
	v_mfma_f32_16x16x32_f16 v[84:87], v[176:179], v[204:207], v[84:87]
	s_waitcnt lgkmcnt(9)
	v_mfma_f32_16x16x32_f16 v[88:91], v[180:183], v[192:195], v[88:91]
	v_mfma_f32_16x16x32_f16 v[92:95], v[180:183], v[196:199], v[92:95]
	v_mfma_f32_16x16x32_f16 v[96:99], v[180:183], v[200:203], v[96:99]
	s_add_u32 m0, s28, 0x4000
	s_nop 0
	global_load_lds_dwordx4 v12, s[4:5]
	v_mfma_f32_16x16x32_f16 v[100:103], v[180:183], v[204:207], v[100:103]
	s_waitcnt lgkmcnt(8)
	v_mfma_f32_16x16x32_f16 v[104:107], v[184:187], v[192:195], v[104:107]
	v_mfma_f32_16x16x32_f16 v[108:111], v[184:187], v[196:199], v[108:111]
	v_mfma_f32_16x16x32_f16 v[112:115], v[184:187], v[200:203], v[112:115]
	v_mfma_f32_16x16x32_f16 v[116:119], v[184:187], v[204:207], v[116:119]
	s_waitcnt lgkmcnt(7)
	ds_read_b128 v[172:175], v16 offset:53248
	ds_read_b128 v[192:195], v18 offset:53248
	ds_read_b128 v[196:199], v18 offset:55296
	ds_read_b128 v[200:203], v18 offset:57344
	ds_read_b128 v[204:207], v18 offset:59392
	ds_read_b128 v[176:179], v16 offset:55296
	ds_read_b128 v[180:183], v16 offset:57344
	ds_read_b128 v[184:187], v16 offset:59392
	s_waitcnt lgkmcnt(14)
	v_mfma_f32_16x16x32_f16 v[56:59], v[136:139], v[156:159], v[56:59]
	s_add_u32 m0, s28, 0x6000
	s_nop 0
	global_load_lds_dwordx4 v13, s[4:5]
	s_add_u32 s4, s4, s20
	s_addc_u32 s5, s5, 0
	s_waitcnt lgkmcnt(13)
	v_mfma_f32_16x16x32_f16 v[60:63], v[136:139], v[160:163], v[60:63]
	s_waitcnt lgkmcnt(12)
	v_mfma_f32_16x16x32_f16 v[64:67], v[136:139], v[164:167], v[64:67]
	s_waitcnt lgkmcnt(11)
	v_mfma_f32_16x16x32_f16 v[68:71], v[136:139], v[168:171], v[68:71]
	s_waitcnt lgkmcnt(10)
	v_mfma_f32_16x16x32_f16 v[72:75], v[140:143], v[156:159], v[72:75]
	v_mfma_f32_16x16x32_f16 v[76:79], v[140:143], v[160:163], v[76:79]
	s_add_u32 m0, s28, 0x9000
	s_nop 0
	global_load_lds_dwordx4 v10, s[6:7]
	v_mfma_f32_16x16x32_f16 v[80:83], v[140:143], v[164:167], v[80:83]
	v_mfma_f32_16x16x32_f16 v[84:87], v[140:143], v[168:171], v[84:87]
	s_waitcnt lgkmcnt(9)
	v_mfma_f32_16x16x32_f16 v[88:91], v[144:147], v[156:159], v[88:91]
	v_mfma_f32_16x16x32_f16 v[92:95], v[144:147], v[160:163], v[92:95]
	v_mfma_f32_16x16x32_f16 v[96:99], v[144:147], v[164:167], v[96:99]
	s_add_u32 m0, s28, 0xb000
	s_nop 0
	global_load_lds_dwordx4 v11, s[6:7]
	s_add_u32 s6, s6, s20
	s_addc_u32 s7, s7, 0
	v_mfma_f32_16x16x32_f16 v[100:103], v[144:147], v[168:171], v[100:103]
	s_waitcnt lgkmcnt(8)
	v_mfma_f32_16x16x32_f16 v[104:107], v[148:151], v[156:159], v[104:107]
	v_mfma_f32_16x16x32_f16 v[108:111], v[148:151], v[160:163], v[108:111]
	v_mfma_f32_16x16x32_f16 v[112:115], v[148:151], v[164:167], v[112:115]
	v_mfma_f32_16x16x32_f16 v[116:119], v[148:151], v[168:171], v[116:119]
	s_waitcnt vmcnt(6) lgkmcnt(0)
	s_barrier
	s_waitcnt lgkmcnt(7)
	ds_read_b128 v[136:139], v19
	ds_read_b128 v[156:159], v21
	ds_read_b128 v[160:163], v21 offset:2048
	ds_read_b128 v[164:167], v21 offset:4096
	ds_read_b128 v[168:171], v21 offset:6144
	ds_read_b128 v[140:143], v19 offset:2048
	ds_read_b128 v[144:147], v19 offset:4096
	ds_read_b128 v[148:151], v19 offset:6144
	s_waitcnt lgkmcnt(14)
	v_mfma_f32_16x16x32_f16 v[56:59], v[172:175], v[192:195], v[56:59]
	s_add_u32 m0, s28, 0xd000
	s_nop 0
	global_load_lds_dwordx4 v10, s[4:5]
	s_waitcnt lgkmcnt(13)
	v_mfma_f32_16x16x32_f16 v[60:63], v[172:175], v[196:199], v[60:63]
	s_waitcnt lgkmcnt(12)
	v_mfma_f32_16x16x32_f16 v[64:67], v[172:175], v[200:203], v[64:67]
	s_waitcnt lgkmcnt(11)
	v_mfma_f32_16x16x32_f16 v[68:71], v[172:175], v[204:207], v[68:71]
	s_waitcnt lgkmcnt(10)
	v_mfma_f32_16x16x32_f16 v[72:75], v[176:179], v[192:195], v[72:75]
	v_mfma_f32_16x16x32_f16 v[76:79], v[176:179], v[196:199], v[76:79]
	s_add_u32 m0, s28, 0xf000
	s_nop 0
	global_load_lds_dwordx4 v11, s[4:5]
	v_mfma_f32_16x16x32_f16 v[80:83], v[176:179], v[200:203], v[80:83]
	v_mfma_f32_16x16x32_f16 v[84:87], v[176:179], v[204:207], v[84:87]
	s_waitcnt lgkmcnt(9)
	v_mfma_f32_16x16x32_f16 v[88:91], v[180:183], v[192:195], v[88:91]
	v_mfma_f32_16x16x32_f16 v[92:95], v[180:183], v[196:199], v[92:95]
	v_mfma_f32_16x16x32_f16 v[96:99], v[180:183], v[200:203], v[96:99]
	s_add_u32 m0, s28, 0x11000
	s_nop 0
	global_load_lds_dwordx4 v12, s[4:5]
	v_mfma_f32_16x16x32_f16 v[100:103], v[180:183], v[204:207], v[100:103]
	s_waitcnt lgkmcnt(8)
	v_mfma_f32_16x16x32_f16 v[104:107], v[184:187], v[192:195], v[104:107]
	v_mfma_f32_16x16x32_f16 v[108:111], v[184:187], v[196:199], v[108:111]
	v_mfma_f32_16x16x32_f16 v[112:115], v[184:187], v[200:203], v[112:115]
	v_mfma_f32_16x16x32_f16 v[116:119], v[184:187], v[204:207], v[116:119]
	s_waitcnt lgkmcnt(7)
	ds_read_b128 v[172:175], v20
	ds_read_b128 v[192:195], v22
	ds_read_b128 v[196:199], v22 offset:2048
	ds_read_b128 v[200:203], v22 offset:4096
	ds_read_b128 v[204:207], v22 offset:6144
	ds_read_b128 v[176:179], v20 offset:2048
	ds_read_b128 v[180:183], v20 offset:4096
	ds_read_b128 v[184:187], v20 offset:6144
	s_waitcnt lgkmcnt(14)
	v_mfma_f32_16x16x32_f16 v[56:59], v[136:139], v[156:159], v[56:59]
	s_add_u32 m0, s28, 0x13000
	s_nop 0
	global_load_lds_dwordx4 v13, s[4:5]
	s_add_u32 s4, s4, s20
	s_addc_u32 s5, s5, 0
	s_waitcnt lgkmcnt(13)
	v_mfma_f32_16x16x32_f16 v[60:63], v[136:139], v[160:163], v[60:63]
	s_waitcnt lgkmcnt(12)
	v_mfma_f32_16x16x32_f16 v[64:67], v[136:139], v[164:167], v[64:67]
	s_waitcnt lgkmcnt(11)
	v_mfma_f32_16x16x32_f16 v[68:71], v[136:139], v[168:171], v[68:71]
	s_waitcnt lgkmcnt(10)
	v_mfma_f32_16x16x32_f16 v[72:75], v[140:143], v[156:159], v[72:75]
	v_mfma_f32_16x16x32_f16 v[76:79], v[140:143], v[160:163], v[76:79]
	s_add_u32 m0, s28, 0x16000
	s_nop 0
	global_load_lds_dwordx4 v10, s[6:7]
	v_mfma_f32_16x16x32_f16 v[80:83], v[140:143], v[164:167], v[80:83]
	v_mfma_f32_16x16x32_f16 v[84:87], v[140:143], v[168:171], v[84:87]
	s_waitcnt lgkmcnt(9)
	v_mfma_f32_16x16x32_f16 v[88:91], v[144:147], v[156:159], v[88:91]
	v_mfma_f32_16x16x32_f16 v[92:95], v[144:147], v[160:163], v[92:95]
	v_mfma_f32_16x16x32_f16 v[96:99], v[144:147], v[164:167], v[96:99]
	s_add_u32 m0, s28, 0x18000
	s_nop 0
	global_load_lds_dwordx4 v11, s[6:7]
	s_add_u32 s6, s6, s20
	s_addc_u32 s7, s7, 0
	v_mfma_f32_16x16x32_f16 v[100:103], v[144:147], v[168:171], v[100:103]
	s_waitcnt lgkmcnt(8)
	v_mfma_f32_16x16x32_f16 v[104:107], v[148:151], v[156:159], v[104:107]
	v_mfma_f32_16x16x32_f16 v[108:111], v[148:151], v[160:163], v[108:111]
	v_mfma_f32_16x16x32_f16 v[112:115], v[148:151], v[164:167], v[112:115]
	v_mfma_f32_16x16x32_f16 v[116:119], v[148:151], v[168:171], v[116:119]
	s_waitcnt vmcnt(6) lgkmcnt(0)
	s_barrier
	s_waitcnt lgkmcnt(7)
	ds_read_b128 v[136:139], v15
	ds_read_b128 v[156:159], v17
	ds_read_b128 v[160:163], v17 offset:2048
	ds_read_b128 v[164:167], v17 offset:4096
	ds_read_b128 v[168:171], v17 offset:6144
	ds_read_b128 v[140:143], v15 offset:2048
	ds_read_b128 v[144:147], v15 offset:4096
	ds_read_b128 v[148:151], v15 offset:6144
	s_waitcnt lgkmcnt(14)
	v_mfma_f32_16x16x32_f16 v[56:59], v[172:175], v[192:195], v[56:59]
	s_add_u32 m0, s28, 0x1a000
	s_nop 0
	global_load_lds_dwordx4 v10, s[4:5]
	s_waitcnt lgkmcnt(13)
	v_mfma_f32_16x16x32_f16 v[60:63], v[172:175], v[196:199], v[60:63]
	s_waitcnt lgkmcnt(12)
	v_mfma_f32_16x16x32_f16 v[64:67], v[172:175], v[200:203], v[64:67]
	s_waitcnt lgkmcnt(11)
	v_mfma_f32_16x16x32_f16 v[68:71], v[172:175], v[204:207], v[68:71]
	s_waitcnt lgkmcnt(10)
	v_mfma_f32_16x16x32_f16 v[72:75], v[176:179], v[192:195], v[72:75]
	v_mfma_f32_16x16x32_f16 v[76:79], v[176:179], v[196:199], v[76:79]
	s_add_u32 m0, s28, 0x1c000
	s_nop 0
	global_load_lds_dwordx4 v11, s[4:5]
	v_mfma_f32_16x16x32_f16 v[80:83], v[176:179], v[200:203], v[80:83]
	v_mfma_f32_16x16x32_f16 v[84:87], v[176:179], v[204:207], v[84:87]
	s_waitcnt lgkmcnt(9)
	v_mfma_f32_16x16x32_f16 v[88:91], v[180:183], v[192:195], v[88:91]
	v_mfma_f32_16x16x32_f16 v[92:95], v[180:183], v[196:199], v[92:95]
	v_mfma_f32_16x16x32_f16 v[96:99], v[180:183], v[200:203], v[96:99]
	s_add_u32 m0, s28, 0x1e000
	s_nop 0
	global_load_lds_dwordx4 v12, s[4:5]
	v_mfma_f32_16x16x32_f16 v[100:103], v[180:183], v[204:207], v[100:103]
	s_waitcnt lgkmcnt(8)
	v_mfma_f32_16x16x32_f16 v[104:107], v[184:187], v[192:195], v[104:107]
	v_mfma_f32_16x16x32_f16 v[108:111], v[184:187], v[196:199], v[108:111]
	v_mfma_f32_16x16x32_f16 v[112:115], v[184:187], v[200:203], v[112:115]
	v_mfma_f32_16x16x32_f16 v[116:119], v[184:187], v[204:207], v[116:119]
	s_waitcnt lgkmcnt(7)
	ds_read_b128 v[172:175], v16
	ds_read_b128 v[192:195], v18
	ds_read_b128 v[196:199], v18 offset:2048
	ds_read_b128 v[200:203], v18 offset:4096
	ds_read_b128 v[204:207], v18 offset:6144
	ds_read_b128 v[176:179], v16 offset:2048
	ds_read_b128 v[180:183], v16 offset:4096
	ds_read_b128 v[184:187], v16 offset:6144
	s_waitcnt lgkmcnt(14)
	v_mfma_f32_16x16x32_f16 v[56:59], v[136:139], v[156:159], v[56:59]
	s_add_u32 m0, s28, 0x20000
	s_nop 0
	global_load_lds_dwordx4 v13, s[4:5]
	s_add_u32 s4, s4, s20
	s_addc_u32 s5, s5, 0
	s_waitcnt lgkmcnt(13)
	v_mfma_f32_16x16x32_f16 v[60:63], v[136:139], v[160:163], v[60:63]
	s_waitcnt lgkmcnt(12)
	v_mfma_f32_16x16x32_f16 v[64:67], v[136:139], v[164:167], v[64:67]
	s_waitcnt lgkmcnt(11)
	v_mfma_f32_16x16x32_f16 v[68:71], v[136:139], v[168:171], v[68:71]
	s_waitcnt lgkmcnt(10)
	v_mfma_f32_16x16x32_f16 v[72:75], v[140:143], v[156:159], v[72:75]
	v_mfma_f32_16x16x32_f16 v[76:79], v[140:143], v[160:163], v[76:79]
	s_add_u32 m0, s28, 0x23000
	s_nop 0
	global_load_lds_dwordx4 v10, s[6:7]
	v_mfma_f32_16x16x32_f16 v[80:83], v[140:143], v[164:167], v[80:83]
	v_mfma_f32_16x16x32_f16 v[84:87], v[140:143], v[168:171], v[84:87]
	s_waitcnt lgkmcnt(9)
	v_mfma_f32_16x16x32_f16 v[88:91], v[144:147], v[156:159], v[88:91]
	v_mfma_f32_16x16x32_f16 v[92:95], v[144:147], v[160:163], v[92:95]
	v_mfma_f32_16x16x32_f16 v[96:99], v[144:147], v[164:167], v[96:99]
	s_add_u32 m0, s28, 0x25000
	s_nop 0
	global_load_lds_dwordx4 v11, s[6:7]
	s_add_u32 s6, s6, s20
	s_addc_u32 s7, s7, 0
	v_mfma_f32_16x16x32_f16 v[100:103], v[144:147], v[168:171], v[100:103]
	s_waitcnt lgkmcnt(8)
	v_mfma_f32_16x16x32_f16 v[104:107], v[148:151], v[156:159], v[104:107]
	v_mfma_f32_16x16x32_f16 v[108:111], v[148:151], v[160:163], v[108:111]
	v_mfma_f32_16x16x32_f16 v[112:115], v[148:151], v[164:167], v[112:115]
	v_mfma_f32_16x16x32_f16 v[116:119], v[148:151], v[168:171], v[116:119]
	s_waitcnt vmcnt(6) lgkmcnt(0)
	s_barrier
	s_waitcnt lgkmcnt(7)
	ds_read_b128 v[136:139], v15 offset:53248
	ds_read_b128 v[156:159], v17 offset:53248
	ds_read_b128 v[160:163], v17 offset:55296
	ds_read_b128 v[164:167], v17 offset:57344
	ds_read_b128 v[168:171], v17 offset:59392
	ds_read_b128 v[140:143], v15 offset:55296
	ds_read_b128 v[144:147], v15 offset:57344
	ds_read_b128 v[148:151], v15 offset:59392
	s_waitcnt lgkmcnt(14)
	v_mfma_f32_16x16x32_f16 v[56:59], v[172:175], v[192:195], v[56:59]
	s_add_u32 m0, s28, 0x0
	s_nop 0
	global_load_lds_dwordx4 v10, s[4:5]
	s_waitcnt lgkmcnt(13)
	v_mfma_f32_16x16x32_f16 v[60:63], v[172:175], v[196:199], v[60:63]
	s_waitcnt lgkmcnt(12)
	v_mfma_f32_16x16x32_f16 v[64:67], v[172:175], v[200:203], v[64:67]
	s_waitcnt lgkmcnt(11)
	v_mfma_f32_16x16x32_f16 v[68:71], v[172:175], v[204:207], v[68:71]
	s_waitcnt lgkmcnt(10)
	v_mfma_f32_16x16x32_f16 v[72:75], v[176:179], v[192:195], v[72:75]
	v_mfma_f32_16x16x32_f16 v[76:79], v[176:179], v[196:199], v[76:79]
	s_add_u32 m0, s28, 0x2000
	s_nop 0
	global_load_lds_dwordx4 v11, s[4:5]
	v_mfma_f32_16x16x32_f16 v[80:83], v[176:179], v[200:203], v[80:83]
	v_mfma_f32_16x16x32_f16 v[84:87], v[176:179], v[204:207], v[84:87]
	s_waitcnt lgkmcnt(9)
	v_mfma_f32_16x16x32_f16 v[88:91], v[180:183], v[192:195], v[88:91]
	v_mfma_f32_16x16x32_f16 v[92:95], v[180:183], v[196:199], v[92:95]
	v_mfma_f32_16x16x32_f16 v[96:99], v[180:183], v[200:203], v[96:99]
	s_add_u32 m0, s28, 0x4000
	s_nop 0
	global_load_lds_dwordx4 v12, s[4:5]
	v_mfma_f32_16x16x32_f16 v[100:103], v[180:183], v[204:207], v[100:103]
	s_waitcnt lgkmcnt(8)
	v_mfma_f32_16x16x32_f16 v[104:107], v[184:187], v[192:195], v[104:107]
	v_mfma_f32_16x16x32_f16 v[108:111], v[184:187], v[196:199], v[108:111]
	v_mfma_f32_16x16x32_f16 v[112:115], v[184:187], v[200:203], v[112:115]
	v_mfma_f32_16x16x32_f16 v[116:119], v[184:187], v[204:207], v[116:119]
	s_waitcnt lgkmcnt(7)
	ds_read_b128 v[172:175], v16 offset:53248
	ds_read_b128 v[192:195], v18 offset:53248
	ds_read_b128 v[196:199], v18 offset:55296
	ds_read_b128 v[200:203], v18 offset:57344
	ds_read_b128 v[204:207], v18 offset:59392
	ds_read_b128 v[176:179], v16 offset:55296
	ds_read_b128 v[180:183], v16 offset:57344
	ds_read_b128 v[184:187], v16 offset:59392
	s_waitcnt lgkmcnt(14)
	v_mfma_f32_16x16x32_f16 v[56:59], v[136:139], v[156:159], v[56:59]
	s_add_u32 m0, s28, 0x6000
	s_nop 0
	global_load_lds_dwordx4 v13, s[4:5]
	s_add_u32 s4, s4, s20
	s_addc_u32 s5, s5, 0
	s_waitcnt lgkmcnt(13)
	v_mfma_f32_16x16x32_f16 v[60:63], v[136:139], v[160:163], v[60:63]
	s_waitcnt lgkmcnt(12)
	v_mfma_f32_16x16x32_f16 v[64:67], v[136:139], v[164:167], v[64:67]
	s_waitcnt lgkmcnt(11)
	v_mfma_f32_16x16x32_f16 v[68:71], v[136:139], v[168:171], v[68:71]
	s_waitcnt lgkmcnt(10)
	v_mfma_f32_16x16x32_f16 v[72:75], v[140:143], v[156:159], v[72:75]
	v_mfma_f32_16x16x32_f16 v[76:79], v[140:143], v[160:163], v[76:79]
	s_add_u32 m0, s28, 0x9000
	s_nop 0
	global_load_lds_dwordx4 v10, s[6:7]
	v_mfma_f32_16x16x32_f16 v[80:83], v[140:143], v[164:167], v[80:83]
	v_mfma_f32_16x16x32_f16 v[84:87], v[140:143], v[168:171], v[84:87]
	s_waitcnt lgkmcnt(9)
	v_mfma_f32_16x16x32_f16 v[88:91], v[144:147], v[156:159], v[88:91]
	v_mfma_f32_16x16x32_f16 v[92:95], v[144:147], v[160:163], v[92:95]
	v_mfma_f32_16x16x32_f16 v[96:99], v[144:147], v[164:167], v[96:99]
	s_add_u32 m0, s28, 0xb000
	s_nop 0
	global_load_lds_dwordx4 v11, s[6:7]
	s_add_u32 s6, s6, s20
	s_addc_u32 s7, s7, 0
	v_mfma_f32_16x16x32_f16 v[100:103], v[144:147], v[168:171], v[100:103]
	s_waitcnt lgkmcnt(8)
	v_mfma_f32_16x16x32_f16 v[104:107], v[148:151], v[156:159], v[104:107]
	v_mfma_f32_16x16x32_f16 v[108:111], v[148:151], v[160:163], v[108:111]
	v_mfma_f32_16x16x32_f16 v[112:115], v[148:151], v[164:167], v[112:115]
	v_mfma_f32_16x16x32_f16 v[116:119], v[148:151], v[168:171], v[116:119]
	s_waitcnt vmcnt(6) lgkmcnt(0)
	s_barrier
	s_waitcnt lgkmcnt(7)
	ds_read_b128 v[136:139], v19
	ds_read_b128 v[156:159], v21
	ds_read_b128 v[160:163], v21 offset:2048
	ds_read_b128 v[164:167], v21 offset:4096
	ds_read_b128 v[168:171], v21 offset:6144
	ds_read_b128 v[140:143], v19 offset:2048
	ds_read_b128 v[144:147], v19 offset:4096
	ds_read_b128 v[148:151], v19 offset:6144
	s_waitcnt lgkmcnt(14)
	v_mfma_f32_16x16x32_f16 v[56:59], v[172:175], v[192:195], v[56:59]
	s_add_u32 m0, s28, 0xd000
	s_nop 0
	global_load_lds_dwordx4 v10, s[4:5]
	s_waitcnt lgkmcnt(13)
	v_mfma_f32_16x16x32_f16 v[60:63], v[172:175], v[196:199], v[60:63]
	s_waitcnt lgkmcnt(12)
	v_mfma_f32_16x16x32_f16 v[64:67], v[172:175], v[200:203], v[64:67]
	s_waitcnt lgkmcnt(11)
	v_mfma_f32_16x16x32_f16 v[68:71], v[172:175], v[204:207], v[68:71]
	s_waitcnt lgkmcnt(10)
	v_mfma_f32_16x16x32_f16 v[72:75], v[176:179], v[192:195], v[72:75]
	v_mfma_f32_16x16x32_f16 v[76:79], v[176:179], v[196:199], v[76:79]
	s_add_u32 m0, s28, 0xf000
	s_nop 0
	global_load_lds_dwordx4 v11, s[4:5]
	v_mfma_f32_16x16x32_f16 v[80:83], v[176:179], v[200:203], v[80:83]
	v_mfma_f32_16x16x32_f16 v[84:87], v[176:179], v[204:207], v[84:87]
	s_waitcnt lgkmcnt(9)
	v_mfma_f32_16x16x32_f16 v[88:91], v[180:183], v[192:195], v[88:91]
	v_mfma_f32_16x16x32_f16 v[92:95], v[180:183], v[196:199], v[92:95]
	v_mfma_f32_16x16x32_f16 v[96:99], v[180:183], v[200:203], v[96:99]
	s_add_u32 m0, s28, 0x11000
	s_nop 0
	global_load_lds_dwordx4 v12, s[4:5]
	v_mfma_f32_16x16x32_f16 v[100:103], v[180:183], v[204:207], v[100:103]
	s_waitcnt lgkmcnt(8)
	v_mfma_f32_16x16x32_f16 v[104:107], v[184:187], v[192:195], v[104:107]
	v_mfma_f32_16x16x32_f16 v[108:111], v[184:187], v[196:199], v[108:111]
	v_mfma_f32_16x16x32_f16 v[112:115], v[184:187], v[200:203], v[112:115]
	v_mfma_f32_16x16x32_f16 v[116:119], v[184:187], v[204:207], v[116:119]
	s_waitcnt lgkmcnt(7)
	ds_read_b128 v[172:175], v20
	ds_read_b128 v[192:195], v22
	ds_read_b128 v[196:199], v22 offset:2048
	ds_read_b128 v[200:203], v22 offset:4096
	ds_read_b128 v[204:207], v22 offset:6144
	ds_read_b128 v[176:179], v20 offset:2048
	ds_read_b128 v[180:183], v20 offset:4096
	ds_read_b128 v[184:187], v20 offset:6144
	s_waitcnt lgkmcnt(14)
	v_mfma_f32_16x16x32_f16 v[56:59], v[136:139], v[156:159], v[56:59]
	s_add_u32 m0, s28, 0x13000
	s_nop 0
	global_load_lds_dwordx4 v13, s[4:5]
	s_add_u32 s4, s4, s20
	s_addc_u32 s5, s5, 0
	s_waitcnt lgkmcnt(13)
	v_mfma_f32_16x16x32_f16 v[60:63], v[136:139], v[160:163], v[60:63]
	s_waitcnt lgkmcnt(12)
	v_mfma_f32_16x16x32_f16 v[64:67], v[136:139], v[164:167], v[64:67]
	s_waitcnt lgkmcnt(11)
	v_mfma_f32_16x16x32_f16 v[68:71], v[136:139], v[168:171], v[68:71]
	s_waitcnt lgkmcnt(10)
	v_mfma_f32_16x16x32_f16 v[72:75], v[140:143], v[156:159], v[72:75]
	v_mfma_f32_16x16x32_f16 v[76:79], v[140:143], v[160:163], v[76:79]
	s_add_u32 m0, s28, 0x16000
	s_nop 0
	global_load_lds_dwordx4 v10, s[6:7]
	v_mfma_f32_16x16x32_f16 v[80:83], v[140:143], v[164:167], v[80:83]
	v_mfma_f32_16x16x32_f16 v[84:87], v[140:143], v[168:171], v[84:87]
	s_waitcnt lgkmcnt(9)
	v_mfma_f32_16x16x32_f16 v[88:91], v[144:147], v[156:159], v[88:91]
	v_mfma_f32_16x16x32_f16 v[92:95], v[144:147], v[160:163], v[92:95]
	v_mfma_f32_16x16x32_f16 v[96:99], v[144:147], v[164:167], v[96:99]
	s_add_u32 m0, s28, 0x18000
	s_nop 0
	global_load_lds_dwordx4 v11, s[6:7]
	s_add_u32 s6, s6, s20
	s_addc_u32 s7, s7, 0
	v_mfma_f32_16x16x32_f16 v[100:103], v[144:147], v[168:171], v[100:103]
	s_waitcnt lgkmcnt(8)
	v_mfma_f32_16x16x32_f16 v[104:107], v[148:151], v[156:159], v[104:107]
	v_mfma_f32_16x16x32_f16 v[108:111], v[148:151], v[160:163], v[108:111]
	v_mfma_f32_16x16x32_f16 v[112:115], v[148:151], v[164:167], v[112:115]
	v_mfma_f32_16x16x32_f16 v[116:119], v[148:151], v[168:171], v[116:119]
	s_waitcnt vmcnt(6) lgkmcnt(0)
	s_barrier
	s_waitcnt lgkmcnt(7)
	ds_read_b128 v[136:139], v15
	ds_read_b128 v[156:159], v17
	ds_read_b128 v[160:163], v17 offset:2048
	ds_read_b128 v[164:167], v17 offset:4096
	ds_read_b128 v[168:171], v17 offset:6144
	ds_read_b128 v[140:143], v15 offset:2048
	ds_read_b128 v[144:147], v15 offset:4096
	ds_read_b128 v[148:151], v15 offset:6144
	s_waitcnt lgkmcnt(14)
	v_mfma_f32_16x16x32_f16 v[56:59], v[172:175], v[192:195], v[56:59]
	s_add_u32 m0, s28, 0x1a000
	s_nop 0
	global_load_lds_dwordx4 v10, s[4:5]
	s_waitcnt lgkmcnt(13)
	v_mfma_f32_16x16x32_f16 v[60:63], v[172:175], v[196:199], v[60:63]
	s_waitcnt lgkmcnt(12)
	v_mfma_f32_16x16x32_f16 v[64:67], v[172:175], v[200:203], v[64:67]
	s_waitcnt lgkmcnt(11)
	v_mfma_f32_16x16x32_f16 v[68:71], v[172:175], v[204:207], v[68:71]
	s_waitcnt lgkmcnt(10)
	v_mfma_f32_16x16x32_f16 v[72:75], v[176:179], v[192:195], v[72:75]
	v_mfma_f32_16x16x32_f16 v[76:79], v[176:179], v[196:199], v[76:79]
	s_add_u32 m0, s28, 0x1c000
	s_nop 0
	global_load_lds_dwordx4 v11, s[4:5]
	v_mfma_f32_16x16x32_f16 v[80:83], v[176:179], v[200:203], v[80:83]
	v_mfma_f32_16x16x32_f16 v[84:87], v[176:179], v[204:207], v[84:87]
	s_waitcnt lgkmcnt(9)
	v_mfma_f32_16x16x32_f16 v[88:91], v[180:183], v[192:195], v[88:91]
	v_mfma_f32_16x16x32_f16 v[92:95], v[180:183], v[196:199], v[92:95]
	v_mfma_f32_16x16x32_f16 v[96:99], v[180:183], v[200:203], v[96:99]
	s_add_u32 m0, s28, 0x1e000
	s_nop 0
	global_load_lds_dwordx4 v12, s[4:5]
	v_mfma_f32_16x16x32_f16 v[100:103], v[180:183], v[204:207], v[100:103]
	s_waitcnt lgkmcnt(8)
	v_mfma_f32_16x16x32_f16 v[104:107], v[184:187], v[192:195], v[104:107]
	v_mfma_f32_16x16x32_f16 v[108:111], v[184:187], v[196:199], v[108:111]
	v_mfma_f32_16x16x32_f16 v[112:115], v[184:187], v[200:203], v[112:115]
	v_mfma_f32_16x16x32_f16 v[116:119], v[184:187], v[204:207], v[116:119]
	s_waitcnt lgkmcnt(7)
	ds_read_b128 v[172:175], v16
	ds_read_b128 v[192:195], v18
	ds_read_b128 v[196:199], v18 offset:2048
	ds_read_b128 v[200:203], v18 offset:4096
	ds_read_b128 v[204:207], v18 offset:6144
	ds_read_b128 v[176:179], v16 offset:2048
	ds_read_b128 v[180:183], v16 offset:4096
	ds_read_b128 v[184:187], v16 offset:6144
	s_waitcnt lgkmcnt(14)
	v_mfma_f32_16x16x32_f16 v[56:59], v[136:139], v[156:159], v[56:59]
	s_add_u32 m0, s28, 0x20000
	s_nop 0
	global_load_lds_dwordx4 v13, s[4:5]
	s_add_u32 s4, s4, s20
	s_addc_u32 s5, s5, 0
	s_waitcnt lgkmcnt(13)
	v_mfma_f32_16x16x32_f16 v[60:63], v[136:139], v[160:163], v[60:63]
	s_waitcnt lgkmcnt(12)
	v_mfma_f32_16x16x32_f16 v[64:67], v[136:139], v[164:167], v[64:67]
	s_waitcnt lgkmcnt(11)
	v_mfma_f32_16x16x32_f16 v[68:71], v[136:139], v[168:171], v[68:71]
	s_waitcnt lgkmcnt(10)
	v_mfma_f32_16x16x32_f16 v[72:75], v[140:143], v[156:159], v[72:75]
	v_mfma_f32_16x16x32_f16 v[76:79], v[140:143], v[160:163], v[76:79]
	s_add_u32 m0, s28, 0x23000
	s_nop 0
	global_load_lds_dwordx4 v10, s[6:7]
	v_mfma_f32_16x16x32_f16 v[80:83], v[140:143], v[164:167], v[80:83]
	v_mfma_f32_16x16x32_f16 v[84:87], v[140:143], v[168:171], v[84:87]
	s_waitcnt lgkmcnt(9)
	v_mfma_f32_16x16x32_f16 v[88:91], v[144:147], v[156:159], v[88:91]
	v_mfma_f32_16x16x32_f16 v[92:95], v[144:147], v[160:163], v[92:95]
	v_mfma_f32_16x16x32_f16 v[96:99], v[144:147], v[164:167], v[96:99]
	s_add_u32 m0, s28, 0x25000
	s_nop 0
	global_load_lds_dwordx4 v11, s[6:7]
	s_add_u32 s6, s6, s20
	s_addc_u32 s7, s7, 0
	v_mfma_f32_16x16x32_f16 v[100:103], v[144:147], v[168:171], v[100:103]
	s_waitcnt lgkmcnt(8)
	v_mfma_f32_16x16x32_f16 v[104:107], v[148:151], v[156:159], v[104:107]
	v_mfma_f32_16x16x32_f16 v[108:111], v[148:151], v[160:163], v[108:111]
	v_mfma_f32_16x16x32_f16 v[112:115], v[148:151], v[164:167], v[112:115]
	v_mfma_f32_16x16x32_f16 v[116:119], v[148:151], v[168:171], v[116:119]
	s_waitcnt vmcnt(6) lgkmcnt(0)
	s_barrier
	s_waitcnt lgkmcnt(7)
	ds_read_b128 v[136:139], v15 offset:53248
	ds_read_b128 v[156:159], v17 offset:53248
	ds_read_b128 v[160:163], v17 offset:55296
	ds_read_b128 v[164:167], v17 offset:57344
	ds_read_b128 v[168:171], v17 offset:59392
	ds_read_b128 v[140:143], v15 offset:55296
	ds_read_b128 v[144:147], v15 offset:57344
	ds_read_b128 v[148:151], v15 offset:59392
	s_waitcnt lgkmcnt(14)
	v_mfma_f32_16x16x32_f16 v[56:59], v[172:175], v[192:195], v[56:59]
	s_add_u32 m0, s28, 0x0
	s_nop 0
	global_load_lds_dwordx4 v10, s[4:5]
	s_waitcnt lgkmcnt(13)
	v_mfma_f32_16x16x32_f16 v[60:63], v[172:175], v[196:199], v[60:63]
	s_waitcnt lgkmcnt(12)
	v_mfma_f32_16x16x32_f16 v[64:67], v[172:175], v[200:203], v[64:67]
	s_waitcnt lgkmcnt(11)
	v_mfma_f32_16x16x32_f16 v[68:71], v[172:175], v[204:207], v[68:71]
	s_waitcnt lgkmcnt(10)
	v_mfma_f32_16x16x32_f16 v[72:75], v[176:179], v[192:195], v[72:75]
	v_mfma_f32_16x16x32_f16 v[76:79], v[176:179], v[196:199], v[76:79]
	s_add_u32 m0, s28, 0x2000
	s_nop 0
	global_load_lds_dwordx4 v11, s[4:5]
	v_mfma_f32_16x16x32_f16 v[80:83], v[176:179], v[200:203], v[80:83]
	v_mfma_f32_16x16x32_f16 v[84:87], v[176:179], v[204:207], v[84:87]
	s_waitcnt lgkmcnt(9)
	v_mfma_f32_16x16x32_f16 v[88:91], v[180:183], v[192:195], v[88:91]
	v_mfma_f32_16x16x32_f16 v[92:95], v[180:183], v[196:199], v[92:95]
	v_mfma_f32_16x16x32_f16 v[96:99], v[180:183], v[200:203], v[96:99]
	s_add_u32 m0, s28, 0x4000
	s_nop 0
	global_load_lds_dwordx4 v12, s[4:5]
	v_mfma_f32_16x16x32_f16 v[100:103], v[180:183], v[204:207], v[100:103]
	s_waitcnt lgkmcnt(8)
	v_mfma_f32_16x16x32_f16 v[104:107], v[184:187], v[192:195], v[104:107]
	v_mfma_f32_16x16x32_f16 v[108:111], v[184:187], v[196:199], v[108:111]
	v_mfma_f32_16x16x32_f16 v[112:115], v[184:187], v[200:203], v[112:115]
	v_mfma_f32_16x16x32_f16 v[116:119], v[184:187], v[204:207], v[116:119]
	s_waitcnt lgkmcnt(7)
	ds_read_b128 v[172:175], v16 offset:53248
	ds_read_b128 v[192:195], v18 offset:53248
	ds_read_b128 v[196:199], v18 offset:55296
	ds_read_b128 v[200:203], v18 offset:57344
	ds_read_b128 v[204:207], v18 offset:59392
	ds_read_b128 v[176:179], v16 offset:55296
	ds_read_b128 v[180:183], v16 offset:57344
	ds_read_b128 v[184:187], v16 offset:59392
	s_waitcnt lgkmcnt(14)
	v_mfma_f32_16x16x32_f16 v[56:59], v[136:139], v[156:159], v[56:59]
	s_add_u32 m0, s28, 0x6000
	s_nop 0
	global_load_lds_dwordx4 v13, s[4:5]
	s_add_u32 s4, s4, s20
	s_addc_u32 s5, s5, 0
	s_waitcnt lgkmcnt(13)
	v_mfma_f32_16x16x32_f16 v[60:63], v[136:139], v[160:163], v[60:63]
	s_waitcnt lgkmcnt(12)
	v_mfma_f32_16x16x32_f16 v[64:67], v[136:139], v[164:167], v[64:67]
	s_waitcnt lgkmcnt(11)
	v_mfma_f32_16x16x32_f16 v[68:71], v[136:139], v[168:171], v[68:71]
	s_waitcnt lgkmcnt(10)
	v_mfma_f32_16x16x32_f16 v[72:75], v[140:143], v[156:159], v[72:75]
	v_mfma_f32_16x16x32_f16 v[76:79], v[140:143], v[160:163], v[76:79]
	s_add_u32 m0, s28, 0x9000
	s_nop 0
	global_load_lds_dwordx4 v10, s[6:7]
	v_mfma_f32_16x16x32_f16 v[80:83], v[140:143], v[164:167], v[80:83]
	v_mfma_f32_16x16x32_f16 v[84:87], v[140:143], v[168:171], v[84:87]
	s_waitcnt lgkmcnt(9)
	v_mfma_f32_16x16x32_f16 v[88:91], v[144:147], v[156:159], v[88:91]
	v_mfma_f32_16x16x32_f16 v[92:95], v[144:147], v[160:163], v[92:95]
	v_mfma_f32_16x16x32_f16 v[96:99], v[144:147], v[164:167], v[96:99]
	s_add_u32 m0, s28, 0xb000
	s_nop 0
	global_load_lds_dwordx4 v11, s[6:7]
	s_add_u32 s6, s6, s20
	s_addc_u32 s7, s7, 0
	v_mfma_f32_16x16x32_f16 v[100:103], v[144:147], v[168:171], v[100:103]
	s_waitcnt lgkmcnt(8)
	v_mfma_f32_16x16x32_f16 v[104:107], v[148:151], v[156:159], v[104:107]
	v_mfma_f32_16x16x32_f16 v[108:111], v[148:151], v[160:163], v[108:111]
	v_mfma_f32_16x16x32_f16 v[112:115], v[148:151], v[164:167], v[112:115]
	v_mfma_f32_16x16x32_f16 v[116:119], v[148:151], v[168:171], v[116:119]
	s_waitcnt vmcnt(6) lgkmcnt(0)
	s_barrier
	s_waitcnt lgkmcnt(7)
	ds_read_b128 v[136:139], v19
	ds_read_b128 v[156:159], v21
	ds_read_b128 v[160:163], v21 offset:2048
	ds_read_b128 v[164:167], v21 offset:4096
	ds_read_b128 v[168:171], v21 offset:6144
	ds_read_b128 v[140:143], v19 offset:2048
	ds_read_b128 v[144:147], v19 offset:4096
	ds_read_b128 v[148:151], v19 offset:6144
	s_waitcnt lgkmcnt(14)
	v_mfma_f32_16x16x32_f16 v[56:59], v[172:175], v[192:195], v[56:59]
	s_waitcnt lgkmcnt(13)
	v_mfma_f32_16x16x32_f16 v[60:63], v[172:175], v[196:199], v[60:63]
	s_waitcnt lgkmcnt(12)
	v_mfma_f32_16x16x32_f16 v[64:67], v[172:175], v[200:203], v[64:67]
	s_waitcnt lgkmcnt(11)
	v_mfma_f32_16x16x32_f16 v[68:71], v[172:175], v[204:207], v[68:71]
	s_waitcnt lgkmcnt(10)
	v_mfma_f32_16x16x32_f16 v[72:75], v[176:179], v[192:195], v[72:75]
	v_mfma_f32_16x16x32_f16 v[76:79], v[176:179], v[196:199], v[76:79]
	v_mfma_f32_16x16x32_f16 v[80:83], v[176:179], v[200:203], v[80:83]
	v_mfma_f32_16x16x32_f16 v[84:87], v[176:179], v[204:207], v[84:87]
	s_waitcnt lgkmcnt(9)
	v_mfma_f32_16x16x32_f16 v[88:91], v[180:183], v[192:195], v[88:91]
	v_mfma_f32_16x16x32_f16 v[92:95], v[180:183], v[196:199], v[92:95]
	v_mfma_f32_16x16x32_f16 v[96:99], v[180:183], v[200:203], v[96:99]
	v_mfma_f32_16x16x32_f16 v[100:103], v[180:183], v[204:207], v[100:103]
	s_waitcnt lgkmcnt(8)
	v_mfma_f32_16x16x32_f16 v[104:107], v[184:187], v[192:195], v[104:107]
	v_mfma_f32_16x16x32_f16 v[108:111], v[184:187], v[196:199], v[108:111]
	v_mfma_f32_16x16x32_f16 v[112:115], v[184:187], v[200:203], v[112:115]
	v_mfma_f32_16x16x32_f16 v[116:119], v[184:187], v[204:207], v[116:119]
	s_waitcnt lgkmcnt(7)
	ds_read_b128 v[172:175], v20
	ds_read_b128 v[192:195], v22
	ds_read_b128 v[196:199], v22 offset:2048
	ds_read_b128 v[200:203], v22 offset:4096
	ds_read_b128 v[204:207], v22 offset:6144
	ds_read_b128 v[176:179], v20 offset:2048
	ds_read_b128 v[180:183], v20 offset:4096
	ds_read_b128 v[184:187], v20 offset:6144
	s_waitcnt lgkmcnt(14)
	v_mfma_f32_16x16x32_f16 v[56:59], v[136:139], v[156:159], v[56:59]
	s_waitcnt lgkmcnt(13)
	v_mfma_f32_16x16x32_f16 v[60:63], v[136:139], v[160:163], v[60:63]
	s_waitcnt lgkmcnt(12)
	v_mfma_f32_16x16x32_f16 v[64:67], v[136:139], v[164:167], v[64:67]
	s_waitcnt lgkmcnt(11)
	v_mfma_f32_16x16x32_f16 v[68:71], v[136:139], v[168:171], v[68:71]
	s_waitcnt lgkmcnt(10)
	v_mfma_f32_16x16x32_f16 v[72:75], v[140:143], v[156:159], v[72:75]
	v_mfma_f32_16x16x32_f16 v[76:79], v[140:143], v[160:163], v[76:79]
	v_mfma_f32_16x16x32_f16 v[80:83], v[140:143], v[164:167], v[80:83]
	v_mfma_f32_16x16x32_f16 v[84:87], v[140:143], v[168:171], v[84:87]
	s_waitcnt lgkmcnt(9)
	v_mfma_f32_16x16x32_f16 v[88:91], v[144:147], v[156:159], v[88:91]
	v_mfma_f32_16x16x32_f16 v[92:95], v[144:147], v[160:163], v[92:95]
	v_mfma_f32_16x16x32_f16 v[96:99], v[144:147], v[164:167], v[96:99]
	v_mfma_f32_16x16x32_f16 v[100:103], v[144:147], v[168:171], v[100:103]
	s_waitcnt lgkmcnt(8)
	v_mfma_f32_16x16x32_f16 v[104:107], v[148:151], v[156:159], v[104:107]
	v_mfma_f32_16x16x32_f16 v[108:111], v[148:151], v[160:163], v[108:111]
	v_mfma_f32_16x16x32_f16 v[112:115], v[148:151], v[164:167], v[112:115]
	v_mfma_f32_16x16x32_f16 v[116:119], v[148:151], v[168:171], v[116:119]
	s_waitcnt vmcnt(0) lgkmcnt(0)
	s_barrier
	s_waitcnt lgkmcnt(7)
	ds_read_b128 v[136:139], v15
	ds_read_b128 v[156:159], v17
	ds_read_b128 v[160:163], v17 offset:2048
	ds_read_b128 v[164:167], v17 offset:4096
	ds_read_b128 v[168:171], v17 offset:6144
	ds_read_b128 v[140:143], v15 offset:2048
	ds_read_b128 v[144:147], v15 offset:4096
	ds_read_b128 v[148:151], v15 offset:6144
	s_waitcnt lgkmcnt(14)
	v_mfma_f32_16x16x32_f16 v[56:59], v[172:175], v[192:195], v[56:59]
	s_waitcnt lgkmcnt(13)
	v_mfma_f32_16x16x32_f16 v[60:63], v[172:175], v[196:199], v[60:63]
	s_waitcnt lgkmcnt(12)
	v_mfma_f32_16x16x32_f16 v[64:67], v[172:175], v[200:203], v[64:67]
	s_waitcnt lgkmcnt(11)
	v_mfma_f32_16x16x32_f16 v[68:71], v[172:175], v[204:207], v[68:71]
	s_waitcnt lgkmcnt(10)
	v_mfma_f32_16x16x32_f16 v[72:75], v[176:179], v[192:195], v[72:75]
	v_mfma_f32_16x16x32_f16 v[76:79], v[176:179], v[196:199], v[76:79]
	v_mfma_f32_16x16x32_f16 v[80:83], v[176:179], v[200:203], v[80:83]
	v_mfma_f32_16x16x32_f16 v[84:87], v[176:179], v[204:207], v[84:87]
	s_waitcnt lgkmcnt(9)
	v_mfma_f32_16x16x32_f16 v[88:91], v[180:183], v[192:195], v[88:91]
	v_mfma_f32_16x16x32_f16 v[92:95], v[180:183], v[196:199], v[92:95]
	v_mfma_f32_16x16x32_f16 v[96:99], v[180:183], v[200:203], v[96:99]
	v_mfma_f32_16x16x32_f16 v[100:103], v[180:183], v[204:207], v[100:103]
	s_waitcnt lgkmcnt(8)
	v_mfma_f32_16x16x32_f16 v[104:107], v[184:187], v[192:195], v[104:107]
	v_mfma_f32_16x16x32_f16 v[108:111], v[184:187], v[196:199], v[108:111]
	v_mfma_f32_16x16x32_f16 v[112:115], v[184:187], v[200:203], v[112:115]
	v_mfma_f32_16x16x32_f16 v[116:119], v[184:187], v[204:207], v[116:119]
	s_waitcnt lgkmcnt(7)
	ds_read_b128 v[172:175], v16
	ds_read_b128 v[192:195], v18
	ds_read_b128 v[196:199], v18 offset:2048
	ds_read_b128 v[200:203], v18 offset:4096
	ds_read_b128 v[204:207], v18 offset:6144
	ds_read_b128 v[176:179], v16 offset:2048
	ds_read_b128 v[180:183], v16 offset:4096
	ds_read_b128 v[184:187], v16 offset:6144
	s_waitcnt lgkmcnt(14)
	v_mfma_f32_16x16x32_f16 v[56:59], v[136:139], v[156:159], v[56:59]
	s_waitcnt lgkmcnt(13)
	v_mfma_f32_16x16x32_f16 v[60:63], v[136:139], v[160:163], v[60:63]
	s_waitcnt lgkmcnt(12)
	v_mfma_f32_16x16x32_f16 v[64:67], v[136:139], v[164:167], v[64:67]
	s_waitcnt lgkmcnt(11)
	v_mfma_f32_16x16x32_f16 v[68:71], v[136:139], v[168:171], v[68:71]
	s_waitcnt lgkmcnt(10)
	v_mfma_f32_16x16x32_f16 v[72:75], v[140:143], v[156:159], v[72:75]
	v_mfma_f32_16x16x32_f16 v[76:79], v[140:143], v[160:163], v[76:79]
	v_mfma_f32_16x16x32_f16 v[80:83], v[140:143], v[164:167], v[80:83]
	v_mfma_f32_16x16x32_f16 v[84:87], v[140:143], v[168:171], v[84:87]
	s_waitcnt lgkmcnt(9)
	v_mfma_f32_16x16x32_f16 v[88:91], v[144:147], v[156:159], v[88:91]
	v_mfma_f32_16x16x32_f16 v[92:95], v[144:147], v[160:163], v[92:95]
	v_mfma_f32_16x16x32_f16 v[96:99], v[144:147], v[164:167], v[96:99]
	v_mfma_f32_16x16x32_f16 v[100:103], v[144:147], v[168:171], v[100:103]
	s_waitcnt lgkmcnt(8)
	v_mfma_f32_16x16x32_f16 v[104:107], v[148:151], v[156:159], v[104:107]
	v_mfma_f32_16x16x32_f16 v[108:111], v[148:151], v[160:163], v[108:111]
	v_mfma_f32_16x16x32_f16 v[112:115], v[148:151], v[164:167], v[112:115]
	v_mfma_f32_16x16x32_f16 v[116:119], v[148:151], v[168:171], v[116:119]
	s_waitcnt lgkmcnt(6)
	v_mfma_f32_16x16x32_f16 v[56:59], v[172:175], v[192:195], v[56:59]
	s_waitcnt lgkmcnt(5)
	v_mfma_f32_16x16x32_f16 v[60:63], v[172:175], v[196:199], v[60:63]
	s_waitcnt lgkmcnt(4)
	v_mfma_f32_16x16x32_f16 v[64:67], v[172:175], v[200:203], v[64:67]
	s_waitcnt lgkmcnt(3)
	v_mfma_f32_16x16x32_f16 v[68:71], v[172:175], v[204:207], v[68:71]
	s_waitcnt lgkmcnt(2)
	v_mfma_f32_16x16x32_f16 v[72:75], v[176:179], v[192:195], v[72:75]
	v_mfma_f32_16x16x32_f16 v[76:79], v[176:179], v[196:199], v[76:79]
	v_mfma_f32_16x16x32_f16 v[80:83], v[176:179], v[200:203], v[80:83]
	v_mfma_f32_16x16x32_f16 v[84:87], v[176:179], v[204:207], v[84:87]
	s_waitcnt lgkmcnt(1)
	v_mfma_f32_16x16x32_f16 v[88:91], v[180:183], v[192:195], v[88:91]
	v_mfma_f32_16x16x32_f16 v[92:95], v[180:183], v[196:199], v[92:95]
	v_mfma_f32_16x16x32_f16 v[96:99], v[180:183], v[200:203], v[96:99]
	v_mfma_f32_16x16x32_f16 v[100:103], v[180:183], v[204:207], v[100:103]
	s_waitcnt lgkmcnt(0)
	v_mfma_f32_16x16x32_f16 v[104:107], v[184:187], v[192:195], v[104:107]
	v_mfma_f32_16x16x32_f16 v[108:111], v[184:187], v[196:199], v[108:111]
	v_mfma_f32_16x16x32_f16 v[112:115], v[184:187], v[200:203], v[112:115]
	v_mfma_f32_16x16x32_f16 v[116:119], v[184:187], v[204:207], v[116:119]
	s_nop 7
	s_nop 1
	s_add_u32 s24, s29, 0
	s_lshl_b32 s8, s24, 11
	v_add_u32_e32 v212, s8, v23
	v_pk_add_f32 v[56:57], v[56:57], v[24:25] op_sel_hi:[1,0]
	v_pk_add_f32 v[58:59], v[58:59], v[24:25] op_sel_hi:[1,0]
	v_cvt_pk_f16_f32 v56, v56, v57
	v_cvt_pk_f16_f32 v57, v58, v59
	global_store_dwordx2 v212, v[56:57], s[22:23] offset:0
	v_pk_add_f32 v[60:61], v[60:61], v[26:27] op_sel_hi:[1,0]
	v_pk_add_f32 v[62:63], v[62:63], v[26:27] op_sel_hi:[1,0]
	v_cvt_pk_f16_f32 v60, v60, v61
	v_cvt_pk_f16_f32 v61, v62, v63
	global_store_dwordx2 v212, v[60:61], s[22:23] offset:256
	v_pk_add_f32 v[64:65], v[64:65], v[28:29] op_sel_hi:[1,0]
	v_pk_add_f32 v[66:67], v[66:67], v[28:29] op_sel_hi:[1,0]
	v_cvt_pk_f16_f32 v64, v64, v65
	v_cvt_pk_f16_f32 v65, v66, v67
	global_store_dwordx2 v212, v[64:65], s[22:23] offset:1024
	v_pk_add_f32 v[68:69], v[68:69], v[30:31] op_sel_hi:[1,0]
	v_pk_add_f32 v[70:71], v[70:71], v[30:31] op_sel_hi:[1,0]
	v_cvt_pk_f16_f32 v68, v68, v69
	v_cvt_pk_f16_f32 v69, v70, v71
	global_store_dwordx2 v212, v[68:69], s[22:23] offset:1280
	s_add_u32 s24, s29, 1
	s_lshl_b32 s8, s24, 11
	v_add_u32_e32 v212, s8, v23
	v_pk_add_f32 v[72:73], v[72:73], v[24:25] op_sel_hi:[1,0]
	v_pk_add_f32 v[74:75], v[74:75], v[24:25] op_sel_hi:[1,0]
	v_cvt_pk_f16_f32 v72, v72, v73
	v_cvt_pk_f16_f32 v73, v74, v75
	global_store_dwordx2 v212, v[72:73], s[22:23] offset:0
	v_pk_add_f32 v[76:77], v[76:77], v[26:27] op_sel_hi:[1,0]
	v_pk_add_f32 v[78:79], v[78:79], v[26:27] op_sel_hi:[1,0]
	v_cvt_pk_f16_f32 v76, v76, v77
	v_cvt_pk_f16_f32 v77, v78, v79
	global_store_dwordx2 v212, v[76:77], s[22:23] offset:256
	v_pk_add_f32 v[80:81], v[80:81], v[28:29] op_sel_hi:[1,0]
	v_pk_add_f32 v[82:83], v[82:83], v[28:29] op_sel_hi:[1,0]
	v_cvt_pk_f16_f32 v80, v80, v81
	v_cvt_pk_f16_f32 v81, v82, v83
	global_store_dwordx2 v212, v[80:81], s[22:23] offset:1024
	v_pk_add_f32 v[84:85], v[84:85], v[30:31] op_sel_hi:[1,0]
	v_pk_add_f32 v[86:87], v[86:87], v[30:31] op_sel_hi:[1,0]
	v_cvt_pk_f16_f32 v84, v84, v85
	v_cvt_pk_f16_f32 v85, v86, v87
	global_store_dwordx2 v212, v[84:85], s[22:23] offset:1280
	s_add_u32 s24, s29, 2
	s_lshl_b32 s8, s24, 11
	v_add_u32_e32 v212, s8, v23
	v_pk_add_f32 v[88:89], v[88:89], v[24:25] op_sel_hi:[1,0]
	v_pk_add_f32 v[90:91], v[90:91], v[24:25] op_sel_hi:[1,0]
	v_cvt_pk_f16_f32 v88, v88, v89
	v_cvt_pk_f16_f32 v89, v90, v91
	global_store_dwordx2 v212, v[88:89], s[22:23] offset:0
	v_pk_add_f32 v[92:93], v[92:93], v[26:27] op_sel_hi:[1,0]
	v_pk_add_f32 v[94:95], v[94:95], v[26:27] op_sel_hi:[1,0]
	v_cvt_pk_f16_f32 v92, v92, v93
	v_cvt_pk_f16_f32 v93, v94, v95
	global_store_dwordx2 v212, v[92:93], s[22:23] offset:256
	v_pk_add_f32 v[96:97], v[96:97], v[28:29] op_sel_hi:[1,0]
	v_pk_add_f32 v[98:99], v[98:99], v[28:29] op_sel_hi:[1,0]
	v_cvt_pk_f16_f32 v96, v96, v97
	v_cvt_pk_f16_f32 v97, v98, v99
	global_store_dwordx2 v212, v[96:97], s[22:23] offset:1024
	v_pk_add_f32 v[100:101], v[100:101], v[30:31] op_sel_hi:[1,0]
	v_pk_add_f32 v[102:103], v[102:103], v[30:31] op_sel_hi:[1,0]
	v_cvt_pk_f16_f32 v100, v100, v101
	v_cvt_pk_f16_f32 v101, v102, v103
	global_store_dwordx2 v212, v[100:101], s[22:23] offset:1280
	s_add_u32 s24, s29, 3
	s_lshl_b32 s8, s24, 11
	v_add_u32_e32 v212, s8, v23
	v_pk_add_f32 v[104:105], v[104:105], v[24:25] op_sel_hi:[1,0]
	v_pk_add_f32 v[106:107], v[106:107], v[24:25] op_sel_hi:[1,0]
	v_cvt_pk_f16_f32 v104, v104, v105
	v_cvt_pk_f16_f32 v105, v106, v107
	global_store_dwordx2 v212, v[104:105], s[22:23] offset:0
	v_pk_add_f32 v[108:109], v[108:109], v[26:27] op_sel_hi:[1,0]
	v_pk_add_f32 v[110:111], v[110:111], v[26:27] op_sel_hi:[1,0]
	v_cvt_pk_f16_f32 v108, v108, v109
	v_cvt_pk_f16_f32 v109, v110, v111
	global_store_dwordx2 v212, v[108:109], s[22:23] offset:256
	v_pk_add_f32 v[112:113], v[112:113], v[28:29] op_sel_hi:[1,0]
	v_pk_add_f32 v[114:115], v[114:115], v[28:29] op_sel_hi:[1,0]
	v_cvt_pk_f16_f32 v112, v112, v113
	v_cvt_pk_f16_f32 v113, v114, v115
	global_store_dwordx2 v212, v[112:113], s[22:23] offset:1024
	v_pk_add_f32 v[116:117], v[116:117], v[30:31] op_sel_hi:[1,0]
	v_pk_add_f32 v[118:119], v[118:119], v[30:31] op_sel_hi:[1,0]
	v_cvt_pk_f16_f32 v116, v116, v117
	v_cvt_pk_f16_f32 v117, v118, v119
	global_store_dwordx2 v212, v[116:117], s[22:23] offset:1280
	s_branch .Lpf_done
